# speedup vs baseline: 1.0029x; 1.0029x over previous
.Lpf_vKA:
	s_mul_i32 s25, s25, 0x50
	s_add_u32 s29, s10, s25
	s_lshr_b32 s29, s29, 4
	v_add_u32_e32 v5, s25, v3
	v_lshlrev_b32_e32 v5, 7, v5
	v_add_u32_e32 v15, v5, v6
	v_add_u32_e32 v16, v5, v7
	v_add_u32_e32 v5, 0x9000, v9
	v_add_u32_e32 v17, v5, v6
	v_add_u32_e32 v18, v5, v7
	v_add_u32_e32 v19, 0x1a000, v15
	v_add_u32_e32 v20, 0x1a000, v16
	v_add_u32_e32 v21, 0x1a000, v17
	v_add_u32_e32 v22, 0x1a000, v18
	v_lshlrev_b32_e32 v5, 4, v4
	global_load_dwordx4 v[24:27], v5, s[14:15] offset:0
	global_load_dwordx4 v[28:31], v5, s[14:15] offset:64
	global_load_dwordx4 v[32:35], v5, s[14:15] offset:128
	global_load_dwordx4 v[36:39], v5, s[14:15] offset:192
	global_load_dwordx4 v[40:43], v5, s[16:17] offset:0
	global_load_dwordx4 v[44:47], v5, s[16:17] offset:64
	global_load_dwordx4 v[48:51], v5, s[16:17] offset:128
	global_load_dwordx4 v[52:55], v5, s[16:17] offset:192
	s_add_u32 m0, s28, 0x0
	s_nop 0
	global_load_lds_dwordx4 v10, s[4:5]
	s_add_u32 m0, s28, 0x2000
	s_nop 0
	global_load_lds_dwordx4 v11, s[4:5]
	s_add_u32 m0, s28, 0x4000
	s_nop 0
	global_load_lds_dwordx4 v12, s[4:5]
	s_add_u32 m0, s28, 0x6000
	s_nop 0
	global_load_lds_dwordx4 v13, s[4:5]
	s_add_u32 s4, s4, s20
	s_addc_u32 s5, s5, 0
	s_add_u32 m0, s28, 0x9000
	s_nop 0
	global_load_lds_dwordx4 v10, s[6:7]
	s_add_u32 m0, s28, 0xb000
	s_nop 0
	global_load_lds_dwordx4 v11, s[6:7]
	s_add_u32 s6, s6, s20
	s_addc_u32 s7, s7, 0
	s_add_u32 m0, s28, 0xd000
	s_nop 0
	global_load_lds_dwordx4 v10, s[4:5]
	s_add_u32 m0, s28, 0xf000
	s_nop 0
	global_load_lds_dwordx4 v11, s[4:5]
	s_add_u32 m0, s28, 0x11000
	s_nop 0
	global_load_lds_dwordx4 v12, s[4:5]
	s_add_u32 m0, s28, 0x13000
	s_nop 0
	global_load_lds_dwordx4 v13, s[4:5]
	s_add_u32 s4, s4, s20
	s_addc_u32 s5, s5, 0
	s_add_u32 m0, s28, 0x16000
	s_nop 0
	global_load_lds_dwordx4 v10, s[6:7]
	s_add_u32 m0, s28, 0x18000
	s_nop 0
	global_load_lds_dwordx4 v11, s[6:7]
	s_add_u32 s6, s6, s20
	s_addc_u32 s7, s7, 0
	s_add_u32 m0, s28, 0x1a000
	s_nop 0
	global_load_lds_dwordx4 v10, s[4:5]
	s_add_u32 m0, s28, 0x1c000
	s_nop 0
	global_load_lds_dwordx4 v11, s[4:5]
	s_add_u32 m0, s28, 0x1e000
	s_nop 0
	global_load_lds_dwordx4 v12, s[4:5]
	s_add_u32 m0, s28, 0x20000
	s_nop 0
	global_load_lds_dwordx4 v13, s[4:5]
	s_add_u32 s4, s4, s20
	s_addc_u32 s5, s5, 0
	s_add_u32 m0, s28, 0x23000
	s_nop 0
	global_load_lds_dwordx4 v10, s[6:7]
	s_add_u32 m0, s28, 0x25000
	s_nop 0
	global_load_lds_dwordx4 v11, s[6:7]
	s_add_u32 s6, s6, s20
	s_addc_u32 s7, s7, 0
	s_waitcnt vmcnt(12) lgkmcnt(0)
	s_barrier
	s_waitcnt lgkmcnt(6)
	ds_read_b128 v[136:139], v15
	ds_read_b128 v[156:159], v17
	ds_read_b128 v[160:163], v17 offset:2048
	ds_read_b128 v[164:167], v17 offset:4096
	ds_read_b128 v[168:171], v17 offset:6144
	ds_read_b128 v[140:143], v15 offset:2048
	ds_read_b128 v[144:147], v15 offset:4096
	ds_read_b128 v[148:151], v15 offset:6144
	ds_read_b128 v[152:155], v15 offset:8192
	s_waitcnt lgkmcnt(6)
	ds_read_b128 v[172:175], v16
	ds_read_b128 v[192:195], v18
	ds_read_b128 v[196:199], v18 offset:2048
	ds_read_b128 v[200:203], v18 offset:4096
	ds_read_b128 v[204:207], v18 offset:6144
	ds_read_b128 v[176:179], v16 offset:2048
	ds_read_b128 v[180:183], v16 offset:4096
	ds_read_b128 v[184:187], v16 offset:6144
	ds_read_b128 v[188:191], v16 offset:8192
	v_mfma_f32_16x16x32_f16 v[56:59], v[156:159], v[136:139], 0
	s_waitcnt lgkmcnt(15)
	v_mfma_f32_16x16x32_f16 v[60:63], v[160:163], v[136:139], 0
	s_waitcnt lgkmcnt(14)
	v_mfma_f32_16x16x32_f16 v[64:67], v[164:167], v[136:139], 0
	s_waitcnt lgkmcnt(13)
	v_mfma_f32_16x16x32_f16 v[68:71], v[168:171], v[136:139], 0
	s_waitcnt lgkmcnt(12)
	v_mfma_f32_16x16x32_f16 v[72:75], v[156:159], v[140:143], 0
	v_mfma_f32_16x16x32_f16 v[76:79], v[160:163], v[140:143], 0
	v_mfma_f32_16x16x32_f16 v[80:83], v[164:167], v[140:143], 0
	v_mfma_f32_16x16x32_f16 v[84:87], v[168:171], v[140:143], 0
	s_waitcnt lgkmcnt(11)
	v_mfma_f32_16x16x32_f16 v[88:91], v[156:159], v[144:147], 0
	v_mfma_f32_16x16x32_f16 v[92:95], v[160:163], v[144:147], 0
	v_mfma_f32_16x16x32_f16 v[96:99], v[164:167], v[144:147], 0
	v_mfma_f32_16x16x32_f16 v[100:103], v[168:171], v[144:147], 0
	s_waitcnt lgkmcnt(10)
	v_mfma_f32_16x16x32_f16 v[104:107], v[156:159], v[148:151], 0
	v_mfma_f32_16x16x32_f16 v[108:111], v[160:163], v[148:151], 0
	v_mfma_f32_16x16x32_f16 v[112:115], v[164:167], v[148:151], 0
	v_mfma_f32_16x16x32_f16 v[116:119], v[168:171], v[148:151], 0
	s_waitcnt lgkmcnt(9)
	v_mfma_f32_16x16x32_f16 v[120:123], v[156:159], v[152:155], 0
	v_mfma_f32_16x16x32_f16 v[124:127], v[160:163], v[152:155], 0
	v_mfma_f32_16x16x32_f16 v[128:131], v[164:167], v[152:155], 0
	v_mfma_f32_16x16x32_f16 v[132:135], v[168:171], v[152:155], 0
	s_waitcnt vmcnt(6) lgkmcnt(0)
	s_barrier
	s_waitcnt lgkmcnt(6)
	ds_read_b128 v[136:139], v15 offset:53248
	ds_read_b128 v[156:159], v17 offset:53248
	ds_read_b128 v[160:163], v17 offset:55296
	ds_read_b128 v[164:167], v17 offset:57344
	ds_read_b128 v[168:171], v17 offset:59392
	ds_read_b128 v[140:143], v15 offset:55296
	ds_read_b128 v[144:147], v15 offset:57344
	ds_read_b128 v[148:151], v15 offset:59392
	ds_read_b128 v[152:155], v15 offset:61440
	v_mfma_f32_16x16x32_f16 v[56:59], v[192:195], v[172:175], v[56:59]
	s_add_u32 m0, s28, 0x0
	s_nop 0
	global_load_lds_dwordx4 v10, s[4:5]
	s_waitcnt lgkmcnt(15)
	v_mfma_f32_16x16x32_f16 v[60:63], v[196:199], v[172:175], v[60:63]
	s_waitcnt lgkmcnt(14)
	v_mfma_f32_16x16x32_f16 v[64:67], v[200:203], v[172:175], v[64:67]
	s_waitcnt lgkmcnt(13)
	v_mfma_f32_16x16x32_f16 v[68:71], v[204:207], v[172:175], v[68:71]
	s_waitcnt lgkmcnt(12)
	v_mfma_f32_16x16x32_f16 v[72:75], v[192:195], v[176:179], v[72:75]
	v_mfma_f32_16x16x32_f16 v[76:79], v[196:199], v[176:179], v[76:79]
	v_mfma_f32_16x16x32_f16 v[80:83], v[200:203], v[176:179], v[80:83]
	s_add_u32 m0, s28, 0x2000
	s_nop 0
	global_load_lds_dwordx4 v11, s[4:5]
	v_mfma_f32_16x16x32_f16 v[84:87], v[204:207], v[176:179], v[84:87]
	s_waitcnt lgkmcnt(11)
	v_mfma_f32_16x16x32_f16 v[88:91], v[192:195], v[180:183], v[88:91]
	v_mfma_f32_16x16x32_f16 v[92:95], v[196:199], v[180:183], v[92:95]
	v_mfma_f32_16x16x32_f16 v[96:99], v[200:203], v[180:183], v[96:99]
	v_mfma_f32_16x16x32_f16 v[100:103], v[204:207], v[180:183], v[100:103]
	s_waitcnt lgkmcnt(10)
	v_mfma_f32_16x16x32_f16 v[104:107], v[192:195], v[184:187], v[104:107]
	v_mfma_f32_16x16x32_f16 v[108:111], v[196:199], v[184:187], v[108:111]
	s_add_u32 m0, s28, 0x4000
	s_nop 0
	global_load_lds_dwordx4 v12, s[4:5]
	v_mfma_f32_16x16x32_f16 v[112:115], v[200:203], v[184:187], v[112:115]
	v_mfma_f32_16x16x32_f16 v[116:119], v[204:207], v[184:187], v[116:119]
	s_waitcnt lgkmcnt(9)
	v_mfma_f32_16x16x32_f16 v[120:123], v[192:195], v[188:191], v[120:123]
	v_mfma_f32_16x16x32_f16 v[124:127], v[196:199], v[188:191], v[124:127]
	v_mfma_f32_16x16x32_f16 v[128:131], v[200:203], v[188:191], v[128:131]
	v_mfma_f32_16x16x32_f16 v[132:135], v[204:207], v[188:191], v[132:135]
	s_waitcnt lgkmcnt(6)
	ds_read_b128 v[172:175], v16 offset:53248
	ds_read_b128 v[192:195], v18 offset:53248
	ds_read_b128 v[196:199], v18 offset:55296
	ds_read_b128 v[200:203], v18 offset:57344
	ds_read_b128 v[204:207], v18 offset:59392
	ds_read_b128 v[176:179], v16 offset:55296
	ds_read_b128 v[180:183], v16 offset:57344
	ds_read_b128 v[184:187], v16 offset:59392
	ds_read_b128 v[188:191], v16 offset:61440
	v_mfma_f32_16x16x32_f16 v[56:59], v[156:159], v[136:139], v[56:59]
	s_add_u32 m0, s28, 0x6000
	s_nop 0
	global_load_lds_dwordx4 v13, s[4:5]
	s_add_u32 s4, s4, s20
	s_addc_u32 s5, s5, 0
	s_waitcnt lgkmcnt(15)
	v_mfma_f32_16x16x32_f16 v[60:63], v[160:163], v[136:139], v[60:63]
	s_waitcnt lgkmcnt(14)
	v_mfma_f32_16x16x32_f16 v[64:67], v[164:167], v[136:139], v[64:67]
	s_waitcnt lgkmcnt(13)
	v_mfma_f32_16x16x32_f16 v[68:71], v[168:171], v[136:139], v[68:71]
	s_waitcnt lgkmcnt(12)
	v_mfma_f32_16x16x32_f16 v[72:75], v[156:159], v[140:143], v[72:75]
	v_mfma_f32_16x16x32_f16 v[76:79], v[160:163], v[140:143], v[76:79]
	v_mfma_f32_16x16x32_f16 v[80:83], v[164:167], v[140:143], v[80:83]
	s_add_u32 m0, s28, 0x9000
	s_nop 0
	global_load_lds_dwordx4 v10, s[6:7]
	v_mfma_f32_16x16x32_f16 v[84:87], v[168:171], v[140:143], v[84:87]
	s_waitcnt lgkmcnt(11)
	v_mfma_f32_16x16x32_f16 v[88:91], v[156:159], v[144:147], v[88:91]
	v_mfma_f32_16x16x32_f16 v[92:95], v[160:163], v[144:147], v[92:95]
	v_mfma_f32_16x16x32_f16 v[96:99], v[164:167], v[144:147], v[96:99]
	v_mfma_f32_16x16x32_f16 v[100:103], v[168:171], v[144:147], v[100:103]
	s_waitcnt lgkmcnt(10)
	v_mfma_f32_16x16x32_f16 v[104:107], v[156:159], v[148:151], v[104:107]
	v_mfma_f32_16x16x32_f16 v[108:111], v[160:163], v[148:151], v[108:111]
	s_add_u32 m0, s28, 0xb000
	s_nop 0
	global_load_lds_dwordx4 v11, s[6:7]
	s_add_u32 s6, s6, s20
	s_addc_u32 s7, s7, 0
	v_mfma_f32_16x16x32_f16 v[112:115], v[164:167], v[148:151], v[112:115]
	v_mfma_f32_16x16x32_f16 v[116:119], v[168:171], v[148:151], v[116:119]
	s_waitcnt lgkmcnt(9)
	v_mfma_f32_16x16x32_f16 v[120:123], v[156:159], v[152:155], v[120:123]
	v_mfma_f32_16x16x32_f16 v[124:127], v[160:163], v[152:155], v[124:127]
	v_mfma_f32_16x16x32_f16 v[128:131], v[164:167], v[152:155], v[128:131]
	v_mfma_f32_16x16x32_f16 v[132:135], v[168:171], v[152:155], v[132:135]
	s_waitcnt vmcnt(6) lgkmcnt(0)
	s_barrier
	s_waitcnt lgkmcnt(6)
	ds_read_b128 v[136:139], v19
	ds_read_b128 v[156:159], v21
	ds_read_b128 v[160:163], v21 offset:2048
	ds_read_b128 v[164:167], v21 offset:4096
	ds_read_b128 v[168:171], v21 offset:6144
	ds_read_b128 v[140:143], v19 offset:2048
	ds_read_b128 v[144:147], v19 offset:4096
	ds_read_b128 v[148:151], v19 offset:6144
	ds_read_b128 v[152:155], v19 offset:8192
	v_mfma_f32_16x16x32_f16 v[56:59], v[192:195], v[172:175], v[56:59]
	s_add_u32 m0, s28, 0xd000
	s_nop 0
	global_load_lds_dwordx4 v10, s[4:5]
	s_waitcnt lgkmcnt(15)
	v_mfma_f32_16x16x32_f16 v[60:63], v[196:199], v[172:175], v[60:63]
	s_waitcnt lgkmcnt(14)
	v_mfma_f32_16x16x32_f16 v[64:67], v[200:203], v[172:175], v[64:67]
	s_waitcnt lgkmcnt(13)
	v_mfma_f32_16x16x32_f16 v[68:71], v[204:207], v[172:175], v[68:71]
	s_waitcnt lgkmcnt(12)
	v_mfma_f32_16x16x32_f16 v[72:75], v[192:195], v[176:179], v[72:75]
	v_mfma_f32_16x16x32_f16 v[76:79], v[196:199], v[176:179], v[76:79]
	v_mfma_f32_16x16x32_f16 v[80:83], v[200:203], v[176:179], v[80:83]
	s_add_u32 m0, s28, 0xf000
	s_nop 0
	global_load_lds_dwordx4 v11, s[4:5]
	v_mfma_f32_16x16x32_f16 v[84:87], v[204:207], v[176:179], v[84:87]
	s_waitcnt lgkmcnt(11)
	v_mfma_f32_16x16x32_f16 v[88:91], v[192:195], v[180:183], v[88:91]
	v_mfma_f32_16x16x32_f16 v[92:95], v[196:199], v[180:183], v[92:95]
	v_mfma_f32_16x16x32_f16 v[96:99], v[200:203], v[180:183], v[96:99]
	v_mfma_f32_16x16x32_f16 v[100:103], v[204:207], v[180:183], v[100:103]
	s_waitcnt lgkmcnt(10)
	v_mfma_f32_16x16x32_f16 v[104:107], v[192:195], v[184:187], v[104:107]
	v_mfma_f32_16x16x32_f16 v[108:111], v[196:199], v[184:187], v[108:111]
	s_add_u32 m0, s28, 0x11000
	s_nop 0
	global_load_lds_dwordx4 v12, s[4:5]
	v_mfma_f32_16x16x32_f16 v[112:115], v[200:203], v[184:187], v[112:115]
	v_mfma_f32_16x16x32_f16 v[116:119], v[204:207], v[184:187], v[116:119]
	s_waitcnt lgkmcnt(9)
	v_mfma_f32_16x16x32_f16 v[120:123], v[192:195], v[188:191], v[120:123]
	v_mfma_f32_16x16x32_f16 v[124:127], v[196:199], v[188:191], v[124:127]
	v_mfma_f32_16x16x32_f16 v[128:131], v[200:203], v[188:191], v[128:131]
	v_mfma_f32_16x16x32_f16 v[132:135], v[204:207], v[188:191], v[132:135]
	s_waitcnt lgkmcnt(6)
	ds_read_b128 v[172:175], v20
	ds_read_b128 v[192:195], v22
	ds_read_b128 v[196:199], v22 offset:2048
	ds_read_b128 v[200:203], v22 offset:4096
	ds_read_b128 v[204:207], v22 offset:6144
	ds_read_b128 v[176:179], v20 offset:2048
	ds_read_b128 v[180:183], v20 offset:4096
	ds_read_b128 v[184:187], v20 offset:6144
	ds_read_b128 v[188:191], v20 offset:8192
	v_mfma_f32_16x16x32_f16 v[56:59], v[156:159], v[136:139], v[56:59]
	s_add_u32 m0, s28, 0x13000
	s_nop 0
	global_load_lds_dwordx4 v13, s[4:5]
	s_add_u32 s4, s4, s20
	s_addc_u32 s5, s5, 0
	s_waitcnt lgkmcnt(15)
	v_mfma_f32_16x16x32_f16 v[60:63], v[160:163], v[136:139], v[60:63]
	s_waitcnt lgkmcnt(14)
	v_mfma_f32_16x16x32_f16 v[64:67], v[164:167], v[136:139], v[64:67]
	s_waitcnt lgkmcnt(13)
	v_mfma_f32_16x16x32_f16 v[68:71], v[168:171], v[136:139], v[68:71]
	s_waitcnt lgkmcnt(12)
	v_mfma_f32_16x16x32_f16 v[72:75], v[156:159], v[140:143], v[72:75]
	v_mfma_f32_16x16x32_f16 v[76:79], v[160:163], v[140:143], v[76:79]
	v_mfma_f32_16x16x32_f16 v[80:83], v[164:167], v[140:143], v[80:83]
	s_add_u32 m0, s28, 0x16000
	s_nop 0
	global_load_lds_dwordx4 v10, s[6:7]
	v_mfma_f32_16x16x32_f16 v[84:87], v[168:171], v[140:143], v[84:87]
	s_waitcnt lgkmcnt(11)
	v_mfma_f32_16x16x32_f16 v[88:91], v[156:159], v[144:147], v[88:91]
	v_mfma_f32_16x16x32_f16 v[92:95], v[160:163], v[144:147], v[92:95]
	v_mfma_f32_16x16x32_f16 v[96:99], v[164:167], v[144:147], v[96:99]
	v_mfma_f32_16x16x32_f16 v[100:103], v[168:171], v[144:147], v[100:103]
	s_waitcnt lgkmcnt(10)
	v_mfma_f32_16x16x32_f16 v[104:107], v[156:159], v[148:151], v[104:107]
	v_mfma_f32_16x16x32_f16 v[108:111], v[160:163], v[148:151], v[108:111]
	s_add_u32 m0, s28, 0x18000
	s_nop 0
	global_load_lds_dwordx4 v11, s[6:7]
	s_add_u32 s6, s6, s20
	s_addc_u32 s7, s7, 0
	v_mfma_f32_16x16x32_f16 v[112:115], v[164:167], v[148:151], v[112:115]
	v_mfma_f32_16x16x32_f16 v[116:119], v[168:171], v[148:151], v[116:119]
	s_waitcnt lgkmcnt(9)
	v_mfma_f32_16x16x32_f16 v[120:123], v[156:159], v[152:155], v[120:123]
	v_mfma_f32_16x16x32_f16 v[124:127], v[160:163], v[152:155], v[124:127]
	v_mfma_f32_16x16x32_f16 v[128:131], v[164:167], v[152:155], v[128:131]
	v_mfma_f32_16x16x32_f16 v[132:135], v[168:171], v[152:155], v[132:135]
	s_waitcnt vmcnt(6) lgkmcnt(0)
	s_barrier
	s_waitcnt lgkmcnt(6)
	ds_read_b128 v[136:139], v15
	ds_read_b128 v[156:159], v17
	ds_read_b128 v[160:163], v17 offset:2048
	ds_read_b128 v[164:167], v17 offset:4096
	ds_read_b128 v[168:171], v17 offset:6144
	ds_read_b128 v[140:143], v15 offset:2048
	ds_read_b128 v[144:147], v15 offset:4096
	ds_read_b128 v[148:151], v15 offset:6144
	ds_read_b128 v[152:155], v15 offset:8192
	v_mfma_f32_16x16x32_f16 v[56:59], v[192:195], v[172:175], v[56:59]
	s_add_u32 m0, s28, 0x1a000
	s_nop 0
	global_load_lds_dwordx4 v10, s[4:5]
	s_waitcnt lgkmcnt(15)
	v_mfma_f32_16x16x32_f16 v[60:63], v[196:199], v[172:175], v[60:63]
	s_waitcnt lgkmcnt(14)
	v_mfma_f32_16x16x32_f16 v[64:67], v[200:203], v[172:175], v[64:67]
	s_waitcnt lgkmcnt(13)
	v_mfma_f32_16x16x32_f16 v[68:71], v[204:207], v[172:175], v[68:71]
	s_waitcnt lgkmcnt(12)
	v_mfma_f32_16x16x32_f16 v[72:75], v[192:195], v[176:179], v[72:75]
	v_mfma_f32_16x16x32_f16 v[76:79], v[196:199], v[176:179], v[76:79]
	v_mfma_f32_16x16x32_f16 v[80:83], v[200:203], v[176:179], v[80:83]
	s_add_u32 m0, s28, 0x1c000
	s_nop 0
	global_load_lds_dwordx4 v11, s[4:5]
	v_mfma_f32_16x16x32_f16 v[84:87], v[204:207], v[176:179], v[84:87]
	s_waitcnt lgkmcnt(11)
	v_mfma_f32_16x16x32_f16 v[88:91], v[192:195], v[180:183], v[88:91]
	v_mfma_f32_16x16x32_f16 v[92:95], v[196:199], v[180:183], v[92:95]
	v_mfma_f32_16x16x32_f16 v[96:99], v[200:203], v[180:183], v[96:99]
	v_mfma_f32_16x16x32_f16 v[100:103], v[204:207], v[180:183], v[100:103]
	s_waitcnt lgkmcnt(10)
	v_mfma_f32_16x16x32_f16 v[104:107], v[192:195], v[184:187], v[104:107]
	v_mfma_f32_16x16x32_f16 v[108:111], v[196:199], v[184:187], v[108:111]
	s_add_u32 m0, s28, 0x1e000
	s_nop 0
	global_load_lds_dwordx4 v12, s[4:5]
	v_mfma_f32_16x16x32_f16 v[112:115], v[200:203], v[184:187], v[112:115]
	v_mfma_f32_16x16x32_f16 v[116:119], v[204:207], v[184:187], v[116:119]
	s_waitcnt lgkmcnt(9)
	v_mfma_f32_16x16x32_f16 v[120:123], v[192:195], v[188:191], v[120:123]
	v_mfma_f32_16x16x32_f16 v[124:127], v[196:199], v[188:191], v[124:127]
	v_mfma_f32_16x16x32_f16 v[128:131], v[200:203], v[188:191], v[128:131]
	v_mfma_f32_16x16x32_f16 v[132:135], v[204:207], v[188:191], v[132:135]
	s_waitcnt lgkmcnt(6)
	ds_read_b128 v[172:175], v16
	ds_read_b128 v[192:195], v18
	ds_read_b128 v[196:199], v18 offset:2048
	ds_read_b128 v[200:203], v18 offset:4096
	ds_read_b128 v[204:207], v18 offset:6144
	ds_read_b128 v[176:179], v16 offset:2048
	ds_read_b128 v[180:183], v16 offset:4096
	ds_read_b128 v[184:187], v16 offset:6144
	ds_read_b128 v[188:191], v16 offset:8192
	v_mfma_f32_16x16x32_f16 v[56:59], v[156:159], v[136:139], v[56:59]
	s_add_u32 m0, s28, 0x20000
	s_nop 0
	global_load_lds_dwordx4 v13, s[4:5]
	s_add_u32 s4, s4, s20
	s_addc_u32 s5, s5, 0
	s_waitcnt lgkmcnt(15)
	v_mfma_f32_16x16x32_f16 v[60:63], v[160:163], v[136:139], v[60:63]
	s_waitcnt lgkmcnt(14)
	v_mfma_f32_16x16x32_f16 v[64:67], v[164:167], v[136:139], v[64:67]
	s_waitcnt lgkmcnt(13)
	v_mfma_f32_16x16x32_f16 v[68:71], v[168:171], v[136:139], v[68:71]
	s_waitcnt lgkmcnt(12)
	v_mfma_f32_16x16x32_f16 v[72:75], v[156:159], v[140:143], v[72:75]
	v_mfma_f32_16x16x32_f16 v[76:79], v[160:163], v[140:143], v[76:79]
	v_mfma_f32_16x16x32_f16 v[80:83], v[164:167], v[140:143], v[80:83]
	s_add_u32 m0, s28, 0x23000
	s_nop 0
	global_load_lds_dwordx4 v10, s[6:7]
	v_mfma_f32_16x16x32_f16 v[84:87], v[168:171], v[140:143], v[84:87]
	s_waitcnt lgkmcnt(11)
	v_mfma_f32_16x16x32_f16 v[88:91], v[156:159], v[144:147], v[88:91]
	v_mfma_f32_16x16x32_f16 v[92:95], v[160:163], v[144:147], v[92:95]
	v_mfma_f32_16x16x32_f16 v[96:99], v[164:167], v[144:147], v[96:99]
	v_mfma_f32_16x16x32_f16 v[100:103], v[168:171], v[144:147], v[100:103]
	s_waitcnt lgkmcnt(10)
	v_mfma_f32_16x16x32_f16 v[104:107], v[156:159], v[148:151], v[104:107]
	v_mfma_f32_16x16x32_f16 v[108:111], v[160:163], v[148:151], v[108:111]
	s_add_u32 m0, s28, 0x25000
	s_nop 0
	global_load_lds_dwordx4 v11, s[6:7]
	s_add_u32 s6, s6, s20
	s_addc_u32 s7, s7, 0
	v_mfma_f32_16x16x32_f16 v[112:115], v[164:167], v[148:151], v[112:115]
	v_mfma_f32_16x16x32_f16 v[116:119], v[168:171], v[148:151], v[116:119]
	s_waitcnt lgkmcnt(9)
	v_mfma_f32_16x16x32_f16 v[120:123], v[156:159], v[152:155], v[120:123]
	v_mfma_f32_16x16x32_f16 v[124:127], v[160:163], v[152:155], v[124:127]
	v_mfma_f32_16x16x32_f16 v[128:131], v[164:167], v[152:155], v[128:131]
	v_mfma_f32_16x16x32_f16 v[132:135], v[168:171], v[152:155], v[132:135]
	s_waitcnt vmcnt(6) lgkmcnt(0)
	s_barrier
	s_waitcnt lgkmcnt(6)
	ds_read_b128 v[136:139], v15 offset:53248
	ds_read_b128 v[156:159], v17 offset:53248
	ds_read_b128 v[160:163], v17 offset:55296
	ds_read_b128 v[164:167], v17 offset:57344
	ds_read_b128 v[168:171], v17 offset:59392
	ds_read_b128 v[140:143], v15 offset:55296
	ds_read_b128 v[144:147], v15 offset:57344
	ds_read_b128 v[148:151], v15 offset:59392
	ds_read_b128 v[152:155], v15 offset:61440
	v_mfma_f32_16x16x32_f16 v[56:59], v[192:195], v[172:175], v[56:59]
	s_add_u32 m0, s28, 0x0
	s_nop 0
	global_load_lds_dwordx4 v10, s[4:5]
	s_waitcnt lgkmcnt(15)
	v_mfma_f32_16x16x32_f16 v[60:63], v[196:199], v[172:175], v[60:63]
	s_waitcnt lgkmcnt(14)
	v_mfma_f32_16x16x32_f16 v[64:67], v[200:203], v[172:175], v[64:67]
	s_waitcnt lgkmcnt(13)
	v_mfma_f32_16x16x32_f16 v[68:71], v[204:207], v[172:175], v[68:71]
	s_waitcnt lgkmcnt(12)
	v_mfma_f32_16x16x32_f16 v[72:75], v[192:195], v[176:179], v[72:75]
	v_mfma_f32_16x16x32_f16 v[76:79], v[196:199], v[176:179], v[76:79]
	v_mfma_f32_16x16x32_f16 v[80:83], v[200:203], v[176:179], v[80:83]
	s_add_u32 m0, s28, 0x2000
	s_nop 0
	global_load_lds_dwordx4 v11, s[4:5]
	v_mfma_f32_16x16x32_f16 v[84:87], v[204:207], v[176:179], v[84:87]
	s_waitcnt lgkmcnt(11)
	v_mfma_f32_16x16x32_f16 v[88:91], v[192:195], v[180:183], v[88:91]
	v_mfma_f32_16x16x32_f16 v[92:95], v[196:199], v[180:183], v[92:95]
	v_mfma_f32_16x16x32_f16 v[96:99], v[200:203], v[180:183], v[96:99]
	v_mfma_f32_16x16x32_f16 v[100:103], v[204:207], v[180:183], v[100:103]
	s_waitcnt lgkmcnt(10)
	v_mfma_f32_16x16x32_f16 v[104:107], v[192:195], v[184:187], v[104:107]
	v_mfma_f32_16x16x32_f16 v[108:111], v[196:199], v[184:187], v[108:111]
	s_add_u32 m0, s28, 0x4000
	s_nop 0
	global_load_lds_dwordx4 v12, s[4:5]
	v_mfma_f32_16x16x32_f16 v[112:115], v[200:203], v[184:187], v[112:115]
	v_mfma_f32_16x16x32_f16 v[116:119], v[204:207], v[184:187], v[116:119]
	s_waitcnt lgkmcnt(9)
	v_mfma_f32_16x16x32_f16 v[120:123], v[192:195], v[188:191], v[120:123]
	v_mfma_f32_16x16x32_f16 v[124:127], v[196:199], v[188:191], v[124:127]
	v_mfma_f32_16x16x32_f16 v[128:131], v[200:203], v[188:191], v[128:131]
	v_mfma_f32_16x16x32_f16 v[132:135], v[204:207], v[188:191], v[132:135]
	s_waitcnt lgkmcnt(6)
	ds_read_b128 v[172:175], v16 offset:53248
	ds_read_b128 v[192:195], v18 offset:53248
	ds_read_b128 v[196:199], v18 offset:55296
	ds_read_b128 v[200:203], v18 offset:57344
	ds_read_b128 v[204:207], v18 offset:59392
	ds_read_b128 v[176:179], v16 offset:55296
	ds_read_b128 v[180:183], v16 offset:57344
	ds_read_b128 v[184:187], v16 offset:59392
	ds_read_b128 v[188:191], v16 offset:61440
	v_mfma_f32_16x16x32_f16 v[56:59], v[156:159], v[136:139], v[56:59]
	s_add_u32 m0, s28, 0x6000
	s_nop 0
	global_load_lds_dwordx4 v13, s[4:5]
	s_add_u32 s4, s4, s20
	s_addc_u32 s5, s5, 0
	s_waitcnt lgkmcnt(15)
	v_mfma_f32_16x16x32_f16 v[60:63], v[160:163], v[136:139], v[60:63]
	s_waitcnt lgkmcnt(14)
	v_mfma_f32_16x16x32_f16 v[64:67], v[164:167], v[136:139], v[64:67]
	s_waitcnt lgkmcnt(13)
	v_mfma_f32_16x16x32_f16 v[68:71], v[168:171], v[136:139], v[68:71]
	s_waitcnt lgkmcnt(12)
	v_mfma_f32_16x16x32_f16 v[72:75], v[156:159], v[140:143], v[72:75]
	v_mfma_f32_16x16x32_f16 v[76:79], v[160:163], v[140:143], v[76:79]
	v_mfma_f32_16x16x32_f16 v[80:83], v[164:167], v[140:143], v[80:83]
	s_add_u32 m0, s28, 0x9000
	s_nop 0
	global_load_lds_dwordx4 v10, s[6:7]
	v_mfma_f32_16x16x32_f16 v[84:87], v[168:171], v[140:143], v[84:87]
	s_waitcnt lgkmcnt(11)
	v_mfma_f32_16x16x32_f16 v[88:91], v[156:159], v[144:147], v[88:91]
	v_mfma_f32_16x16x32_f16 v[92:95], v[160:163], v[144:147], v[92:95]
	v_mfma_f32_16x16x32_f16 v[96:99], v[164:167], v[144:147], v[96:99]
	v_mfma_f32_16x16x32_f16 v[100:103], v[168:171], v[144:147], v[100:103]
	s_waitcnt lgkmcnt(10)
	v_mfma_f32_16x16x32_f16 v[104:107], v[156:159], v[148:151], v[104:107]
	v_mfma_f32_16x16x32_f16 v[108:111], v[160:163], v[148:151], v[108:111]
	s_add_u32 m0, s28, 0xb000
	s_nop 0
	global_load_lds_dwordx4 v11, s[6:7]
	s_add_u32 s6, s6, s20
	s_addc_u32 s7, s7, 0
	v_mfma_f32_16x16x32_f16 v[112:115], v[164:167], v[148:151], v[112:115]
	v_mfma_f32_16x16x32_f16 v[116:119], v[168:171], v[148:151], v[116:119]
	s_waitcnt lgkmcnt(9)
	v_mfma_f32_16x16x32_f16 v[120:123], v[156:159], v[152:155], v[120:123]
	v_mfma_f32_16x16x32_f16 v[124:127], v[160:163], v[152:155], v[124:127]
	v_mfma_f32_16x16x32_f16 v[128:131], v[164:167], v[152:155], v[128:131]
	v_mfma_f32_16x16x32_f16 v[132:135], v[168:171], v[152:155], v[132:135]
	s_waitcnt vmcnt(6) lgkmcnt(0)
	s_barrier
	s_waitcnt lgkmcnt(6)
	ds_read_b128 v[136:139], v19
	ds_read_b128 v[156:159], v21
	ds_read_b128 v[160:163], v21 offset:2048
	ds_read_b128 v[164:167], v21 offset:4096
	ds_read_b128 v[168:171], v21 offset:6144
	ds_read_b128 v[140:143], v19 offset:2048
	ds_read_b128 v[144:147], v19 offset:4096
	ds_read_b128 v[148:151], v19 offset:6144
	ds_read_b128 v[152:155], v19 offset:8192
	v_mfma_f32_16x16x32_f16 v[56:59], v[192:195], v[172:175], v[56:59]
	s_add_u32 m0, s28, 0xd000
	s_nop 0
	global_load_lds_dwordx4 v10, s[4:5]
	s_waitcnt lgkmcnt(15)
	v_mfma_f32_16x16x32_f16 v[60:63], v[196:199], v[172:175], v[60:63]
	s_waitcnt lgkmcnt(14)
	v_mfma_f32_16x16x32_f16 v[64:67], v[200:203], v[172:175], v[64:67]
	s_waitcnt lgkmcnt(13)
	v_mfma_f32_16x16x32_f16 v[68:71], v[204:207], v[172:175], v[68:71]
	s_waitcnt lgkmcnt(12)
	v_mfma_f32_16x16x32_f16 v[72:75], v[192:195], v[176:179], v[72:75]
	v_mfma_f32_16x16x32_f16 v[76:79], v[196:199], v[176:179], v[76:79]
	v_mfma_f32_16x16x32_f16 v[80:83], v[200:203], v[176:179], v[80:83]
	s_add_u32 m0, s28, 0xf000
	s_nop 0
	global_load_lds_dwordx4 v11, s[4:5]
	v_mfma_f32_16x16x32_f16 v[84:87], v[204:207], v[176:179], v[84:87]
	s_waitcnt lgkmcnt(11)
	v_mfma_f32_16x16x32_f16 v[88:91], v[192:195], v[180:183], v[88:91]
	v_mfma_f32_16x16x32_f16 v[92:95], v[196:199], v[180:183], v[92:95]
	v_mfma_f32_16x16x32_f16 v[96:99], v[200:203], v[180:183], v[96:99]
	v_mfma_f32_16x16x32_f16 v[100:103], v[204:207], v[180:183], v[100:103]
	s_waitcnt lgkmcnt(10)
	v_mfma_f32_16x16x32_f16 v[104:107], v[192:195], v[184:187], v[104:107]
	v_mfma_f32_16x16x32_f16 v[108:111], v[196:199], v[184:187], v[108:111]
	s_add_u32 m0, s28, 0x11000
	s_nop 0
	global_load_lds_dwordx4 v12, s[4:5]
	v_mfma_f32_16x16x32_f16 v[112:115], v[200:203], v[184:187], v[112:115]
	v_mfma_f32_16x16x32_f16 v[116:119], v[204:207], v[184:187], v[116:119]
	s_waitcnt lgkmcnt(9)
	v_mfma_f32_16x16x32_f16 v[120:123], v[192:195], v[188:191], v[120:123]
	v_mfma_f32_16x16x32_f16 v[124:127], v[196:199], v[188:191], v[124:127]
	v_mfma_f32_16x16x32_f16 v[128:131], v[200:203], v[188:191], v[128:131]
	v_mfma_f32_16x16x32_f16 v[132:135], v[204:207], v[188:191], v[132:135]
	s_waitcnt lgkmcnt(6)
	ds_read_b128 v[172:175], v20
	ds_read_b128 v[192:195], v22
	ds_read_b128 v[196:199], v22 offset:2048
	ds_read_b128 v[200:203], v22 offset:4096
	ds_read_b128 v[204:207], v22 offset:6144
	ds_read_b128 v[176:179], v20 offset:2048
	ds_read_b128 v[180:183], v20 offset:4096
	ds_read_b128 v[184:187], v20 offset:6144
	ds_read_b128 v[188:191], v20 offset:8192
	v_mfma_f32_16x16x32_f16 v[56:59], v[156:159], v[136:139], v[56:59]
	s_add_u32 m0, s28, 0x13000
	s_nop 0
	global_load_lds_dwordx4 v13, s[4:5]
	s_add_u32 s4, s4, s20
	s_addc_u32 s5, s5, 0
	s_waitcnt lgkmcnt(15)
	v_mfma_f32_16x16x32_f16 v[60:63], v[160:163], v[136:139], v[60:63]
	s_waitcnt lgkmcnt(14)
	v_mfma_f32_16x16x32_f16 v[64:67], v[164:167], v[136:139], v[64:67]
	s_waitcnt lgkmcnt(13)
	v_mfma_f32_16x16x32_f16 v[68:71], v[168:171], v[136:139], v[68:71]
	s_waitcnt lgkmcnt(12)
	v_mfma_f32_16x16x32_f16 v[72:75], v[156:159], v[140:143], v[72:75]
	v_mfma_f32_16x16x32_f16 v[76:79], v[160:163], v[140:143], v[76:79]
	v_mfma_f32_16x16x32_f16 v[80:83], v[164:167], v[140:143], v[80:83]
	s_add_u32 m0, s28, 0x16000
	s_nop 0
	global_load_lds_dwordx4 v10, s[6:7]
	v_mfma_f32_16x16x32_f16 v[84:87], v[168:171], v[140:143], v[84:87]
	s_waitcnt lgkmcnt(11)
	v_mfma_f32_16x16x32_f16 v[88:91], v[156:159], v[144:147], v[88:91]
	v_mfma_f32_16x16x32_f16 v[92:95], v[160:163], v[144:147], v[92:95]
	v_mfma_f32_16x16x32_f16 v[96:99], v[164:167], v[144:147], v[96:99]
	v_mfma_f32_16x16x32_f16 v[100:103], v[168:171], v[144:147], v[100:103]
	s_waitcnt lgkmcnt(10)
	v_mfma_f32_16x16x32_f16 v[104:107], v[156:159], v[148:151], v[104:107]
	v_mfma_f32_16x16x32_f16 v[108:111], v[160:163], v[148:151], v[108:111]
	s_add_u32 m0, s28, 0x18000
	s_nop 0
	global_load_lds_dwordx4 v11, s[6:7]
	s_add_u32 s6, s6, s20
	s_addc_u32 s7, s7, 0
	v_mfma_f32_16x16x32_f16 v[112:115], v[164:167], v[148:151], v[112:115]
	v_mfma_f32_16x16x32_f16 v[116:119], v[168:171], v[148:151], v[116:119]
	s_waitcnt lgkmcnt(9)
	v_mfma_f32_16x16x32_f16 v[120:123], v[156:159], v[152:155], v[120:123]
	v_mfma_f32_16x16x32_f16 v[124:127], v[160:163], v[152:155], v[124:127]
	v_mfma_f32_16x16x32_f16 v[128:131], v[164:167], v[152:155], v[128:131]
	v_mfma_f32_16x16x32_f16 v[132:135], v[168:171], v[152:155], v[132:135]
	s_waitcnt vmcnt(6) lgkmcnt(0)
	s_barrier
	s_waitcnt lgkmcnt(6)
	ds_read_b128 v[136:139], v15
	ds_read_b128 v[156:159], v17
	ds_read_b128 v[160:163], v17 offset:2048
	ds_read_b128 v[164:167], v17 offset:4096
	ds_read_b128 v[168:171], v17 offset:6144
	ds_read_b128 v[140:143], v15 offset:2048
	ds_read_b128 v[144:147], v15 offset:4096
	ds_read_b128 v[148:151], v15 offset:6144
	ds_read_b128 v[152:155], v15 offset:8192
	v_mfma_f32_16x16x32_f16 v[56:59], v[192:195], v[172:175], v[56:59]
	s_add_u32 m0, s28, 0x1a000
	s_nop 0
	global_load_lds_dwordx4 v10, s[4:5]
	s_waitcnt lgkmcnt(15)
	v_mfma_f32_16x16x32_f16 v[60:63], v[196:199], v[172:175], v[60:63]
	s_waitcnt lgkmcnt(14)
	v_mfma_f32_16x16x32_f16 v[64:67], v[200:203], v[172:175], v[64:67]
	s_waitcnt lgkmcnt(13)
	v_mfma_f32_16x16x32_f16 v[68:71], v[204:207], v[172:175], v[68:71]
	s_waitcnt lgkmcnt(12)
	v_mfma_f32_16x16x32_f16 v[72:75], v[192:195], v[176:179], v[72:75]
	v_mfma_f32_16x16x32_f16 v[76:79], v[196:199], v[176:179], v[76:79]
	v_mfma_f32_16x16x32_f16 v[80:83], v[200:203], v[176:179], v[80:83]
	s_add_u32 m0, s28, 0x1c000
	s_nop 0
	global_load_lds_dwordx4 v11, s[4:5]
	v_mfma_f32_16x16x32_f16 v[84:87], v[204:207], v[176:179], v[84:87]
	s_waitcnt lgkmcnt(11)
	v_mfma_f32_16x16x32_f16 v[88:91], v[192:195], v[180:183], v[88:91]
	v_mfma_f32_16x16x32_f16 v[92:95], v[196:199], v[180:183], v[92:95]
	v_mfma_f32_16x16x32_f16 v[96:99], v[200:203], v[180:183], v[96:99]
	v_mfma_f32_16x16x32_f16 v[100:103], v[204:207], v[180:183], v[100:103]
	s_waitcnt lgkmcnt(10)
	v_mfma_f32_16x16x32_f16 v[104:107], v[192:195], v[184:187], v[104:107]
	v_mfma_f32_16x16x32_f16 v[108:111], v[196:199], v[184:187], v[108:111]
	s_add_u32 m0, s28, 0x1e000
	s_nop 0
	global_load_lds_dwordx4 v12, s[4:5]
	v_mfma_f32_16x16x32_f16 v[112:115], v[200:203], v[184:187], v[112:115]
	v_mfma_f32_16x16x32_f16 v[116:119], v[204:207], v[184:187], v[116:119]
	s_waitcnt lgkmcnt(9)
	v_mfma_f32_16x16x32_f16 v[120:123], v[192:195], v[188:191], v[120:123]
	v_mfma_f32_16x16x32_f16 v[124:127], v[196:199], v[188:191], v[124:127]
	v_mfma_f32_16x16x32_f16 v[128:131], v[200:203], v[188:191], v[128:131]
	v_mfma_f32_16x16x32_f16 v[132:135], v[204:207], v[188:191], v[132:135]
	s_waitcnt lgkmcnt(6)
	ds_read_b128 v[172:175], v16
	ds_read_b128 v[192:195], v18
	ds_read_b128 v[196:199], v18 offset:2048
	ds_read_b128 v[200:203], v18 offset:4096
	ds_read_b128 v[204:207], v18 offset:6144
	ds_read_b128 v[176:179], v16 offset:2048
	ds_read_b128 v[180:183], v16 offset:4096
	ds_read_b128 v[184:187], v16 offset:6144
	ds_read_b128 v[188:191], v16 offset:8192
	v_mfma_f32_16x16x32_f16 v[56:59], v[156:159], v[136:139], v[56:59]
	s_add_u32 m0, s28, 0x20000
	s_nop 0
	global_load_lds_dwordx4 v13, s[4:5]
	s_add_u32 s4, s4, s20
	s_addc_u32 s5, s5, 0
	s_waitcnt lgkmcnt(15)
	v_mfma_f32_16x16x32_f16 v[60:63], v[160:163], v[136:139], v[60:63]
	s_waitcnt lgkmcnt(14)
	v_mfma_f32_16x16x32_f16 v[64:67], v[164:167], v[136:139], v[64:67]
	s_waitcnt lgkmcnt(13)
	v_mfma_f32_16x16x32_f16 v[68:71], v[168:171], v[136:139], v[68:71]
	s_waitcnt lgkmcnt(12)
	v_mfma_f32_16x16x32_f16 v[72:75], v[156:159], v[140:143], v[72:75]
	v_mfma_f32_16x16x32_f16 v[76:79], v[160:163], v[140:143], v[76:79]
	v_mfma_f32_16x16x32_f16 v[80:83], v[164:167], v[140:143], v[80:83]
	s_add_u32 m0, s28, 0x23000
	s_nop 0
	global_load_lds_dwordx4 v10, s[6:7]
	v_mfma_f32_16x16x32_f16 v[84:87], v[168:171], v[140:143], v[84:87]
	s_waitcnt lgkmcnt(11)
	v_mfma_f32_16x16x32_f16 v[88:91], v[156:159], v[144:147], v[88:91]
	v_mfma_f32_16x16x32_f16 v[92:95], v[160:163], v[144:147], v[92:95]
	v_mfma_f32_16x16x32_f16 v[96:99], v[164:167], v[144:147], v[96:99]
	v_mfma_f32_16x16x32_f16 v[100:103], v[168:171], v[144:147], v[100:103]
	s_waitcnt lgkmcnt(10)
	v_mfma_f32_16x16x32_f16 v[104:107], v[156:159], v[148:151], v[104:107]
	v_mfma_f32_16x16x32_f16 v[108:111], v[160:163], v[148:151], v[108:111]
	s_add_u32 m0, s28, 0x25000
	s_nop 0
	global_load_lds_dwordx4 v11, s[6:7]
	s_add_u32 s6, s6, s20
	s_addc_u32 s7, s7, 0
	v_mfma_f32_16x16x32_f16 v[112:115], v[164:167], v[148:151], v[112:115]
	v_mfma_f32_16x16x32_f16 v[116:119], v[168:171], v[148:151], v[116:119]
	s_waitcnt lgkmcnt(9)
	v_mfma_f32_16x16x32_f16 v[120:123], v[156:159], v[152:155], v[120:123]
	v_mfma_f32_16x16x32_f16 v[124:127], v[160:163], v[152:155], v[124:127]
	v_mfma_f32_16x16x32_f16 v[128:131], v[164:167], v[152:155], v[128:131]
	v_mfma_f32_16x16x32_f16 v[132:135], v[168:171], v[152:155], v[132:135]
	s_waitcnt vmcnt(6) lgkmcnt(0)
	s_barrier
	s_waitcnt lgkmcnt(6)
	ds_read_b128 v[136:139], v15 offset:53248
	ds_read_b128 v[156:159], v17 offset:53248
	ds_read_b128 v[160:163], v17 offset:55296
	ds_read_b128 v[164:167], v17 offset:57344
	ds_read_b128 v[168:171], v17 offset:59392
	ds_read_b128 v[140:143], v15 offset:55296
	ds_read_b128 v[144:147], v15 offset:57344
	ds_read_b128 v[148:151], v15 offset:59392
	ds_read_b128 v[152:155], v15 offset:61440
	v_mfma_f32_16x16x32_f16 v[56:59], v[192:195], v[172:175], v[56:59]
	s_add_u32 m0, s28, 0x0
	s_nop 0
	global_load_lds_dwordx4 v10, s[4:5]
	s_waitcnt lgkmcnt(15)
	v_mfma_f32_16x16x32_f16 v[60:63], v[196:199], v[172:175], v[60:63]
	s_waitcnt lgkmcnt(14)
	v_mfma_f32_16x16x32_f16 v[64:67], v[200:203], v[172:175], v[64:67]
	s_waitcnt lgkmcnt(13)
	v_mfma_f32_16x16x32_f16 v[68:71], v[204:207], v[172:175], v[68:71]
	s_waitcnt lgkmcnt(12)
	v_mfma_f32_16x16x32_f16 v[72:75], v[192:195], v[176:179], v[72:75]
	v_mfma_f32_16x16x32_f16 v[76:79], v[196:199], v[176:179], v[76:79]
	v_mfma_f32_16x16x32_f16 v[80:83], v[200:203], v[176:179], v[80:83]
	s_add_u32 m0, s28, 0x2000
	s_nop 0
	global_load_lds_dwordx4 v11, s[4:5]
	v_mfma_f32_16x16x32_f16 v[84:87], v[204:207], v[176:179], v[84:87]
	s_waitcnt lgkmcnt(11)
	v_mfma_f32_16x16x32_f16 v[88:91], v[192:195], v[180:183], v[88:91]
	v_mfma_f32_16x16x32_f16 v[92:95], v[196:199], v[180:183], v[92:95]
	v_mfma_f32_16x16x32_f16 v[96:99], v[200:203], v[180:183], v[96:99]
	v_mfma_f32_16x16x32_f16 v[100:103], v[204:207], v[180:183], v[100:103]
	s_waitcnt lgkmcnt(10)
	v_mfma_f32_16x16x32_f16 v[104:107], v[192:195], v[184:187], v[104:107]
	v_mfma_f32_16x16x32_f16 v[108:111], v[196:199], v[184:187], v[108:111]
	s_add_u32 m0, s28, 0x4000
	s_nop 0
	global_load_lds_dwordx4 v12, s[4:5]
	v_mfma_f32_16x16x32_f16 v[112:115], v[200:203], v[184:187], v[112:115]
	v_mfma_f32_16x16x32_f16 v[116:119], v[204:207], v[184:187], v[116:119]
	s_waitcnt lgkmcnt(9)
	v_mfma_f32_16x16x32_f16 v[120:123], v[192:195], v[188:191], v[120:123]
	v_mfma_f32_16x16x32_f16 v[124:127], v[196:199], v[188:191], v[124:127]
	v_mfma_f32_16x16x32_f16 v[128:131], v[200:203], v[188:191], v[128:131]
	v_mfma_f32_16x16x32_f16 v[132:135], v[204:207], v[188:191], v[132:135]
	s_waitcnt lgkmcnt(6)
	ds_read_b128 v[172:175], v16 offset:53248
	ds_read_b128 v[192:195], v18 offset:53248
	ds_read_b128 v[196:199], v18 offset:55296
	ds_read_b128 v[200:203], v18 offset:57344
	ds_read_b128 v[204:207], v18 offset:59392
	ds_read_b128 v[176:179], v16 offset:55296
	ds_read_b128 v[180:183], v16 offset:57344
	ds_read_b128 v[184:187], v16 offset:59392
	ds_read_b128 v[188:191], v16 offset:61440
	v_mfma_f32_16x16x32_f16 v[56:59], v[156:159], v[136:139], v[56:59]
	s_add_u32 m0, s28, 0x6000
	s_nop 0
	global_load_lds_dwordx4 v13, s[4:5]
	s_add_u32 s4, s4, s20
	s_addc_u32 s5, s5, 0
	s_waitcnt lgkmcnt(15)
	v_mfma_f32_16x16x32_f16 v[60:63], v[160:163], v[136:139], v[60:63]
	s_waitcnt lgkmcnt(14)
	v_mfma_f32_16x16x32_f16 v[64:67], v[164:167], v[136:139], v[64:67]
	s_waitcnt lgkmcnt(13)
	v_mfma_f32_16x16x32_f16 v[68:71], v[168:171], v[136:139], v[68:71]
	s_waitcnt lgkmcnt(12)
	v_mfma_f32_16x16x32_f16 v[72:75], v[156:159], v[140:143], v[72:75]
	v_mfma_f32_16x16x32_f16 v[76:79], v[160:163], v[140:143], v[76:79]
	v_mfma_f32_16x16x32_f16 v[80:83], v[164:167], v[140:143], v[80:83]
	s_add_u32 m0, s28, 0x9000
	s_nop 0
	global_load_lds_dwordx4 v10, s[6:7]
	v_mfma_f32_16x16x32_f16 v[84:87], v[168:171], v[140:143], v[84:87]
	s_waitcnt lgkmcnt(11)
	v_mfma_f32_16x16x32_f16 v[88:91], v[156:159], v[144:147], v[88:91]
	v_mfma_f32_16x16x32_f16 v[92:95], v[160:163], v[144:147], v[92:95]
	v_mfma_f32_16x16x32_f16 v[96:99], v[164:167], v[144:147], v[96:99]
	v_mfma_f32_16x16x32_f16 v[100:103], v[168:171], v[144:147], v[100:103]
	s_waitcnt lgkmcnt(10)
	v_mfma_f32_16x16x32_f16 v[104:107], v[156:159], v[148:151], v[104:107]
	v_mfma_f32_16x16x32_f16 v[108:111], v[160:163], v[148:151], v[108:111]
	s_add_u32 m0, s28, 0xb000
	s_nop 0
	global_load_lds_dwordx4 v11, s[6:7]
	s_add_u32 s6, s6, s20
	s_addc_u32 s7, s7, 0
	v_mfma_f32_16x16x32_f16 v[112:115], v[164:167], v[148:151], v[112:115]
	v_mfma_f32_16x16x32_f16 v[116:119], v[168:171], v[148:151], v[116:119]
	s_waitcnt lgkmcnt(9)
	v_mfma_f32_16x16x32_f16 v[120:123], v[156:159], v[152:155], v[120:123]
	v_mfma_f32_16x16x32_f16 v[124:127], v[160:163], v[152:155], v[124:127]
	v_mfma_f32_16x16x32_f16 v[128:131], v[164:167], v[152:155], v[128:131]
	v_mfma_f32_16x16x32_f16 v[132:135], v[168:171], v[152:155], v[132:135]
	s_waitcnt vmcnt(6) lgkmcnt(0)
	s_barrier
	s_waitcnt lgkmcnt(6)
	ds_read_b128 v[136:139], v19
	ds_read_b128 v[156:159], v21
	ds_read_b128 v[160:163], v21 offset:2048
	ds_read_b128 v[164:167], v21 offset:4096
	ds_read_b128 v[168:171], v21 offset:6144
	ds_read_b128 v[140:143], v19 offset:2048
	ds_read_b128 v[144:147], v19 offset:4096
	ds_read_b128 v[148:151], v19 offset:6144
	ds_read_b128 v[152:155], v19 offset:8192
	v_mfma_f32_16x16x32_f16 v[56:59], v[192:195], v[172:175], v[56:59]
	s_add_u32 m0, s28, 0xd000
	s_nop 0
	global_load_lds_dwordx4 v10, s[4:5]
	s_waitcnt lgkmcnt(15)
	v_mfma_f32_16x16x32_f16 v[60:63], v[196:199], v[172:175], v[60:63]
	s_waitcnt lgkmcnt(14)
	v_mfma_f32_16x16x32_f16 v[64:67], v[200:203], v[172:175], v[64:67]
	s_waitcnt lgkmcnt(13)
	v_mfma_f32_16x16x32_f16 v[68:71], v[204:207], v[172:175], v[68:71]
	s_waitcnt lgkmcnt(12)
	v_mfma_f32_16x16x32_f16 v[72:75], v[192:195], v[176:179], v[72:75]
	v_mfma_f32_16x16x32_f16 v[76:79], v[196:199], v[176:179], v[76:79]
	v_mfma_f32_16x16x32_f16 v[80:83], v[200:203], v[176:179], v[80:83]
	s_add_u32 m0, s28, 0xf000
	s_nop 0
	global_load_lds_dwordx4 v11, s[4:5]
	v_mfma_f32_16x16x32_f16 v[84:87], v[204:207], v[176:179], v[84:87]
	s_waitcnt lgkmcnt(11)
	v_mfma_f32_16x16x32_f16 v[88:91], v[192:195], v[180:183], v[88:91]
	v_mfma_f32_16x16x32_f16 v[92:95], v[196:199], v[180:183], v[92:95]
	v_mfma_f32_16x16x32_f16 v[96:99], v[200:203], v[180:183], v[96:99]
	v_mfma_f32_16x16x32_f16 v[100:103], v[204:207], v[180:183], v[100:103]
	s_waitcnt lgkmcnt(10)
	v_mfma_f32_16x16x32_f16 v[104:107], v[192:195], v[184:187], v[104:107]
	v_mfma_f32_16x16x32_f16 v[108:111], v[196:199], v[184:187], v[108:111]
	s_add_u32 m0, s28, 0x11000
	s_nop 0
	global_load_lds_dwordx4 v12, s[4:5]
	v_mfma_f32_16x16x32_f16 v[112:115], v[200:203], v[184:187], v[112:115]
	v_mfma_f32_16x16x32_f16 v[116:119], v[204:207], v[184:187], v[116:119]
	s_waitcnt lgkmcnt(9)
	v_mfma_f32_16x16x32_f16 v[120:123], v[192:195], v[188:191], v[120:123]
	v_mfma_f32_16x16x32_f16 v[124:127], v[196:199], v[188:191], v[124:127]
	v_mfma_f32_16x16x32_f16 v[128:131], v[200:203], v[188:191], v[128:131]
	v_mfma_f32_16x16x32_f16 v[132:135], v[204:207], v[188:191], v[132:135]
	s_waitcnt lgkmcnt(6)
	ds_read_b128 v[172:175], v20
	ds_read_b128 v[192:195], v22
	ds_read_b128 v[196:199], v22 offset:2048
	ds_read_b128 v[200:203], v22 offset:4096
	ds_read_b128 v[204:207], v22 offset:6144
	ds_read_b128 v[176:179], v20 offset:2048
	ds_read_b128 v[180:183], v20 offset:4096
	ds_read_b128 v[184:187], v20 offset:6144
	ds_read_b128 v[188:191], v20 offset:8192
	v_mfma_f32_16x16x32_f16 v[56:59], v[156:159], v[136:139], v[56:59]
	s_add_u32 m0, s28, 0x13000
	s_nop 0
	global_load_lds_dwordx4 v13, s[4:5]
	s_add_u32 s4, s4, s20
	s_addc_u32 s5, s5, 0
	s_waitcnt lgkmcnt(15)
	v_mfma_f32_16x16x32_f16 v[60:63], v[160:163], v[136:139], v[60:63]
	s_waitcnt lgkmcnt(14)
	v_mfma_f32_16x16x32_f16 v[64:67], v[164:167], v[136:139], v[64:67]
	s_waitcnt lgkmcnt(13)
	v_mfma_f32_16x16x32_f16 v[68:71], v[168:171], v[136:139], v[68:71]
	s_waitcnt lgkmcnt(12)
	v_mfma_f32_16x16x32_f16 v[72:75], v[156:159], v[140:143], v[72:75]
	v_mfma_f32_16x16x32_f16 v[76:79], v[160:163], v[140:143], v[76:79]
	v_mfma_f32_16x16x32_f16 v[80:83], v[164:167], v[140:143], v[80:83]
	s_add_u32 m0, s28, 0x16000
	s_nop 0
	global_load_lds_dwordx4 v10, s[6:7]
	v_mfma_f32_16x16x32_f16 v[84:87], v[168:171], v[140:143], v[84:87]
	s_waitcnt lgkmcnt(11)
	v_mfma_f32_16x16x32_f16 v[88:91], v[156:159], v[144:147], v[88:91]
	v_mfma_f32_16x16x32_f16 v[92:95], v[160:163], v[144:147], v[92:95]
	v_mfma_f32_16x16x32_f16 v[96:99], v[164:167], v[144:147], v[96:99]
	v_mfma_f32_16x16x32_f16 v[100:103], v[168:171], v[144:147], v[100:103]
	s_waitcnt lgkmcnt(10)
	v_mfma_f32_16x16x32_f16 v[104:107], v[156:159], v[148:151], v[104:107]
	v_mfma_f32_16x16x32_f16 v[108:111], v[160:163], v[148:151], v[108:111]
	s_add_u32 m0, s28, 0x18000
	s_nop 0
	global_load_lds_dwordx4 v11, s[6:7]
	s_add_u32 s6, s6, s20
	s_addc_u32 s7, s7, 0
	v_mfma_f32_16x16x32_f16 v[112:115], v[164:167], v[148:151], v[112:115]
	v_mfma_f32_16x16x32_f16 v[116:119], v[168:171], v[148:151], v[116:119]
	s_waitcnt lgkmcnt(9)
	v_mfma_f32_16x16x32_f16 v[120:123], v[156:159], v[152:155], v[120:123]
	v_mfma_f32_16x16x32_f16 v[124:127], v[160:163], v[152:155], v[124:127]
	v_mfma_f32_16x16x32_f16 v[128:131], v[164:167], v[152:155], v[128:131]
	v_mfma_f32_16x16x32_f16 v[132:135], v[168:171], v[152:155], v[132:135]
	s_waitcnt vmcnt(6) lgkmcnt(0)
	s_barrier
	s_waitcnt lgkmcnt(6)
	ds_read_b128 v[136:139], v15
	ds_read_b128 v[156:159], v17
	ds_read_b128 v[160:163], v17 offset:2048
	ds_read_b128 v[164:167], v17 offset:4096
	ds_read_b128 v[168:171], v17 offset:6144
	ds_read_b128 v[140:143], v15 offset:2048
	ds_read_b128 v[144:147], v15 offset:4096
	ds_read_b128 v[148:151], v15 offset:6144
	ds_read_b128 v[152:155], v15 offset:8192
	v_mfma_f32_16x16x32_f16 v[56:59], v[192:195], v[172:175], v[56:59]
	s_add_u32 m0, s28, 0x1a000
	s_nop 0
	global_load_lds_dwordx4 v10, s[4:5]
	s_waitcnt lgkmcnt(15)
	v_mfma_f32_16x16x32_f16 v[60:63], v[196:199], v[172:175], v[60:63]
	s_waitcnt lgkmcnt(14)
	v_mfma_f32_16x16x32_f16 v[64:67], v[200:203], v[172:175], v[64:67]
	s_waitcnt lgkmcnt(13)
	v_mfma_f32_16x16x32_f16 v[68:71], v[204:207], v[172:175], v[68:71]
	s_waitcnt lgkmcnt(12)
	v_mfma_f32_16x16x32_f16 v[72:75], v[192:195], v[176:179], v[72:75]
	v_mfma_f32_16x16x32_f16 v[76:79], v[196:199], v[176:179], v[76:79]
	v_mfma_f32_16x16x32_f16 v[80:83], v[200:203], v[176:179], v[80:83]
	s_add_u32 m0, s28, 0x1c000
	s_nop 0
	global_load_lds_dwordx4 v11, s[4:5]
	v_mfma_f32_16x16x32_f16 v[84:87], v[204:207], v[176:179], v[84:87]
	s_waitcnt lgkmcnt(11)
	v_mfma_f32_16x16x32_f16 v[88:91], v[192:195], v[180:183], v[88:91]
	v_mfma_f32_16x16x32_f16 v[92:95], v[196:199], v[180:183], v[92:95]
	v_mfma_f32_16x16x32_f16 v[96:99], v[200:203], v[180:183], v[96:99]
	v_mfma_f32_16x16x32_f16 v[100:103], v[204:207], v[180:183], v[100:103]
	s_waitcnt lgkmcnt(10)
	v_mfma_f32_16x16x32_f16 v[104:107], v[192:195], v[184:187], v[104:107]
	v_mfma_f32_16x16x32_f16 v[108:111], v[196:199], v[184:187], v[108:111]
	s_add_u32 m0, s28, 0x1e000
	s_nop 0
	global_load_lds_dwordx4 v12, s[4:5]
	v_mfma_f32_16x16x32_f16 v[112:115], v[200:203], v[184:187], v[112:115]
	v_mfma_f32_16x16x32_f16 v[116:119], v[204:207], v[184:187], v[116:119]
	s_waitcnt lgkmcnt(9)
	v_mfma_f32_16x16x32_f16 v[120:123], v[192:195], v[188:191], v[120:123]
	v_mfma_f32_16x16x32_f16 v[124:127], v[196:199], v[188:191], v[124:127]
	v_mfma_f32_16x16x32_f16 v[128:131], v[200:203], v[188:191], v[128:131]
	v_mfma_f32_16x16x32_f16 v[132:135], v[204:207], v[188:191], v[132:135]
	s_waitcnt lgkmcnt(6)
	ds_read_b128 v[172:175], v16
	ds_read_b128 v[192:195], v18
	ds_read_b128 v[196:199], v18 offset:2048
	ds_read_b128 v[200:203], v18 offset:4096
	ds_read_b128 v[204:207], v18 offset:6144
	ds_read_b128 v[176:179], v16 offset:2048
	ds_read_b128 v[180:183], v16 offset:4096
	ds_read_b128 v[184:187], v16 offset:6144
	ds_read_b128 v[188:191], v16 offset:8192
	v_mfma_f32_16x16x32_f16 v[56:59], v[156:159], v[136:139], v[56:59]
	s_add_u32 m0, s28, 0x20000
	s_nop 0
	global_load_lds_dwordx4 v13, s[4:5]
	s_add_u32 s4, s4, s20
	s_addc_u32 s5, s5, 0
	s_waitcnt lgkmcnt(15)
	v_mfma_f32_16x16x32_f16 v[60:63], v[160:163], v[136:139], v[60:63]
	s_waitcnt lgkmcnt(14)
	v_mfma_f32_16x16x32_f16 v[64:67], v[164:167], v[136:139], v[64:67]
	s_waitcnt lgkmcnt(13)
	v_mfma_f32_16x16x32_f16 v[68:71], v[168:171], v[136:139], v[68:71]
	s_waitcnt lgkmcnt(12)
	v_mfma_f32_16x16x32_f16 v[72:75], v[156:159], v[140:143], v[72:75]
	v_mfma_f32_16x16x32_f16 v[76:79], v[160:163], v[140:143], v[76:79]
	v_mfma_f32_16x16x32_f16 v[80:83], v[164:167], v[140:143], v[80:83]
	s_add_u32 m0, s28, 0x23000
	s_nop 0
	global_load_lds_dwordx4 v10, s[6:7]
	v_mfma_f32_16x16x32_f16 v[84:87], v[168:171], v[140:143], v[84:87]
	s_waitcnt lgkmcnt(11)
	v_mfma_f32_16x16x32_f16 v[88:91], v[156:159], v[144:147], v[88:91]
	v_mfma_f32_16x16x32_f16 v[92:95], v[160:163], v[144:147], v[92:95]
	v_mfma_f32_16x16x32_f16 v[96:99], v[164:167], v[144:147], v[96:99]
	v_mfma_f32_16x16x32_f16 v[100:103], v[168:171], v[144:147], v[100:103]
	s_waitcnt lgkmcnt(10)
	v_mfma_f32_16x16x32_f16 v[104:107], v[156:159], v[148:151], v[104:107]
	v_mfma_f32_16x16x32_f16 v[108:111], v[160:163], v[148:151], v[108:111]
	s_add_u32 m0, s28, 0x25000
	s_nop 0
	global_load_lds_dwordx4 v11, s[6:7]
	s_add_u32 s6, s6, s20
	s_addc_u32 s7, s7, 0
	v_mfma_f32_16x16x32_f16 v[112:115], v[164:167], v[148:151], v[112:115]
	v_mfma_f32_16x16x32_f16 v[116:119], v[168:171], v[148:151], v[116:119]
	s_waitcnt lgkmcnt(9)
	v_mfma_f32_16x16x32_f16 v[120:123], v[156:159], v[152:155], v[120:123]
	v_mfma_f32_16x16x32_f16 v[124:127], v[160:163], v[152:155], v[124:127]
	v_mfma_f32_16x16x32_f16 v[128:131], v[164:167], v[152:155], v[128:131]
	v_mfma_f32_16x16x32_f16 v[132:135], v[168:171], v[152:155], v[132:135]
	s_waitcnt vmcnt(6) lgkmcnt(0)
	s_barrier
	s_waitcnt lgkmcnt(6)
	ds_read_b128 v[136:139], v15 offset:53248
	ds_read_b128 v[156:159], v17 offset:53248
	ds_read_b128 v[160:163], v17 offset:55296
	ds_read_b128 v[164:167], v17 offset:57344
	ds_read_b128 v[168:171], v17 offset:59392
	ds_read_b128 v[140:143], v15 offset:55296
	ds_read_b128 v[144:147], v15 offset:57344
	ds_read_b128 v[148:151], v15 offset:59392
	ds_read_b128 v[152:155], v15 offset:61440
	v_mfma_f32_16x16x32_f16 v[56:59], v[192:195], v[172:175], v[56:59]
	s_add_u32 m0, s28, 0x0
	s_nop 0
	global_load_lds_dwordx4 v10, s[4:5]
	s_waitcnt lgkmcnt(15)
	v_mfma_f32_16x16x32_f16 v[60:63], v[196:199], v[172:175], v[60:63]
	s_waitcnt lgkmcnt(14)
	v_mfma_f32_16x16x32_f16 v[64:67], v[200:203], v[172:175], v[64:67]
	s_waitcnt lgkmcnt(13)
	v_mfma_f32_16x16x32_f16 v[68:71], v[204:207], v[172:175], v[68:71]
	s_waitcnt lgkmcnt(12)
	v_mfma_f32_16x16x32_f16 v[72:75], v[192:195], v[176:179], v[72:75]
	v_mfma_f32_16x16x32_f16 v[76:79], v[196:199], v[176:179], v[76:79]
	v_mfma_f32_16x16x32_f16 v[80:83], v[200:203], v[176:179], v[80:83]
	s_add_u32 m0, s28, 0x2000
	s_nop 0
	global_load_lds_dwordx4 v11, s[4:5]
	v_mfma_f32_16x16x32_f16 v[84:87], v[204:207], v[176:179], v[84:87]
	s_waitcnt lgkmcnt(11)
	v_mfma_f32_16x16x32_f16 v[88:91], v[192:195], v[180:183], v[88:91]
	v_mfma_f32_16x16x32_f16 v[92:95], v[196:199], v[180:183], v[92:95]
	v_mfma_f32_16x16x32_f16 v[96:99], v[200:203], v[180:183], v[96:99]
	v_mfma_f32_16x16x32_f16 v[100:103], v[204:207], v[180:183], v[100:103]
	s_waitcnt lgkmcnt(10)
	v_mfma_f32_16x16x32_f16 v[104:107], v[192:195], v[184:187], v[104:107]
	v_mfma_f32_16x16x32_f16 v[108:111], v[196:199], v[184:187], v[108:111]
	s_add_u32 m0, s28, 0x4000
	s_nop 0
	global_load_lds_dwordx4 v12, s[4:5]
	v_mfma_f32_16x16x32_f16 v[112:115], v[200:203], v[184:187], v[112:115]
	v_mfma_f32_16x16x32_f16 v[116:119], v[204:207], v[184:187], v[116:119]
	s_waitcnt lgkmcnt(9)
	v_mfma_f32_16x16x32_f16 v[120:123], v[192:195], v[188:191], v[120:123]
	v_mfma_f32_16x16x32_f16 v[124:127], v[196:199], v[188:191], v[124:127]
	v_mfma_f32_16x16x32_f16 v[128:131], v[200:203], v[188:191], v[128:131]
	v_mfma_f32_16x16x32_f16 v[132:135], v[204:207], v[188:191], v[132:135]
	s_waitcnt lgkmcnt(6)
	ds_read_b128 v[172:175], v16 offset:53248
	ds_read_b128 v[192:195], v18 offset:53248
	ds_read_b128 v[196:199], v18 offset:55296
	ds_read_b128 v[200:203], v18 offset:57344
	ds_read_b128 v[204:207], v18 offset:59392
	ds_read_b128 v[176:179], v16 offset:55296
	ds_read_b128 v[180:183], v16 offset:57344
	ds_read_b128 v[184:187], v16 offset:59392
	ds_read_b128 v[188:191], v16 offset:61440
	v_mfma_f32_16x16x32_f16 v[56:59], v[156:159], v[136:139], v[56:59]
	s_add_u32 m0, s28, 0x6000
	s_nop 0
	global_load_lds_dwordx4 v13, s[4:5]
	s_add_u32 s4, s4, s20
	s_addc_u32 s5, s5, 0
	s_waitcnt lgkmcnt(15)
	v_mfma_f32_16x16x32_f16 v[60:63], v[160:163], v[136:139], v[60:63]
	s_waitcnt lgkmcnt(14)
	v_mfma_f32_16x16x32_f16 v[64:67], v[164:167], v[136:139], v[64:67]
	s_waitcnt lgkmcnt(13)
	v_mfma_f32_16x16x32_f16 v[68:71], v[168:171], v[136:139], v[68:71]
	s_waitcnt lgkmcnt(12)
	v_mfma_f32_16x16x32_f16 v[72:75], v[156:159], v[140:143], v[72:75]
	v_mfma_f32_16x16x32_f16 v[76:79], v[160:163], v[140:143], v[76:79]
	v_mfma_f32_16x16x32_f16 v[80:83], v[164:167], v[140:143], v[80:83]
	s_add_u32 m0, s28, 0x9000
	s_nop 0
	global_load_lds_dwordx4 v10, s[6:7]
	v_mfma_f32_16x16x32_f16 v[84:87], v[168:171], v[140:143], v[84:87]
	s_waitcnt lgkmcnt(11)
	v_mfma_f32_16x16x32_f16 v[88:91], v[156:159], v[144:147], v[88:91]
	v_mfma_f32_16x16x32_f16 v[92:95], v[160:163], v[144:147], v[92:95]
	v_mfma_f32_16x16x32_f16 v[96:99], v[164:167], v[144:147], v[96:99]
	v_mfma_f32_16x16x32_f16 v[100:103], v[168:171], v[144:147], v[100:103]
	s_waitcnt lgkmcnt(10)
	v_mfma_f32_16x16x32_f16 v[104:107], v[156:159], v[148:151], v[104:107]
	v_mfma_f32_16x16x32_f16 v[108:111], v[160:163], v[148:151], v[108:111]
	s_add_u32 m0, s28, 0xb000
	s_nop 0
	global_load_lds_dwordx4 v11, s[6:7]
	s_add_u32 s6, s6, s20
	s_addc_u32 s7, s7, 0
	v_mfma_f32_16x16x32_f16 v[112:115], v[164:167], v[148:151], v[112:115]
	v_mfma_f32_16x16x32_f16 v[116:119], v[168:171], v[148:151], v[116:119]
	s_waitcnt lgkmcnt(9)
	v_mfma_f32_16x16x32_f16 v[120:123], v[156:159], v[152:155], v[120:123]
	v_mfma_f32_16x16x32_f16 v[124:127], v[160:163], v[152:155], v[124:127]
	v_mfma_f32_16x16x32_f16 v[128:131], v[164:167], v[152:155], v[128:131]
	v_mfma_f32_16x16x32_f16 v[132:135], v[168:171], v[152:155], v[132:135]
	s_waitcnt vmcnt(6) lgkmcnt(0)
	s_barrier
	s_waitcnt lgkmcnt(6)
	ds_read_b128 v[136:139], v19
	ds_read_b128 v[156:159], v21
	ds_read_b128 v[160:163], v21 offset:2048
	ds_read_b128 v[164:167], v21 offset:4096
	ds_read_b128 v[168:171], v21 offset:6144
	ds_read_b128 v[140:143], v19 offset:2048
	ds_read_b128 v[144:147], v19 offset:4096
	ds_read_b128 v[148:151], v19 offset:6144
	ds_read_b128 v[152:155], v19 offset:8192
	v_mfma_f32_16x16x32_f16 v[56:59], v[192:195], v[172:175], v[56:59]
	s_add_u32 m0, s28, 0xd000
	s_nop 0
	global_load_lds_dwordx4 v10, s[4:5]
	s_waitcnt lgkmcnt(15)
	v_mfma_f32_16x16x32_f16 v[60:63], v[196:199], v[172:175], v[60:63]
	s_waitcnt lgkmcnt(14)
	v_mfma_f32_16x16x32_f16 v[64:67], v[200:203], v[172:175], v[64:67]
	s_waitcnt lgkmcnt(13)
	v_mfma_f32_16x16x32_f16 v[68:71], v[204:207], v[172:175], v[68:71]
	s_waitcnt lgkmcnt(12)
	v_mfma_f32_16x16x32_f16 v[72:75], v[192:195], v[176:179], v[72:75]
	v_mfma_f32_16x16x32_f16 v[76:79], v[196:199], v[176:179], v[76:79]
	v_mfma_f32_16x16x32_f16 v[80:83], v[200:203], v[176:179], v[80:83]
	s_add_u32 m0, s28, 0xf000
	s_nop 0
	global_load_lds_dwordx4 v11, s[4:5]
	v_mfma_f32_16x16x32_f16 v[84:87], v[204:207], v[176:179], v[84:87]
	s_waitcnt lgkmcnt(11)
	v_mfma_f32_16x16x32_f16 v[88:91], v[192:195], v[180:183], v[88:91]
	v_mfma_f32_16x16x32_f16 v[92:95], v[196:199], v[180:183], v[92:95]
	v_mfma_f32_16x16x32_f16 v[96:99], v[200:203], v[180:183], v[96:99]
	v_mfma_f32_16x16x32_f16 v[100:103], v[204:207], v[180:183], v[100:103]
	s_waitcnt lgkmcnt(10)
	v_mfma_f32_16x16x32_f16 v[104:107], v[192:195], v[184:187], v[104:107]
	v_mfma_f32_16x16x32_f16 v[108:111], v[196:199], v[184:187], v[108:111]
	s_add_u32 m0, s28, 0x11000
	s_nop 0
	global_load_lds_dwordx4 v12, s[4:5]
	v_mfma_f32_16x16x32_f16 v[112:115], v[200:203], v[184:187], v[112:115]
	v_mfma_f32_16x16x32_f16 v[116:119], v[204:207], v[184:187], v[116:119]
	s_waitcnt lgkmcnt(9)
	v_mfma_f32_16x16x32_f16 v[120:123], v[192:195], v[188:191], v[120:123]
	v_mfma_f32_16x16x32_f16 v[124:127], v[196:199], v[188:191], v[124:127]
	v_mfma_f32_16x16x32_f16 v[128:131], v[200:203], v[188:191], v[128:131]
	v_mfma_f32_16x16x32_f16 v[132:135], v[204:207], v[188:191], v[132:135]
	s_waitcnt lgkmcnt(6)
	ds_read_b128 v[172:175], v20
	ds_read_b128 v[192:195], v22
	ds_read_b128 v[196:199], v22 offset:2048
	ds_read_b128 v[200:203], v22 offset:4096
	ds_read_b128 v[204:207], v22 offset:6144
	ds_read_b128 v[176:179], v20 offset:2048
	ds_read_b128 v[180:183], v20 offset:4096
	ds_read_b128 v[184:187], v20 offset:6144
	ds_read_b128 v[188:191], v20 offset:8192
	v_mfma_f32_16x16x32_f16 v[56:59], v[156:159], v[136:139], v[56:59]
	s_add_u32 m0, s28, 0x13000
	s_nop 0
	global_load_lds_dwordx4 v13, s[4:5]
	s_add_u32 s4, s4, s20
	s_addc_u32 s5, s5, 0
	s_waitcnt lgkmcnt(15)
	v_mfma_f32_16x16x32_f16 v[60:63], v[160:163], v[136:139], v[60:63]
	s_waitcnt lgkmcnt(14)
	v_mfma_f32_16x16x32_f16 v[64:67], v[164:167], v[136:139], v[64:67]
	s_waitcnt lgkmcnt(13)
	v_mfma_f32_16x16x32_f16 v[68:71], v[168:171], v[136:139], v[68:71]
	s_waitcnt lgkmcnt(12)
	v_mfma_f32_16x16x32_f16 v[72:75], v[156:159], v[140:143], v[72:75]
	v_mfma_f32_16x16x32_f16 v[76:79], v[160:163], v[140:143], v[76:79]
	v_mfma_f32_16x16x32_f16 v[80:83], v[164:167], v[140:143], v[80:83]
	s_add_u32 m0, s28, 0x16000
	s_nop 0
	global_load_lds_dwordx4 v10, s[6:7]
	v_mfma_f32_16x16x32_f16 v[84:87], v[168:171], v[140:143], v[84:87]
	s_waitcnt lgkmcnt(11)
	v_mfma_f32_16x16x32_f16 v[88:91], v[156:159], v[144:147], v[88:91]
	v_mfma_f32_16x16x32_f16 v[92:95], v[160:163], v[144:147], v[92:95]
	v_mfma_f32_16x16x32_f16 v[96:99], v[164:167], v[144:147], v[96:99]
	v_mfma_f32_16x16x32_f16 v[100:103], v[168:171], v[144:147], v[100:103]
	s_waitcnt lgkmcnt(10)
	v_mfma_f32_16x16x32_f16 v[104:107], v[156:159], v[148:151], v[104:107]
	v_mfma_f32_16x16x32_f16 v[108:111], v[160:163], v[148:151], v[108:111]
	s_add_u32 m0, s28, 0x18000
	s_nop 0
	global_load_lds_dwordx4 v11, s[6:7]
	s_add_u32 s6, s6, s20
	s_addc_u32 s7, s7, 0
	v_mfma_f32_16x16x32_f16 v[112:115], v[164:167], v[148:151], v[112:115]
	v_mfma_f32_16x16x32_f16 v[116:119], v[168:171], v[148:151], v[116:119]
	s_waitcnt lgkmcnt(9)
	v_mfma_f32_16x16x32_f16 v[120:123], v[156:159], v[152:155], v[120:123]
	v_mfma_f32_16x16x32_f16 v[124:127], v[160:163], v[152:155], v[124:127]
	v_mfma_f32_16x16x32_f16 v[128:131], v[164:167], v[152:155], v[128:131]
	v_mfma_f32_16x16x32_f16 v[132:135], v[168:171], v[152:155], v[132:135]
	s_waitcnt vmcnt(6) lgkmcnt(0)
	s_barrier
	s_waitcnt lgkmcnt(6)
	ds_read_b128 v[136:139], v15
	ds_read_b128 v[156:159], v17
	ds_read_b128 v[160:163], v17 offset:2048
	ds_read_b128 v[164:167], v17 offset:4096
	ds_read_b128 v[168:171], v17 offset:6144
	ds_read_b128 v[140:143], v15 offset:2048
	ds_read_b128 v[144:147], v15 offset:4096
	ds_read_b128 v[148:151], v15 offset:6144
	ds_read_b128 v[152:155], v15 offset:8192
	v_mfma_f32_16x16x32_f16 v[56:59], v[192:195], v[172:175], v[56:59]
	s_add_u32 m0, s28, 0x1a000
	s_nop 0
	global_load_lds_dwordx4 v10, s[4:5]
	s_waitcnt lgkmcnt(15)
	v_mfma_f32_16x16x32_f16 v[60:63], v[196:199], v[172:175], v[60:63]
	s_waitcnt lgkmcnt(14)
	v_mfma_f32_16x16x32_f16 v[64:67], v[200:203], v[172:175], v[64:67]
	s_waitcnt lgkmcnt(13)
	v_mfma_f32_16x16x32_f16 v[68:71], v[204:207], v[172:175], v[68:71]
	s_waitcnt lgkmcnt(12)
	v_mfma_f32_16x16x32_f16 v[72:75], v[192:195], v[176:179], v[72:75]
	v_mfma_f32_16x16x32_f16 v[76:79], v[196:199], v[176:179], v[76:79]
	v_mfma_f32_16x16x32_f16 v[80:83], v[200:203], v[176:179], v[80:83]
	s_add_u32 m0, s28, 0x1c000
	s_nop 0
	global_load_lds_dwordx4 v11, s[4:5]
	v_mfma_f32_16x16x32_f16 v[84:87], v[204:207], v[176:179], v[84:87]
	s_waitcnt lgkmcnt(11)
	v_mfma_f32_16x16x32_f16 v[88:91], v[192:195], v[180:183], v[88:91]
	v_mfma_f32_16x16x32_f16 v[92:95], v[196:199], v[180:183], v[92:95]
	v_mfma_f32_16x16x32_f16 v[96:99], v[200:203], v[180:183], v[96:99]
	v_mfma_f32_16x16x32_f16 v[100:103], v[204:207], v[180:183], v[100:103]
	s_waitcnt lgkmcnt(10)
	v_mfma_f32_16x16x32_f16 v[104:107], v[192:195], v[184:187], v[104:107]
	v_mfma_f32_16x16x32_f16 v[108:111], v[196:199], v[184:187], v[108:111]
	s_add_u32 m0, s28, 0x1e000
	s_nop 0
	global_load_lds_dwordx4 v12, s[4:5]
	v_mfma_f32_16x16x32_f16 v[112:115], v[200:203], v[184:187], v[112:115]
	v_mfma_f32_16x16x32_f16 v[116:119], v[204:207], v[184:187], v[116:119]
	s_waitcnt lgkmcnt(9)
	v_mfma_f32_16x16x32_f16 v[120:123], v[192:195], v[188:191], v[120:123]
	v_mfma_f32_16x16x32_f16 v[124:127], v[196:199], v[188:191], v[124:127]
	v_mfma_f32_16x16x32_f16 v[128:131], v[200:203], v[188:191], v[128:131]
	v_mfma_f32_16x16x32_f16 v[132:135], v[204:207], v[188:191], v[132:135]
	s_waitcnt lgkmcnt(6)
	ds_read_b128 v[172:175], v16
	ds_read_b128 v[192:195], v18
	ds_read_b128 v[196:199], v18 offset:2048
	ds_read_b128 v[200:203], v18 offset:4096
	ds_read_b128 v[204:207], v18 offset:6144
	ds_read_b128 v[176:179], v16 offset:2048
	ds_read_b128 v[180:183], v16 offset:4096
	ds_read_b128 v[184:187], v16 offset:6144
	ds_read_b128 v[188:191], v16 offset:8192
	v_mfma_f32_16x16x32_f16 v[56:59], v[156:159], v[136:139], v[56:59]
	s_add_u32 m0, s28, 0x20000
	s_nop 0
	global_load_lds_dwordx4 v13, s[4:5]
	s_add_u32 s4, s4, s20
	s_addc_u32 s5, s5, 0
	s_waitcnt lgkmcnt(15)
	v_mfma_f32_16x16x32_f16 v[60:63], v[160:163], v[136:139], v[60:63]
	s_waitcnt lgkmcnt(14)
	v_mfma_f32_16x16x32_f16 v[64:67], v[164:167], v[136:139], v[64:67]
	s_waitcnt lgkmcnt(13)
	v_mfma_f32_16x16x32_f16 v[68:71], v[168:171], v[136:139], v[68:71]
	s_waitcnt lgkmcnt(12)
	v_mfma_f32_16x16x32_f16 v[72:75], v[156:159], v[140:143], v[72:75]
	v_mfma_f32_16x16x32_f16 v[76:79], v[160:163], v[140:143], v[76:79]
	v_mfma_f32_16x16x32_f16 v[80:83], v[164:167], v[140:143], v[80:83]
	s_add_u32 m0, s28, 0x23000
	s_nop 0
	global_load_lds_dwordx4 v10, s[6:7]
	v_mfma_f32_16x16x32_f16 v[84:87], v[168:171], v[140:143], v[84:87]
	s_waitcnt lgkmcnt(11)
	v_mfma_f32_16x16x32_f16 v[88:91], v[156:159], v[144:147], v[88:91]
	v_mfma_f32_16x16x32_f16 v[92:95], v[160:163], v[144:147], v[92:95]
	v_mfma_f32_16x16x32_f16 v[96:99], v[164:167], v[144:147], v[96:99]
	v_mfma_f32_16x16x32_f16 v[100:103], v[168:171], v[144:147], v[100:103]
	s_waitcnt lgkmcnt(10)
	v_mfma_f32_16x16x32_f16 v[104:107], v[156:159], v[148:151], v[104:107]
	v_mfma_f32_16x16x32_f16 v[108:111], v[160:163], v[148:151], v[108:111]
	s_add_u32 m0, s28, 0x25000
	s_nop 0
	global_load_lds_dwordx4 v11, s[6:7]
	s_add_u32 s6, s6, s20
	s_addc_u32 s7, s7, 0
	v_mfma_f32_16x16x32_f16 v[112:115], v[164:167], v[148:151], v[112:115]
	v_mfma_f32_16x16x32_f16 v[116:119], v[168:171], v[148:151], v[116:119]
	s_waitcnt lgkmcnt(9)
	v_mfma_f32_16x16x32_f16 v[120:123], v[156:159], v[152:155], v[120:123]
	v_mfma_f32_16x16x32_f16 v[124:127], v[160:163], v[152:155], v[124:127]
	v_mfma_f32_16x16x32_f16 v[128:131], v[164:167], v[152:155], v[128:131]
	v_mfma_f32_16x16x32_f16 v[132:135], v[168:171], v[152:155], v[132:135]
	s_waitcnt vmcnt(6) lgkmcnt(0)
	s_barrier
	s_waitcnt lgkmcnt(6)
	ds_read_b128 v[136:139], v15 offset:53248
	ds_read_b128 v[156:159], v17 offset:53248
	ds_read_b128 v[160:163], v17 offset:55296
	ds_read_b128 v[164:167], v17 offset:57344
	ds_read_b128 v[168:171], v17 offset:59392
	ds_read_b128 v[140:143], v15 offset:55296
	ds_read_b128 v[144:147], v15 offset:57344
	ds_read_b128 v[148:151], v15 offset:59392
	ds_read_b128 v[152:155], v15 offset:61440
	v_mfma_f32_16x16x32_f16 v[56:59], v[192:195], v[172:175], v[56:59]
	s_add_u32 m0, s28, 0x0
	s_nop 0
	global_load_lds_dwordx4 v10, s[4:5]
	s_waitcnt lgkmcnt(15)
	v_mfma_f32_16x16x32_f16 v[60:63], v[196:199], v[172:175], v[60:63]
	s_waitcnt lgkmcnt(14)
	v_mfma_f32_16x16x32_f16 v[64:67], v[200:203], v[172:175], v[64:67]
	s_waitcnt lgkmcnt(13)
	v_mfma_f32_16x16x32_f16 v[68:71], v[204:207], v[172:175], v[68:71]
	s_waitcnt lgkmcnt(12)
	v_mfma_f32_16x16x32_f16 v[72:75], v[192:195], v[176:179], v[72:75]
	v_mfma_f32_16x16x32_f16 v[76:79], v[196:199], v[176:179], v[76:79]
	v_mfma_f32_16x16x32_f16 v[80:83], v[200:203], v[176:179], v[80:83]
	s_add_u32 m0, s28, 0x2000
	s_nop 0
	global_load_lds_dwordx4 v11, s[4:5]
	v_mfma_f32_16x16x32_f16 v[84:87], v[204:207], v[176:179], v[84:87]
	s_waitcnt lgkmcnt(11)
	v_mfma_f32_16x16x32_f16 v[88:91], v[192:195], v[180:183], v[88:91]
	v_mfma_f32_16x16x32_f16 v[92:95], v[196:199], v[180:183], v[92:95]
	v_mfma_f32_16x16x32_f16 v[96:99], v[200:203], v[180:183], v[96:99]
	v_mfma_f32_16x16x32_f16 v[100:103], v[204:207], v[180:183], v[100:103]
	s_waitcnt lgkmcnt(10)
	v_mfma_f32_16x16x32_f16 v[104:107], v[192:195], v[184:187], v[104:107]
	v_mfma_f32_16x16x32_f16 v[108:111], v[196:199], v[184:187], v[108:111]
	s_add_u32 m0, s28, 0x4000
	s_nop 0
	global_load_lds_dwordx4 v12, s[4:5]
	v_mfma_f32_16x16x32_f16 v[112:115], v[200:203], v[184:187], v[112:115]
	v_mfma_f32_16x16x32_f16 v[116:119], v[204:207], v[184:187], v[116:119]
	s_waitcnt lgkmcnt(9)
	v_mfma_f32_16x16x32_f16 v[120:123], v[192:195], v[188:191], v[120:123]
	v_mfma_f32_16x16x32_f16 v[124:127], v[196:199], v[188:191], v[124:127]
	v_mfma_f32_16x16x32_f16 v[128:131], v[200:203], v[188:191], v[128:131]
	v_mfma_f32_16x16x32_f16 v[132:135], v[204:207], v[188:191], v[132:135]
	s_waitcnt lgkmcnt(6)
	ds_read_b128 v[172:175], v16 offset:53248
	ds_read_b128 v[192:195], v18 offset:53248
	ds_read_b128 v[196:199], v18 offset:55296
	ds_read_b128 v[200:203], v18 offset:57344
	ds_read_b128 v[204:207], v18 offset:59392
	ds_read_b128 v[176:179], v16 offset:55296
	ds_read_b128 v[180:183], v16 offset:57344
	ds_read_b128 v[184:187], v16 offset:59392
	ds_read_b128 v[188:191], v16 offset:61440
	v_mfma_f32_16x16x32_f16 v[56:59], v[156:159], v[136:139], v[56:59]
	s_add_u32 m0, s28, 0x6000
	s_nop 0
	global_load_lds_dwordx4 v13, s[4:5]
	s_add_u32 s4, s4, s20
	s_addc_u32 s5, s5, 0
	s_waitcnt lgkmcnt(15)
	v_mfma_f32_16x16x32_f16 v[60:63], v[160:163], v[136:139], v[60:63]
	s_waitcnt lgkmcnt(14)
	v_mfma_f32_16x16x32_f16 v[64:67], v[164:167], v[136:139], v[64:67]
	s_waitcnt lgkmcnt(13)
	v_mfma_f32_16x16x32_f16 v[68:71], v[168:171], v[136:139], v[68:71]
	s_waitcnt lgkmcnt(12)
	v_mfma_f32_16x16x32_f16 v[72:75], v[156:159], v[140:143], v[72:75]
	v_mfma_f32_16x16x32_f16 v[76:79], v[160:163], v[140:143], v[76:79]
	v_mfma_f32_16x16x32_f16 v[80:83], v[164:167], v[140:143], v[80:83]
	s_add_u32 m0, s28, 0x9000
	s_nop 0
	global_load_lds_dwordx4 v10, s[6:7]
	v_mfma_f32_16x16x32_f16 v[84:87], v[168:171], v[140:143], v[84:87]
	s_waitcnt lgkmcnt(11)
	v_mfma_f32_16x16x32_f16 v[88:91], v[156:159], v[144:147], v[88:91]
	v_mfma_f32_16x16x32_f16 v[92:95], v[160:163], v[144:147], v[92:95]
	v_mfma_f32_16x16x32_f16 v[96:99], v[164:167], v[144:147], v[96:99]
	v_mfma_f32_16x16x32_f16 v[100:103], v[168:171], v[144:147], v[100:103]
	s_waitcnt lgkmcnt(10)
	v_mfma_f32_16x16x32_f16 v[104:107], v[156:159], v[148:151], v[104:107]
	v_mfma_f32_16x16x32_f16 v[108:111], v[160:163], v[148:151], v[108:111]
	s_add_u32 m0, s28, 0xb000
	s_nop 0
	global_load_lds_dwordx4 v11, s[6:7]
	s_add_u32 s6, s6, s20
	s_addc_u32 s7, s7, 0
	v_mfma_f32_16x16x32_f16 v[112:115], v[164:167], v[148:151], v[112:115]
	v_mfma_f32_16x16x32_f16 v[116:119], v[168:171], v[148:151], v[116:119]
	s_waitcnt lgkmcnt(9)
	v_mfma_f32_16x16x32_f16 v[120:123], v[156:159], v[152:155], v[120:123]
	v_mfma_f32_16x16x32_f16 v[124:127], v[160:163], v[152:155], v[124:127]
	v_mfma_f32_16x16x32_f16 v[128:131], v[164:167], v[152:155], v[128:131]
	v_mfma_f32_16x16x32_f16 v[132:135], v[168:171], v[152:155], v[132:135]
	s_waitcnt vmcnt(6) lgkmcnt(0)
	s_barrier
	s_waitcnt lgkmcnt(6)
	ds_read_b128 v[136:139], v19
	ds_read_b128 v[156:159], v21
	ds_read_b128 v[160:163], v21 offset:2048
	ds_read_b128 v[164:167], v21 offset:4096
	ds_read_b128 v[168:171], v21 offset:6144
	ds_read_b128 v[140:143], v19 offset:2048
	ds_read_b128 v[144:147], v19 offset:4096
	ds_read_b128 v[148:151], v19 offset:6144
	ds_read_b128 v[152:155], v19 offset:8192
	v_mfma_f32_16x16x32_f16 v[56:59], v[192:195], v[172:175], v[56:59]
	s_waitcnt lgkmcnt(15)
	v_mfma_f32_16x16x32_f16 v[60:63], v[196:199], v[172:175], v[60:63]
	s_waitcnt lgkmcnt(14)
	v_mfma_f32_16x16x32_f16 v[64:67], v[200:203], v[172:175], v[64:67]
	s_waitcnt lgkmcnt(13)
	v_mfma_f32_16x16x32_f16 v[68:71], v[204:207], v[172:175], v[68:71]
	s_waitcnt lgkmcnt(12)
	v_mfma_f32_16x16x32_f16 v[72:75], v[192:195], v[176:179], v[72:75]
	v_mfma_f32_16x16x32_f16 v[76:79], v[196:199], v[176:179], v[76:79]
	v_mfma_f32_16x16x32_f16 v[80:83], v[200:203], v[176:179], v[80:83]
	v_mfma_f32_16x16x32_f16 v[84:87], v[204:207], v[176:179], v[84:87]
	s_waitcnt lgkmcnt(11)
	v_mfma_f32_16x16x32_f16 v[88:91], v[192:195], v[180:183], v[88:91]
	v_mfma_f32_16x16x32_f16 v[92:95], v[196:199], v[180:183], v[92:95]
	v_mfma_f32_16x16x32_f16 v[96:99], v[200:203], v[180:183], v[96:99]
	v_mfma_f32_16x16x32_f16 v[100:103], v[204:207], v[180:183], v[100:103]
	s_waitcnt lgkmcnt(10)
	v_mfma_f32_16x16x32_f16 v[104:107], v[192:195], v[184:187], v[104:107]
	v_mfma_f32_16x16x32_f16 v[108:111], v[196:199], v[184:187], v[108:111]
	v_mfma_f32_16x16x32_f16 v[112:115], v[200:203], v[184:187], v[112:115]
	v_mfma_f32_16x16x32_f16 v[116:119], v[204:207], v[184:187], v[116:119]
	s_waitcnt lgkmcnt(9)
	v_mfma_f32_16x16x32_f16 v[120:123], v[192:195], v[188:191], v[120:123]
	v_mfma_f32_16x16x32_f16 v[124:127], v[196:199], v[188:191], v[124:127]
	v_mfma_f32_16x16x32_f16 v[128:131], v[200:203], v[188:191], v[128:131]
	v_mfma_f32_16x16x32_f16 v[132:135], v[204:207], v[188:191], v[132:135]
	s_waitcnt lgkmcnt(6)
	ds_read_b128 v[172:175], v20
	ds_read_b128 v[192:195], v22
	ds_read_b128 v[196:199], v22 offset:2048
	ds_read_b128 v[200:203], v22 offset:4096
	ds_read_b128 v[204:207], v22 offset:6144
	ds_read_b128 v[176:179], v20 offset:2048
	ds_read_b128 v[180:183], v20 offset:4096
	ds_read_b128 v[184:187], v20 offset:6144
	ds_read_b128 v[188:191], v20 offset:8192
	v_mfma_f32_16x16x32_f16 v[56:59], v[156:159], v[136:139], v[56:59]
	s_waitcnt lgkmcnt(15)
	v_mfma_f32_16x16x32_f16 v[60:63], v[160:163], v[136:139], v[60:63]
	s_waitcnt lgkmcnt(14)
	v_mfma_f32_16x16x32_f16 v[64:67], v[164:167], v[136:139], v[64:67]
	s_waitcnt lgkmcnt(13)
	v_mfma_f32_16x16x32_f16 v[68:71], v[168:171], v[136:139], v[68:71]
	s_waitcnt lgkmcnt(12)
	v_mfma_f32_16x16x32_f16 v[72:75], v[156:159], v[140:143], v[72:75]
	v_mfma_f32_16x16x32_f16 v[76:79], v[160:163], v[140:143], v[76:79]
	v_mfma_f32_16x16x32_f16 v[80:83], v[164:167], v[140:143], v[80:83]
	v_mfma_f32_16x16x32_f16 v[84:87], v[168:171], v[140:143], v[84:87]
	s_waitcnt lgkmcnt(11)
	v_mfma_f32_16x16x32_f16 v[88:91], v[156:159], v[144:147], v[88:91]
	v_mfma_f32_16x16x32_f16 v[92:95], v[160:163], v[144:147], v[92:95]
	v_mfma_f32_16x16x32_f16 v[96:99], v[164:167], v[144:147], v[96:99]
	v_mfma_f32_16x16x32_f16 v[100:103], v[168:171], v[144:147], v[100:103]
	s_waitcnt lgkmcnt(10)
	v_mfma_f32_16x16x32_f16 v[104:107], v[156:159], v[148:151], v[104:107]
	v_mfma_f32_16x16x32_f16 v[108:111], v[160:163], v[148:151], v[108:111]
	v_mfma_f32_16x16x32_f16 v[112:115], v[164:167], v[148:151], v[112:115]
	v_mfma_f32_16x16x32_f16 v[116:119], v[168:171], v[148:151], v[116:119]
	s_waitcnt lgkmcnt(9)
	v_mfma_f32_16x16x32_f16 v[120:123], v[156:159], v[152:155], v[120:123]
	v_mfma_f32_16x16x32_f16 v[124:127], v[160:163], v[152:155], v[124:127]
	v_mfma_f32_16x16x32_f16 v[128:131], v[164:167], v[152:155], v[128:131]
	v_mfma_f32_16x16x32_f16 v[132:135], v[168:171], v[152:155], v[132:135]
	s_waitcnt vmcnt(0) lgkmcnt(0)
	s_barrier
	s_waitcnt lgkmcnt(6)
	ds_read_b128 v[136:139], v15
	ds_read_b128 v[156:159], v17
	ds_read_b128 v[160:163], v17 offset:2048
	ds_read_b128 v[164:167], v17 offset:4096
	ds_read_b128 v[168:171], v17 offset:6144
	ds_read_b128 v[140:143], v15 offset:2048
	ds_read_b128 v[144:147], v15 offset:4096
	ds_read_b128 v[148:151], v15 offset:6144
	ds_read_b128 v[152:155], v15 offset:8192
	v_mfma_f32_16x16x32_f16 v[56:59], v[192:195], v[172:175], v[56:59]
	s_waitcnt lgkmcnt(15)
	v_mfma_f32_16x16x32_f16 v[60:63], v[196:199], v[172:175], v[60:63]
	s_waitcnt lgkmcnt(14)
	v_mfma_f32_16x16x32_f16 v[64:67], v[200:203], v[172:175], v[64:67]
	s_waitcnt lgkmcnt(13)
	v_mfma_f32_16x16x32_f16 v[68:71], v[204:207], v[172:175], v[68:71]
	s_waitcnt lgkmcnt(12)
	v_mfma_f32_16x16x32_f16 v[72:75], v[192:195], v[176:179], v[72:75]
	v_mfma_f32_16x16x32_f16 v[76:79], v[196:199], v[176:179], v[76:79]
	v_mfma_f32_16x16x32_f16 v[80:83], v[200:203], v[176:179], v[80:83]
	v_mfma_f32_16x16x32_f16 v[84:87], v[204:207], v[176:179], v[84:87]
	s_waitcnt lgkmcnt(11)
	v_mfma_f32_16x16x32_f16 v[88:91], v[192:195], v[180:183], v[88:91]
	v_mfma_f32_16x16x32_f16 v[92:95], v[196:199], v[180:183], v[92:95]
	v_mfma_f32_16x16x32_f16 v[96:99], v[200:203], v[180:183], v[96:99]
	v_mfma_f32_16x16x32_f16 v[100:103], v[204:207], v[180:183], v[100:103]
	s_waitcnt lgkmcnt(10)
	v_mfma_f32_16x16x32_f16 v[104:107], v[192:195], v[184:187], v[104:107]
	v_mfma_f32_16x16x32_f16 v[108:111], v[196:199], v[184:187], v[108:111]
	v_mfma_f32_16x16x32_f16 v[112:115], v[200:203], v[184:187], v[112:115]
	v_mfma_f32_16x16x32_f16 v[116:119], v[204:207], v[184:187], v[116:119]
	s_waitcnt lgkmcnt(9)
	v_mfma_f32_16x16x32_f16 v[120:123], v[192:195], v[188:191], v[120:123]
	v_mfma_f32_16x16x32_f16 v[124:127], v[196:199], v[188:191], v[124:127]
	v_mfma_f32_16x16x32_f16 v[128:131], v[200:203], v[188:191], v[128:131]
	v_mfma_f32_16x16x32_f16 v[132:135], v[204:207], v[188:191], v[132:135]
	s_waitcnt lgkmcnt(6)
	ds_read_b128 v[172:175], v16
	ds_read_b128 v[192:195], v18
	ds_read_b128 v[196:199], v18 offset:2048
	ds_read_b128 v[200:203], v18 offset:4096
	ds_read_b128 v[204:207], v18 offset:6144
	ds_read_b128 v[176:179], v16 offset:2048
	ds_read_b128 v[180:183], v16 offset:4096
	ds_read_b128 v[184:187], v16 offset:6144
	ds_read_b128 v[188:191], v16 offset:8192
	v_mfma_f32_16x16x32_f16 v[56:59], v[156:159], v[136:139], v[56:59]
	s_waitcnt lgkmcnt(15)
	v_mfma_f32_16x16x32_f16 v[60:63], v[160:163], v[136:139], v[60:63]
	s_waitcnt lgkmcnt(14)
	v_mfma_f32_16x16x32_f16 v[64:67], v[164:167], v[136:139], v[64:67]
	s_waitcnt lgkmcnt(13)
	v_mfma_f32_16x16x32_f16 v[68:71], v[168:171], v[136:139], v[68:71]
	s_waitcnt lgkmcnt(12)
	v_mfma_f32_16x16x32_f16 v[72:75], v[156:159], v[140:143], v[72:75]
	v_mfma_f32_16x16x32_f16 v[76:79], v[160:163], v[140:143], v[76:79]
	v_mfma_f32_16x16x32_f16 v[80:83], v[164:167], v[140:143], v[80:83]
	v_mfma_f32_16x16x32_f16 v[84:87], v[168:171], v[140:143], v[84:87]
	s_waitcnt lgkmcnt(11)
	v_mfma_f32_16x16x32_f16 v[88:91], v[156:159], v[144:147], v[88:91]
	v_mfma_f32_16x16x32_f16 v[92:95], v[160:163], v[144:147], v[92:95]
	v_mfma_f32_16x16x32_f16 v[96:99], v[164:167], v[144:147], v[96:99]
	v_mfma_f32_16x16x32_f16 v[100:103], v[168:171], v[144:147], v[100:103]
	s_waitcnt lgkmcnt(10)
	v_mfma_f32_16x16x32_f16 v[104:107], v[156:159], v[148:151], v[104:107]
	v_mfma_f32_16x16x32_f16 v[108:111], v[160:163], v[148:151], v[108:111]
	v_mfma_f32_16x16x32_f16 v[112:115], v[164:167], v[148:151], v[112:115]
	v_mfma_f32_16x16x32_f16 v[116:119], v[168:171], v[148:151], v[116:119]
	s_waitcnt lgkmcnt(9)
	v_mfma_f32_16x16x32_f16 v[120:123], v[156:159], v[152:155], v[120:123]
	v_mfma_f32_16x16x32_f16 v[124:127], v[160:163], v[152:155], v[124:127]
	v_mfma_f32_16x16x32_f16 v[128:131], v[164:167], v[152:155], v[128:131]
	v_mfma_f32_16x16x32_f16 v[132:135], v[168:171], v[152:155], v[132:135]
	s_waitcnt lgkmcnt(7)
	v_mfma_f32_16x16x32_f16 v[56:59], v[192:195], v[172:175], v[56:59]
	s_waitcnt lgkmcnt(6)
	v_mfma_f32_16x16x32_f16 v[60:63], v[196:199], v[172:175], v[60:63]
	s_waitcnt lgkmcnt(5)
	v_mfma_f32_16x16x32_f16 v[64:67], v[200:203], v[172:175], v[64:67]
	s_waitcnt lgkmcnt(4)
	v_mfma_f32_16x16x32_f16 v[68:71], v[204:207], v[172:175], v[68:71]
	s_waitcnt lgkmcnt(3)
	v_mfma_f32_16x16x32_f16 v[72:75], v[192:195], v[176:179], v[72:75]
	v_mfma_f32_16x16x32_f16 v[76:79], v[196:199], v[176:179], v[76:79]
	v_mfma_f32_16x16x32_f16 v[80:83], v[200:203], v[176:179], v[80:83]
	v_mfma_f32_16x16x32_f16 v[84:87], v[204:207], v[176:179], v[84:87]
	s_waitcnt lgkmcnt(2)
	v_mfma_f32_16x16x32_f16 v[88:91], v[192:195], v[180:183], v[88:91]
	v_mfma_f32_16x16x32_f16 v[92:95], v[196:199], v[180:183], v[92:95]
	v_mfma_f32_16x16x32_f16 v[96:99], v[200:203], v[180:183], v[96:99]
	v_mfma_f32_16x16x32_f16 v[100:103], v[204:207], v[180:183], v[100:103]
	s_waitcnt lgkmcnt(1)
	v_mfma_f32_16x16x32_f16 v[104:107], v[192:195], v[184:187], v[104:107]
	v_mfma_f32_16x16x32_f16 v[108:111], v[196:199], v[184:187], v[108:111]
	v_mfma_f32_16x16x32_f16 v[112:115], v[200:203], v[184:187], v[112:115]
	v_mfma_f32_16x16x32_f16 v[116:119], v[204:207], v[184:187], v[116:119]
	s_waitcnt lgkmcnt(0)
	v_mfma_f32_16x16x32_f16 v[120:123], v[192:195], v[188:191], v[120:123]
	v_mfma_f32_16x16x32_f16 v[124:127], v[196:199], v[188:191], v[124:127]
	v_mfma_f32_16x16x32_f16 v[128:131], v[200:203], v[188:191], v[128:131]
	v_mfma_f32_16x16x32_f16 v[132:135], v[204:207], v[188:191], v[132:135]
	s_nop 7
	s_nop 1
	v_mov_b32_e32 v213, s19
	v_pk_add_f32 v[56:57], v[56:57], v[24:25]
	v_pk_add_f32 v[58:59], v[58:59], v[26:27]
	v_pk_add_f32 v[60:61], v[60:61], v[28:29]
	v_pk_add_f32 v[62:63], v[62:63], v[30:31]
	v_pk_add_f32 v[64:65], v[64:65], v[32:33]
	v_pk_add_f32 v[66:67], v[66:67], v[34:35]
	v_pk_add_f32 v[68:69], v[68:69], v[36:37]
	v_pk_add_f32 v[70:71], v[70:71], v[38:39]
	v_pk_mul_f32 v[208:209], v[56:57], v[56:57]
	v_pk_fma_f32 v[208:209], v[58:59], v[58:59], v[208:209]
	v_pk_fma_f32 v[208:209], v[60:61], v[60:61], v[208:209]
	v_pk_fma_f32 v[208:209], v[62:63], v[62:63], v[208:209]
	v_pk_fma_f32 v[208:209], v[64:65], v[64:65], v[208:209]
	v_pk_fma_f32 v[208:209], v[66:67], v[66:67], v[208:209]
	v_pk_fma_f32 v[208:209], v[68:69], v[68:69], v[208:209]
	v_pk_fma_f32 v[208:209], v[70:71], v[70:71], v[208:209]
	v_add_f32_e32 v208, v208, v209
	v_mov_b32_e32 v209, v208
	s_nop 1
	v_permlane16_swap_b32_e32 v208, v209
	v_add_f32_e32 v208, v208, v209
	v_mov_b32_e32 v209, v208
	s_nop 1
	v_permlane32_swap_b32_e32 v208, v209
	v_add_f32_e32 v208, v208, v209
	v_mov_b32_e32 v210, 0x358637bd
	v_fmac_f32_e32 v210, 0x3c800000, v208
	v_rsq_f32_e32 v210, v210
	s_add_u32 s24, s29, 0
	s_lshr_b32 s8, s24, 1
	s_lshl_b32 s8, s8, 12
	s_and_b32 s24, s24, 1
	s_lshl_b32 s24, s24, 8
	s_add_u32 s8, s8, s24
	v_mul_f32_e32 v210, v213, v210
	v_add_u32_e32 v212, s8, v23
	v_pk_mul_f32 v[56:57], v[56:57], v[210:211] op_sel_hi:[1,0]
	v_pk_mul_f32 v[58:59], v[58:59], v[210:211] op_sel_hi:[1,0]
	v_pk_mul_f32 v[56:57], v[56:57], v[40:41]
	v_pk_mul_f32 v[58:59], v[58:59], v[42:43]
	v_cvt_pk_f16_f32 v56, v56, v57
	v_cvt_pk_f16_f32 v57, v58, v59
	global_store_dwordx2 v212, v[56:57], s[22:23] offset:0
	v_pk_mul_f32 v[60:61], v[60:61], v[210:211] op_sel_hi:[1,0]
	v_pk_mul_f32 v[62:63], v[62:63], v[210:211] op_sel_hi:[1,0]
	v_pk_mul_f32 v[60:61], v[60:61], v[44:45]
	v_pk_mul_f32 v[62:63], v[62:63], v[46:47]
	v_cvt_pk_f16_f32 v60, v60, v61
	v_cvt_pk_f16_f32 v61, v62, v63
	global_store_dwordx2 v212, v[60:61], s[22:23] offset:1024
	v_pk_mul_f32 v[64:65], v[64:65], v[210:211] op_sel_hi:[1,0]
	v_pk_mul_f32 v[66:67], v[66:67], v[210:211] op_sel_hi:[1,0]
	v_pk_mul_f32 v[64:65], v[64:65], v[48:49]
	v_pk_mul_f32 v[66:67], v[66:67], v[50:51]
	v_cvt_pk_f16_f32 v64, v64, v65
	v_cvt_pk_f16_f32 v65, v66, v67
	global_store_dwordx2 v212, v[64:65], s[22:23] offset:2048
	v_pk_mul_f32 v[68:69], v[68:69], v[210:211] op_sel_hi:[1,0]
	v_pk_mul_f32 v[70:71], v[70:71], v[210:211] op_sel_hi:[1,0]
	v_pk_mul_f32 v[68:69], v[68:69], v[52:53]
	v_pk_mul_f32 v[70:71], v[70:71], v[54:55]
	v_cvt_pk_f16_f32 v68, v68, v69
	v_cvt_pk_f16_f32 v69, v70, v71
	global_store_dwordx2 v212, v[68:69], s[22:23] offset:3072
	v_pk_add_f32 v[72:73], v[72:73], v[24:25]
	v_pk_add_f32 v[74:75], v[74:75], v[26:27]
	v_pk_add_f32 v[76:77], v[76:77], v[28:29]
	v_pk_add_f32 v[78:79], v[78:79], v[30:31]
	v_pk_add_f32 v[80:81], v[80:81], v[32:33]
	v_pk_add_f32 v[82:83], v[82:83], v[34:35]
	v_pk_add_f32 v[84:85], v[84:85], v[36:37]
	v_pk_add_f32 v[86:87], v[86:87], v[38:39]
	v_pk_mul_f32 v[208:209], v[72:73], v[72:73]
	v_pk_fma_f32 v[208:209], v[74:75], v[74:75], v[208:209]
	v_pk_fma_f32 v[208:209], v[76:77], v[76:77], v[208:209]
	v_pk_fma_f32 v[208:209], v[78:79], v[78:79], v[208:209]
	v_pk_fma_f32 v[208:209], v[80:81], v[80:81], v[208:209]
	v_pk_fma_f32 v[208:209], v[82:83], v[82:83], v[208:209]
	v_pk_fma_f32 v[208:209], v[84:85], v[84:85], v[208:209]
	v_pk_fma_f32 v[208:209], v[86:87], v[86:87], v[208:209]
	v_add_f32_e32 v208, v208, v209
	v_mov_b32_e32 v209, v208
	s_nop 1
	v_permlane16_swap_b32_e32 v208, v209
	v_add_f32_e32 v208, v208, v209
	v_mov_b32_e32 v209, v208
	s_nop 1
	v_permlane32_swap_b32_e32 v208, v209
	v_add_f32_e32 v208, v208, v209
	v_mov_b32_e32 v210, 0x358637bd
	v_fmac_f32_e32 v210, 0x3c800000, v208
	v_rsq_f32_e32 v210, v210
	s_add_u32 s24, s29, 1
	s_lshr_b32 s8, s24, 1
	s_lshl_b32 s8, s8, 12
	s_and_b32 s24, s24, 1
	s_lshl_b32 s24, s24, 8
	s_add_u32 s8, s8, s24
	v_mul_f32_e32 v210, v213, v210
	v_add_u32_e32 v212, s8, v23
	v_pk_mul_f32 v[72:73], v[72:73], v[210:211] op_sel_hi:[1,0]
	v_pk_mul_f32 v[74:75], v[74:75], v[210:211] op_sel_hi:[1,0]
	v_pk_mul_f32 v[72:73], v[72:73], v[40:41]
	v_pk_mul_f32 v[74:75], v[74:75], v[42:43]
	v_cvt_pk_f16_f32 v72, v72, v73
	v_cvt_pk_f16_f32 v73, v74, v75
	global_store_dwordx2 v212, v[72:73], s[22:23] offset:0
	v_pk_mul_f32 v[76:77], v[76:77], v[210:211] op_sel_hi:[1,0]
	v_pk_mul_f32 v[78:79], v[78:79], v[210:211] op_sel_hi:[1,0]
	v_pk_mul_f32 v[76:77], v[76:77], v[44:45]
	v_pk_mul_f32 v[78:79], v[78:79], v[46:47]
	v_cvt_pk_f16_f32 v76, v76, v77
	v_cvt_pk_f16_f32 v77, v78, v79
	global_store_dwordx2 v212, v[76:77], s[22:23] offset:1024
	v_pk_mul_f32 v[80:81], v[80:81], v[210:211] op_sel_hi:[1,0]
	v_pk_mul_f32 v[82:83], v[82:83], v[210:211] op_sel_hi:[1,0]
	v_pk_mul_f32 v[80:81], v[80:81], v[48:49]
	v_pk_mul_f32 v[82:83], v[82:83], v[50:51]
	v_cvt_pk_f16_f32 v80, v80, v81
	v_cvt_pk_f16_f32 v81, v82, v83
	global_store_dwordx2 v212, v[80:81], s[22:23] offset:2048
	v_pk_mul_f32 v[84:85], v[84:85], v[210:211] op_sel_hi:[1,0]
	v_pk_mul_f32 v[86:87], v[86:87], v[210:211] op_sel_hi:[1,0]
	v_pk_mul_f32 v[84:85], v[84:85], v[52:53]
	v_pk_mul_f32 v[86:87], v[86:87], v[54:55]
	v_cvt_pk_f16_f32 v84, v84, v85
	v_cvt_pk_f16_f32 v85, v86, v87
	global_store_dwordx2 v212, v[84:85], s[22:23] offset:3072
	v_pk_add_f32 v[88:89], v[88:89], v[24:25]
	v_pk_add_f32 v[90:91], v[90:91], v[26:27]
	v_pk_add_f32 v[92:93], v[92:93], v[28:29]
	v_pk_add_f32 v[94:95], v[94:95], v[30:31]
	v_pk_add_f32 v[96:97], v[96:97], v[32:33]
	v_pk_add_f32 v[98:99], v[98:99], v[34:35]
	v_pk_add_f32 v[100:101], v[100:101], v[36:37]
	v_pk_add_f32 v[102:103], v[102:103], v[38:39]
	v_pk_mul_f32 v[208:209], v[88:89], v[88:89]
	v_pk_fma_f32 v[208:209], v[90:91], v[90:91], v[208:209]
	v_pk_fma_f32 v[208:209], v[92:93], v[92:93], v[208:209]
	v_pk_fma_f32 v[208:209], v[94:95], v[94:95], v[208:209]
	v_pk_fma_f32 v[208:209], v[96:97], v[96:97], v[208:209]
	v_pk_fma_f32 v[208:209], v[98:99], v[98:99], v[208:209]
	v_pk_fma_f32 v[208:209], v[100:101], v[100:101], v[208:209]
	v_pk_fma_f32 v[208:209], v[102:103], v[102:103], v[208:209]
	v_add_f32_e32 v208, v208, v209
	v_mov_b32_e32 v209, v208
	s_nop 1
	v_permlane16_swap_b32_e32 v208, v209
	v_add_f32_e32 v208, v208, v209
	v_mov_b32_e32 v209, v208
	s_nop 1
	v_permlane32_swap_b32_e32 v208, v209
	v_add_f32_e32 v208, v208, v209
	v_mov_b32_e32 v210, 0x358637bd
	v_fmac_f32_e32 v210, 0x3c800000, v208
	v_rsq_f32_e32 v210, v210
	s_add_u32 s24, s29, 2
	s_lshr_b32 s8, s24, 1
	s_lshl_b32 s8, s8, 12
	s_and_b32 s24, s24, 1
	s_lshl_b32 s24, s24, 8
	s_add_u32 s8, s8, s24
	v_mul_f32_e32 v210, v213, v210
	v_add_u32_e32 v212, s8, v23
	v_pk_mul_f32 v[88:89], v[88:89], v[210:211] op_sel_hi:[1,0]
	v_pk_mul_f32 v[90:91], v[90:91], v[210:211] op_sel_hi:[1,0]
	v_pk_mul_f32 v[88:89], v[88:89], v[40:41]
	v_pk_mul_f32 v[90:91], v[90:91], v[42:43]
	v_cvt_pk_f16_f32 v88, v88, v89
	v_cvt_pk_f16_f32 v89, v90, v91
	global_store_dwordx2 v212, v[88:89], s[22:23] offset:0
	v_pk_mul_f32 v[92:93], v[92:93], v[210:211] op_sel_hi:[1,0]
	v_pk_mul_f32 v[94:95], v[94:95], v[210:211] op_sel_hi:[1,0]
	v_pk_mul_f32 v[92:93], v[92:93], v[44:45]
	v_pk_mul_f32 v[94:95], v[94:95], v[46:47]
	v_cvt_pk_f16_f32 v92, v92, v93
	v_cvt_pk_f16_f32 v93, v94, v95
	global_store_dwordx2 v212, v[92:93], s[22:23] offset:1024
	v_pk_mul_f32 v[96:97], v[96:97], v[210:211] op_sel_hi:[1,0]
	v_pk_mul_f32 v[98:99], v[98:99], v[210:211] op_sel_hi:[1,0]
	v_pk_mul_f32 v[96:97], v[96:97], v[48:49]
	v_pk_mul_f32 v[98:99], v[98:99], v[50:51]
	v_cvt_pk_f16_f32 v96, v96, v97
	v_cvt_pk_f16_f32 v97, v98, v99
	global_store_dwordx2 v212, v[96:97], s[22:23] offset:2048
	v_pk_mul_f32 v[100:101], v[100:101], v[210:211] op_sel_hi:[1,0]
	v_pk_mul_f32 v[102:103], v[102:103], v[210:211] op_sel_hi:[1,0]
	v_pk_mul_f32 v[100:101], v[100:101], v[52:53]
	v_pk_mul_f32 v[102:103], v[102:103], v[54:55]
	v_cvt_pk_f16_f32 v100, v100, v101
	v_cvt_pk_f16_f32 v101, v102, v103
	global_store_dwordx2 v212, v[100:101], s[22:23] offset:3072
	v_pk_add_f32 v[104:105], v[104:105], v[24:25]
	v_pk_add_f32 v[106:107], v[106:107], v[26:27]
	v_pk_add_f32 v[108:109], v[108:109], v[28:29]
	v_pk_add_f32 v[110:111], v[110:111], v[30:31]
	v_pk_add_f32 v[112:113], v[112:113], v[32:33]
	v_pk_add_f32 v[114:115], v[114:115], v[34:35]
	v_pk_add_f32 v[116:117], v[116:117], v[36:37]
	v_pk_add_f32 v[118:119], v[118:119], v[38:39]
	v_pk_mul_f32 v[208:209], v[104:105], v[104:105]
	v_pk_fma_f32 v[208:209], v[106:107], v[106:107], v[208:209]
	v_pk_fma_f32 v[208:209], v[108:109], v[108:109], v[208:209]
	v_pk_fma_f32 v[208:209], v[110:111], v[110:111], v[208:209]
	v_pk_fma_f32 v[208:209], v[112:113], v[112:113], v[208:209]
	v_pk_fma_f32 v[208:209], v[114:115], v[114:115], v[208:209]
	v_pk_fma_f32 v[208:209], v[116:117], v[116:117], v[208:209]
	v_pk_fma_f32 v[208:209], v[118:119], v[118:119], v[208:209]
	v_add_f32_e32 v208, v208, v209
	v_mov_b32_e32 v209, v208
	s_nop 1
	v_permlane16_swap_b32_e32 v208, v209
	v_add_f32_e32 v208, v208, v209
	v_mov_b32_e32 v209, v208
	s_nop 1
	v_permlane32_swap_b32_e32 v208, v209
	v_add_f32_e32 v208, v208, v209
	v_mov_b32_e32 v210, 0x358637bd
	v_fmac_f32_e32 v210, 0x3c800000, v208
	v_rsq_f32_e32 v210, v210
	s_add_u32 s24, s29, 3
	s_lshr_b32 s8, s24, 1
	s_lshl_b32 s8, s8, 12
	s_and_b32 s24, s24, 1
	s_lshl_b32 s24, s24, 8
	s_add_u32 s8, s8, s24
	v_mul_f32_e32 v210, v213, v210
	v_add_u32_e32 v212, s8, v23
	v_pk_mul_f32 v[104:105], v[104:105], v[210:211] op_sel_hi:[1,0]
	v_pk_mul_f32 v[106:107], v[106:107], v[210:211] op_sel_hi:[1,0]
	v_pk_mul_f32 v[104:105], v[104:105], v[40:41]
	v_pk_mul_f32 v[106:107], v[106:107], v[42:43]
	v_cvt_pk_f16_f32 v104, v104, v105
	v_cvt_pk_f16_f32 v105, v106, v107
	global_store_dwordx2 v212, v[104:105], s[22:23] offset:0
	v_pk_mul_f32 v[108:109], v[108:109], v[210:211] op_sel_hi:[1,0]
	v_pk_mul_f32 v[110:111], v[110:111], v[210:211] op_sel_hi:[1,0]
	v_pk_mul_f32 v[108:109], v[108:109], v[44:45]
	v_pk_mul_f32 v[110:111], v[110:111], v[46:47]
	v_cvt_pk_f16_f32 v108, v108, v109
	v_cvt_pk_f16_f32 v109, v110, v111
	global_store_dwordx2 v212, v[108:109], s[22:23] offset:1024
	v_pk_mul_f32 v[112:113], v[112:113], v[210:211] op_sel_hi:[1,0]
	v_pk_mul_f32 v[114:115], v[114:115], v[210:211] op_sel_hi:[1,0]
	v_pk_mul_f32 v[112:113], v[112:113], v[48:49]
	v_pk_mul_f32 v[114:115], v[114:115], v[50:51]
	v_cvt_pk_f16_f32 v112, v112, v113
	v_cvt_pk_f16_f32 v113, v114, v115
	global_store_dwordx2 v212, v[112:113], s[22:23] offset:2048
	v_pk_mul_f32 v[116:117], v[116:117], v[210:211] op_sel_hi:[1,0]
	v_pk_mul_f32 v[118:119], v[118:119], v[210:211] op_sel_hi:[1,0]
	v_pk_mul_f32 v[116:117], v[116:117], v[52:53]
	v_pk_mul_f32 v[118:119], v[118:119], v[54:55]
	v_cvt_pk_f16_f32 v116, v116, v117
	v_cvt_pk_f16_f32 v117, v118, v119
	global_store_dwordx2 v212, v[116:117], s[22:23] offset:3072
	v_pk_add_f32 v[120:121], v[120:121], v[24:25]
	v_pk_add_f32 v[122:123], v[122:123], v[26:27]
	v_pk_add_f32 v[124:125], v[124:125], v[28:29]
	v_pk_add_f32 v[126:127], v[126:127], v[30:31]
	v_pk_add_f32 v[128:129], v[128:129], v[32:33]
	v_pk_add_f32 v[130:131], v[130:131], v[34:35]
	v_pk_add_f32 v[132:133], v[132:133], v[36:37]
	v_pk_add_f32 v[134:135], v[134:135], v[38:39]
	v_pk_mul_f32 v[208:209], v[120:121], v[120:121]
	v_pk_fma_f32 v[208:209], v[122:123], v[122:123], v[208:209]
	v_pk_fma_f32 v[208:209], v[124:125], v[124:125], v[208:209]
	v_pk_fma_f32 v[208:209], v[126:127], v[126:127], v[208:209]
	v_pk_fma_f32 v[208:209], v[128:129], v[128:129], v[208:209]
	v_pk_fma_f32 v[208:209], v[130:131], v[130:131], v[208:209]
	v_pk_fma_f32 v[208:209], v[132:133], v[132:133], v[208:209]
	v_pk_fma_f32 v[208:209], v[134:135], v[134:135], v[208:209]
	v_add_f32_e32 v208, v208, v209
	v_mov_b32_e32 v209, v208
	s_nop 1
	v_permlane16_swap_b32_e32 v208, v209
	v_add_f32_e32 v208, v208, v209
	v_mov_b32_e32 v209, v208
	s_nop 1
	v_permlane32_swap_b32_e32 v208, v209
	v_add_f32_e32 v208, v208, v209
	v_mov_b32_e32 v210, 0x358637bd
	v_fmac_f32_e32 v210, 0x3c800000, v208
	v_rsq_f32_e32 v210, v210
	s_add_u32 s24, s29, 4
	s_lshr_b32 s8, s24, 1
	s_lshl_b32 s8, s8, 12
	s_and_b32 s24, s24, 1
	s_lshl_b32 s24, s24, 8
	s_add_u32 s8, s8, s24
	v_mul_f32_e32 v210, v213, v210
	v_add_u32_e32 v212, s8, v23
	v_pk_mul_f32 v[120:121], v[120:121], v[210:211] op_sel_hi:[1,0]
	v_pk_mul_f32 v[122:123], v[122:123], v[210:211] op_sel_hi:[1,0]
	v_pk_mul_f32 v[120:121], v[120:121], v[40:41]
	v_pk_mul_f32 v[122:123], v[122:123], v[42:43]
	v_cvt_pk_f16_f32 v120, v120, v121
	v_cvt_pk_f16_f32 v121, v122, v123
	global_store_dwordx2 v212, v[120:121], s[22:23] offset:0
	v_pk_mul_f32 v[124:125], v[124:125], v[210:211] op_sel_hi:[1,0]
	v_pk_mul_f32 v[126:127], v[126:127], v[210:211] op_sel_hi:[1,0]
	v_pk_mul_f32 v[124:125], v[124:125], v[44:45]
	v_pk_mul_f32 v[126:127], v[126:127], v[46:47]
	v_cvt_pk_f16_f32 v124, v124, v125
	v_cvt_pk_f16_f32 v125, v126, v127
	global_store_dwordx2 v212, v[124:125], s[22:23] offset:1024
	v_pk_mul_f32 v[128:129], v[128:129], v[210:211] op_sel_hi:[1,0]
	v_pk_mul_f32 v[130:131], v[130:131], v[210:211] op_sel_hi:[1,0]
	v_pk_mul_f32 v[128:129], v[128:129], v[48:49]
	v_pk_mul_f32 v[130:131], v[130:131], v[50:51]
	v_cvt_pk_f16_f32 v128, v128, v129
	v_cvt_pk_f16_f32 v129, v130, v131
	global_store_dwordx2 v212, v[128:129], s[22:23] offset:2048
	v_pk_mul_f32 v[132:133], v[132:133], v[210:211] op_sel_hi:[1,0]
	v_pk_mul_f32 v[134:135], v[134:135], v[210:211] op_sel_hi:[1,0]
	v_pk_mul_f32 v[132:133], v[132:133], v[52:53]
	v_pk_mul_f32 v[134:135], v[134:135], v[54:55]
	v_cvt_pk_f16_f32 v132, v132, v133
	v_cvt_pk_f16_f32 v133, v134, v135
	global_store_dwordx2 v212, v[132:133], s[22:23] offset:3072
	s_branch .Lpf_done
.Lpf_vKB:
	v_add_u32_e32 v8, 0x77000, v10
	s_lshl_b32 s25, s25, 6
	s_add_u32 s25, s25, 32
	s_add_u32 s29, s10, s25
	s_lshr_b32 s29, s29, 4
	v_add_u32_e32 v5, s25, v3
	v_lshlrev_b32_e32 v5, 7, v5
	v_add_u32_e32 v15, v5, v6
	v_add_u32_e32 v16, v5, v7
	v_add_u32_e32 v5, 0x9000, v9
	v_add_u32_e32 v17, v5, v6
	v_add_u32_e32 v18, v5, v7
	v_add_u32_e32 v19, 0x1a000, v15
	v_add_u32_e32 v20, 0x1a000, v16
	v_add_u32_e32 v21, 0x1a000, v17
	v_add_u32_e32 v22, 0x1a000, v18
	v_lshlrev_b32_e32 v5, 4, v4
	global_load_dwordx4 v[24:27], v5, s[14:15] offset:0
	global_load_dwordx4 v[28:31], v5, s[14:15] offset:64
	global_load_dwordx4 v[32:35], v5, s[14:15] offset:128
	global_load_dwordx4 v[36:39], v5, s[14:15] offset:192
	global_load_dwordx4 v[40:43], v5, s[16:17] offset:0
	global_load_dwordx4 v[44:47], v5, s[16:17] offset:64
	global_load_dwordx4 v[48:51], v5, s[16:17] offset:128
	global_load_dwordx4 v[52:55], v5, s[16:17] offset:192
	s_add_u32 m0, s28, 0x0
	s_nop 0
	global_load_lds_dwordx4 v10, s[4:5]
	s_add_u32 m0, s28, 0x2000
	s_nop 0
	global_load_lds_dwordx4 v11, s[4:5]
	s_add_u32 m0, s28, 0x4000
	s_nop 0
	global_load_lds_dwordx4 v12, s[4:5]
	s_add_u32 m0, s28, 0x6000
	s_nop 0
	global_load_lds_dwordx4 v13, s[4:5]
	s_add_u32 m0, s28, 0x7000
	s_nop 0
	global_load_lds_dwordx4 v8, s[4:5]
	s_add_u32 s4, s4, s20
	s_addc_u32 s5, s5, 0
	s_add_u32 m0, s28, 0x9000
	s_nop 0
	global_load_lds_dwordx4 v10, s[6:7]
	s_add_u32 m0, s28, 0xb000
	s_nop 0
	global_load_lds_dwordx4 v11, s[6:7]
	s_add_u32 s6, s6, s20
	s_addc_u32 s7, s7, 0
	s_add_u32 m0, s28, 0xd000
	s_nop 0
	global_load_lds_dwordx4 v10, s[4:5]
	s_add_u32 m0, s28, 0xf000
	s_nop 0
	global_load_lds_dwordx4 v11, s[4:5]
	s_add_u32 m0, s28, 0x11000
	s_nop 0
	global_load_lds_dwordx4 v12, s[4:5]
	s_add_u32 m0, s28, 0x13000
	s_nop 0
	global_load_lds_dwordx4 v13, s[4:5]
	s_add_u32 m0, s28, 0x14000
	s_nop 0
	global_load_lds_dwordx4 v8, s[4:5]
	s_add_u32 s4, s4, s20
	s_addc_u32 s5, s5, 0
	s_add_u32 m0, s28, 0x16000
	s_nop 0
	global_load_lds_dwordx4 v10, s[6:7]
	s_add_u32 m0, s28, 0x18000
	s_nop 0
	global_load_lds_dwordx4 v11, s[6:7]
	s_add_u32 s6, s6, s20
	s_addc_u32 s7, s7, 0
	s_add_u32 m0, s28, 0x1a000
	s_nop 0
	global_load_lds_dwordx4 v10, s[4:5]
	s_add_u32 m0, s28, 0x1c000
	s_nop 0
	global_load_lds_dwordx4 v11, s[4:5]
	s_add_u32 m0, s28, 0x1e000
	s_nop 0
	global_load_lds_dwordx4 v12, s[4:5]
	s_add_u32 m0, s28, 0x20000
	s_nop 0
	global_load_lds_dwordx4 v13, s[4:5]
	s_add_u32 m0, s28, 0x21000
	s_nop 0
	global_load_lds_dwordx4 v8, s[4:5]
	s_add_u32 s4, s4, s20
	s_addc_u32 s5, s5, 0
	s_add_u32 m0, s28, 0x23000
	s_nop 0
	global_load_lds_dwordx4 v10, s[6:7]
	s_add_u32 m0, s28, 0x25000
	s_nop 0
	global_load_lds_dwordx4 v11, s[6:7]
	s_add_u32 s6, s6, s20
	s_addc_u32 s7, s7, 0
	s_waitcnt vmcnt(14) lgkmcnt(0)
	s_barrier
	s_waitcnt lgkmcnt(7)
	ds_read_b128 v[136:139], v15
	ds_read_b128 v[156:159], v17
	ds_read_b128 v[160:163], v17 offset:2048
	ds_read_b128 v[164:167], v17 offset:4096
	ds_read_b128 v[168:171], v17 offset:6144
	ds_read_b128 v[140:143], v15 offset:2048
	ds_read_b128 v[144:147], v15 offset:4096
	ds_read_b128 v[148:151], v15 offset:6144
	s_waitcnt lgkmcnt(7)
	ds_read_b128 v[172:175], v16
	ds_read_b128 v[192:195], v18
	ds_read_b128 v[196:199], v18 offset:2048
	ds_read_b128 v[200:203], v18 offset:4096
	ds_read_b128 v[204:207], v18 offset:6144
	ds_read_b128 v[176:179], v16 offset:2048
	ds_read_b128 v[180:183], v16 offset:4096
	ds_read_b128 v[184:187], v16 offset:6144
	s_waitcnt lgkmcnt(14)
	v_mfma_f32_16x16x32_f16 v[56:59], v[156:159], v[136:139], 0
	s_waitcnt lgkmcnt(13)
	v_mfma_f32_16x16x32_f16 v[60:63], v[160:163], v[136:139], 0
	s_waitcnt lgkmcnt(12)
	v_mfma_f32_16x16x32_f16 v[64:67], v[164:167], v[136:139], 0
	s_waitcnt lgkmcnt(11)
	v_mfma_f32_16x16x32_f16 v[68:71], v[168:171], v[136:139], 0
	s_waitcnt lgkmcnt(10)
	v_mfma_f32_16x16x32_f16 v[72:75], v[156:159], v[140:143], 0
	v_mfma_f32_16x16x32_f16 v[76:79], v[160:163], v[140:143], 0
	v_mfma_f32_16x16x32_f16 v[80:83], v[164:167], v[140:143], 0
	v_mfma_f32_16x16x32_f16 v[84:87], v[168:171], v[140:143], 0
	s_waitcnt lgkmcnt(9)
	v_mfma_f32_16x16x32_f16 v[88:91], v[156:159], v[144:147], 0
	v_mfma_f32_16x16x32_f16 v[92:95], v[160:163], v[144:147], 0
	v_mfma_f32_16x16x32_f16 v[96:99], v[164:167], v[144:147], 0
	v_mfma_f32_16x16x32_f16 v[100:103], v[168:171], v[144:147], 0
	s_waitcnt lgkmcnt(8)
	v_mfma_f32_16x16x32_f16 v[104:107], v[156:159], v[148:151], 0
	v_mfma_f32_16x16x32_f16 v[108:111], v[160:163], v[148:151], 0
	v_mfma_f32_16x16x32_f16 v[112:115], v[164:167], v[148:151], 0
	v_mfma_f32_16x16x32_f16 v[116:119], v[168:171], v[148:151], 0
	s_waitcnt vmcnt(7) lgkmcnt(0)
	s_barrier
	s_waitcnt lgkmcnt(7)
	ds_read_b128 v[136:139], v15 offset:53248
	ds_read_b128 v[156:159], v17 offset:53248
	ds_read_b128 v[160:163], v17 offset:55296
	ds_read_b128 v[164:167], v17 offset:57344
	ds_read_b128 v[168:171], v17 offset:59392
	ds_read_b128 v[140:143], v15 offset:55296
	ds_read_b128 v[144:147], v15 offset:57344
	ds_read_b128 v[148:151], v15 offset:59392
	s_waitcnt lgkmcnt(14)
	v_mfma_f32_16x16x32_f16 v[56:59], v[192:195], v[172:175], v[56:59]
	s_add_u32 m0, s28, 0x0
	s_nop 0
	global_load_lds_dwordx4 v10, s[4:5]
	s_waitcnt lgkmcnt(13)
	v_mfma_f32_16x16x32_f16 v[60:63], v[196:199], v[172:175], v[60:63]
	s_waitcnt lgkmcnt(12)
	v_mfma_f32_16x16x32_f16 v[64:67], v[200:203], v[172:175], v[64:67]
	s_waitcnt lgkmcnt(11)
	v_mfma_f32_16x16x32_f16 v[68:71], v[204:207], v[172:175], v[68:71]
	s_waitcnt lgkmcnt(10)
	v_mfma_f32_16x16x32_f16 v[72:75], v[192:195], v[176:179], v[72:75]
	s_add_u32 m0, s28, 0x2000
	s_nop 0
	global_load_lds_dwordx4 v11, s[4:5]
	v_mfma_f32_16x16x32_f16 v[76:79], v[196:199], v[176:179], v[76:79]
	v_mfma_f32_16x16x32_f16 v[80:83], v[200:203], v[176:179], v[80:83]
	v_mfma_f32_16x16x32_f16 v[84:87], v[204:207], v[176:179], v[84:87]
	s_waitcnt lgkmcnt(9)
	v_mfma_f32_16x16x32_f16 v[88:91], v[192:195], v[180:183], v[88:91]
	s_add_u32 m0, s28, 0x4000
	s_nop 0
	global_load_lds_dwordx4 v12, s[4:5]
	v_mfma_f32_16x16x32_f16 v[92:95], v[196:199], v[180:183], v[92:95]
	v_mfma_f32_16x16x32_f16 v[96:99], v[200:203], v[180:183], v[96:99]
	v_mfma_f32_16x16x32_f16 v[100:103], v[204:207], v[180:183], v[100:103]
	s_waitcnt lgkmcnt(8)
	v_mfma_f32_16x16x32_f16 v[104:107], v[192:195], v[184:187], v[104:107]
	s_add_u32 m0, s28, 0x6000
	s_nop 0
	global_load_lds_dwordx4 v13, s[4:5]
	v_mfma_f32_16x16x32_f16 v[108:111], v[196:199], v[184:187], v[108:111]
	v_mfma_f32_16x16x32_f16 v[112:115], v[200:203], v[184:187], v[112:115]
	v_mfma_f32_16x16x32_f16 v[116:119], v[204:207], v[184:187], v[116:119]
	s_waitcnt lgkmcnt(7)
	ds_read_b128 v[172:175], v16 offset:53248
	ds_read_b128 v[192:195], v18 offset:53248
	ds_read_b128 v[196:199], v18 offset:55296
	ds_read_b128 v[200:203], v18 offset:57344
	ds_read_b128 v[204:207], v18 offset:59392
	ds_read_b128 v[176:179], v16 offset:55296
	ds_read_b128 v[180:183], v16 offset:57344
	ds_read_b128 v[184:187], v16 offset:59392
	s_waitcnt lgkmcnt(14)
	v_mfma_f32_16x16x32_f16 v[56:59], v[156:159], v[136:139], v[56:59]
	s_add_u32 m0, s28, 0x7000
	s_nop 0
	global_load_lds_dwordx4 v8, s[4:5]
	s_add_u32 s4, s4, s20
	s_addc_u32 s5, s5, 0
	s_waitcnt lgkmcnt(13)
	v_mfma_f32_16x16x32_f16 v[60:63], v[160:163], v[136:139], v[60:63]
	s_waitcnt lgkmcnt(12)
	v_mfma_f32_16x16x32_f16 v[64:67], v[164:167], v[136:139], v[64:67]
	s_waitcnt lgkmcnt(11)
	v_mfma_f32_16x16x32_f16 v[68:71], v[168:171], v[136:139], v[68:71]
	s_waitcnt lgkmcnt(10)
	v_mfma_f32_16x16x32_f16 v[72:75], v[156:159], v[140:143], v[72:75]
	v_mfma_f32_16x16x32_f16 v[76:79], v[160:163], v[140:143], v[76:79]
	s_add_u32 m0, s28, 0x9000
	s_nop 0
	global_load_lds_dwordx4 v10, s[6:7]
	v_mfma_f32_16x16x32_f16 v[80:83], v[164:167], v[140:143], v[80:83]
	v_mfma_f32_16x16x32_f16 v[84:87], v[168:171], v[140:143], v[84:87]
	s_waitcnt lgkmcnt(9)
	v_mfma_f32_16x16x32_f16 v[88:91], v[156:159], v[144:147], v[88:91]
	v_mfma_f32_16x16x32_f16 v[92:95], v[160:163], v[144:147], v[92:95]
	v_mfma_f32_16x16x32_f16 v[96:99], v[164:167], v[144:147], v[96:99]
	s_add_u32 m0, s28, 0xb000
	s_nop 0
	global_load_lds_dwordx4 v11, s[6:7]
	s_add_u32 s6, s6, s20
	s_addc_u32 s7, s7, 0
	v_mfma_f32_16x16x32_f16 v[100:103], v[168:171], v[144:147], v[100:103]
	s_waitcnt lgkmcnt(8)
	v_mfma_f32_16x16x32_f16 v[104:107], v[156:159], v[148:151], v[104:107]
	v_mfma_f32_16x16x32_f16 v[108:111], v[160:163], v[148:151], v[108:111]
	v_mfma_f32_16x16x32_f16 v[112:115], v[164:167], v[148:151], v[112:115]
	v_mfma_f32_16x16x32_f16 v[116:119], v[168:171], v[148:151], v[116:119]
	s_waitcnt vmcnt(7) lgkmcnt(0)
	s_barrier
	s_waitcnt lgkmcnt(7)
	ds_read_b128 v[136:139], v19
	ds_read_b128 v[156:159], v21
	ds_read_b128 v[160:163], v21 offset:2048
	ds_read_b128 v[164:167], v21 offset:4096
	ds_read_b128 v[168:171], v21 offset:6144
	ds_read_b128 v[140:143], v19 offset:2048
	ds_read_b128 v[144:147], v19 offset:4096
	ds_read_b128 v[148:151], v19 offset:6144
	s_waitcnt lgkmcnt(14)
	v_mfma_f32_16x16x32_f16 v[56:59], v[192:195], v[172:175], v[56:59]
	s_add_u32 m0, s28, 0xd000
	s_nop 0
	global_load_lds_dwordx4 v10, s[4:5]
	s_waitcnt lgkmcnt(13)
	v_mfma_f32_16x16x32_f16 v[60:63], v[196:199], v[172:175], v[60:63]
	s_waitcnt lgkmcnt(12)
	v_mfma_f32_16x16x32_f16 v[64:67], v[200:203], v[172:175], v[64:67]
	s_waitcnt lgkmcnt(11)
	v_mfma_f32_16x16x32_f16 v[68:71], v[204:207], v[172:175], v[68:71]
	s_waitcnt lgkmcnt(10)
	v_mfma_f32_16x16x32_f16 v[72:75], v[192:195], v[176:179], v[72:75]
	s_add_u32 m0, s28, 0xf000
	s_nop 0
	global_load_lds_dwordx4 v11, s[4:5]
	v_mfma_f32_16x16x32_f16 v[76:79], v[196:199], v[176:179], v[76:79]
	v_mfma_f32_16x16x32_f16 v[80:83], v[200:203], v[176:179], v[80:83]
	v_mfma_f32_16x16x32_f16 v[84:87], v[204:207], v[176:179], v[84:87]
	s_waitcnt lgkmcnt(9)
	v_mfma_f32_16x16x32_f16 v[88:91], v[192:195], v[180:183], v[88:91]
	s_add_u32 m0, s28, 0x11000
	s_nop 0
	global_load_lds_dwordx4 v12, s[4:5]
	v_mfma_f32_16x16x32_f16 v[92:95], v[196:199], v[180:183], v[92:95]
	v_mfma_f32_16x16x32_f16 v[96:99], v[200:203], v[180:183], v[96:99]
	v_mfma_f32_16x16x32_f16 v[100:103], v[204:207], v[180:183], v[100:103]
	s_waitcnt lgkmcnt(8)
	v_mfma_f32_16x16x32_f16 v[104:107], v[192:195], v[184:187], v[104:107]
	s_add_u32 m0, s28, 0x13000
	s_nop 0
	global_load_lds_dwordx4 v13, s[4:5]
	v_mfma_f32_16x16x32_f16 v[108:111], v[196:199], v[184:187], v[108:111]
	v_mfma_f32_16x16x32_f16 v[112:115], v[200:203], v[184:187], v[112:115]
	v_mfma_f32_16x16x32_f16 v[116:119], v[204:207], v[184:187], v[116:119]
	s_waitcnt lgkmcnt(7)
	ds_read_b128 v[172:175], v20
	ds_read_b128 v[192:195], v22
	ds_read_b128 v[196:199], v22 offset:2048
	ds_read_b128 v[200:203], v22 offset:4096
	ds_read_b128 v[204:207], v22 offset:6144
	ds_read_b128 v[176:179], v20 offset:2048
	ds_read_b128 v[180:183], v20 offset:4096
	ds_read_b128 v[184:187], v20 offset:6144
	s_waitcnt lgkmcnt(14)
	v_mfma_f32_16x16x32_f16 v[56:59], v[156:159], v[136:139], v[56:59]
	s_add_u32 m0, s28, 0x14000
	s_nop 0
	global_load_lds_dwordx4 v8, s[4:5]
	s_add_u32 s4, s4, s20
	s_addc_u32 s5, s5, 0
	s_waitcnt lgkmcnt(13)
	v_mfma_f32_16x16x32_f16 v[60:63], v[160:163], v[136:139], v[60:63]
	s_waitcnt lgkmcnt(12)
	v_mfma_f32_16x16x32_f16 v[64:67], v[164:167], v[136:139], v[64:67]
	s_waitcnt lgkmcnt(11)
	v_mfma_f32_16x16x32_f16 v[68:71], v[168:171], v[136:139], v[68:71]
	s_waitcnt lgkmcnt(10)
	v_mfma_f32_16x16x32_f16 v[72:75], v[156:159], v[140:143], v[72:75]
	v_mfma_f32_16x16x32_f16 v[76:79], v[160:163], v[140:143], v[76:79]
	s_add_u32 m0, s28, 0x16000
	s_nop 0
	global_load_lds_dwordx4 v10, s[6:7]
	v_mfma_f32_16x16x32_f16 v[80:83], v[164:167], v[140:143], v[80:83]
	v_mfma_f32_16x16x32_f16 v[84:87], v[168:171], v[140:143], v[84:87]
	s_waitcnt lgkmcnt(9)
	v_mfma_f32_16x16x32_f16 v[88:91], v[156:159], v[144:147], v[88:91]
	v_mfma_f32_16x16x32_f16 v[92:95], v[160:163], v[144:147], v[92:95]
	v_mfma_f32_16x16x32_f16 v[96:99], v[164:167], v[144:147], v[96:99]
	s_add_u32 m0, s28, 0x18000
	s_nop 0
	global_load_lds_dwordx4 v11, s[6:7]
	s_add_u32 s6, s6, s20
	s_addc_u32 s7, s7, 0
	v_mfma_f32_16x16x32_f16 v[100:103], v[168:171], v[144:147], v[100:103]
	s_waitcnt lgkmcnt(8)
	v_mfma_f32_16x16x32_f16 v[104:107], v[156:159], v[148:151], v[104:107]
	v_mfma_f32_16x16x32_f16 v[108:111], v[160:163], v[148:151], v[108:111]
	v_mfma_f32_16x16x32_f16 v[112:115], v[164:167], v[148:151], v[112:115]
	v_mfma_f32_16x16x32_f16 v[116:119], v[168:171], v[148:151], v[116:119]
	s_waitcnt vmcnt(7) lgkmcnt(0)
	s_barrier
	s_waitcnt lgkmcnt(7)
	ds_read_b128 v[136:139], v15
	ds_read_b128 v[156:159], v17
	ds_read_b128 v[160:163], v17 offset:2048
	ds_read_b128 v[164:167], v17 offset:4096
	ds_read_b128 v[168:171], v17 offset:6144
	ds_read_b128 v[140:143], v15 offset:2048
	ds_read_b128 v[144:147], v15 offset:4096
	ds_read_b128 v[148:151], v15 offset:6144
	s_waitcnt lgkmcnt(14)
	v_mfma_f32_16x16x32_f16 v[56:59], v[192:195], v[172:175], v[56:59]
	s_add_u32 m0, s28, 0x1a000
	s_nop 0
	global_load_lds_dwordx4 v10, s[4:5]
	s_waitcnt lgkmcnt(13)
	v_mfma_f32_16x16x32_f16 v[60:63], v[196:199], v[172:175], v[60:63]
	s_waitcnt lgkmcnt(12)
	v_mfma_f32_16x16x32_f16 v[64:67], v[200:203], v[172:175], v[64:67]
	s_waitcnt lgkmcnt(11)
	v_mfma_f32_16x16x32_f16 v[68:71], v[204:207], v[172:175], v[68:71]
	s_waitcnt lgkmcnt(10)
	v_mfma_f32_16x16x32_f16 v[72:75], v[192:195], v[176:179], v[72:75]
	s_add_u32 m0, s28, 0x1c000
	s_nop 0
	global_load_lds_dwordx4 v11, s[4:5]
	v_mfma_f32_16x16x32_f16 v[76:79], v[196:199], v[176:179], v[76:79]
	v_mfma_f32_16x16x32_f16 v[80:83], v[200:203], v[176:179], v[80:83]
	v_mfma_f32_16x16x32_f16 v[84:87], v[204:207], v[176:179], v[84:87]
	s_waitcnt lgkmcnt(9)
	v_mfma_f32_16x16x32_f16 v[88:91], v[192:195], v[180:183], v[88:91]
	s_add_u32 m0, s28, 0x1e000
	s_nop 0
	global_load_lds_dwordx4 v12, s[4:5]
	v_mfma_f32_16x16x32_f16 v[92:95], v[196:199], v[180:183], v[92:95]
	v_mfma_f32_16x16x32_f16 v[96:99], v[200:203], v[180:183], v[96:99]
	v_mfma_f32_16x16x32_f16 v[100:103], v[204:207], v[180:183], v[100:103]
	s_waitcnt lgkmcnt(8)
	v_mfma_f32_16x16x32_f16 v[104:107], v[192:195], v[184:187], v[104:107]
	s_add_u32 m0, s28, 0x20000
	s_nop 0
	global_load_lds_dwordx4 v13, s[4:5]
	v_mfma_f32_16x16x32_f16 v[108:111], v[196:199], v[184:187], v[108:111]
	v_mfma_f32_16x16x32_f16 v[112:115], v[200:203], v[184:187], v[112:115]
	v_mfma_f32_16x16x32_f16 v[116:119], v[204:207], v[184:187], v[116:119]
	s_waitcnt lgkmcnt(7)
	ds_read_b128 v[172:175], v16
	ds_read_b128 v[192:195], v18
	ds_read_b128 v[196:199], v18 offset:2048
	ds_read_b128 v[200:203], v18 offset:4096
	ds_read_b128 v[204:207], v18 offset:6144
	ds_read_b128 v[176:179], v16 offset:2048
	ds_read_b128 v[180:183], v16 offset:4096
	ds_read_b128 v[184:187], v16 offset:6144
	s_waitcnt lgkmcnt(14)
	v_mfma_f32_16x16x32_f16 v[56:59], v[156:159], v[136:139], v[56:59]
	s_add_u32 m0, s28, 0x21000
	s_nop 0
	global_load_lds_dwordx4 v8, s[4:5]
	s_add_u32 s4, s4, s20
	s_addc_u32 s5, s5, 0
	s_waitcnt lgkmcnt(13)
	v_mfma_f32_16x16x32_f16 v[60:63], v[160:163], v[136:139], v[60:63]
	s_waitcnt lgkmcnt(12)
	v_mfma_f32_16x16x32_f16 v[64:67], v[164:167], v[136:139], v[64:67]
	s_waitcnt lgkmcnt(11)
	v_mfma_f32_16x16x32_f16 v[68:71], v[168:171], v[136:139], v[68:71]
	s_waitcnt lgkmcnt(10)
	v_mfma_f32_16x16x32_f16 v[72:75], v[156:159], v[140:143], v[72:75]
	v_mfma_f32_16x16x32_f16 v[76:79], v[160:163], v[140:143], v[76:79]
	s_add_u32 m0, s28, 0x23000
	s_nop 0
	global_load_lds_dwordx4 v10, s[6:7]
	v_mfma_f32_16x16x32_f16 v[80:83], v[164:167], v[140:143], v[80:83]
	v_mfma_f32_16x16x32_f16 v[84:87], v[168:171], v[140:143], v[84:87]
	s_waitcnt lgkmcnt(9)
	v_mfma_f32_16x16x32_f16 v[88:91], v[156:159], v[144:147], v[88:91]
	v_mfma_f32_16x16x32_f16 v[92:95], v[160:163], v[144:147], v[92:95]
	v_mfma_f32_16x16x32_f16 v[96:99], v[164:167], v[144:147], v[96:99]
	s_add_u32 m0, s28, 0x25000
	s_nop 0
	global_load_lds_dwordx4 v11, s[6:7]
	s_add_u32 s6, s6, s20
	s_addc_u32 s7, s7, 0
	v_mfma_f32_16x16x32_f16 v[100:103], v[168:171], v[144:147], v[100:103]
	s_waitcnt lgkmcnt(8)
	v_mfma_f32_16x16x32_f16 v[104:107], v[156:159], v[148:151], v[104:107]
	v_mfma_f32_16x16x32_f16 v[108:111], v[160:163], v[148:151], v[108:111]
	v_mfma_f32_16x16x32_f16 v[112:115], v[164:167], v[148:151], v[112:115]
	v_mfma_f32_16x16x32_f16 v[116:119], v[168:171], v[148:151], v[116:119]
	s_waitcnt vmcnt(7) lgkmcnt(0)
	s_barrier
	s_waitcnt lgkmcnt(7)
	ds_read_b128 v[136:139], v15 offset:53248
	ds_read_b128 v[156:159], v17 offset:53248
	ds_read_b128 v[160:163], v17 offset:55296
	ds_read_b128 v[164:167], v17 offset:57344
	ds_read_b128 v[168:171], v17 offset:59392
	ds_read_b128 v[140:143], v15 offset:55296
	ds_read_b128 v[144:147], v15 offset:57344
	ds_read_b128 v[148:151], v15 offset:59392
	s_waitcnt lgkmcnt(14)
	v_mfma_f32_16x16x32_f16 v[56:59], v[192:195], v[172:175], v[56:59]
	s_add_u32 m0, s28, 0x0
	s_nop 0
	global_load_lds_dwordx4 v10, s[4:5]
	s_waitcnt lgkmcnt(13)
	v_mfma_f32_16x16x32_f16 v[60:63], v[196:199], v[172:175], v[60:63]
	s_waitcnt lgkmcnt(12)
	v_mfma_f32_16x16x32_f16 v[64:67], v[200:203], v[172:175], v[64:67]
	s_waitcnt lgkmcnt(11)
	v_mfma_f32_16x16x32_f16 v[68:71], v[204:207], v[172:175], v[68:71]
	s_waitcnt lgkmcnt(10)
	v_mfma_f32_16x16x32_f16 v[72:75], v[192:195], v[176:179], v[72:75]
	s_add_u32 m0, s28, 0x2000
	s_nop 0
	global_load_lds_dwordx4 v11, s[4:5]
	v_mfma_f32_16x16x32_f16 v[76:79], v[196:199], v[176:179], v[76:79]
	v_mfma_f32_16x16x32_f16 v[80:83], v[200:203], v[176:179], v[80:83]
	v_mfma_f32_16x16x32_f16 v[84:87], v[204:207], v[176:179], v[84:87]
	s_waitcnt lgkmcnt(9)
	v_mfma_f32_16x16x32_f16 v[88:91], v[192:195], v[180:183], v[88:91]
	s_add_u32 m0, s28, 0x4000
	s_nop 0
	global_load_lds_dwordx4 v12, s[4:5]
	v_mfma_f32_16x16x32_f16 v[92:95], v[196:199], v[180:183], v[92:95]
	v_mfma_f32_16x16x32_f16 v[96:99], v[200:203], v[180:183], v[96:99]
	v_mfma_f32_16x16x32_f16 v[100:103], v[204:207], v[180:183], v[100:103]
	s_waitcnt lgkmcnt(8)
	v_mfma_f32_16x16x32_f16 v[104:107], v[192:195], v[184:187], v[104:107]
	s_add_u32 m0, s28, 0x6000
	s_nop 0
	global_load_lds_dwordx4 v13, s[4:5]
	v_mfma_f32_16x16x32_f16 v[108:111], v[196:199], v[184:187], v[108:111]
	v_mfma_f32_16x16x32_f16 v[112:115], v[200:203], v[184:187], v[112:115]
	v_mfma_f32_16x16x32_f16 v[116:119], v[204:207], v[184:187], v[116:119]
	s_waitcnt lgkmcnt(7)
	ds_read_b128 v[172:175], v16 offset:53248
	ds_read_b128 v[192:195], v18 offset:53248
	ds_read_b128 v[196:199], v18 offset:55296
	ds_read_b128 v[200:203], v18 offset:57344
	ds_read_b128 v[204:207], v18 offset:59392
	ds_read_b128 v[176:179], v16 offset:55296
	ds_read_b128 v[180:183], v16 offset:57344
	ds_read_b128 v[184:187], v16 offset:59392
	s_waitcnt lgkmcnt(14)
	v_mfma_f32_16x16x32_f16 v[56:59], v[156:159], v[136:139], v[56:59]
	s_add_u32 m0, s28, 0x7000
	s_nop 0
	global_load_lds_dwordx4 v8, s[4:5]
	s_add_u32 s4, s4, s20
	s_addc_u32 s5, s5, 0
	s_waitcnt lgkmcnt(13)
	v_mfma_f32_16x16x32_f16 v[60:63], v[160:163], v[136:139], v[60:63]
	s_waitcnt lgkmcnt(12)
	v_mfma_f32_16x16x32_f16 v[64:67], v[164:167], v[136:139], v[64:67]
	s_waitcnt lgkmcnt(11)
	v_mfma_f32_16x16x32_f16 v[68:71], v[168:171], v[136:139], v[68:71]
	s_waitcnt lgkmcnt(10)
	v_mfma_f32_16x16x32_f16 v[72:75], v[156:159], v[140:143], v[72:75]
	v_mfma_f32_16x16x32_f16 v[76:79], v[160:163], v[140:143], v[76:79]
	s_add_u32 m0, s28, 0x9000
	s_nop 0
	global_load_lds_dwordx4 v10, s[6:7]
	v_mfma_f32_16x16x32_f16 v[80:83], v[164:167], v[140:143], v[80:83]
	v_mfma_f32_16x16x32_f16 v[84:87], v[168:171], v[140:143], v[84:87]
	s_waitcnt lgkmcnt(9)
	v_mfma_f32_16x16x32_f16 v[88:91], v[156:159], v[144:147], v[88:91]
	v_mfma_f32_16x16x32_f16 v[92:95], v[160:163], v[144:147], v[92:95]
	v_mfma_f32_16x16x32_f16 v[96:99], v[164:167], v[144:147], v[96:99]
	s_add_u32 m0, s28, 0xb000
	s_nop 0
	global_load_lds_dwordx4 v11, s[6:7]
	s_add_u32 s6, s6, s20
	s_addc_u32 s7, s7, 0
	v_mfma_f32_16x16x32_f16 v[100:103], v[168:171], v[144:147], v[100:103]
	s_waitcnt lgkmcnt(8)
	v_mfma_f32_16x16x32_f16 v[104:107], v[156:159], v[148:151], v[104:107]
	v_mfma_f32_16x16x32_f16 v[108:111], v[160:163], v[148:151], v[108:111]
	v_mfma_f32_16x16x32_f16 v[112:115], v[164:167], v[148:151], v[112:115]
	v_mfma_f32_16x16x32_f16 v[116:119], v[168:171], v[148:151], v[116:119]
	s_waitcnt vmcnt(7) lgkmcnt(0)
	s_barrier
	s_waitcnt lgkmcnt(7)
	ds_read_b128 v[136:139], v19
	ds_read_b128 v[156:159], v21
	ds_read_b128 v[160:163], v21 offset:2048
	ds_read_b128 v[164:167], v21 offset:4096
	ds_read_b128 v[168:171], v21 offset:6144
	ds_read_b128 v[140:143], v19 offset:2048
	ds_read_b128 v[144:147], v19 offset:4096
	ds_read_b128 v[148:151], v19 offset:6144
	s_waitcnt lgkmcnt(14)
	v_mfma_f32_16x16x32_f16 v[56:59], v[192:195], v[172:175], v[56:59]
	s_add_u32 m0, s28, 0xd000
	s_nop 0
	global_load_lds_dwordx4 v10, s[4:5]
	s_waitcnt lgkmcnt(13)
	v_mfma_f32_16x16x32_f16 v[60:63], v[196:199], v[172:175], v[60:63]
	s_waitcnt lgkmcnt(12)
	v_mfma_f32_16x16x32_f16 v[64:67], v[200:203], v[172:175], v[64:67]
	s_waitcnt lgkmcnt(11)
	v_mfma_f32_16x16x32_f16 v[68:71], v[204:207], v[172:175], v[68:71]
	s_waitcnt lgkmcnt(10)
	v_mfma_f32_16x16x32_f16 v[72:75], v[192:195], v[176:179], v[72:75]
	s_add_u32 m0, s28, 0xf000
	s_nop 0
	global_load_lds_dwordx4 v11, s[4:5]
	v_mfma_f32_16x16x32_f16 v[76:79], v[196:199], v[176:179], v[76:79]
	v_mfma_f32_16x16x32_f16 v[80:83], v[200:203], v[176:179], v[80:83]
	v_mfma_f32_16x16x32_f16 v[84:87], v[204:207], v[176:179], v[84:87]
	s_waitcnt lgkmcnt(9)
	v_mfma_f32_16x16x32_f16 v[88:91], v[192:195], v[180:183], v[88:91]
	s_add_u32 m0, s28, 0x11000
	s_nop 0
	global_load_lds_dwordx4 v12, s[4:5]
	v_mfma_f32_16x16x32_f16 v[92:95], v[196:199], v[180:183], v[92:95]
	v_mfma_f32_16x16x32_f16 v[96:99], v[200:203], v[180:183], v[96:99]
	v_mfma_f32_16x16x32_f16 v[100:103], v[204:207], v[180:183], v[100:103]
	s_waitcnt lgkmcnt(8)
	v_mfma_f32_16x16x32_f16 v[104:107], v[192:195], v[184:187], v[104:107]
	s_add_u32 m0, s28, 0x13000
	s_nop 0
	global_load_lds_dwordx4 v13, s[4:5]
	v_mfma_f32_16x16x32_f16 v[108:111], v[196:199], v[184:187], v[108:111]
	v_mfma_f32_16x16x32_f16 v[112:115], v[200:203], v[184:187], v[112:115]
	v_mfma_f32_16x16x32_f16 v[116:119], v[204:207], v[184:187], v[116:119]
	s_waitcnt lgkmcnt(7)
	ds_read_b128 v[172:175], v20
	ds_read_b128 v[192:195], v22
	ds_read_b128 v[196:199], v22 offset:2048
	ds_read_b128 v[200:203], v22 offset:4096
	ds_read_b128 v[204:207], v22 offset:6144
	ds_read_b128 v[176:179], v20 offset:2048
	ds_read_b128 v[180:183], v20 offset:4096
	ds_read_b128 v[184:187], v20 offset:6144
	s_waitcnt lgkmcnt(14)
	v_mfma_f32_16x16x32_f16 v[56:59], v[156:159], v[136:139], v[56:59]
	s_add_u32 m0, s28, 0x14000
	s_nop 0
	global_load_lds_dwordx4 v8, s[4:5]
	s_add_u32 s4, s4, s20
	s_addc_u32 s5, s5, 0
	s_waitcnt lgkmcnt(13)
	v_mfma_f32_16x16x32_f16 v[60:63], v[160:163], v[136:139], v[60:63]
	s_waitcnt lgkmcnt(12)
	v_mfma_f32_16x16x32_f16 v[64:67], v[164:167], v[136:139], v[64:67]
	s_waitcnt lgkmcnt(11)
	v_mfma_f32_16x16x32_f16 v[68:71], v[168:171], v[136:139], v[68:71]
	s_waitcnt lgkmcnt(10)
	v_mfma_f32_16x16x32_f16 v[72:75], v[156:159], v[140:143], v[72:75]
	v_mfma_f32_16x16x32_f16 v[76:79], v[160:163], v[140:143], v[76:79]
	s_add_u32 m0, s28, 0x16000
	s_nop 0
	global_load_lds_dwordx4 v10, s[6:7]
	v_mfma_f32_16x16x32_f16 v[80:83], v[164:167], v[140:143], v[80:83]
	v_mfma_f32_16x16x32_f16 v[84:87], v[168:171], v[140:143], v[84:87]
	s_waitcnt lgkmcnt(9)
	v_mfma_f32_16x16x32_f16 v[88:91], v[156:159], v[144:147], v[88:91]
	v_mfma_f32_16x16x32_f16 v[92:95], v[160:163], v[144:147], v[92:95]
	v_mfma_f32_16x16x32_f16 v[96:99], v[164:167], v[144:147], v[96:99]
	s_add_u32 m0, s28, 0x18000
	s_nop 0
	global_load_lds_dwordx4 v11, s[6:7]
	s_add_u32 s6, s6, s20
	s_addc_u32 s7, s7, 0
	v_mfma_f32_16x16x32_f16 v[100:103], v[168:171], v[144:147], v[100:103]
	s_waitcnt lgkmcnt(8)
	v_mfma_f32_16x16x32_f16 v[104:107], v[156:159], v[148:151], v[104:107]
	v_mfma_f32_16x16x32_f16 v[108:111], v[160:163], v[148:151], v[108:111]
	v_mfma_f32_16x16x32_f16 v[112:115], v[164:167], v[148:151], v[112:115]
	v_mfma_f32_16x16x32_f16 v[116:119], v[168:171], v[148:151], v[116:119]
	s_waitcnt vmcnt(7) lgkmcnt(0)
	s_barrier
	s_waitcnt lgkmcnt(7)
	ds_read_b128 v[136:139], v15
	ds_read_b128 v[156:159], v17
	ds_read_b128 v[160:163], v17 offset:2048
	ds_read_b128 v[164:167], v17 offset:4096
	ds_read_b128 v[168:171], v17 offset:6144
	ds_read_b128 v[140:143], v15 offset:2048
	ds_read_b128 v[144:147], v15 offset:4096
	ds_read_b128 v[148:151], v15 offset:6144
	s_waitcnt lgkmcnt(14)
	v_mfma_f32_16x16x32_f16 v[56:59], v[192:195], v[172:175], v[56:59]
	s_add_u32 m0, s28, 0x1a000
	s_nop 0
	global_load_lds_dwordx4 v10, s[4:5]
	s_waitcnt lgkmcnt(13)
	v_mfma_f32_16x16x32_f16 v[60:63], v[196:199], v[172:175], v[60:63]
	s_waitcnt lgkmcnt(12)
	v_mfma_f32_16x16x32_f16 v[64:67], v[200:203], v[172:175], v[64:67]
	s_waitcnt lgkmcnt(11)
	v_mfma_f32_16x16x32_f16 v[68:71], v[204:207], v[172:175], v[68:71]
	s_waitcnt lgkmcnt(10)
	v_mfma_f32_16x16x32_f16 v[72:75], v[192:195], v[176:179], v[72:75]
	s_add_u32 m0, s28, 0x1c000
	s_nop 0
	global_load_lds_dwordx4 v11, s[4:5]
	v_mfma_f32_16x16x32_f16 v[76:79], v[196:199], v[176:179], v[76:79]
	v_mfma_f32_16x16x32_f16 v[80:83], v[200:203], v[176:179], v[80:83]
	v_mfma_f32_16x16x32_f16 v[84:87], v[204:207], v[176:179], v[84:87]
	s_waitcnt lgkmcnt(9)
	v_mfma_f32_16x16x32_f16 v[88:91], v[192:195], v[180:183], v[88:91]
	s_add_u32 m0, s28, 0x1e000
	s_nop 0
	global_load_lds_dwordx4 v12, s[4:5]
	v_mfma_f32_16x16x32_f16 v[92:95], v[196:199], v[180:183], v[92:95]
	v_mfma_f32_16x16x32_f16 v[96:99], v[200:203], v[180:183], v[96:99]
	v_mfma_f32_16x16x32_f16 v[100:103], v[204:207], v[180:183], v[100:103]
	s_waitcnt lgkmcnt(8)
	v_mfma_f32_16x16x32_f16 v[104:107], v[192:195], v[184:187], v[104:107]
	s_add_u32 m0, s28, 0x20000
	s_nop 0
	global_load_lds_dwordx4 v13, s[4:5]
	v_mfma_f32_16x16x32_f16 v[108:111], v[196:199], v[184:187], v[108:111]
	v_mfma_f32_16x16x32_f16 v[112:115], v[200:203], v[184:187], v[112:115]
	v_mfma_f32_16x16x32_f16 v[116:119], v[204:207], v[184:187], v[116:119]
	s_waitcnt lgkmcnt(7)
	ds_read_b128 v[172:175], v16
	ds_read_b128 v[192:195], v18
	ds_read_b128 v[196:199], v18 offset:2048
	ds_read_b128 v[200:203], v18 offset:4096
	ds_read_b128 v[204:207], v18 offset:6144
	ds_read_b128 v[176:179], v16 offset:2048
	ds_read_b128 v[180:183], v16 offset:4096
	ds_read_b128 v[184:187], v16 offset:6144
	s_waitcnt lgkmcnt(14)
	v_mfma_f32_16x16x32_f16 v[56:59], v[156:159], v[136:139], v[56:59]
	s_add_u32 m0, s28, 0x21000
	s_nop 0
	global_load_lds_dwordx4 v8, s[4:5]
	s_add_u32 s4, s4, s20
	s_addc_u32 s5, s5, 0
	s_waitcnt lgkmcnt(13)
	v_mfma_f32_16x16x32_f16 v[60:63], v[160:163], v[136:139], v[60:63]
	s_waitcnt lgkmcnt(12)
	v_mfma_f32_16x16x32_f16 v[64:67], v[164:167], v[136:139], v[64:67]
	s_waitcnt lgkmcnt(11)
	v_mfma_f32_16x16x32_f16 v[68:71], v[168:171], v[136:139], v[68:71]
	s_waitcnt lgkmcnt(10)
	v_mfma_f32_16x16x32_f16 v[72:75], v[156:159], v[140:143], v[72:75]
	v_mfma_f32_16x16x32_f16 v[76:79], v[160:163], v[140:143], v[76:79]
	s_add_u32 m0, s28, 0x23000
	s_nop 0
	global_load_lds_dwordx4 v10, s[6:7]
	v_mfma_f32_16x16x32_f16 v[80:83], v[164:167], v[140:143], v[80:83]
	v_mfma_f32_16x16x32_f16 v[84:87], v[168:171], v[140:143], v[84:87]
	s_waitcnt lgkmcnt(9)
	v_mfma_f32_16x16x32_f16 v[88:91], v[156:159], v[144:147], v[88:91]
	v_mfma_f32_16x16x32_f16 v[92:95], v[160:163], v[144:147], v[92:95]
	v_mfma_f32_16x16x32_f16 v[96:99], v[164:167], v[144:147], v[96:99]
	s_add_u32 m0, s28, 0x25000
	s_nop 0
	global_load_lds_dwordx4 v11, s[6:7]
	s_add_u32 s6, s6, s20
	s_addc_u32 s7, s7, 0
	v_mfma_f32_16x16x32_f16 v[100:103], v[168:171], v[144:147], v[100:103]
	s_waitcnt lgkmcnt(8)
	v_mfma_f32_16x16x32_f16 v[104:107], v[156:159], v[148:151], v[104:107]
	v_mfma_f32_16x16x32_f16 v[108:111], v[160:163], v[148:151], v[108:111]
	v_mfma_f32_16x16x32_f16 v[112:115], v[164:167], v[148:151], v[112:115]
	v_mfma_f32_16x16x32_f16 v[116:119], v[168:171], v[148:151], v[116:119]
	s_waitcnt vmcnt(7) lgkmcnt(0)
	s_barrier
	s_waitcnt lgkmcnt(7)
	ds_read_b128 v[136:139], v15 offset:53248
	ds_read_b128 v[156:159], v17 offset:53248
	ds_read_b128 v[160:163], v17 offset:55296
	ds_read_b128 v[164:167], v17 offset:57344
	ds_read_b128 v[168:171], v17 offset:59392
	ds_read_b128 v[140:143], v15 offset:55296
	ds_read_b128 v[144:147], v15 offset:57344
	ds_read_b128 v[148:151], v15 offset:59392
	s_waitcnt lgkmcnt(14)
	v_mfma_f32_16x16x32_f16 v[56:59], v[192:195], v[172:175], v[56:59]
	s_add_u32 m0, s28, 0x0
	s_nop 0
	global_load_lds_dwordx4 v10, s[4:5]
	s_waitcnt lgkmcnt(13)
	v_mfma_f32_16x16x32_f16 v[60:63], v[196:199], v[172:175], v[60:63]
	s_waitcnt lgkmcnt(12)
	v_mfma_f32_16x16x32_f16 v[64:67], v[200:203], v[172:175], v[64:67]
	s_waitcnt lgkmcnt(11)
	v_mfma_f32_16x16x32_f16 v[68:71], v[204:207], v[172:175], v[68:71]
	s_waitcnt lgkmcnt(10)
	v_mfma_f32_16x16x32_f16 v[72:75], v[192:195], v[176:179], v[72:75]
	s_add_u32 m0, s28, 0x2000
	s_nop 0
	global_load_lds_dwordx4 v11, s[4:5]
	v_mfma_f32_16x16x32_f16 v[76:79], v[196:199], v[176:179], v[76:79]
	v_mfma_f32_16x16x32_f16 v[80:83], v[200:203], v[176:179], v[80:83]
	v_mfma_f32_16x16x32_f16 v[84:87], v[204:207], v[176:179], v[84:87]
	s_waitcnt lgkmcnt(9)
	v_mfma_f32_16x16x32_f16 v[88:91], v[192:195], v[180:183], v[88:91]
	s_add_u32 m0, s28, 0x4000
	s_nop 0
	global_load_lds_dwordx4 v12, s[4:5]
	v_mfma_f32_16x16x32_f16 v[92:95], v[196:199], v[180:183], v[92:95]
	v_mfma_f32_16x16x32_f16 v[96:99], v[200:203], v[180:183], v[96:99]
	v_mfma_f32_16x16x32_f16 v[100:103], v[204:207], v[180:183], v[100:103]
	s_waitcnt lgkmcnt(8)
	v_mfma_f32_16x16x32_f16 v[104:107], v[192:195], v[184:187], v[104:107]
	s_add_u32 m0, s28, 0x6000
	s_nop 0
	global_load_lds_dwordx4 v13, s[4:5]
	v_mfma_f32_16x16x32_f16 v[108:111], v[196:199], v[184:187], v[108:111]
	v_mfma_f32_16x16x32_f16 v[112:115], v[200:203], v[184:187], v[112:115]
	v_mfma_f32_16x16x32_f16 v[116:119], v[204:207], v[184:187], v[116:119]
	s_waitcnt lgkmcnt(7)
	ds_read_b128 v[172:175], v16 offset:53248
	ds_read_b128 v[192:195], v18 offset:53248
	ds_read_b128 v[196:199], v18 offset:55296
	ds_read_b128 v[200:203], v18 offset:57344
	ds_read_b128 v[204:207], v18 offset:59392
	ds_read_b128 v[176:179], v16 offset:55296
	ds_read_b128 v[180:183], v16 offset:57344
	ds_read_b128 v[184:187], v16 offset:59392
	s_waitcnt lgkmcnt(14)
	v_mfma_f32_16x16x32_f16 v[56:59], v[156:159], v[136:139], v[56:59]
	s_add_u32 m0, s28, 0x7000
	s_nop 0
	global_load_lds_dwordx4 v8, s[4:5]
	s_add_u32 s4, s4, s20
	s_addc_u32 s5, s5, 0
	s_waitcnt lgkmcnt(13)
	v_mfma_f32_16x16x32_f16 v[60:63], v[160:163], v[136:139], v[60:63]
	s_waitcnt lgkmcnt(12)
	v_mfma_f32_16x16x32_f16 v[64:67], v[164:167], v[136:139], v[64:67]
	s_waitcnt lgkmcnt(11)
	v_mfma_f32_16x16x32_f16 v[68:71], v[168:171], v[136:139], v[68:71]
	s_waitcnt lgkmcnt(10)
	v_mfma_f32_16x16x32_f16 v[72:75], v[156:159], v[140:143], v[72:75]
	v_mfma_f32_16x16x32_f16 v[76:79], v[160:163], v[140:143], v[76:79]
	s_add_u32 m0, s28, 0x9000
	s_nop 0
	global_load_lds_dwordx4 v10, s[6:7]
	v_mfma_f32_16x16x32_f16 v[80:83], v[164:167], v[140:143], v[80:83]
	v_mfma_f32_16x16x32_f16 v[84:87], v[168:171], v[140:143], v[84:87]
	s_waitcnt lgkmcnt(9)
	v_mfma_f32_16x16x32_f16 v[88:91], v[156:159], v[144:147], v[88:91]
	v_mfma_f32_16x16x32_f16 v[92:95], v[160:163], v[144:147], v[92:95]
	v_mfma_f32_16x16x32_f16 v[96:99], v[164:167], v[144:147], v[96:99]
	s_add_u32 m0, s28, 0xb000
	s_nop 0
	global_load_lds_dwordx4 v11, s[6:7]
	s_add_u32 s6, s6, s20
	s_addc_u32 s7, s7, 0
	v_mfma_f32_16x16x32_f16 v[100:103], v[168:171], v[144:147], v[100:103]
	s_waitcnt lgkmcnt(8)
	v_mfma_f32_16x16x32_f16 v[104:107], v[156:159], v[148:151], v[104:107]
	v_mfma_f32_16x16x32_f16 v[108:111], v[160:163], v[148:151], v[108:111]
	v_mfma_f32_16x16x32_f16 v[112:115], v[164:167], v[148:151], v[112:115]
	v_mfma_f32_16x16x32_f16 v[116:119], v[168:171], v[148:151], v[116:119]
	s_waitcnt vmcnt(7) lgkmcnt(0)
	s_barrier
	s_waitcnt lgkmcnt(7)
	ds_read_b128 v[136:139], v19
	ds_read_b128 v[156:159], v21
	ds_read_b128 v[160:163], v21 offset:2048
	ds_read_b128 v[164:167], v21 offset:4096
	ds_read_b128 v[168:171], v21 offset:6144
	ds_read_b128 v[140:143], v19 offset:2048
	ds_read_b128 v[144:147], v19 offset:4096
	ds_read_b128 v[148:151], v19 offset:6144
	s_waitcnt lgkmcnt(14)
	v_mfma_f32_16x16x32_f16 v[56:59], v[192:195], v[172:175], v[56:59]
	s_add_u32 m0, s28, 0xd000
	s_nop 0
	global_load_lds_dwordx4 v10, s[4:5]
	s_waitcnt lgkmcnt(13)
	v_mfma_f32_16x16x32_f16 v[60:63], v[196:199], v[172:175], v[60:63]
	s_waitcnt lgkmcnt(12)
	v_mfma_f32_16x16x32_f16 v[64:67], v[200:203], v[172:175], v[64:67]
	s_waitcnt lgkmcnt(11)
	v_mfma_f32_16x16x32_f16 v[68:71], v[204:207], v[172:175], v[68:71]
	s_waitcnt lgkmcnt(10)
	v_mfma_f32_16x16x32_f16 v[72:75], v[192:195], v[176:179], v[72:75]
	s_add_u32 m0, s28, 0xf000
	s_nop 0
	global_load_lds_dwordx4 v11, s[4:5]
	v_mfma_f32_16x16x32_f16 v[76:79], v[196:199], v[176:179], v[76:79]
	v_mfma_f32_16x16x32_f16 v[80:83], v[200:203], v[176:179], v[80:83]
	v_mfma_f32_16x16x32_f16 v[84:87], v[204:207], v[176:179], v[84:87]
	s_waitcnt lgkmcnt(9)
	v_mfma_f32_16x16x32_f16 v[88:91], v[192:195], v[180:183], v[88:91]
	s_add_u32 m0, s28, 0x11000
	s_nop 0
	global_load_lds_dwordx4 v12, s[4:5]
	v_mfma_f32_16x16x32_f16 v[92:95], v[196:199], v[180:183], v[92:95]
	v_mfma_f32_16x16x32_f16 v[96:99], v[200:203], v[180:183], v[96:99]
	v_mfma_f32_16x16x32_f16 v[100:103], v[204:207], v[180:183], v[100:103]
	s_waitcnt lgkmcnt(8)
	v_mfma_f32_16x16x32_f16 v[104:107], v[192:195], v[184:187], v[104:107]
	s_add_u32 m0, s28, 0x13000
	s_nop 0
	global_load_lds_dwordx4 v13, s[4:5]
	v_mfma_f32_16x16x32_f16 v[108:111], v[196:199], v[184:187], v[108:111]
	v_mfma_f32_16x16x32_f16 v[112:115], v[200:203], v[184:187], v[112:115]
	v_mfma_f32_16x16x32_f16 v[116:119], v[204:207], v[184:187], v[116:119]
	s_waitcnt lgkmcnt(7)
	ds_read_b128 v[172:175], v20
	ds_read_b128 v[192:195], v22
	ds_read_b128 v[196:199], v22 offset:2048
	ds_read_b128 v[200:203], v22 offset:4096
	ds_read_b128 v[204:207], v22 offset:6144
	ds_read_b128 v[176:179], v20 offset:2048
	ds_read_b128 v[180:183], v20 offset:4096
	ds_read_b128 v[184:187], v20 offset:6144
	s_waitcnt lgkmcnt(14)
	v_mfma_f32_16x16x32_f16 v[56:59], v[156:159], v[136:139], v[56:59]
	s_add_u32 m0, s28, 0x14000
	s_nop 0
	global_load_lds_dwordx4 v8, s[4:5]
	s_add_u32 s4, s4, s20
	s_addc_u32 s5, s5, 0
	s_waitcnt lgkmcnt(13)
	v_mfma_f32_16x16x32_f16 v[60:63], v[160:163], v[136:139], v[60:63]
	s_waitcnt lgkmcnt(12)
	v_mfma_f32_16x16x32_f16 v[64:67], v[164:167], v[136:139], v[64:67]
	s_waitcnt lgkmcnt(11)
	v_mfma_f32_16x16x32_f16 v[68:71], v[168:171], v[136:139], v[68:71]
	s_waitcnt lgkmcnt(10)
	v_mfma_f32_16x16x32_f16 v[72:75], v[156:159], v[140:143], v[72:75]
	v_mfma_f32_16x16x32_f16 v[76:79], v[160:163], v[140:143], v[76:79]
	s_add_u32 m0, s28, 0x16000
	s_nop 0
	global_load_lds_dwordx4 v10, s[6:7]
	v_mfma_f32_16x16x32_f16 v[80:83], v[164:167], v[140:143], v[80:83]
	v_mfma_f32_16x16x32_f16 v[84:87], v[168:171], v[140:143], v[84:87]
	s_waitcnt lgkmcnt(9)
	v_mfma_f32_16x16x32_f16 v[88:91], v[156:159], v[144:147], v[88:91]
	v_mfma_f32_16x16x32_f16 v[92:95], v[160:163], v[144:147], v[92:95]
	v_mfma_f32_16x16x32_f16 v[96:99], v[164:167], v[144:147], v[96:99]
	s_add_u32 m0, s28, 0x18000
	s_nop 0
	global_load_lds_dwordx4 v11, s[6:7]
	s_add_u32 s6, s6, s20
	s_addc_u32 s7, s7, 0
	v_mfma_f32_16x16x32_f16 v[100:103], v[168:171], v[144:147], v[100:103]
	s_waitcnt lgkmcnt(8)
	v_mfma_f32_16x16x32_f16 v[104:107], v[156:159], v[148:151], v[104:107]
	v_mfma_f32_16x16x32_f16 v[108:111], v[160:163], v[148:151], v[108:111]
	v_mfma_f32_16x16x32_f16 v[112:115], v[164:167], v[148:151], v[112:115]
	v_mfma_f32_16x16x32_f16 v[116:119], v[168:171], v[148:151], v[116:119]
	s_waitcnt vmcnt(7) lgkmcnt(0)
	s_barrier
	s_waitcnt lgkmcnt(7)
	ds_read_b128 v[136:139], v15
	ds_read_b128 v[156:159], v17
	ds_read_b128 v[160:163], v17 offset:2048
	ds_read_b128 v[164:167], v17 offset:4096
	ds_read_b128 v[168:171], v17 offset:6144
	ds_read_b128 v[140:143], v15 offset:2048
	ds_read_b128 v[144:147], v15 offset:4096
	ds_read_b128 v[148:151], v15 offset:6144
	s_waitcnt lgkmcnt(14)
	v_mfma_f32_16x16x32_f16 v[56:59], v[192:195], v[172:175], v[56:59]
	s_add_u32 m0, s28, 0x1a000
	s_nop 0
	global_load_lds_dwordx4 v10, s[4:5]
	s_waitcnt lgkmcnt(13)
	v_mfma_f32_16x16x32_f16 v[60:63], v[196:199], v[172:175], v[60:63]
	s_waitcnt lgkmcnt(12)
	v_mfma_f32_16x16x32_f16 v[64:67], v[200:203], v[172:175], v[64:67]
	s_waitcnt lgkmcnt(11)
	v_mfma_f32_16x16x32_f16 v[68:71], v[204:207], v[172:175], v[68:71]
	s_waitcnt lgkmcnt(10)
	v_mfma_f32_16x16x32_f16 v[72:75], v[192:195], v[176:179], v[72:75]
	s_add_u32 m0, s28, 0x1c000
	s_nop 0
	global_load_lds_dwordx4 v11, s[4:5]
	v_mfma_f32_16x16x32_f16 v[76:79], v[196:199], v[176:179], v[76:79]
	v_mfma_f32_16x16x32_f16 v[80:83], v[200:203], v[176:179], v[80:83]
	v_mfma_f32_16x16x32_f16 v[84:87], v[204:207], v[176:179], v[84:87]
	s_waitcnt lgkmcnt(9)
	v_mfma_f32_16x16x32_f16 v[88:91], v[192:195], v[180:183], v[88:91]
	s_add_u32 m0, s28, 0x1e000
	s_nop 0
	global_load_lds_dwordx4 v12, s[4:5]
	v_mfma_f32_16x16x32_f16 v[92:95], v[196:199], v[180:183], v[92:95]
	v_mfma_f32_16x16x32_f16 v[96:99], v[200:203], v[180:183], v[96:99]
	v_mfma_f32_16x16x32_f16 v[100:103], v[204:207], v[180:183], v[100:103]
	s_waitcnt lgkmcnt(8)
	v_mfma_f32_16x16x32_f16 v[104:107], v[192:195], v[184:187], v[104:107]
	s_add_u32 m0, s28, 0x20000
	s_nop 0
	global_load_lds_dwordx4 v13, s[4:5]
	v_mfma_f32_16x16x32_f16 v[108:111], v[196:199], v[184:187], v[108:111]
	v_mfma_f32_16x16x32_f16 v[112:115], v[200:203], v[184:187], v[112:115]
	v_mfma_f32_16x16x32_f16 v[116:119], v[204:207], v[184:187], v[116:119]
	s_waitcnt lgkmcnt(7)
	ds_read_b128 v[172:175], v16
	ds_read_b128 v[192:195], v18
	ds_read_b128 v[196:199], v18 offset:2048
	ds_read_b128 v[200:203], v18 offset:4096
	ds_read_b128 v[204:207], v18 offset:6144
	ds_read_b128 v[176:179], v16 offset:2048
	ds_read_b128 v[180:183], v16 offset:4096
	ds_read_b128 v[184:187], v16 offset:6144
	s_waitcnt lgkmcnt(14)
	v_mfma_f32_16x16x32_f16 v[56:59], v[156:159], v[136:139], v[56:59]
	s_add_u32 m0, s28, 0x21000
	s_nop 0
	global_load_lds_dwordx4 v8, s[4:5]
	s_add_u32 s4, s4, s20
	s_addc_u32 s5, s5, 0
	s_waitcnt lgkmcnt(13)
	v_mfma_f32_16x16x32_f16 v[60:63], v[160:163], v[136:139], v[60:63]
	s_waitcnt lgkmcnt(12)
	v_mfma_f32_16x16x32_f16 v[64:67], v[164:167], v[136:139], v[64:67]
	s_waitcnt lgkmcnt(11)
	v_mfma_f32_16x16x32_f16 v[68:71], v[168:171], v[136:139], v[68:71]
	s_waitcnt lgkmcnt(10)
	v_mfma_f32_16x16x32_f16 v[72:75], v[156:159], v[140:143], v[72:75]
	v_mfma_f32_16x16x32_f16 v[76:79], v[160:163], v[140:143], v[76:79]
	s_add_u32 m0, s28, 0x23000
	s_nop 0
	global_load_lds_dwordx4 v10, s[6:7]
	v_mfma_f32_16x16x32_f16 v[80:83], v[164:167], v[140:143], v[80:83]
	v_mfma_f32_16x16x32_f16 v[84:87], v[168:171], v[140:143], v[84:87]
	s_waitcnt lgkmcnt(9)
	v_mfma_f32_16x16x32_f16 v[88:91], v[156:159], v[144:147], v[88:91]
	v_mfma_f32_16x16x32_f16 v[92:95], v[160:163], v[144:147], v[92:95]
	v_mfma_f32_16x16x32_f16 v[96:99], v[164:167], v[144:147], v[96:99]
	s_add_u32 m0, s28, 0x25000
	s_nop 0
	global_load_lds_dwordx4 v11, s[6:7]
	s_add_u32 s6, s6, s20
	s_addc_u32 s7, s7, 0
	v_mfma_f32_16x16x32_f16 v[100:103], v[168:171], v[144:147], v[100:103]
	s_waitcnt lgkmcnt(8)
	v_mfma_f32_16x16x32_f16 v[104:107], v[156:159], v[148:151], v[104:107]
	v_mfma_f32_16x16x32_f16 v[108:111], v[160:163], v[148:151], v[108:111]
	v_mfma_f32_16x16x32_f16 v[112:115], v[164:167], v[148:151], v[112:115]
	v_mfma_f32_16x16x32_f16 v[116:119], v[168:171], v[148:151], v[116:119]
	s_waitcnt vmcnt(7) lgkmcnt(0)
	s_barrier
	s_waitcnt lgkmcnt(7)
	ds_read_b128 v[136:139], v15 offset:53248
	ds_read_b128 v[156:159], v17 offset:53248
	ds_read_b128 v[160:163], v17 offset:55296
	ds_read_b128 v[164:167], v17 offset:57344
	ds_read_b128 v[168:171], v17 offset:59392
	ds_read_b128 v[140:143], v15 offset:55296
	ds_read_b128 v[144:147], v15 offset:57344
	ds_read_b128 v[148:151], v15 offset:59392
	s_waitcnt lgkmcnt(14)
	v_mfma_f32_16x16x32_f16 v[56:59], v[192:195], v[172:175], v[56:59]
	s_add_u32 m0, s28, 0x0
	s_nop 0
	global_load_lds_dwordx4 v10, s[4:5]
	s_waitcnt lgkmcnt(13)
	v_mfma_f32_16x16x32_f16 v[60:63], v[196:199], v[172:175], v[60:63]
	s_waitcnt lgkmcnt(12)
	v_mfma_f32_16x16x32_f16 v[64:67], v[200:203], v[172:175], v[64:67]
	s_waitcnt lgkmcnt(11)
	v_mfma_f32_16x16x32_f16 v[68:71], v[204:207], v[172:175], v[68:71]
	s_waitcnt lgkmcnt(10)
	v_mfma_f32_16x16x32_f16 v[72:75], v[192:195], v[176:179], v[72:75]
	s_add_u32 m0, s28, 0x2000
	s_nop 0
	global_load_lds_dwordx4 v11, s[4:5]
	v_mfma_f32_16x16x32_f16 v[76:79], v[196:199], v[176:179], v[76:79]
	v_mfma_f32_16x16x32_f16 v[80:83], v[200:203], v[176:179], v[80:83]
	v_mfma_f32_16x16x32_f16 v[84:87], v[204:207], v[176:179], v[84:87]
	s_waitcnt lgkmcnt(9)
	v_mfma_f32_16x16x32_f16 v[88:91], v[192:195], v[180:183], v[88:91]
	s_add_u32 m0, s28, 0x4000
	s_nop 0
	global_load_lds_dwordx4 v12, s[4:5]
	v_mfma_f32_16x16x32_f16 v[92:95], v[196:199], v[180:183], v[92:95]
	v_mfma_f32_16x16x32_f16 v[96:99], v[200:203], v[180:183], v[96:99]
	v_mfma_f32_16x16x32_f16 v[100:103], v[204:207], v[180:183], v[100:103]
	s_waitcnt lgkmcnt(8)
	v_mfma_f32_16x16x32_f16 v[104:107], v[192:195], v[184:187], v[104:107]
	s_add_u32 m0, s28, 0x6000
	s_nop 0
	global_load_lds_dwordx4 v13, s[4:5]
	v_mfma_f32_16x16x32_f16 v[108:111], v[196:199], v[184:187], v[108:111]
	v_mfma_f32_16x16x32_f16 v[112:115], v[200:203], v[184:187], v[112:115]
	v_mfma_f32_16x16x32_f16 v[116:119], v[204:207], v[184:187], v[116:119]
	s_waitcnt lgkmcnt(7)
	ds_read_b128 v[172:175], v16 offset:53248
	ds_read_b128 v[192:195], v18 offset:53248
	ds_read_b128 v[196:199], v18 offset:55296
	ds_read_b128 v[200:203], v18 offset:57344
	ds_read_b128 v[204:207], v18 offset:59392
	ds_read_b128 v[176:179], v16 offset:55296
	ds_read_b128 v[180:183], v16 offset:57344
	ds_read_b128 v[184:187], v16 offset:59392
	s_waitcnt lgkmcnt(14)
	v_mfma_f32_16x16x32_f16 v[56:59], v[156:159], v[136:139], v[56:59]
	s_add_u32 m0, s28, 0x7000
	s_nop 0
	global_load_lds_dwordx4 v8, s[4:5]
	s_add_u32 s4, s4, s20
	s_addc_u32 s5, s5, 0
	s_waitcnt lgkmcnt(13)
	v_mfma_f32_16x16x32_f16 v[60:63], v[160:163], v[136:139], v[60:63]
	s_waitcnt lgkmcnt(12)
	v_mfma_f32_16x16x32_f16 v[64:67], v[164:167], v[136:139], v[64:67]
	s_waitcnt lgkmcnt(11)
	v_mfma_f32_16x16x32_f16 v[68:71], v[168:171], v[136:139], v[68:71]
	s_waitcnt lgkmcnt(10)
	v_mfma_f32_16x16x32_f16 v[72:75], v[156:159], v[140:143], v[72:75]
	v_mfma_f32_16x16x32_f16 v[76:79], v[160:163], v[140:143], v[76:79]
	s_add_u32 m0, s28, 0x9000
	s_nop 0
	global_load_lds_dwordx4 v10, s[6:7]
	v_mfma_f32_16x16x32_f16 v[80:83], v[164:167], v[140:143], v[80:83]
	v_mfma_f32_16x16x32_f16 v[84:87], v[168:171], v[140:143], v[84:87]
	s_waitcnt lgkmcnt(9)
	v_mfma_f32_16x16x32_f16 v[88:91], v[156:159], v[144:147], v[88:91]
	v_mfma_f32_16x16x32_f16 v[92:95], v[160:163], v[144:147], v[92:95]
	v_mfma_f32_16x16x32_f16 v[96:99], v[164:167], v[144:147], v[96:99]
	s_add_u32 m0, s28, 0xb000
	s_nop 0
	global_load_lds_dwordx4 v11, s[6:7]
	s_add_u32 s6, s6, s20
	s_addc_u32 s7, s7, 0
	v_mfma_f32_16x16x32_f16 v[100:103], v[168:171], v[144:147], v[100:103]
	s_waitcnt lgkmcnt(8)
	v_mfma_f32_16x16x32_f16 v[104:107], v[156:159], v[148:151], v[104:107]
	v_mfma_f32_16x16x32_f16 v[108:111], v[160:163], v[148:151], v[108:111]
	v_mfma_f32_16x16x32_f16 v[112:115], v[164:167], v[148:151], v[112:115]
	v_mfma_f32_16x16x32_f16 v[116:119], v[168:171], v[148:151], v[116:119]
	s_waitcnt vmcnt(7) lgkmcnt(0)
	s_barrier
	s_waitcnt lgkmcnt(7)
	ds_read_b128 v[136:139], v19
	ds_read_b128 v[156:159], v21
	ds_read_b128 v[160:163], v21 offset:2048
	ds_read_b128 v[164:167], v21 offset:4096
	ds_read_b128 v[168:171], v21 offset:6144
	ds_read_b128 v[140:143], v19 offset:2048
	ds_read_b128 v[144:147], v19 offset:4096
	ds_read_b128 v[148:151], v19 offset:6144
	s_waitcnt lgkmcnt(14)
	v_mfma_f32_16x16x32_f16 v[56:59], v[192:195], v[172:175], v[56:59]
	s_add_u32 m0, s28, 0xd000
	s_nop 0
	global_load_lds_dwordx4 v10, s[4:5]
	s_waitcnt lgkmcnt(13)
	v_mfma_f32_16x16x32_f16 v[60:63], v[196:199], v[172:175], v[60:63]
	s_waitcnt lgkmcnt(12)
	v_mfma_f32_16x16x32_f16 v[64:67], v[200:203], v[172:175], v[64:67]
	s_waitcnt lgkmcnt(11)
	v_mfma_f32_16x16x32_f16 v[68:71], v[204:207], v[172:175], v[68:71]
	s_waitcnt lgkmcnt(10)
	v_mfma_f32_16x16x32_f16 v[72:75], v[192:195], v[176:179], v[72:75]
	s_add_u32 m0, s28, 0xf000
	s_nop 0
	global_load_lds_dwordx4 v11, s[4:5]
	v_mfma_f32_16x16x32_f16 v[76:79], v[196:199], v[176:179], v[76:79]
	v_mfma_f32_16x16x32_f16 v[80:83], v[200:203], v[176:179], v[80:83]
	v_mfma_f32_16x16x32_f16 v[84:87], v[204:207], v[176:179], v[84:87]
	s_waitcnt lgkmcnt(9)
	v_mfma_f32_16x16x32_f16 v[88:91], v[192:195], v[180:183], v[88:91]
	s_add_u32 m0, s28, 0x11000
	s_nop 0
	global_load_lds_dwordx4 v12, s[4:5]
	v_mfma_f32_16x16x32_f16 v[92:95], v[196:199], v[180:183], v[92:95]
	v_mfma_f32_16x16x32_f16 v[96:99], v[200:203], v[180:183], v[96:99]
	v_mfma_f32_16x16x32_f16 v[100:103], v[204:207], v[180:183], v[100:103]
	s_waitcnt lgkmcnt(8)
	v_mfma_f32_16x16x32_f16 v[104:107], v[192:195], v[184:187], v[104:107]
	s_add_u32 m0, s28, 0x13000
	s_nop 0
	global_load_lds_dwordx4 v13, s[4:5]
	v_mfma_f32_16x16x32_f16 v[108:111], v[196:199], v[184:187], v[108:111]
	v_mfma_f32_16x16x32_f16 v[112:115], v[200:203], v[184:187], v[112:115]
	v_mfma_f32_16x16x32_f16 v[116:119], v[204:207], v[184:187], v[116:119]
	s_waitcnt lgkmcnt(7)
	ds_read_b128 v[172:175], v20
	ds_read_b128 v[192:195], v22
	ds_read_b128 v[196:199], v22 offset:2048
	ds_read_b128 v[200:203], v22 offset:4096
	ds_read_b128 v[204:207], v22 offset:6144
	ds_read_b128 v[176:179], v20 offset:2048
	ds_read_b128 v[180:183], v20 offset:4096
	ds_read_b128 v[184:187], v20 offset:6144
	s_waitcnt lgkmcnt(14)
	v_mfma_f32_16x16x32_f16 v[56:59], v[156:159], v[136:139], v[56:59]
	s_add_u32 m0, s28, 0x14000
	s_nop 0
	global_load_lds_dwordx4 v8, s[4:5]
	s_add_u32 s4, s4, s20
	s_addc_u32 s5, s5, 0
	s_waitcnt lgkmcnt(13)
	v_mfma_f32_16x16x32_f16 v[60:63], v[160:163], v[136:139], v[60:63]
	s_waitcnt lgkmcnt(12)
	v_mfma_f32_16x16x32_f16 v[64:67], v[164:167], v[136:139], v[64:67]
	s_waitcnt lgkmcnt(11)
	v_mfma_f32_16x16x32_f16 v[68:71], v[168:171], v[136:139], v[68:71]
	s_waitcnt lgkmcnt(10)
	v_mfma_f32_16x16x32_f16 v[72:75], v[156:159], v[140:143], v[72:75]
	v_mfma_f32_16x16x32_f16 v[76:79], v[160:163], v[140:143], v[76:79]
	s_add_u32 m0, s28, 0x16000
	s_nop 0
	global_load_lds_dwordx4 v10, s[6:7]
	v_mfma_f32_16x16x32_f16 v[80:83], v[164:167], v[140:143], v[80:83]
	v_mfma_f32_16x16x32_f16 v[84:87], v[168:171], v[140:143], v[84:87]
	s_waitcnt lgkmcnt(9)
	v_mfma_f32_16x16x32_f16 v[88:91], v[156:159], v[144:147], v[88:91]
	v_mfma_f32_16x16x32_f16 v[92:95], v[160:163], v[144:147], v[92:95]
	v_mfma_f32_16x16x32_f16 v[96:99], v[164:167], v[144:147], v[96:99]
	s_add_u32 m0, s28, 0x18000
	s_nop 0
	global_load_lds_dwordx4 v11, s[6:7]
	s_add_u32 s6, s6, s20
	s_addc_u32 s7, s7, 0
	v_mfma_f32_16x16x32_f16 v[100:103], v[168:171], v[144:147], v[100:103]
	s_waitcnt lgkmcnt(8)
	v_mfma_f32_16x16x32_f16 v[104:107], v[156:159], v[148:151], v[104:107]
	v_mfma_f32_16x16x32_f16 v[108:111], v[160:163], v[148:151], v[108:111]
	v_mfma_f32_16x16x32_f16 v[112:115], v[164:167], v[148:151], v[112:115]
	v_mfma_f32_16x16x32_f16 v[116:119], v[168:171], v[148:151], v[116:119]
	s_waitcnt vmcnt(7) lgkmcnt(0)
	s_barrier
	s_waitcnt lgkmcnt(7)
	ds_read_b128 v[136:139], v15
	ds_read_b128 v[156:159], v17
	ds_read_b128 v[160:163], v17 offset:2048
	ds_read_b128 v[164:167], v17 offset:4096
	ds_read_b128 v[168:171], v17 offset:6144
	ds_read_b128 v[140:143], v15 offset:2048
	ds_read_b128 v[144:147], v15 offset:4096
	ds_read_b128 v[148:151], v15 offset:6144
	s_waitcnt lgkmcnt(14)
	v_mfma_f32_16x16x32_f16 v[56:59], v[192:195], v[172:175], v[56:59]
	s_add_u32 m0, s28, 0x1a000
	s_nop 0
	global_load_lds_dwordx4 v10, s[4:5]
	s_waitcnt lgkmcnt(13)
	v_mfma_f32_16x16x32_f16 v[60:63], v[196:199], v[172:175], v[60:63]
	s_waitcnt lgkmcnt(12)
	v_mfma_f32_16x16x32_f16 v[64:67], v[200:203], v[172:175], v[64:67]
	s_waitcnt lgkmcnt(11)
	v_mfma_f32_16x16x32_f16 v[68:71], v[204:207], v[172:175], v[68:71]
	s_waitcnt lgkmcnt(10)
	v_mfma_f32_16x16x32_f16 v[72:75], v[192:195], v[176:179], v[72:75]
	s_add_u32 m0, s28, 0x1c000
	s_nop 0
	global_load_lds_dwordx4 v11, s[4:5]
	v_mfma_f32_16x16x32_f16 v[76:79], v[196:199], v[176:179], v[76:79]
	v_mfma_f32_16x16x32_f16 v[80:83], v[200:203], v[176:179], v[80:83]
	v_mfma_f32_16x16x32_f16 v[84:87], v[204:207], v[176:179], v[84:87]
	s_waitcnt lgkmcnt(9)
	v_mfma_f32_16x16x32_f16 v[88:91], v[192:195], v[180:183], v[88:91]
	s_add_u32 m0, s28, 0x1e000
	s_nop 0
	global_load_lds_dwordx4 v12, s[4:5]
	v_mfma_f32_16x16x32_f16 v[92:95], v[196:199], v[180:183], v[92:95]
	v_mfma_f32_16x16x32_f16 v[96:99], v[200:203], v[180:183], v[96:99]
	v_mfma_f32_16x16x32_f16 v[100:103], v[204:207], v[180:183], v[100:103]
	s_waitcnt lgkmcnt(8)
	v_mfma_f32_16x16x32_f16 v[104:107], v[192:195], v[184:187], v[104:107]
	s_add_u32 m0, s28, 0x20000
	s_nop 0
	global_load_lds_dwordx4 v13, s[4:5]
	v_mfma_f32_16x16x32_f16 v[108:111], v[196:199], v[184:187], v[108:111]
	v_mfma_f32_16x16x32_f16 v[112:115], v[200:203], v[184:187], v[112:115]
	v_mfma_f32_16x16x32_f16 v[116:119], v[204:207], v[184:187], v[116:119]
	s_waitcnt lgkmcnt(7)
	ds_read_b128 v[172:175], v16
	ds_read_b128 v[192:195], v18
	ds_read_b128 v[196:199], v18 offset:2048
	ds_read_b128 v[200:203], v18 offset:4096
	ds_read_b128 v[204:207], v18 offset:6144
	ds_read_b128 v[176:179], v16 offset:2048
	ds_read_b128 v[180:183], v16 offset:4096
	ds_read_b128 v[184:187], v16 offset:6144
	s_waitcnt lgkmcnt(14)
	v_mfma_f32_16x16x32_f16 v[56:59], v[156:159], v[136:139], v[56:59]
	s_add_u32 m0, s28, 0x21000
	s_nop 0
	global_load_lds_dwordx4 v8, s[4:5]
	s_add_u32 s4, s4, s20
	s_addc_u32 s5, s5, 0
	s_waitcnt lgkmcnt(13)
	v_mfma_f32_16x16x32_f16 v[60:63], v[160:163], v[136:139], v[60:63]
	s_waitcnt lgkmcnt(12)
	v_mfma_f32_16x16x32_f16 v[64:67], v[164:167], v[136:139], v[64:67]
	s_waitcnt lgkmcnt(11)
	v_mfma_f32_16x16x32_f16 v[68:71], v[168:171], v[136:139], v[68:71]
	s_waitcnt lgkmcnt(10)
	v_mfma_f32_16x16x32_f16 v[72:75], v[156:159], v[140:143], v[72:75]
	v_mfma_f32_16x16x32_f16 v[76:79], v[160:163], v[140:143], v[76:79]
	s_add_u32 m0, s28, 0x23000
	s_nop 0
	global_load_lds_dwordx4 v10, s[6:7]
	v_mfma_f32_16x16x32_f16 v[80:83], v[164:167], v[140:143], v[80:83]
	v_mfma_f32_16x16x32_f16 v[84:87], v[168:171], v[140:143], v[84:87]
	s_waitcnt lgkmcnt(9)
	v_mfma_f32_16x16x32_f16 v[88:91], v[156:159], v[144:147], v[88:91]
	v_mfma_f32_16x16x32_f16 v[92:95], v[160:163], v[144:147], v[92:95]
	v_mfma_f32_16x16x32_f16 v[96:99], v[164:167], v[144:147], v[96:99]
	s_add_u32 m0, s28, 0x25000
	s_nop 0
	global_load_lds_dwordx4 v11, s[6:7]
	s_add_u32 s6, s6, s20
	s_addc_u32 s7, s7, 0
	v_mfma_f32_16x16x32_f16 v[100:103], v[168:171], v[144:147], v[100:103]
	s_waitcnt lgkmcnt(8)
	v_mfma_f32_16x16x32_f16 v[104:107], v[156:159], v[148:151], v[104:107]
	v_mfma_f32_16x16x32_f16 v[108:111], v[160:163], v[148:151], v[108:111]
	v_mfma_f32_16x16x32_f16 v[112:115], v[164:167], v[148:151], v[112:115]
	v_mfma_f32_16x16x32_f16 v[116:119], v[168:171], v[148:151], v[116:119]
	s_waitcnt vmcnt(7) lgkmcnt(0)
	s_barrier
	s_waitcnt lgkmcnt(7)
	ds_read_b128 v[136:139], v15 offset:53248
	ds_read_b128 v[156:159], v17 offset:53248
	ds_read_b128 v[160:163], v17 offset:55296
	ds_read_b128 v[164:167], v17 offset:57344
	ds_read_b128 v[168:171], v17 offset:59392
	ds_read_b128 v[140:143], v15 offset:55296
	ds_read_b128 v[144:147], v15 offset:57344
	ds_read_b128 v[148:151], v15 offset:59392
	s_waitcnt lgkmcnt(14)
	v_mfma_f32_16x16x32_f16 v[56:59], v[192:195], v[172:175], v[56:59]
	s_add_u32 m0, s28, 0x0
	s_nop 0
	global_load_lds_dwordx4 v10, s[4:5]
	s_waitcnt lgkmcnt(13)
	v_mfma_f32_16x16x32_f16 v[60:63], v[196:199], v[172:175], v[60:63]
	s_waitcnt lgkmcnt(12)
	v_mfma_f32_16x16x32_f16 v[64:67], v[200:203], v[172:175], v[64:67]
	s_waitcnt lgkmcnt(11)
	v_mfma_f32_16x16x32_f16 v[68:71], v[204:207], v[172:175], v[68:71]
	s_waitcnt lgkmcnt(10)
	v_mfma_f32_16x16x32_f16 v[72:75], v[192:195], v[176:179], v[72:75]
	s_add_u32 m0, s28, 0x2000
	s_nop 0
	global_load_lds_dwordx4 v11, s[4:5]
	v_mfma_f32_16x16x32_f16 v[76:79], v[196:199], v[176:179], v[76:79]
	v_mfma_f32_16x16x32_f16 v[80:83], v[200:203], v[176:179], v[80:83]
	v_mfma_f32_16x16x32_f16 v[84:87], v[204:207], v[176:179], v[84:87]
	s_waitcnt lgkmcnt(9)
	v_mfma_f32_16x16x32_f16 v[88:91], v[192:195], v[180:183], v[88:91]
	s_add_u32 m0, s28, 0x4000
	s_nop 0
	global_load_lds_dwordx4 v12, s[4:5]
	v_mfma_f32_16x16x32_f16 v[92:95], v[196:199], v[180:183], v[92:95]
	v_mfma_f32_16x16x32_f16 v[96:99], v[200:203], v[180:183], v[96:99]
	v_mfma_f32_16x16x32_f16 v[100:103], v[204:207], v[180:183], v[100:103]
	s_waitcnt lgkmcnt(8)
	v_mfma_f32_16x16x32_f16 v[104:107], v[192:195], v[184:187], v[104:107]
	s_add_u32 m0, s28, 0x6000
	s_nop 0
	global_load_lds_dwordx4 v13, s[4:5]
	v_mfma_f32_16x16x32_f16 v[108:111], v[196:199], v[184:187], v[108:111]
	v_mfma_f32_16x16x32_f16 v[112:115], v[200:203], v[184:187], v[112:115]
	v_mfma_f32_16x16x32_f16 v[116:119], v[204:207], v[184:187], v[116:119]
	s_waitcnt lgkmcnt(7)
	ds_read_b128 v[172:175], v16 offset:53248
	ds_read_b128 v[192:195], v18 offset:53248
	ds_read_b128 v[196:199], v18 offset:55296
	ds_read_b128 v[200:203], v18 offset:57344
	ds_read_b128 v[204:207], v18 offset:59392
	ds_read_b128 v[176:179], v16 offset:55296
	ds_read_b128 v[180:183], v16 offset:57344
	ds_read_b128 v[184:187], v16 offset:59392
	s_waitcnt lgkmcnt(14)
	v_mfma_f32_16x16x32_f16 v[56:59], v[156:159], v[136:139], v[56:59]
	s_add_u32 m0, s28, 0x7000
	s_nop 0
	global_load_lds_dwordx4 v8, s[4:5]
	s_add_u32 s4, s4, s20
	s_addc_u32 s5, s5, 0
	s_waitcnt lgkmcnt(13)
	v_mfma_f32_16x16x32_f16 v[60:63], v[160:163], v[136:139], v[60:63]
	s_waitcnt lgkmcnt(12)
	v_mfma_f32_16x16x32_f16 v[64:67], v[164:167], v[136:139], v[64:67]
	s_waitcnt lgkmcnt(11)
	v_mfma_f32_16x16x32_f16 v[68:71], v[168:171], v[136:139], v[68:71]
	s_waitcnt lgkmcnt(10)
	v_mfma_f32_16x16x32_f16 v[72:75], v[156:159], v[140:143], v[72:75]
	v_mfma_f32_16x16x32_f16 v[76:79], v[160:163], v[140:143], v[76:79]
	s_add_u32 m0, s28, 0x9000
	s_nop 0
	global_load_lds_dwordx4 v10, s[6:7]
	v_mfma_f32_16x16x32_f16 v[80:83], v[164:167], v[140:143], v[80:83]
	v_mfma_f32_16x16x32_f16 v[84:87], v[168:171], v[140:143], v[84:87]
	s_waitcnt lgkmcnt(9)
	v_mfma_f32_16x16x32_f16 v[88:91], v[156:159], v[144:147], v[88:91]
	v_mfma_f32_16x16x32_f16 v[92:95], v[160:163], v[144:147], v[92:95]
	v_mfma_f32_16x16x32_f16 v[96:99], v[164:167], v[144:147], v[96:99]
	s_add_u32 m0, s28, 0xb000
	s_nop 0
	global_load_lds_dwordx4 v11, s[6:7]
	s_add_u32 s6, s6, s20
	s_addc_u32 s7, s7, 0
	v_mfma_f32_16x16x32_f16 v[100:103], v[168:171], v[144:147], v[100:103]
	s_waitcnt lgkmcnt(8)
	v_mfma_f32_16x16x32_f16 v[104:107], v[156:159], v[148:151], v[104:107]
	v_mfma_f32_16x16x32_f16 v[108:111], v[160:163], v[148:151], v[108:111]
	v_mfma_f32_16x16x32_f16 v[112:115], v[164:167], v[148:151], v[112:115]
	v_mfma_f32_16x16x32_f16 v[116:119], v[168:171], v[148:151], v[116:119]
	s_waitcnt vmcnt(7) lgkmcnt(0)
	s_barrier
	s_waitcnt lgkmcnt(7)
	ds_read_b128 v[136:139], v19
	ds_read_b128 v[156:159], v21
	ds_read_b128 v[160:163], v21 offset:2048
	ds_read_b128 v[164:167], v21 offset:4096
	ds_read_b128 v[168:171], v21 offset:6144
	ds_read_b128 v[140:143], v19 offset:2048
	ds_read_b128 v[144:147], v19 offset:4096
	ds_read_b128 v[148:151], v19 offset:6144
	s_waitcnt lgkmcnt(14)
	v_mfma_f32_16x16x32_f16 v[56:59], v[192:195], v[172:175], v[56:59]
	s_waitcnt lgkmcnt(13)
	v_mfma_f32_16x16x32_f16 v[60:63], v[196:199], v[172:175], v[60:63]
	s_waitcnt lgkmcnt(12)
	v_mfma_f32_16x16x32_f16 v[64:67], v[200:203], v[172:175], v[64:67]
	s_waitcnt lgkmcnt(11)
	v_mfma_f32_16x16x32_f16 v[68:71], v[204:207], v[172:175], v[68:71]
	s_waitcnt lgkmcnt(10)
	v_mfma_f32_16x16x32_f16 v[72:75], v[192:195], v[176:179], v[72:75]
	v_mfma_f32_16x16x32_f16 v[76:79], v[196:199], v[176:179], v[76:79]
	v_mfma_f32_16x16x32_f16 v[80:83], v[200:203], v[176:179], v[80:83]
	v_mfma_f32_16x16x32_f16 v[84:87], v[204:207], v[176:179], v[84:87]
	s_waitcnt lgkmcnt(9)
	v_mfma_f32_16x16x32_f16 v[88:91], v[192:195], v[180:183], v[88:91]
	v_mfma_f32_16x16x32_f16 v[92:95], v[196:199], v[180:183], v[92:95]
	v_mfma_f32_16x16x32_f16 v[96:99], v[200:203], v[180:183], v[96:99]
	v_mfma_f32_16x16x32_f16 v[100:103], v[204:207], v[180:183], v[100:103]
	s_waitcnt lgkmcnt(8)
	v_mfma_f32_16x16x32_f16 v[104:107], v[192:195], v[184:187], v[104:107]
	v_mfma_f32_16x16x32_f16 v[108:111], v[196:199], v[184:187], v[108:111]
	v_mfma_f32_16x16x32_f16 v[112:115], v[200:203], v[184:187], v[112:115]
	v_mfma_f32_16x16x32_f16 v[116:119], v[204:207], v[184:187], v[116:119]
	s_waitcnt lgkmcnt(7)
	ds_read_b128 v[172:175], v20
	ds_read_b128 v[192:195], v22
	ds_read_b128 v[196:199], v22 offset:2048
	ds_read_b128 v[200:203], v22 offset:4096
	ds_read_b128 v[204:207], v22 offset:6144
	ds_read_b128 v[176:179], v20 offset:2048
	ds_read_b128 v[180:183], v20 offset:4096
	ds_read_b128 v[184:187], v20 offset:6144
	s_waitcnt lgkmcnt(14)
	v_mfma_f32_16x16x32_f16 v[56:59], v[156:159], v[136:139], v[56:59]
	s_waitcnt lgkmcnt(13)
	v_mfma_f32_16x16x32_f16 v[60:63], v[160:163], v[136:139], v[60:63]
	s_waitcnt lgkmcnt(12)
	v_mfma_f32_16x16x32_f16 v[64:67], v[164:167], v[136:139], v[64:67]
	s_waitcnt lgkmcnt(11)
	v_mfma_f32_16x16x32_f16 v[68:71], v[168:171], v[136:139], v[68:71]
	s_waitcnt lgkmcnt(10)
	v_mfma_f32_16x16x32_f16 v[72:75], v[156:159], v[140:143], v[72:75]
	v_mfma_f32_16x16x32_f16 v[76:79], v[160:163], v[140:143], v[76:79]
	v_mfma_f32_16x16x32_f16 v[80:83], v[164:167], v[140:143], v[80:83]
	v_mfma_f32_16x16x32_f16 v[84:87], v[168:171], v[140:143], v[84:87]
	s_waitcnt lgkmcnt(9)
	v_mfma_f32_16x16x32_f16 v[88:91], v[156:159], v[144:147], v[88:91]
	v_mfma_f32_16x16x32_f16 v[92:95], v[160:163], v[144:147], v[92:95]
	v_mfma_f32_16x16x32_f16 v[96:99], v[164:167], v[144:147], v[96:99]
	v_mfma_f32_16x16x32_f16 v[100:103], v[168:171], v[144:147], v[100:103]
	s_waitcnt lgkmcnt(8)
	v_mfma_f32_16x16x32_f16 v[104:107], v[156:159], v[148:151], v[104:107]
	v_mfma_f32_16x16x32_f16 v[108:111], v[160:163], v[148:151], v[108:111]
	v_mfma_f32_16x16x32_f16 v[112:115], v[164:167], v[148:151], v[112:115]
	v_mfma_f32_16x16x32_f16 v[116:119], v[168:171], v[148:151], v[116:119]
	s_waitcnt vmcnt(0) lgkmcnt(0)
	s_barrier
	s_waitcnt lgkmcnt(7)
	ds_read_b128 v[136:139], v15
	ds_read_b128 v[156:159], v17
	ds_read_b128 v[160:163], v17 offset:2048
	ds_read_b128 v[164:167], v17 offset:4096
	ds_read_b128 v[168:171], v17 offset:6144
	ds_read_b128 v[140:143], v15 offset:2048
	ds_read_b128 v[144:147], v15 offset:4096
	ds_read_b128 v[148:151], v15 offset:6144
	s_waitcnt lgkmcnt(14)
	v_mfma_f32_16x16x32_f16 v[56:59], v[192:195], v[172:175], v[56:59]
	s_waitcnt lgkmcnt(13)
	v_mfma_f32_16x16x32_f16 v[60:63], v[196:199], v[172:175], v[60:63]
	s_waitcnt lgkmcnt(12)
	v_mfma_f32_16x16x32_f16 v[64:67], v[200:203], v[172:175], v[64:67]
	s_waitcnt lgkmcnt(11)
	v_mfma_f32_16x16x32_f16 v[68:71], v[204:207], v[172:175], v[68:71]
	s_waitcnt lgkmcnt(10)
	v_mfma_f32_16x16x32_f16 v[72:75], v[192:195], v[176:179], v[72:75]
	v_mfma_f32_16x16x32_f16 v[76:79], v[196:199], v[176:179], v[76:79]
	v_mfma_f32_16x16x32_f16 v[80:83], v[200:203], v[176:179], v[80:83]
	v_mfma_f32_16x16x32_f16 v[84:87], v[204:207], v[176:179], v[84:87]
	s_waitcnt lgkmcnt(9)
	v_mfma_f32_16x16x32_f16 v[88:91], v[192:195], v[180:183], v[88:91]
	v_mfma_f32_16x16x32_f16 v[92:95], v[196:199], v[180:183], v[92:95]
	v_mfma_f32_16x16x32_f16 v[96:99], v[200:203], v[180:183], v[96:99]
	v_mfma_f32_16x16x32_f16 v[100:103], v[204:207], v[180:183], v[100:103]
	s_waitcnt lgkmcnt(8)
	v_mfma_f32_16x16x32_f16 v[104:107], v[192:195], v[184:187], v[104:107]
	v_mfma_f32_16x16x32_f16 v[108:111], v[196:199], v[184:187], v[108:111]
	v_mfma_f32_16x16x32_f16 v[112:115], v[200:203], v[184:187], v[112:115]
	v_mfma_f32_16x16x32_f16 v[116:119], v[204:207], v[184:187], v[116:119]
	s_waitcnt lgkmcnt(7)
	ds_read_b128 v[172:175], v16
	ds_read_b128 v[192:195], v18
	ds_read_b128 v[196:199], v18 offset:2048
	ds_read_b128 v[200:203], v18 offset:4096
	ds_read_b128 v[204:207], v18 offset:6144
	ds_read_b128 v[176:179], v16 offset:2048
	ds_read_b128 v[180:183], v16 offset:4096
	ds_read_b128 v[184:187], v16 offset:6144
	s_waitcnt lgkmcnt(14)
	v_mfma_f32_16x16x32_f16 v[56:59], v[156:159], v[136:139], v[56:59]
	s_waitcnt lgkmcnt(13)
	v_mfma_f32_16x16x32_f16 v[60:63], v[160:163], v[136:139], v[60:63]
	s_waitcnt lgkmcnt(12)
	v_mfma_f32_16x16x32_f16 v[64:67], v[164:167], v[136:139], v[64:67]
	s_waitcnt lgkmcnt(11)
	v_mfma_f32_16x16x32_f16 v[68:71], v[168:171], v[136:139], v[68:71]
	s_waitcnt lgkmcnt(10)
	v_mfma_f32_16x16x32_f16 v[72:75], v[156:159], v[140:143], v[72:75]
	v_mfma_f32_16x16x32_f16 v[76:79], v[160:163], v[140:143], v[76:79]
	v_mfma_f32_16x16x32_f16 v[80:83], v[164:167], v[140:143], v[80:83]
	v_mfma_f32_16x16x32_f16 v[84:87], v[168:171], v[140:143], v[84:87]
	s_waitcnt lgkmcnt(9)
	v_mfma_f32_16x16x32_f16 v[88:91], v[156:159], v[144:147], v[88:91]
	v_mfma_f32_16x16x32_f16 v[92:95], v[160:163], v[144:147], v[92:95]
	v_mfma_f32_16x16x32_f16 v[96:99], v[164:167], v[144:147], v[96:99]
	v_mfma_f32_16x16x32_f16 v[100:103], v[168:171], v[144:147], v[100:103]
	s_waitcnt lgkmcnt(8)
	v_mfma_f32_16x16x32_f16 v[104:107], v[156:159], v[148:151], v[104:107]
	v_mfma_f32_16x16x32_f16 v[108:111], v[160:163], v[148:151], v[108:111]
	v_mfma_f32_16x16x32_f16 v[112:115], v[164:167], v[148:151], v[112:115]
	v_mfma_f32_16x16x32_f16 v[116:119], v[168:171], v[148:151], v[116:119]
	s_waitcnt lgkmcnt(6)
	v_mfma_f32_16x16x32_f16 v[56:59], v[192:195], v[172:175], v[56:59]
	s_waitcnt lgkmcnt(5)
	v_mfma_f32_16x16x32_f16 v[60:63], v[196:199], v[172:175], v[60:63]
	s_waitcnt lgkmcnt(4)
	v_mfma_f32_16x16x32_f16 v[64:67], v[200:203], v[172:175], v[64:67]
	s_waitcnt lgkmcnt(3)
	v_mfma_f32_16x16x32_f16 v[68:71], v[204:207], v[172:175], v[68:71]
	s_waitcnt lgkmcnt(2)
	v_mfma_f32_16x16x32_f16 v[72:75], v[192:195], v[176:179], v[72:75]
	v_mfma_f32_16x16x32_f16 v[76:79], v[196:199], v[176:179], v[76:79]
	v_mfma_f32_16x16x32_f16 v[80:83], v[200:203], v[176:179], v[80:83]
	v_mfma_f32_16x16x32_f16 v[84:87], v[204:207], v[176:179], v[84:87]
	s_waitcnt lgkmcnt(1)
	v_mfma_f32_16x16x32_f16 v[88:91], v[192:195], v[180:183], v[88:91]
	v_mfma_f32_16x16x32_f16 v[92:95], v[196:199], v[180:183], v[92:95]
	v_mfma_f32_16x16x32_f16 v[96:99], v[200:203], v[180:183], v[96:99]
	v_mfma_f32_16x16x32_f16 v[100:103], v[204:207], v[180:183], v[100:103]
	s_waitcnt lgkmcnt(0)
	v_mfma_f32_16x16x32_f16 v[104:107], v[192:195], v[184:187], v[104:107]
	v_mfma_f32_16x16x32_f16 v[108:111], v[196:199], v[184:187], v[108:111]
	v_mfma_f32_16x16x32_f16 v[112:115], v[200:203], v[184:187], v[112:115]
	v_mfma_f32_16x16x32_f16 v[116:119], v[204:207], v[184:187], v[116:119]
	s_nop 7
	s_nop 1
	v_mov_b32_e32 v213, s19
	v_pk_add_f32 v[56:57], v[56:57], v[24:25]
	v_pk_add_f32 v[58:59], v[58:59], v[26:27]
	v_pk_add_f32 v[60:61], v[60:61], v[28:29]
	v_pk_add_f32 v[62:63], v[62:63], v[30:31]
	v_pk_add_f32 v[64:65], v[64:65], v[32:33]
	v_pk_add_f32 v[66:67], v[66:67], v[34:35]
	v_pk_add_f32 v[68:69], v[68:69], v[36:37]
	v_pk_add_f32 v[70:71], v[70:71], v[38:39]
	v_pk_mul_f32 v[208:209], v[56:57], v[56:57]
	v_pk_fma_f32 v[208:209], v[58:59], v[58:59], v[208:209]
	v_pk_fma_f32 v[208:209], v[60:61], v[60:61], v[208:209]
	v_pk_fma_f32 v[208:209], v[62:63], v[62:63], v[208:209]
	v_pk_fma_f32 v[208:209], v[64:65], v[64:65], v[208:209]
	v_pk_fma_f32 v[208:209], v[66:67], v[66:67], v[208:209]
	v_pk_fma_f32 v[208:209], v[68:69], v[68:69], v[208:209]
	v_pk_fma_f32 v[208:209], v[70:71], v[70:71], v[208:209]
	v_add_f32_e32 v208, v208, v209
	v_mov_b32_e32 v209, v208
	s_nop 1
	v_permlane16_swap_b32_e32 v208, v209
	v_add_f32_e32 v208, v208, v209
	v_mov_b32_e32 v209, v208
	s_nop 1
	v_permlane32_swap_b32_e32 v208, v209
	v_add_f32_e32 v208, v208, v209
	v_mov_b32_e32 v210, 0x358637bd
	v_fmac_f32_e32 v210, 0x3c800000, v208
	v_rsq_f32_e32 v210, v210
	s_add_u32 s24, s29, 0
	s_lshr_b32 s8, s24, 1
	s_lshl_b32 s8, s8, 12
	s_and_b32 s24, s24, 1
	s_lshl_b32 s24, s24, 8
	s_add_u32 s8, s8, s24
	v_mul_f32_e32 v210, v213, v210
	v_add_u32_e32 v212, s8, v23
	v_pk_mul_f32 v[56:57], v[56:57], v[210:211] op_sel_hi:[1,0]
	v_pk_mul_f32 v[58:59], v[58:59], v[210:211] op_sel_hi:[1,0]
	v_pk_mul_f32 v[56:57], v[56:57], v[40:41]
	v_pk_mul_f32 v[58:59], v[58:59], v[42:43]
	v_cvt_pk_f16_f32 v56, v56, v57
	v_cvt_pk_f16_f32 v57, v58, v59
	global_store_dwordx2 v212, v[56:57], s[22:23] offset:0
	v_pk_mul_f32 v[60:61], v[60:61], v[210:211] op_sel_hi:[1,0]
	v_pk_mul_f32 v[62:63], v[62:63], v[210:211] op_sel_hi:[1,0]
	v_pk_mul_f32 v[60:61], v[60:61], v[44:45]
	v_pk_mul_f32 v[62:63], v[62:63], v[46:47]
	v_cvt_pk_f16_f32 v60, v60, v61
	v_cvt_pk_f16_f32 v61, v62, v63
	global_store_dwordx2 v212, v[60:61], s[22:23] offset:1024
	v_pk_mul_f32 v[64:65], v[64:65], v[210:211] op_sel_hi:[1,0]
	v_pk_mul_f32 v[66:67], v[66:67], v[210:211] op_sel_hi:[1,0]
	v_pk_mul_f32 v[64:65], v[64:65], v[48:49]
	v_pk_mul_f32 v[66:67], v[66:67], v[50:51]
	v_cvt_pk_f16_f32 v64, v64, v65
	v_cvt_pk_f16_f32 v65, v66, v67
	global_store_dwordx2 v212, v[64:65], s[22:23] offset:2048
	v_pk_mul_f32 v[68:69], v[68:69], v[210:211] op_sel_hi:[1,0]
	v_pk_mul_f32 v[70:71], v[70:71], v[210:211] op_sel_hi:[1,0]
	v_pk_mul_f32 v[68:69], v[68:69], v[52:53]
	v_pk_mul_f32 v[70:71], v[70:71], v[54:55]
	v_cvt_pk_f16_f32 v68, v68, v69
	v_cvt_pk_f16_f32 v69, v70, v71
	global_store_dwordx2 v212, v[68:69], s[22:23] offset:3072
	v_pk_add_f32 v[72:73], v[72:73], v[24:25]
	v_pk_add_f32 v[74:75], v[74:75], v[26:27]
	v_pk_add_f32 v[76:77], v[76:77], v[28:29]
	v_pk_add_f32 v[78:79], v[78:79], v[30:31]
	v_pk_add_f32 v[80:81], v[80:81], v[32:33]
	v_pk_add_f32 v[82:83], v[82:83], v[34:35]
	v_pk_add_f32 v[84:85], v[84:85], v[36:37]
	v_pk_add_f32 v[86:87], v[86:87], v[38:39]
	v_pk_mul_f32 v[208:209], v[72:73], v[72:73]
	v_pk_fma_f32 v[208:209], v[74:75], v[74:75], v[208:209]
	v_pk_fma_f32 v[208:209], v[76:77], v[76:77], v[208:209]
	v_pk_fma_f32 v[208:209], v[78:79], v[78:79], v[208:209]
	v_pk_fma_f32 v[208:209], v[80:81], v[80:81], v[208:209]
	v_pk_fma_f32 v[208:209], v[82:83], v[82:83], v[208:209]
	v_pk_fma_f32 v[208:209], v[84:85], v[84:85], v[208:209]
	v_pk_fma_f32 v[208:209], v[86:87], v[86:87], v[208:209]
	v_add_f32_e32 v208, v208, v209
	v_mov_b32_e32 v209, v208
	s_nop 1
	v_permlane16_swap_b32_e32 v208, v209
	v_add_f32_e32 v208, v208, v209
	v_mov_b32_e32 v209, v208
	s_nop 1
	v_permlane32_swap_b32_e32 v208, v209
	v_add_f32_e32 v208, v208, v209
	v_mov_b32_e32 v210, 0x358637bd
	v_fmac_f32_e32 v210, 0x3c800000, v208
	v_rsq_f32_e32 v210, v210
	s_add_u32 s24, s29, 1
	s_lshr_b32 s8, s24, 1
	s_lshl_b32 s8, s8, 12
	s_and_b32 s24, s24, 1
	s_lshl_b32 s24, s24, 8
	s_add_u32 s8, s8, s24
	v_mul_f32_e32 v210, v213, v210
	v_add_u32_e32 v212, s8, v23
	v_pk_mul_f32 v[72:73], v[72:73], v[210:211] op_sel_hi:[1,0]
	v_pk_mul_f32 v[74:75], v[74:75], v[210:211] op_sel_hi:[1,0]
	v_pk_mul_f32 v[72:73], v[72:73], v[40:41]
	v_pk_mul_f32 v[74:75], v[74:75], v[42:43]
	v_cvt_pk_f16_f32 v72, v72, v73
	v_cvt_pk_f16_f32 v73, v74, v75
	global_store_dwordx2 v212, v[72:73], s[22:23] offset:0
	v_pk_mul_f32 v[76:77], v[76:77], v[210:211] op_sel_hi:[1,0]
	v_pk_mul_f32 v[78:79], v[78:79], v[210:211] op_sel_hi:[1,0]
	v_pk_mul_f32 v[76:77], v[76:77], v[44:45]
	v_pk_mul_f32 v[78:79], v[78:79], v[46:47]
	v_cvt_pk_f16_f32 v76, v76, v77
	v_cvt_pk_f16_f32 v77, v78, v79
	global_store_dwordx2 v212, v[76:77], s[22:23] offset:1024
	v_pk_mul_f32 v[80:81], v[80:81], v[210:211] op_sel_hi:[1,0]
	v_pk_mul_f32 v[82:83], v[82:83], v[210:211] op_sel_hi:[1,0]
	v_pk_mul_f32 v[80:81], v[80:81], v[48:49]
	v_pk_mul_f32 v[82:83], v[82:83], v[50:51]
	v_cvt_pk_f16_f32 v80, v80, v81
	v_cvt_pk_f16_f32 v81, v82, v83
	global_store_dwordx2 v212, v[80:81], s[22:23] offset:2048
	v_pk_mul_f32 v[84:85], v[84:85], v[210:211] op_sel_hi:[1,0]
	v_pk_mul_f32 v[86:87], v[86:87], v[210:211] op_sel_hi:[1,0]
	v_pk_mul_f32 v[84:85], v[84:85], v[52:53]
	v_pk_mul_f32 v[86:87], v[86:87], v[54:55]
	v_cvt_pk_f16_f32 v84, v84, v85
	v_cvt_pk_f16_f32 v85, v86, v87
	global_store_dwordx2 v212, v[84:85], s[22:23] offset:3072
	v_pk_add_f32 v[88:89], v[88:89], v[24:25]
	v_pk_add_f32 v[90:91], v[90:91], v[26:27]
	v_pk_add_f32 v[92:93], v[92:93], v[28:29]
	v_pk_add_f32 v[94:95], v[94:95], v[30:31]
	v_pk_add_f32 v[96:97], v[96:97], v[32:33]
	v_pk_add_f32 v[98:99], v[98:99], v[34:35]
	v_pk_add_f32 v[100:101], v[100:101], v[36:37]
	v_pk_add_f32 v[102:103], v[102:103], v[38:39]
	v_pk_mul_f32 v[208:209], v[88:89], v[88:89]
	v_pk_fma_f32 v[208:209], v[90:91], v[90:91], v[208:209]
	v_pk_fma_f32 v[208:209], v[92:93], v[92:93], v[208:209]
	v_pk_fma_f32 v[208:209], v[94:95], v[94:95], v[208:209]
	v_pk_fma_f32 v[208:209], v[96:97], v[96:97], v[208:209]
	v_pk_fma_f32 v[208:209], v[98:99], v[98:99], v[208:209]
	v_pk_fma_f32 v[208:209], v[100:101], v[100:101], v[208:209]
	v_pk_fma_f32 v[208:209], v[102:103], v[102:103], v[208:209]
	v_add_f32_e32 v208, v208, v209
	v_mov_b32_e32 v209, v208
	s_nop 1
	v_permlane16_swap_b32_e32 v208, v209
	v_add_f32_e32 v208, v208, v209
	v_mov_b32_e32 v209, v208
	s_nop 1
	v_permlane32_swap_b32_e32 v208, v209
	v_add_f32_e32 v208, v208, v209
	v_mov_b32_e32 v210, 0x358637bd
	v_fmac_f32_e32 v210, 0x3c800000, v208
	v_rsq_f32_e32 v210, v210
	s_add_u32 s24, s29, 2
	s_lshr_b32 s8, s24, 1
	s_lshl_b32 s8, s8, 12
	s_and_b32 s24, s24, 1
	s_lshl_b32 s24, s24, 8
	s_add_u32 s8, s8, s24
	v_mul_f32_e32 v210, v213, v210
	v_add_u32_e32 v212, s8, v23
	v_pk_mul_f32 v[88:89], v[88:89], v[210:211] op_sel_hi:[1,0]
	v_pk_mul_f32 v[90:91], v[90:91], v[210:211] op_sel_hi:[1,0]
	v_pk_mul_f32 v[88:89], v[88:89], v[40:41]
	v_pk_mul_f32 v[90:91], v[90:91], v[42:43]
	v_cvt_pk_f16_f32 v88, v88, v89
	v_cvt_pk_f16_f32 v89, v90, v91
	global_store_dwordx2 v212, v[88:89], s[22:23] offset:0
	v_pk_mul_f32 v[92:93], v[92:93], v[210:211] op_sel_hi:[1,0]
	v_pk_mul_f32 v[94:95], v[94:95], v[210:211] op_sel_hi:[1,0]
	v_pk_mul_f32 v[92:93], v[92:93], v[44:45]
	v_pk_mul_f32 v[94:95], v[94:95], v[46:47]
	v_cvt_pk_f16_f32 v92, v92, v93
	v_cvt_pk_f16_f32 v93, v94, v95
	global_store_dwordx2 v212, v[92:93], s[22:23] offset:1024
	v_pk_mul_f32 v[96:97], v[96:97], v[210:211] op_sel_hi:[1,0]
	v_pk_mul_f32 v[98:99], v[98:99], v[210:211] op_sel_hi:[1,0]
	v_pk_mul_f32 v[96:97], v[96:97], v[48:49]
	v_pk_mul_f32 v[98:99], v[98:99], v[50:51]
	v_cvt_pk_f16_f32 v96, v96, v97
	v_cvt_pk_f16_f32 v97, v98, v99
	global_store_dwordx2 v212, v[96:97], s[22:23] offset:2048
	v_pk_mul_f32 v[100:101], v[100:101], v[210:211] op_sel_hi:[1,0]
	v_pk_mul_f32 v[102:103], v[102:103], v[210:211] op_sel_hi:[1,0]
	v_pk_mul_f32 v[100:101], v[100:101], v[52:53]
	v_pk_mul_f32 v[102:103], v[102:103], v[54:55]
	v_cvt_pk_f16_f32 v100, v100, v101
	v_cvt_pk_f16_f32 v101, v102, v103
	global_store_dwordx2 v212, v[100:101], s[22:23] offset:3072
	v_pk_add_f32 v[104:105], v[104:105], v[24:25]
	v_pk_add_f32 v[106:107], v[106:107], v[26:27]
	v_pk_add_f32 v[108:109], v[108:109], v[28:29]
	v_pk_add_f32 v[110:111], v[110:111], v[30:31]
	v_pk_add_f32 v[112:113], v[112:113], v[32:33]
	v_pk_add_f32 v[114:115], v[114:115], v[34:35]
	v_pk_add_f32 v[116:117], v[116:117], v[36:37]
	v_pk_add_f32 v[118:119], v[118:119], v[38:39]
	v_pk_mul_f32 v[208:209], v[104:105], v[104:105]
	v_pk_fma_f32 v[208:209], v[106:107], v[106:107], v[208:209]
	v_pk_fma_f32 v[208:209], v[108:109], v[108:109], v[208:209]
	v_pk_fma_f32 v[208:209], v[110:111], v[110:111], v[208:209]
	v_pk_fma_f32 v[208:209], v[112:113], v[112:113], v[208:209]
	v_pk_fma_f32 v[208:209], v[114:115], v[114:115], v[208:209]
	v_pk_fma_f32 v[208:209], v[116:117], v[116:117], v[208:209]
	v_pk_fma_f32 v[208:209], v[118:119], v[118:119], v[208:209]
	v_add_f32_e32 v208, v208, v209
	v_mov_b32_e32 v209, v208
	s_nop 1
	v_permlane16_swap_b32_e32 v208, v209
	v_add_f32_e32 v208, v208, v209
	v_mov_b32_e32 v209, v208
	s_nop 1
	v_permlane32_swap_b32_e32 v208, v209
	v_add_f32_e32 v208, v208, v209
	v_mov_b32_e32 v210, 0x358637bd
	v_fmac_f32_e32 v210, 0x3c800000, v208
	v_rsq_f32_e32 v210, v210
	s_add_u32 s24, s29, 3
	s_lshr_b32 s8, s24, 1
	s_lshl_b32 s8, s8, 12
	s_and_b32 s24, s24, 1
	s_lshl_b32 s24, s24, 8
	s_add_u32 s8, s8, s24
	v_mul_f32_e32 v210, v213, v210
	v_add_u32_e32 v212, s8, v23
	v_pk_mul_f32 v[104:105], v[104:105], v[210:211] op_sel_hi:[1,0]
	v_pk_mul_f32 v[106:107], v[106:107], v[210:211] op_sel_hi:[1,0]
	v_pk_mul_f32 v[104:105], v[104:105], v[40:41]
	v_pk_mul_f32 v[106:107], v[106:107], v[42:43]
	v_cvt_pk_f16_f32 v104, v104, v105
	v_cvt_pk_f16_f32 v105, v106, v107
	global_store_dwordx2 v212, v[104:105], s[22:23] offset:0
	v_pk_mul_f32 v[108:109], v[108:109], v[210:211] op_sel_hi:[1,0]
	v_pk_mul_f32 v[110:111], v[110:111], v[210:211] op_sel_hi:[1,0]
	v_pk_mul_f32 v[108:109], v[108:109], v[44:45]
	v_pk_mul_f32 v[110:111], v[110:111], v[46:47]
	v_cvt_pk_f16_f32 v108, v108, v109
	v_cvt_pk_f16_f32 v109, v110, v111
	global_store_dwordx2 v212, v[108:109], s[22:23] offset:1024
	v_pk_mul_f32 v[112:113], v[112:113], v[210:211] op_sel_hi:[1,0]
	v_pk_mul_f32 v[114:115], v[114:115], v[210:211] op_sel_hi:[1,0]
	v_pk_mul_f32 v[112:113], v[112:113], v[48:49]
	v_pk_mul_f32 v[114:115], v[114:115], v[50:51]
	v_cvt_pk_f16_f32 v112, v112, v113
	v_cvt_pk_f16_f32 v113, v114, v115
	global_store_dwordx2 v212, v[112:113], s[22:23] offset:2048
	v_pk_mul_f32 v[116:117], v[116:117], v[210:211] op_sel_hi:[1,0]
	v_pk_mul_f32 v[118:119], v[118:119], v[210:211] op_sel_hi:[1,0]
	v_pk_mul_f32 v[116:117], v[116:117], v[52:53]
	v_pk_mul_f32 v[118:119], v[118:119], v[54:55]
	v_cvt_pk_f16_f32 v116, v116, v117
	v_cvt_pk_f16_f32 v117, v118, v119
	global_store_dwordx2 v212, v[116:117], s[22:23] offset:3072
	s_branch .Lpf_done
.Lpf_vVA:
	s_mul_i32 s25, s25, 0x50
	s_add_u32 s29, s10, s25
	s_lshr_b32 s29, s29, 4
	v_add_u32_e32 v5, s25, v3
	v_lshlrev_b32_e32 v5, 7, v5
	v_add_u32_e32 v15, v5, v6
	v_add_u32_e32 v16, v5, v7
	v_add_u32_e32 v5, 0x9000, v9
	v_add_u32_e32 v17, v5, v6
	v_add_u32_e32 v18, v5, v7
	v_add_u32_e32 v19, 0x1a000, v15
	v_add_u32_e32 v20, 0x1a000, v16
	v_add_u32_e32 v21, 0x1a000, v17
	v_add_u32_e32 v22, 0x1a000, v18
	v_lshlrev_b32_e32 v5, 2, v3
	global_load_dword v24, v5, s[14:15] offset:0
	global_load_dword v26, v5, s[14:15] offset:64
	global_load_dword v28, v5, s[14:15] offset:128
	global_load_dword v30, v5, s[14:15] offset:192
	s_add_u32 m0, s28, 0x0
	s_nop 0
	global_load_lds_dwordx4 v10, s[4:5]
	s_add_u32 m0, s28, 0x2000
	s_nop 0
	global_load_lds_dwordx4 v11, s[4:5]
	s_add_u32 m0, s28, 0x4000
	s_nop 0
	global_load_lds_dwordx4 v12, s[4:5]
	s_add_u32 m0, s28, 0x6000
	s_nop 0
	global_load_lds_dwordx4 v13, s[4:5]
	s_add_u32 s4, s4, s20
	s_addc_u32 s5, s5, 0
	s_add_u32 m0, s28, 0x9000
	s_nop 0
	global_load_lds_dwordx4 v10, s[6:7]
	s_add_u32 m0, s28, 0xb000
	s_nop 0
	global_load_lds_dwordx4 v11, s[6:7]
	s_add_u32 s6, s6, s20
	s_addc_u32 s7, s7, 0
	s_add_u32 m0, s28, 0xd000
	s_nop 0
	global_load_lds_dwordx4 v10, s[4:5]
	s_add_u32 m0, s28, 0xf000
	s_nop 0
	global_load_lds_dwordx4 v11, s[4:5]
	s_add_u32 m0, s28, 0x11000
	s_nop 0
	global_load_lds_dwordx4 v12, s[4:5]
	s_add_u32 m0, s28, 0x13000
	s_nop 0
	global_load_lds_dwordx4 v13, s[4:5]
	s_add_u32 s4, s4, s20
	s_addc_u32 s5, s5, 0
	s_add_u32 m0, s28, 0x16000
	s_nop 0
	global_load_lds_dwordx4 v10, s[6:7]
	s_add_u32 m0, s28, 0x18000
	s_nop 0
	global_load_lds_dwordx4 v11, s[6:7]
	s_add_u32 s6, s6, s20
	s_addc_u32 s7, s7, 0
	s_add_u32 m0, s28, 0x1a000
	s_nop 0
	global_load_lds_dwordx4 v10, s[4:5]
	s_add_u32 m0, s28, 0x1c000
	s_nop 0
	global_load_lds_dwordx4 v11, s[4:5]
	s_add_u32 m0, s28, 0x1e000
	s_nop 0
	global_load_lds_dwordx4 v12, s[4:5]
	s_add_u32 m0, s28, 0x20000
	s_nop 0
	global_load_lds_dwordx4 v13, s[4:5]
	s_add_u32 s4, s4, s20
	s_addc_u32 s5, s5, 0
	s_add_u32 m0, s28, 0x23000
	s_nop 0
	global_load_lds_dwordx4 v10, s[6:7]
	s_add_u32 m0, s28, 0x25000
	s_nop 0
	global_load_lds_dwordx4 v11, s[6:7]
	s_add_u32 s6, s6, s20
	s_addc_u32 s7, s7, 0
	s_waitcnt vmcnt(12) lgkmcnt(0)
	s_barrier
	s_waitcnt lgkmcnt(6)
	ds_read_b128 v[136:139], v15
	ds_read_b128 v[156:159], v17
	ds_read_b128 v[160:163], v17 offset:2048
	ds_read_b128 v[164:167], v17 offset:4096
	ds_read_b128 v[168:171], v17 offset:6144
	ds_read_b128 v[140:143], v15 offset:2048
	ds_read_b128 v[144:147], v15 offset:4096
	ds_read_b128 v[148:151], v15 offset:6144
	ds_read_b128 v[152:155], v15 offset:8192
	s_waitcnt lgkmcnt(6)
	ds_read_b128 v[172:175], v16
	ds_read_b128 v[192:195], v18
	ds_read_b128 v[196:199], v18 offset:2048
	ds_read_b128 v[200:203], v18 offset:4096
	ds_read_b128 v[204:207], v18 offset:6144
	ds_read_b128 v[176:179], v16 offset:2048
	ds_read_b128 v[180:183], v16 offset:4096
	ds_read_b128 v[184:187], v16 offset:6144
	ds_read_b128 v[188:191], v16 offset:8192
	v_mfma_f32_16x16x32_f16 v[56:59], v[136:139], v[156:159], 0
	s_waitcnt lgkmcnt(15)
	v_mfma_f32_16x16x32_f16 v[60:63], v[136:139], v[160:163], 0
	s_waitcnt lgkmcnt(14)
	v_mfma_f32_16x16x32_f16 v[64:67], v[136:139], v[164:167], 0
	s_waitcnt lgkmcnt(13)
	v_mfma_f32_16x16x32_f16 v[68:71], v[136:139], v[168:171], 0
	s_waitcnt lgkmcnt(12)
	v_mfma_f32_16x16x32_f16 v[72:75], v[140:143], v[156:159], 0
	v_mfma_f32_16x16x32_f16 v[76:79], v[140:143], v[160:163], 0
	v_mfma_f32_16x16x32_f16 v[80:83], v[140:143], v[164:167], 0
	v_mfma_f32_16x16x32_f16 v[84:87], v[140:143], v[168:171], 0
	s_waitcnt lgkmcnt(11)
	v_mfma_f32_16x16x32_f16 v[88:91], v[144:147], v[156:159], 0
	v_mfma_f32_16x16x32_f16 v[92:95], v[144:147], v[160:163], 0
	v_mfma_f32_16x16x32_f16 v[96:99], v[144:147], v[164:167], 0
	v_mfma_f32_16x16x32_f16 v[100:103], v[144:147], v[168:171], 0
	s_waitcnt lgkmcnt(10)
	v_mfma_f32_16x16x32_f16 v[104:107], v[148:151], v[156:159], 0
	v_mfma_f32_16x16x32_f16 v[108:111], v[148:151], v[160:163], 0
	v_mfma_f32_16x16x32_f16 v[112:115], v[148:151], v[164:167], 0
	v_mfma_f32_16x16x32_f16 v[116:119], v[148:151], v[168:171], 0
	s_waitcnt lgkmcnt(9)
	v_mfma_f32_16x16x32_f16 v[120:123], v[152:155], v[156:159], 0
	v_mfma_f32_16x16x32_f16 v[124:127], v[152:155], v[160:163], 0
	v_mfma_f32_16x16x32_f16 v[128:131], v[152:155], v[164:167], 0
	v_mfma_f32_16x16x32_f16 v[132:135], v[152:155], v[168:171], 0
	s_waitcnt vmcnt(6) lgkmcnt(0)
	s_barrier
	s_waitcnt lgkmcnt(6)
	ds_read_b128 v[136:139], v15 offset:53248
	ds_read_b128 v[156:159], v17 offset:53248
	ds_read_b128 v[160:163], v17 offset:55296
	ds_read_b128 v[164:167], v17 offset:57344
	ds_read_b128 v[168:171], v17 offset:59392
	ds_read_b128 v[140:143], v15 offset:55296
	ds_read_b128 v[144:147], v15 offset:57344
	ds_read_b128 v[148:151], v15 offset:59392
	ds_read_b128 v[152:155], v15 offset:61440
	v_mfma_f32_16x16x32_f16 v[56:59], v[172:175], v[192:195], v[56:59]
	s_add_u32 m0, s28, 0x0
	s_nop 0
	global_load_lds_dwordx4 v10, s[4:5]
	s_waitcnt lgkmcnt(15)
	v_mfma_f32_16x16x32_f16 v[60:63], v[172:175], v[196:199], v[60:63]
	s_waitcnt lgkmcnt(14)
	v_mfma_f32_16x16x32_f16 v[64:67], v[172:175], v[200:203], v[64:67]
	s_waitcnt lgkmcnt(13)
	v_mfma_f32_16x16x32_f16 v[68:71], v[172:175], v[204:207], v[68:71]
	s_waitcnt lgkmcnt(12)
	v_mfma_f32_16x16x32_f16 v[72:75], v[176:179], v[192:195], v[72:75]
	v_mfma_f32_16x16x32_f16 v[76:79], v[176:179], v[196:199], v[76:79]
	v_mfma_f32_16x16x32_f16 v[80:83], v[176:179], v[200:203], v[80:83]
	s_add_u32 m0, s28, 0x2000
	s_nop 0
	global_load_lds_dwordx4 v11, s[4:5]
	v_mfma_f32_16x16x32_f16 v[84:87], v[176:179], v[204:207], v[84:87]
	s_waitcnt lgkmcnt(11)
	v_mfma_f32_16x16x32_f16 v[88:91], v[180:183], v[192:195], v[88:91]
	v_mfma_f32_16x16x32_f16 v[92:95], v[180:183], v[196:199], v[92:95]
	v_mfma_f32_16x16x32_f16 v[96:99], v[180:183], v[200:203], v[96:99]
	v_mfma_f32_16x16x32_f16 v[100:103], v[180:183], v[204:207], v[100:103]
	s_waitcnt lgkmcnt(10)
	v_mfma_f32_16x16x32_f16 v[104:107], v[184:187], v[192:195], v[104:107]
	v_mfma_f32_16x16x32_f16 v[108:111], v[184:187], v[196:199], v[108:111]
	s_add_u32 m0, s28, 0x4000
	s_nop 0
	global_load_lds_dwordx4 v12, s[4:5]
	v_mfma_f32_16x16x32_f16 v[112:115], v[184:187], v[200:203], v[112:115]
	v_mfma_f32_16x16x32_f16 v[116:119], v[184:187], v[204:207], v[116:119]
	s_waitcnt lgkmcnt(9)
	v_mfma_f32_16x16x32_f16 v[120:123], v[188:191], v[192:195], v[120:123]
	v_mfma_f32_16x16x32_f16 v[124:127], v[188:191], v[196:199], v[124:127]
	v_mfma_f32_16x16x32_f16 v[128:131], v[188:191], v[200:203], v[128:131]
	v_mfma_f32_16x16x32_f16 v[132:135], v[188:191], v[204:207], v[132:135]
	s_waitcnt lgkmcnt(6)
	ds_read_b128 v[172:175], v16 offset:53248
	ds_read_b128 v[192:195], v18 offset:53248
	ds_read_b128 v[196:199], v18 offset:55296
	ds_read_b128 v[200:203], v18 offset:57344
	ds_read_b128 v[204:207], v18 offset:59392
	ds_read_b128 v[176:179], v16 offset:55296
	ds_read_b128 v[180:183], v16 offset:57344
	ds_read_b128 v[184:187], v16 offset:59392
	ds_read_b128 v[188:191], v16 offset:61440
	v_mfma_f32_16x16x32_f16 v[56:59], v[136:139], v[156:159], v[56:59]
	s_add_u32 m0, s28, 0x6000
	s_nop 0
	global_load_lds_dwordx4 v13, s[4:5]
	s_add_u32 s4, s4, s20
	s_addc_u32 s5, s5, 0
	s_waitcnt lgkmcnt(15)
	v_mfma_f32_16x16x32_f16 v[60:63], v[136:139], v[160:163], v[60:63]
	s_waitcnt lgkmcnt(14)
	v_mfma_f32_16x16x32_f16 v[64:67], v[136:139], v[164:167], v[64:67]
	s_waitcnt lgkmcnt(13)
	v_mfma_f32_16x16x32_f16 v[68:71], v[136:139], v[168:171], v[68:71]
	s_waitcnt lgkmcnt(12)
	v_mfma_f32_16x16x32_f16 v[72:75], v[140:143], v[156:159], v[72:75]
	v_mfma_f32_16x16x32_f16 v[76:79], v[140:143], v[160:163], v[76:79]
	v_mfma_f32_16x16x32_f16 v[80:83], v[140:143], v[164:167], v[80:83]
	s_add_u32 m0, s28, 0x9000
	s_nop 0
	global_load_lds_dwordx4 v10, s[6:7]
	v_mfma_f32_16x16x32_f16 v[84:87], v[140:143], v[168:171], v[84:87]
	s_waitcnt lgkmcnt(11)
	v_mfma_f32_16x16x32_f16 v[88:91], v[144:147], v[156:159], v[88:91]
	v_mfma_f32_16x16x32_f16 v[92:95], v[144:147], v[160:163], v[92:95]
	v_mfma_f32_16x16x32_f16 v[96:99], v[144:147], v[164:167], v[96:99]
	v_mfma_f32_16x16x32_f16 v[100:103], v[144:147], v[168:171], v[100:103]
	s_waitcnt lgkmcnt(10)
	v_mfma_f32_16x16x32_f16 v[104:107], v[148:151], v[156:159], v[104:107]
	v_mfma_f32_16x16x32_f16 v[108:111], v[148:151], v[160:163], v[108:111]
	s_add_u32 m0, s28, 0xb000
	s_nop 0
	global_load_lds_dwordx4 v11, s[6:7]
	s_add_u32 s6, s6, s20
	s_addc_u32 s7, s7, 0
	v_mfma_f32_16x16x32_f16 v[112:115], v[148:151], v[164:167], v[112:115]
	v_mfma_f32_16x16x32_f16 v[116:119], v[148:151], v[168:171], v[116:119]
	s_waitcnt lgkmcnt(9)
	v_mfma_f32_16x16x32_f16 v[120:123], v[152:155], v[156:159], v[120:123]
	v_mfma_f32_16x16x32_f16 v[124:127], v[152:155], v[160:163], v[124:127]
	v_mfma_f32_16x16x32_f16 v[128:131], v[152:155], v[164:167], v[128:131]
	v_mfma_f32_16x16x32_f16 v[132:135], v[152:155], v[168:171], v[132:135]
	s_waitcnt vmcnt(6) lgkmcnt(0)
	s_barrier
	s_waitcnt lgkmcnt(6)
	ds_read_b128 v[136:139], v19
	ds_read_b128 v[156:159], v21
	ds_read_b128 v[160:163], v21 offset:2048
	ds_read_b128 v[164:167], v21 offset:4096
	ds_read_b128 v[168:171], v21 offset:6144
	ds_read_b128 v[140:143], v19 offset:2048
	ds_read_b128 v[144:147], v19 offset:4096
	ds_read_b128 v[148:151], v19 offset:6144
	ds_read_b128 v[152:155], v19 offset:8192
	v_mfma_f32_16x16x32_f16 v[56:59], v[172:175], v[192:195], v[56:59]
	s_add_u32 m0, s28, 0xd000
	s_nop 0
	global_load_lds_dwordx4 v10, s[4:5]
	s_waitcnt lgkmcnt(15)
	v_mfma_f32_16x16x32_f16 v[60:63], v[172:175], v[196:199], v[60:63]
	s_waitcnt lgkmcnt(14)
	v_mfma_f32_16x16x32_f16 v[64:67], v[172:175], v[200:203], v[64:67]
	s_waitcnt lgkmcnt(13)
	v_mfma_f32_16x16x32_f16 v[68:71], v[172:175], v[204:207], v[68:71]
	s_waitcnt lgkmcnt(12)
	v_mfma_f32_16x16x32_f16 v[72:75], v[176:179], v[192:195], v[72:75]
	v_mfma_f32_16x16x32_f16 v[76:79], v[176:179], v[196:199], v[76:79]
	v_mfma_f32_16x16x32_f16 v[80:83], v[176:179], v[200:203], v[80:83]
	s_add_u32 m0, s28, 0xf000
	s_nop 0
	global_load_lds_dwordx4 v11, s[4:5]
	v_mfma_f32_16x16x32_f16 v[84:87], v[176:179], v[204:207], v[84:87]
	s_waitcnt lgkmcnt(11)
	v_mfma_f32_16x16x32_f16 v[88:91], v[180:183], v[192:195], v[88:91]
	v_mfma_f32_16x16x32_f16 v[92:95], v[180:183], v[196:199], v[92:95]
	v_mfma_f32_16x16x32_f16 v[96:99], v[180:183], v[200:203], v[96:99]
	v_mfma_f32_16x16x32_f16 v[100:103], v[180:183], v[204:207], v[100:103]
	s_waitcnt lgkmcnt(10)
	v_mfma_f32_16x16x32_f16 v[104:107], v[184:187], v[192:195], v[104:107]
	v_mfma_f32_16x16x32_f16 v[108:111], v[184:187], v[196:199], v[108:111]
	s_add_u32 m0, s28, 0x11000
	s_nop 0
	global_load_lds_dwordx4 v12, s[4:5]
	v_mfma_f32_16x16x32_f16 v[112:115], v[184:187], v[200:203], v[112:115]
	v_mfma_f32_16x16x32_f16 v[116:119], v[184:187], v[204:207], v[116:119]
	s_waitcnt lgkmcnt(9)
	v_mfma_f32_16x16x32_f16 v[120:123], v[188:191], v[192:195], v[120:123]
	v_mfma_f32_16x16x32_f16 v[124:127], v[188:191], v[196:199], v[124:127]
	v_mfma_f32_16x16x32_f16 v[128:131], v[188:191], v[200:203], v[128:131]
	v_mfma_f32_16x16x32_f16 v[132:135], v[188:191], v[204:207], v[132:135]
	s_waitcnt lgkmcnt(6)
	ds_read_b128 v[172:175], v20
	ds_read_b128 v[192:195], v22
	ds_read_b128 v[196:199], v22 offset:2048
	ds_read_b128 v[200:203], v22 offset:4096
	ds_read_b128 v[204:207], v22 offset:6144
	ds_read_b128 v[176:179], v20 offset:2048
	ds_read_b128 v[180:183], v20 offset:4096
	ds_read_b128 v[184:187], v20 offset:6144
	ds_read_b128 v[188:191], v20 offset:8192
	v_mfma_f32_16x16x32_f16 v[56:59], v[136:139], v[156:159], v[56:59]
	s_add_u32 m0, s28, 0x13000
	s_nop 0
	global_load_lds_dwordx4 v13, s[4:5]
	s_add_u32 s4, s4, s20
	s_addc_u32 s5, s5, 0
	s_waitcnt lgkmcnt(15)
	v_mfma_f32_16x16x32_f16 v[60:63], v[136:139], v[160:163], v[60:63]
	s_waitcnt lgkmcnt(14)
	v_mfma_f32_16x16x32_f16 v[64:67], v[136:139], v[164:167], v[64:67]
	s_waitcnt lgkmcnt(13)
	v_mfma_f32_16x16x32_f16 v[68:71], v[136:139], v[168:171], v[68:71]
	s_waitcnt lgkmcnt(12)
	v_mfma_f32_16x16x32_f16 v[72:75], v[140:143], v[156:159], v[72:75]
	v_mfma_f32_16x16x32_f16 v[76:79], v[140:143], v[160:163], v[76:79]
	v_mfma_f32_16x16x32_f16 v[80:83], v[140:143], v[164:167], v[80:83]
	s_add_u32 m0, s28, 0x16000
	s_nop 0
	global_load_lds_dwordx4 v10, s[6:7]
	v_mfma_f32_16x16x32_f16 v[84:87], v[140:143], v[168:171], v[84:87]
	s_waitcnt lgkmcnt(11)
	v_mfma_f32_16x16x32_f16 v[88:91], v[144:147], v[156:159], v[88:91]
	v_mfma_f32_16x16x32_f16 v[92:95], v[144:147], v[160:163], v[92:95]
	v_mfma_f32_16x16x32_f16 v[96:99], v[144:147], v[164:167], v[96:99]
	v_mfma_f32_16x16x32_f16 v[100:103], v[144:147], v[168:171], v[100:103]
	s_waitcnt lgkmcnt(10)
	v_mfma_f32_16x16x32_f16 v[104:107], v[148:151], v[156:159], v[104:107]
	v_mfma_f32_16x16x32_f16 v[108:111], v[148:151], v[160:163], v[108:111]
	s_add_u32 m0, s28, 0x18000
	s_nop 0
	global_load_lds_dwordx4 v11, s[6:7]
	s_add_u32 s6, s6, s20
	s_addc_u32 s7, s7, 0
	v_mfma_f32_16x16x32_f16 v[112:115], v[148:151], v[164:167], v[112:115]
	v_mfma_f32_16x16x32_f16 v[116:119], v[148:151], v[168:171], v[116:119]
	s_waitcnt lgkmcnt(9)
	v_mfma_f32_16x16x32_f16 v[120:123], v[152:155], v[156:159], v[120:123]
	v_mfma_f32_16x16x32_f16 v[124:127], v[152:155], v[160:163], v[124:127]
	v_mfma_f32_16x16x32_f16 v[128:131], v[152:155], v[164:167], v[128:131]
	v_mfma_f32_16x16x32_f16 v[132:135], v[152:155], v[168:171], v[132:135]
	s_waitcnt vmcnt(6) lgkmcnt(0)
	s_barrier
	s_waitcnt lgkmcnt(6)
	ds_read_b128 v[136:139], v15
	ds_read_b128 v[156:159], v17
	ds_read_b128 v[160:163], v17 offset:2048
	ds_read_b128 v[164:167], v17 offset:4096
	ds_read_b128 v[168:171], v17 offset:6144
	ds_read_b128 v[140:143], v15 offset:2048
	ds_read_b128 v[144:147], v15 offset:4096
	ds_read_b128 v[148:151], v15 offset:6144
	ds_read_b128 v[152:155], v15 offset:8192
	v_mfma_f32_16x16x32_f16 v[56:59], v[172:175], v[192:195], v[56:59]
	s_add_u32 m0, s28, 0x1a000
	s_nop 0
	global_load_lds_dwordx4 v10, s[4:5]
	s_waitcnt lgkmcnt(15)
	v_mfma_f32_16x16x32_f16 v[60:63], v[172:175], v[196:199], v[60:63]
	s_waitcnt lgkmcnt(14)
	v_mfma_f32_16x16x32_f16 v[64:67], v[172:175], v[200:203], v[64:67]
	s_waitcnt lgkmcnt(13)
	v_mfma_f32_16x16x32_f16 v[68:71], v[172:175], v[204:207], v[68:71]
	s_waitcnt lgkmcnt(12)
	v_mfma_f32_16x16x32_f16 v[72:75], v[176:179], v[192:195], v[72:75]
	v_mfma_f32_16x16x32_f16 v[76:79], v[176:179], v[196:199], v[76:79]
	v_mfma_f32_16x16x32_f16 v[80:83], v[176:179], v[200:203], v[80:83]
	s_add_u32 m0, s28, 0x1c000
	s_nop 0
	global_load_lds_dwordx4 v11, s[4:5]
	v_mfma_f32_16x16x32_f16 v[84:87], v[176:179], v[204:207], v[84:87]
	s_waitcnt lgkmcnt(11)
	v_mfma_f32_16x16x32_f16 v[88:91], v[180:183], v[192:195], v[88:91]
	v_mfma_f32_16x16x32_f16 v[92:95], v[180:183], v[196:199], v[92:95]
	v_mfma_f32_16x16x32_f16 v[96:99], v[180:183], v[200:203], v[96:99]
	v_mfma_f32_16x16x32_f16 v[100:103], v[180:183], v[204:207], v[100:103]
	s_waitcnt lgkmcnt(10)
	v_mfma_f32_16x16x32_f16 v[104:107], v[184:187], v[192:195], v[104:107]
	v_mfma_f32_16x16x32_f16 v[108:111], v[184:187], v[196:199], v[108:111]
	s_add_u32 m0, s28, 0x1e000
	s_nop 0
	global_load_lds_dwordx4 v12, s[4:5]
	v_mfma_f32_16x16x32_f16 v[112:115], v[184:187], v[200:203], v[112:115]
	v_mfma_f32_16x16x32_f16 v[116:119], v[184:187], v[204:207], v[116:119]
	s_waitcnt lgkmcnt(9)
	v_mfma_f32_16x16x32_f16 v[120:123], v[188:191], v[192:195], v[120:123]
	v_mfma_f32_16x16x32_f16 v[124:127], v[188:191], v[196:199], v[124:127]
	v_mfma_f32_16x16x32_f16 v[128:131], v[188:191], v[200:203], v[128:131]
	v_mfma_f32_16x16x32_f16 v[132:135], v[188:191], v[204:207], v[132:135]
	s_waitcnt lgkmcnt(6)
	ds_read_b128 v[172:175], v16
	ds_read_b128 v[192:195], v18
	ds_read_b128 v[196:199], v18 offset:2048
	ds_read_b128 v[200:203], v18 offset:4096
	ds_read_b128 v[204:207], v18 offset:6144
	ds_read_b128 v[176:179], v16 offset:2048
	ds_read_b128 v[180:183], v16 offset:4096
	ds_read_b128 v[184:187], v16 offset:6144
	ds_read_b128 v[188:191], v16 offset:8192
	v_mfma_f32_16x16x32_f16 v[56:59], v[136:139], v[156:159], v[56:59]
	s_add_u32 m0, s28, 0x20000
	s_nop 0
	global_load_lds_dwordx4 v13, s[4:5]
	s_add_u32 s4, s4, s20
	s_addc_u32 s5, s5, 0
	s_waitcnt lgkmcnt(15)
	v_mfma_f32_16x16x32_f16 v[60:63], v[136:139], v[160:163], v[60:63]
	s_waitcnt lgkmcnt(14)
	v_mfma_f32_16x16x32_f16 v[64:67], v[136:139], v[164:167], v[64:67]
	s_waitcnt lgkmcnt(13)
	v_mfma_f32_16x16x32_f16 v[68:71], v[136:139], v[168:171], v[68:71]
	s_waitcnt lgkmcnt(12)
	v_mfma_f32_16x16x32_f16 v[72:75], v[140:143], v[156:159], v[72:75]
	v_mfma_f32_16x16x32_f16 v[76:79], v[140:143], v[160:163], v[76:79]
	v_mfma_f32_16x16x32_f16 v[80:83], v[140:143], v[164:167], v[80:83]
	s_add_u32 m0, s28, 0x23000
	s_nop 0
	global_load_lds_dwordx4 v10, s[6:7]
	v_mfma_f32_16x16x32_f16 v[84:87], v[140:143], v[168:171], v[84:87]
	s_waitcnt lgkmcnt(11)
	v_mfma_f32_16x16x32_f16 v[88:91], v[144:147], v[156:159], v[88:91]
	v_mfma_f32_16x16x32_f16 v[92:95], v[144:147], v[160:163], v[92:95]
	v_mfma_f32_16x16x32_f16 v[96:99], v[144:147], v[164:167], v[96:99]
	v_mfma_f32_16x16x32_f16 v[100:103], v[144:147], v[168:171], v[100:103]
	s_waitcnt lgkmcnt(10)
	v_mfma_f32_16x16x32_f16 v[104:107], v[148:151], v[156:159], v[104:107]
	v_mfma_f32_16x16x32_f16 v[108:111], v[148:151], v[160:163], v[108:111]
	s_add_u32 m0, s28, 0x25000
	s_nop 0
	global_load_lds_dwordx4 v11, s[6:7]
	s_add_u32 s6, s6, s20
	s_addc_u32 s7, s7, 0
	v_mfma_f32_16x16x32_f16 v[112:115], v[148:151], v[164:167], v[112:115]
	v_mfma_f32_16x16x32_f16 v[116:119], v[148:151], v[168:171], v[116:119]
	s_waitcnt lgkmcnt(9)
	v_mfma_f32_16x16x32_f16 v[120:123], v[152:155], v[156:159], v[120:123]
	v_mfma_f32_16x16x32_f16 v[124:127], v[152:155], v[160:163], v[124:127]
	v_mfma_f32_16x16x32_f16 v[128:131], v[152:155], v[164:167], v[128:131]
	v_mfma_f32_16x16x32_f16 v[132:135], v[152:155], v[168:171], v[132:135]
	s_waitcnt vmcnt(6) lgkmcnt(0)
	s_barrier
	s_waitcnt lgkmcnt(6)
	ds_read_b128 v[136:139], v15 offset:53248
	ds_read_b128 v[156:159], v17 offset:53248
	ds_read_b128 v[160:163], v17 offset:55296
	ds_read_b128 v[164:167], v17 offset:57344
	ds_read_b128 v[168:171], v17 offset:59392
	ds_read_b128 v[140:143], v15 offset:55296
	ds_read_b128 v[144:147], v15 offset:57344
	ds_read_b128 v[148:151], v15 offset:59392
	ds_read_b128 v[152:155], v15 offset:61440
	v_mfma_f32_16x16x32_f16 v[56:59], v[172:175], v[192:195], v[56:59]
	s_add_u32 m0, s28, 0x0
	s_nop 0
	global_load_lds_dwordx4 v10, s[4:5]
	s_waitcnt lgkmcnt(15)
	v_mfma_f32_16x16x32_f16 v[60:63], v[172:175], v[196:199], v[60:63]
	s_waitcnt lgkmcnt(14)
	v_mfma_f32_16x16x32_f16 v[64:67], v[172:175], v[200:203], v[64:67]
	s_waitcnt lgkmcnt(13)
	v_mfma_f32_16x16x32_f16 v[68:71], v[172:175], v[204:207], v[68:71]
	s_waitcnt lgkmcnt(12)
	v_mfma_f32_16x16x32_f16 v[72:75], v[176:179], v[192:195], v[72:75]
	v_mfma_f32_16x16x32_f16 v[76:79], v[176:179], v[196:199], v[76:79]
	v_mfma_f32_16x16x32_f16 v[80:83], v[176:179], v[200:203], v[80:83]
	s_add_u32 m0, s28, 0x2000
	s_nop 0
	global_load_lds_dwordx4 v11, s[4:5]
	v_mfma_f32_16x16x32_f16 v[84:87], v[176:179], v[204:207], v[84:87]
	s_waitcnt lgkmcnt(11)
	v_mfma_f32_16x16x32_f16 v[88:91], v[180:183], v[192:195], v[88:91]
	v_mfma_f32_16x16x32_f16 v[92:95], v[180:183], v[196:199], v[92:95]
	v_mfma_f32_16x16x32_f16 v[96:99], v[180:183], v[200:203], v[96:99]
	v_mfma_f32_16x16x32_f16 v[100:103], v[180:183], v[204:207], v[100:103]
	s_waitcnt lgkmcnt(10)
	v_mfma_f32_16x16x32_f16 v[104:107], v[184:187], v[192:195], v[104:107]
	v_mfma_f32_16x16x32_f16 v[108:111], v[184:187], v[196:199], v[108:111]
	s_add_u32 m0, s28, 0x4000
	s_nop 0
	global_load_lds_dwordx4 v12, s[4:5]
	v_mfma_f32_16x16x32_f16 v[112:115], v[184:187], v[200:203], v[112:115]
	v_mfma_f32_16x16x32_f16 v[116:119], v[184:187], v[204:207], v[116:119]
	s_waitcnt lgkmcnt(9)
	v_mfma_f32_16x16x32_f16 v[120:123], v[188:191], v[192:195], v[120:123]
	v_mfma_f32_16x16x32_f16 v[124:127], v[188:191], v[196:199], v[124:127]
	v_mfma_f32_16x16x32_f16 v[128:131], v[188:191], v[200:203], v[128:131]
	v_mfma_f32_16x16x32_f16 v[132:135], v[188:191], v[204:207], v[132:135]
	s_waitcnt lgkmcnt(6)
	ds_read_b128 v[172:175], v16 offset:53248
	ds_read_b128 v[192:195], v18 offset:53248
	ds_read_b128 v[196:199], v18 offset:55296
	ds_read_b128 v[200:203], v18 offset:57344
	ds_read_b128 v[204:207], v18 offset:59392
	ds_read_b128 v[176:179], v16 offset:55296
	ds_read_b128 v[180:183], v16 offset:57344
	ds_read_b128 v[184:187], v16 offset:59392
	ds_read_b128 v[188:191], v16 offset:61440
	v_mfma_f32_16x16x32_f16 v[56:59], v[136:139], v[156:159], v[56:59]
	s_add_u32 m0, s28, 0x6000
	s_nop 0
	global_load_lds_dwordx4 v13, s[4:5]
	s_add_u32 s4, s4, s20
	s_addc_u32 s5, s5, 0
	s_waitcnt lgkmcnt(15)
	v_mfma_f32_16x16x32_f16 v[60:63], v[136:139], v[160:163], v[60:63]
	s_waitcnt lgkmcnt(14)
	v_mfma_f32_16x16x32_f16 v[64:67], v[136:139], v[164:167], v[64:67]
	s_waitcnt lgkmcnt(13)
	v_mfma_f32_16x16x32_f16 v[68:71], v[136:139], v[168:171], v[68:71]
	s_waitcnt lgkmcnt(12)
	v_mfma_f32_16x16x32_f16 v[72:75], v[140:143], v[156:159], v[72:75]
	v_mfma_f32_16x16x32_f16 v[76:79], v[140:143], v[160:163], v[76:79]
	v_mfma_f32_16x16x32_f16 v[80:83], v[140:143], v[164:167], v[80:83]
	s_add_u32 m0, s28, 0x9000
	s_nop 0
	global_load_lds_dwordx4 v10, s[6:7]
	v_mfma_f32_16x16x32_f16 v[84:87], v[140:143], v[168:171], v[84:87]
	s_waitcnt lgkmcnt(11)
	v_mfma_f32_16x16x32_f16 v[88:91], v[144:147], v[156:159], v[88:91]
	v_mfma_f32_16x16x32_f16 v[92:95], v[144:147], v[160:163], v[92:95]
	v_mfma_f32_16x16x32_f16 v[96:99], v[144:147], v[164:167], v[96:99]
	v_mfma_f32_16x16x32_f16 v[100:103], v[144:147], v[168:171], v[100:103]
	s_waitcnt lgkmcnt(10)
	v_mfma_f32_16x16x32_f16 v[104:107], v[148:151], v[156:159], v[104:107]
	v_mfma_f32_16x16x32_f16 v[108:111], v[148:151], v[160:163], v[108:111]
	s_add_u32 m0, s28, 0xb000
	s_nop 0
	global_load_lds_dwordx4 v11, s[6:7]
	s_add_u32 s6, s6, s20
	s_addc_u32 s7, s7, 0
	v_mfma_f32_16x16x32_f16 v[112:115], v[148:151], v[164:167], v[112:115]
	v_mfma_f32_16x16x32_f16 v[116:119], v[148:151], v[168:171], v[116:119]
	s_waitcnt lgkmcnt(9)
	v_mfma_f32_16x16x32_f16 v[120:123], v[152:155], v[156:159], v[120:123]
	v_mfma_f32_16x16x32_f16 v[124:127], v[152:155], v[160:163], v[124:127]
	v_mfma_f32_16x16x32_f16 v[128:131], v[152:155], v[164:167], v[128:131]
	v_mfma_f32_16x16x32_f16 v[132:135], v[152:155], v[168:171], v[132:135]
	s_waitcnt vmcnt(6) lgkmcnt(0)
	s_barrier
	s_waitcnt lgkmcnt(6)
	ds_read_b128 v[136:139], v19
	ds_read_b128 v[156:159], v21
	ds_read_b128 v[160:163], v21 offset:2048
	ds_read_b128 v[164:167], v21 offset:4096
	ds_read_b128 v[168:171], v21 offset:6144
	ds_read_b128 v[140:143], v19 offset:2048
	ds_read_b128 v[144:147], v19 offset:4096
	ds_read_b128 v[148:151], v19 offset:6144
	ds_read_b128 v[152:155], v19 offset:8192
	v_mfma_f32_16x16x32_f16 v[56:59], v[172:175], v[192:195], v[56:59]
	s_add_u32 m0, s28, 0xd000
	s_nop 0
	global_load_lds_dwordx4 v10, s[4:5]
	s_waitcnt lgkmcnt(15)
	v_mfma_f32_16x16x32_f16 v[60:63], v[172:175], v[196:199], v[60:63]
	s_waitcnt lgkmcnt(14)
	v_mfma_f32_16x16x32_f16 v[64:67], v[172:175], v[200:203], v[64:67]
	s_waitcnt lgkmcnt(13)
	v_mfma_f32_16x16x32_f16 v[68:71], v[172:175], v[204:207], v[68:71]
	s_waitcnt lgkmcnt(12)
	v_mfma_f32_16x16x32_f16 v[72:75], v[176:179], v[192:195], v[72:75]
	v_mfma_f32_16x16x32_f16 v[76:79], v[176:179], v[196:199], v[76:79]
	v_mfma_f32_16x16x32_f16 v[80:83], v[176:179], v[200:203], v[80:83]
	s_add_u32 m0, s28, 0xf000
	s_nop 0
	global_load_lds_dwordx4 v11, s[4:5]
	v_mfma_f32_16x16x32_f16 v[84:87], v[176:179], v[204:207], v[84:87]
	s_waitcnt lgkmcnt(11)
	v_mfma_f32_16x16x32_f16 v[88:91], v[180:183], v[192:195], v[88:91]
	v_mfma_f32_16x16x32_f16 v[92:95], v[180:183], v[196:199], v[92:95]
	v_mfma_f32_16x16x32_f16 v[96:99], v[180:183], v[200:203], v[96:99]
	v_mfma_f32_16x16x32_f16 v[100:103], v[180:183], v[204:207], v[100:103]
	s_waitcnt lgkmcnt(10)
	v_mfma_f32_16x16x32_f16 v[104:107], v[184:187], v[192:195], v[104:107]
	v_mfma_f32_16x16x32_f16 v[108:111], v[184:187], v[196:199], v[108:111]
	s_add_u32 m0, s28, 0x11000
	s_nop 0
	global_load_lds_dwordx4 v12, s[4:5]
	v_mfma_f32_16x16x32_f16 v[112:115], v[184:187], v[200:203], v[112:115]
	v_mfma_f32_16x16x32_f16 v[116:119], v[184:187], v[204:207], v[116:119]
	s_waitcnt lgkmcnt(9)
	v_mfma_f32_16x16x32_f16 v[120:123], v[188:191], v[192:195], v[120:123]
	v_mfma_f32_16x16x32_f16 v[124:127], v[188:191], v[196:199], v[124:127]
	v_mfma_f32_16x16x32_f16 v[128:131], v[188:191], v[200:203], v[128:131]
	v_mfma_f32_16x16x32_f16 v[132:135], v[188:191], v[204:207], v[132:135]
	s_waitcnt lgkmcnt(6)
	ds_read_b128 v[172:175], v20
	ds_read_b128 v[192:195], v22
	ds_read_b128 v[196:199], v22 offset:2048
	ds_read_b128 v[200:203], v22 offset:4096
	ds_read_b128 v[204:207], v22 offset:6144
	ds_read_b128 v[176:179], v20 offset:2048
	ds_read_b128 v[180:183], v20 offset:4096
	ds_read_b128 v[184:187], v20 offset:6144
	ds_read_b128 v[188:191], v20 offset:8192
	v_mfma_f32_16x16x32_f16 v[56:59], v[136:139], v[156:159], v[56:59]
	s_add_u32 m0, s28, 0x13000
	s_nop 0
	global_load_lds_dwordx4 v13, s[4:5]
	s_add_u32 s4, s4, s20
	s_addc_u32 s5, s5, 0
	s_waitcnt lgkmcnt(15)
	v_mfma_f32_16x16x32_f16 v[60:63], v[136:139], v[160:163], v[60:63]
	s_waitcnt lgkmcnt(14)
	v_mfma_f32_16x16x32_f16 v[64:67], v[136:139], v[164:167], v[64:67]
	s_waitcnt lgkmcnt(13)
	v_mfma_f32_16x16x32_f16 v[68:71], v[136:139], v[168:171], v[68:71]
	s_waitcnt lgkmcnt(12)
	v_mfma_f32_16x16x32_f16 v[72:75], v[140:143], v[156:159], v[72:75]
	v_mfma_f32_16x16x32_f16 v[76:79], v[140:143], v[160:163], v[76:79]
	v_mfma_f32_16x16x32_f16 v[80:83], v[140:143], v[164:167], v[80:83]
	s_add_u32 m0, s28, 0x16000
	s_nop 0
	global_load_lds_dwordx4 v10, s[6:7]
	v_mfma_f32_16x16x32_f16 v[84:87], v[140:143], v[168:171], v[84:87]
	s_waitcnt lgkmcnt(11)
	v_mfma_f32_16x16x32_f16 v[88:91], v[144:147], v[156:159], v[88:91]
	v_mfma_f32_16x16x32_f16 v[92:95], v[144:147], v[160:163], v[92:95]
	v_mfma_f32_16x16x32_f16 v[96:99], v[144:147], v[164:167], v[96:99]
	v_mfma_f32_16x16x32_f16 v[100:103], v[144:147], v[168:171], v[100:103]
	s_waitcnt lgkmcnt(10)
	v_mfma_f32_16x16x32_f16 v[104:107], v[148:151], v[156:159], v[104:107]
	v_mfma_f32_16x16x32_f16 v[108:111], v[148:151], v[160:163], v[108:111]
	s_add_u32 m0, s28, 0x18000
	s_nop 0
	global_load_lds_dwordx4 v11, s[6:7]
	s_add_u32 s6, s6, s20
	s_addc_u32 s7, s7, 0
	v_mfma_f32_16x16x32_f16 v[112:115], v[148:151], v[164:167], v[112:115]
	v_mfma_f32_16x16x32_f16 v[116:119], v[148:151], v[168:171], v[116:119]
	s_waitcnt lgkmcnt(9)
	v_mfma_f32_16x16x32_f16 v[120:123], v[152:155], v[156:159], v[120:123]
	v_mfma_f32_16x16x32_f16 v[124:127], v[152:155], v[160:163], v[124:127]
	v_mfma_f32_16x16x32_f16 v[128:131], v[152:155], v[164:167], v[128:131]
	v_mfma_f32_16x16x32_f16 v[132:135], v[152:155], v[168:171], v[132:135]
	s_waitcnt vmcnt(6) lgkmcnt(0)
	s_barrier
	s_waitcnt lgkmcnt(6)
	ds_read_b128 v[136:139], v15
	ds_read_b128 v[156:159], v17
	ds_read_b128 v[160:163], v17 offset:2048
	ds_read_b128 v[164:167], v17 offset:4096
	ds_read_b128 v[168:171], v17 offset:6144
	ds_read_b128 v[140:143], v15 offset:2048
	ds_read_b128 v[144:147], v15 offset:4096
	ds_read_b128 v[148:151], v15 offset:6144
	ds_read_b128 v[152:155], v15 offset:8192
	v_mfma_f32_16x16x32_f16 v[56:59], v[172:175], v[192:195], v[56:59]
	s_add_u32 m0, s28, 0x1a000
	s_nop 0
	global_load_lds_dwordx4 v10, s[4:5]
	s_waitcnt lgkmcnt(15)
	v_mfma_f32_16x16x32_f16 v[60:63], v[172:175], v[196:199], v[60:63]
	s_waitcnt lgkmcnt(14)
	v_mfma_f32_16x16x32_f16 v[64:67], v[172:175], v[200:203], v[64:67]
	s_waitcnt lgkmcnt(13)
	v_mfma_f32_16x16x32_f16 v[68:71], v[172:175], v[204:207], v[68:71]
	s_waitcnt lgkmcnt(12)
	v_mfma_f32_16x16x32_f16 v[72:75], v[176:179], v[192:195], v[72:75]
	v_mfma_f32_16x16x32_f16 v[76:79], v[176:179], v[196:199], v[76:79]
	v_mfma_f32_16x16x32_f16 v[80:83], v[176:179], v[200:203], v[80:83]
	s_add_u32 m0, s28, 0x1c000
	s_nop 0
	global_load_lds_dwordx4 v11, s[4:5]
	v_mfma_f32_16x16x32_f16 v[84:87], v[176:179], v[204:207], v[84:87]
	s_waitcnt lgkmcnt(11)
	v_mfma_f32_16x16x32_f16 v[88:91], v[180:183], v[192:195], v[88:91]
	v_mfma_f32_16x16x32_f16 v[92:95], v[180:183], v[196:199], v[92:95]
	v_mfma_f32_16x16x32_f16 v[96:99], v[180:183], v[200:203], v[96:99]
	v_mfma_f32_16x16x32_f16 v[100:103], v[180:183], v[204:207], v[100:103]
	s_waitcnt lgkmcnt(10)
	v_mfma_f32_16x16x32_f16 v[104:107], v[184:187], v[192:195], v[104:107]
	v_mfma_f32_16x16x32_f16 v[108:111], v[184:187], v[196:199], v[108:111]
	s_add_u32 m0, s28, 0x1e000
	s_nop 0
	global_load_lds_dwordx4 v12, s[4:5]
	v_mfma_f32_16x16x32_f16 v[112:115], v[184:187], v[200:203], v[112:115]
	v_mfma_f32_16x16x32_f16 v[116:119], v[184:187], v[204:207], v[116:119]
	s_waitcnt lgkmcnt(9)
	v_mfma_f32_16x16x32_f16 v[120:123], v[188:191], v[192:195], v[120:123]
	v_mfma_f32_16x16x32_f16 v[124:127], v[188:191], v[196:199], v[124:127]
	v_mfma_f32_16x16x32_f16 v[128:131], v[188:191], v[200:203], v[128:131]
	v_mfma_f32_16x16x32_f16 v[132:135], v[188:191], v[204:207], v[132:135]
	s_waitcnt lgkmcnt(6)
	ds_read_b128 v[172:175], v16
	ds_read_b128 v[192:195], v18
	ds_read_b128 v[196:199], v18 offset:2048
	ds_read_b128 v[200:203], v18 offset:4096
	ds_read_b128 v[204:207], v18 offset:6144
	ds_read_b128 v[176:179], v16 offset:2048
	ds_read_b128 v[180:183], v16 offset:4096
	ds_read_b128 v[184:187], v16 offset:6144
	ds_read_b128 v[188:191], v16 offset:8192
	v_mfma_f32_16x16x32_f16 v[56:59], v[136:139], v[156:159], v[56:59]
	s_add_u32 m0, s28, 0x20000
	s_nop 0
	global_load_lds_dwordx4 v13, s[4:5]
	s_add_u32 s4, s4, s20
	s_addc_u32 s5, s5, 0
	s_waitcnt lgkmcnt(15)
	v_mfma_f32_16x16x32_f16 v[60:63], v[136:139], v[160:163], v[60:63]
	s_waitcnt lgkmcnt(14)
	v_mfma_f32_16x16x32_f16 v[64:67], v[136:139], v[164:167], v[64:67]
	s_waitcnt lgkmcnt(13)
	v_mfma_f32_16x16x32_f16 v[68:71], v[136:139], v[168:171], v[68:71]
	s_waitcnt lgkmcnt(12)
	v_mfma_f32_16x16x32_f16 v[72:75], v[140:143], v[156:159], v[72:75]
	v_mfma_f32_16x16x32_f16 v[76:79], v[140:143], v[160:163], v[76:79]
	v_mfma_f32_16x16x32_f16 v[80:83], v[140:143], v[164:167], v[80:83]
	s_add_u32 m0, s28, 0x23000
	s_nop 0
	global_load_lds_dwordx4 v10, s[6:7]
	v_mfma_f32_16x16x32_f16 v[84:87], v[140:143], v[168:171], v[84:87]
	s_waitcnt lgkmcnt(11)
	v_mfma_f32_16x16x32_f16 v[88:91], v[144:147], v[156:159], v[88:91]
	v_mfma_f32_16x16x32_f16 v[92:95], v[144:147], v[160:163], v[92:95]
	v_mfma_f32_16x16x32_f16 v[96:99], v[144:147], v[164:167], v[96:99]
	v_mfma_f32_16x16x32_f16 v[100:103], v[144:147], v[168:171], v[100:103]
	s_waitcnt lgkmcnt(10)
	v_mfma_f32_16x16x32_f16 v[104:107], v[148:151], v[156:159], v[104:107]
	v_mfma_f32_16x16x32_f16 v[108:111], v[148:151], v[160:163], v[108:111]
	s_add_u32 m0, s28, 0x25000
	s_nop 0
	global_load_lds_dwordx4 v11, s[6:7]
	s_add_u32 s6, s6, s20
	s_addc_u32 s7, s7, 0
	v_mfma_f32_16x16x32_f16 v[112:115], v[148:151], v[164:167], v[112:115]
	v_mfma_f32_16x16x32_f16 v[116:119], v[148:151], v[168:171], v[116:119]
	s_waitcnt lgkmcnt(9)
	v_mfma_f32_16x16x32_f16 v[120:123], v[152:155], v[156:159], v[120:123]
	v_mfma_f32_16x16x32_f16 v[124:127], v[152:155], v[160:163], v[124:127]
	v_mfma_f32_16x16x32_f16 v[128:131], v[152:155], v[164:167], v[128:131]
	v_mfma_f32_16x16x32_f16 v[132:135], v[152:155], v[168:171], v[132:135]
	s_waitcnt vmcnt(6) lgkmcnt(0)
	s_barrier
	s_waitcnt lgkmcnt(6)
	ds_read_b128 v[136:139], v15 offset:53248
	ds_read_b128 v[156:159], v17 offset:53248
	ds_read_b128 v[160:163], v17 offset:55296
	ds_read_b128 v[164:167], v17 offset:57344
	ds_read_b128 v[168:171], v17 offset:59392
	ds_read_b128 v[140:143], v15 offset:55296
	ds_read_b128 v[144:147], v15 offset:57344
	ds_read_b128 v[148:151], v15 offset:59392
	ds_read_b128 v[152:155], v15 offset:61440
	v_mfma_f32_16x16x32_f16 v[56:59], v[172:175], v[192:195], v[56:59]
	s_add_u32 m0, s28, 0x0
	s_nop 0
	global_load_lds_dwordx4 v10, s[4:5]
	s_waitcnt lgkmcnt(15)
	v_mfma_f32_16x16x32_f16 v[60:63], v[172:175], v[196:199], v[60:63]
	s_waitcnt lgkmcnt(14)
	v_mfma_f32_16x16x32_f16 v[64:67], v[172:175], v[200:203], v[64:67]
	s_waitcnt lgkmcnt(13)
	v_mfma_f32_16x16x32_f16 v[68:71], v[172:175], v[204:207], v[68:71]
	s_waitcnt lgkmcnt(12)
	v_mfma_f32_16x16x32_f16 v[72:75], v[176:179], v[192:195], v[72:75]
	v_mfma_f32_16x16x32_f16 v[76:79], v[176:179], v[196:199], v[76:79]
	v_mfma_f32_16x16x32_f16 v[80:83], v[176:179], v[200:203], v[80:83]
	s_add_u32 m0, s28, 0x2000
	s_nop 0
	global_load_lds_dwordx4 v11, s[4:5]
	v_mfma_f32_16x16x32_f16 v[84:87], v[176:179], v[204:207], v[84:87]
	s_waitcnt lgkmcnt(11)
	v_mfma_f32_16x16x32_f16 v[88:91], v[180:183], v[192:195], v[88:91]
	v_mfma_f32_16x16x32_f16 v[92:95], v[180:183], v[196:199], v[92:95]
	v_mfma_f32_16x16x32_f16 v[96:99], v[180:183], v[200:203], v[96:99]
	v_mfma_f32_16x16x32_f16 v[100:103], v[180:183], v[204:207], v[100:103]
	s_waitcnt lgkmcnt(10)
	v_mfma_f32_16x16x32_f16 v[104:107], v[184:187], v[192:195], v[104:107]
	v_mfma_f32_16x16x32_f16 v[108:111], v[184:187], v[196:199], v[108:111]
	s_add_u32 m0, s28, 0x4000
	s_nop 0
	global_load_lds_dwordx4 v12, s[4:5]
	v_mfma_f32_16x16x32_f16 v[112:115], v[184:187], v[200:203], v[112:115]
	v_mfma_f32_16x16x32_f16 v[116:119], v[184:187], v[204:207], v[116:119]
	s_waitcnt lgkmcnt(9)
	v_mfma_f32_16x16x32_f16 v[120:123], v[188:191], v[192:195], v[120:123]
	v_mfma_f32_16x16x32_f16 v[124:127], v[188:191], v[196:199], v[124:127]
	v_mfma_f32_16x16x32_f16 v[128:131], v[188:191], v[200:203], v[128:131]
	v_mfma_f32_16x16x32_f16 v[132:135], v[188:191], v[204:207], v[132:135]
	s_waitcnt lgkmcnt(6)
	ds_read_b128 v[172:175], v16 offset:53248
	ds_read_b128 v[192:195], v18 offset:53248
	ds_read_b128 v[196:199], v18 offset:55296
	ds_read_b128 v[200:203], v18 offset:57344
	ds_read_b128 v[204:207], v18 offset:59392
	ds_read_b128 v[176:179], v16 offset:55296
	ds_read_b128 v[180:183], v16 offset:57344
	ds_read_b128 v[184:187], v16 offset:59392
	ds_read_b128 v[188:191], v16 offset:61440
	v_mfma_f32_16x16x32_f16 v[56:59], v[136:139], v[156:159], v[56:59]
	s_add_u32 m0, s28, 0x6000
	s_nop 0
	global_load_lds_dwordx4 v13, s[4:5]
	s_add_u32 s4, s4, s20
	s_addc_u32 s5, s5, 0
	s_waitcnt lgkmcnt(15)
	v_mfma_f32_16x16x32_f16 v[60:63], v[136:139], v[160:163], v[60:63]
	s_waitcnt lgkmcnt(14)
	v_mfma_f32_16x16x32_f16 v[64:67], v[136:139], v[164:167], v[64:67]
	s_waitcnt lgkmcnt(13)
	v_mfma_f32_16x16x32_f16 v[68:71], v[136:139], v[168:171], v[68:71]
	s_waitcnt lgkmcnt(12)
	v_mfma_f32_16x16x32_f16 v[72:75], v[140:143], v[156:159], v[72:75]
	v_mfma_f32_16x16x32_f16 v[76:79], v[140:143], v[160:163], v[76:79]
	v_mfma_f32_16x16x32_f16 v[80:83], v[140:143], v[164:167], v[80:83]
	s_add_u32 m0, s28, 0x9000
	s_nop 0
	global_load_lds_dwordx4 v10, s[6:7]
	v_mfma_f32_16x16x32_f16 v[84:87], v[140:143], v[168:171], v[84:87]
	s_waitcnt lgkmcnt(11)
	v_mfma_f32_16x16x32_f16 v[88:91], v[144:147], v[156:159], v[88:91]
	v_mfma_f32_16x16x32_f16 v[92:95], v[144:147], v[160:163], v[92:95]
	v_mfma_f32_16x16x32_f16 v[96:99], v[144:147], v[164:167], v[96:99]
	v_mfma_f32_16x16x32_f16 v[100:103], v[144:147], v[168:171], v[100:103]
	s_waitcnt lgkmcnt(10)
	v_mfma_f32_16x16x32_f16 v[104:107], v[148:151], v[156:159], v[104:107]
	v_mfma_f32_16x16x32_f16 v[108:111], v[148:151], v[160:163], v[108:111]
	s_add_u32 m0, s28, 0xb000
	s_nop 0
	global_load_lds_dwordx4 v11, s[6:7]
	s_add_u32 s6, s6, s20
	s_addc_u32 s7, s7, 0
	v_mfma_f32_16x16x32_f16 v[112:115], v[148:151], v[164:167], v[112:115]
	v_mfma_f32_16x16x32_f16 v[116:119], v[148:151], v[168:171], v[116:119]
	s_waitcnt lgkmcnt(9)
	v_mfma_f32_16x16x32_f16 v[120:123], v[152:155], v[156:159], v[120:123]
	v_mfma_f32_16x16x32_f16 v[124:127], v[152:155], v[160:163], v[124:127]
	v_mfma_f32_16x16x32_f16 v[128:131], v[152:155], v[164:167], v[128:131]
	v_mfma_f32_16x16x32_f16 v[132:135], v[152:155], v[168:171], v[132:135]
	s_waitcnt vmcnt(6) lgkmcnt(0)
	s_barrier
	s_waitcnt lgkmcnt(6)
	ds_read_b128 v[136:139], v19
	ds_read_b128 v[156:159], v21
	ds_read_b128 v[160:163], v21 offset:2048
	ds_read_b128 v[164:167], v21 offset:4096
	ds_read_b128 v[168:171], v21 offset:6144
	ds_read_b128 v[140:143], v19 offset:2048
	ds_read_b128 v[144:147], v19 offset:4096
	ds_read_b128 v[148:151], v19 offset:6144
	ds_read_b128 v[152:155], v19 offset:8192
	v_mfma_f32_16x16x32_f16 v[56:59], v[172:175], v[192:195], v[56:59]
	s_add_u32 m0, s28, 0xd000
	s_nop 0
	global_load_lds_dwordx4 v10, s[4:5]
	s_waitcnt lgkmcnt(15)
	v_mfma_f32_16x16x32_f16 v[60:63], v[172:175], v[196:199], v[60:63]
	s_waitcnt lgkmcnt(14)
	v_mfma_f32_16x16x32_f16 v[64:67], v[172:175], v[200:203], v[64:67]
	s_waitcnt lgkmcnt(13)
	v_mfma_f32_16x16x32_f16 v[68:71], v[172:175], v[204:207], v[68:71]
	s_waitcnt lgkmcnt(12)
	v_mfma_f32_16x16x32_f16 v[72:75], v[176:179], v[192:195], v[72:75]
	v_mfma_f32_16x16x32_f16 v[76:79], v[176:179], v[196:199], v[76:79]
	v_mfma_f32_16x16x32_f16 v[80:83], v[176:179], v[200:203], v[80:83]
	s_add_u32 m0, s28, 0xf000
	s_nop 0
	global_load_lds_dwordx4 v11, s[4:5]
	v_mfma_f32_16x16x32_f16 v[84:87], v[176:179], v[204:207], v[84:87]
	s_waitcnt lgkmcnt(11)
	v_mfma_f32_16x16x32_f16 v[88:91], v[180:183], v[192:195], v[88:91]
	v_mfma_f32_16x16x32_f16 v[92:95], v[180:183], v[196:199], v[92:95]
	v_mfma_f32_16x16x32_f16 v[96:99], v[180:183], v[200:203], v[96:99]
	v_mfma_f32_16x16x32_f16 v[100:103], v[180:183], v[204:207], v[100:103]
	s_waitcnt lgkmcnt(10)
	v_mfma_f32_16x16x32_f16 v[104:107], v[184:187], v[192:195], v[104:107]
	v_mfma_f32_16x16x32_f16 v[108:111], v[184:187], v[196:199], v[108:111]
	s_add_u32 m0, s28, 0x11000
	s_nop 0
	global_load_lds_dwordx4 v12, s[4:5]
	v_mfma_f32_16x16x32_f16 v[112:115], v[184:187], v[200:203], v[112:115]
	v_mfma_f32_16x16x32_f16 v[116:119], v[184:187], v[204:207], v[116:119]
	s_waitcnt lgkmcnt(9)
	v_mfma_f32_16x16x32_f16 v[120:123], v[188:191], v[192:195], v[120:123]
	v_mfma_f32_16x16x32_f16 v[124:127], v[188:191], v[196:199], v[124:127]
	v_mfma_f32_16x16x32_f16 v[128:131], v[188:191], v[200:203], v[128:131]
	v_mfma_f32_16x16x32_f16 v[132:135], v[188:191], v[204:207], v[132:135]
	s_waitcnt lgkmcnt(6)
	ds_read_b128 v[172:175], v20
	ds_read_b128 v[192:195], v22
	ds_read_b128 v[196:199], v22 offset:2048
	ds_read_b128 v[200:203], v22 offset:4096
	ds_read_b128 v[204:207], v22 offset:6144
	ds_read_b128 v[176:179], v20 offset:2048
	ds_read_b128 v[180:183], v20 offset:4096
	ds_read_b128 v[184:187], v20 offset:6144
	ds_read_b128 v[188:191], v20 offset:8192
	v_mfma_f32_16x16x32_f16 v[56:59], v[136:139], v[156:159], v[56:59]
	s_add_u32 m0, s28, 0x13000
	s_nop 0
	global_load_lds_dwordx4 v13, s[4:5]
	s_add_u32 s4, s4, s20
	s_addc_u32 s5, s5, 0
	s_waitcnt lgkmcnt(15)
	v_mfma_f32_16x16x32_f16 v[60:63], v[136:139], v[160:163], v[60:63]
	s_waitcnt lgkmcnt(14)
	v_mfma_f32_16x16x32_f16 v[64:67], v[136:139], v[164:167], v[64:67]
	s_waitcnt lgkmcnt(13)
	v_mfma_f32_16x16x32_f16 v[68:71], v[136:139], v[168:171], v[68:71]
	s_waitcnt lgkmcnt(12)
	v_mfma_f32_16x16x32_f16 v[72:75], v[140:143], v[156:159], v[72:75]
	v_mfma_f32_16x16x32_f16 v[76:79], v[140:143], v[160:163], v[76:79]
	v_mfma_f32_16x16x32_f16 v[80:83], v[140:143], v[164:167], v[80:83]
	s_add_u32 m0, s28, 0x16000
	s_nop 0
	global_load_lds_dwordx4 v10, s[6:7]
	v_mfma_f32_16x16x32_f16 v[84:87], v[140:143], v[168:171], v[84:87]
	s_waitcnt lgkmcnt(11)
	v_mfma_f32_16x16x32_f16 v[88:91], v[144:147], v[156:159], v[88:91]
	v_mfma_f32_16x16x32_f16 v[92:95], v[144:147], v[160:163], v[92:95]
	v_mfma_f32_16x16x32_f16 v[96:99], v[144:147], v[164:167], v[96:99]
	v_mfma_f32_16x16x32_f16 v[100:103], v[144:147], v[168:171], v[100:103]
	s_waitcnt lgkmcnt(10)
	v_mfma_f32_16x16x32_f16 v[104:107], v[148:151], v[156:159], v[104:107]
	v_mfma_f32_16x16x32_f16 v[108:111], v[148:151], v[160:163], v[108:111]
	s_add_u32 m0, s28, 0x18000
	s_nop 0
	global_load_lds_dwordx4 v11, s[6:7]
	s_add_u32 s6, s6, s20
	s_addc_u32 s7, s7, 0
	v_mfma_f32_16x16x32_f16 v[112:115], v[148:151], v[164:167], v[112:115]
	v_mfma_f32_16x16x32_f16 v[116:119], v[148:151], v[168:171], v[116:119]
	s_waitcnt lgkmcnt(9)
	v_mfma_f32_16x16x32_f16 v[120:123], v[152:155], v[156:159], v[120:123]
	v_mfma_f32_16x16x32_f16 v[124:127], v[152:155], v[160:163], v[124:127]
	v_mfma_f32_16x16x32_f16 v[128:131], v[152:155], v[164:167], v[128:131]
	v_mfma_f32_16x16x32_f16 v[132:135], v[152:155], v[168:171], v[132:135]
	s_waitcnt vmcnt(6) lgkmcnt(0)
	s_barrier
	s_waitcnt lgkmcnt(6)
	ds_read_b128 v[136:139], v15
	ds_read_b128 v[156:159], v17
	ds_read_b128 v[160:163], v17 offset:2048
	ds_read_b128 v[164:167], v17 offset:4096
	ds_read_b128 v[168:171], v17 offset:6144
	ds_read_b128 v[140:143], v15 offset:2048
	ds_read_b128 v[144:147], v15 offset:4096
	ds_read_b128 v[148:151], v15 offset:6144
	ds_read_b128 v[152:155], v15 offset:8192
	v_mfma_f32_16x16x32_f16 v[56:59], v[172:175], v[192:195], v[56:59]
	s_add_u32 m0, s28, 0x1a000
	s_nop 0
	global_load_lds_dwordx4 v10, s[4:5]
	s_waitcnt lgkmcnt(15)
	v_mfma_f32_16x16x32_f16 v[60:63], v[172:175], v[196:199], v[60:63]
	s_waitcnt lgkmcnt(14)
	v_mfma_f32_16x16x32_f16 v[64:67], v[172:175], v[200:203], v[64:67]
	s_waitcnt lgkmcnt(13)
	v_mfma_f32_16x16x32_f16 v[68:71], v[172:175], v[204:207], v[68:71]
	s_waitcnt lgkmcnt(12)
	v_mfma_f32_16x16x32_f16 v[72:75], v[176:179], v[192:195], v[72:75]
	v_mfma_f32_16x16x32_f16 v[76:79], v[176:179], v[196:199], v[76:79]
	v_mfma_f32_16x16x32_f16 v[80:83], v[176:179], v[200:203], v[80:83]
	s_add_u32 m0, s28, 0x1c000
	s_nop 0
	global_load_lds_dwordx4 v11, s[4:5]
	v_mfma_f32_16x16x32_f16 v[84:87], v[176:179], v[204:207], v[84:87]
	s_waitcnt lgkmcnt(11)
	v_mfma_f32_16x16x32_f16 v[88:91], v[180:183], v[192:195], v[88:91]
	v_mfma_f32_16x16x32_f16 v[92:95], v[180:183], v[196:199], v[92:95]
	v_mfma_f32_16x16x32_f16 v[96:99], v[180:183], v[200:203], v[96:99]
	v_mfma_f32_16x16x32_f16 v[100:103], v[180:183], v[204:207], v[100:103]
	s_waitcnt lgkmcnt(10)
	v_mfma_f32_16x16x32_f16 v[104:107], v[184:187], v[192:195], v[104:107]
	v_mfma_f32_16x16x32_f16 v[108:111], v[184:187], v[196:199], v[108:111]
	s_add_u32 m0, s28, 0x1e000
	s_nop 0
	global_load_lds_dwordx4 v12, s[4:5]
	v_mfma_f32_16x16x32_f16 v[112:115], v[184:187], v[200:203], v[112:115]
	v_mfma_f32_16x16x32_f16 v[116:119], v[184:187], v[204:207], v[116:119]
	s_waitcnt lgkmcnt(9)
	v_mfma_f32_16x16x32_f16 v[120:123], v[188:191], v[192:195], v[120:123]
	v_mfma_f32_16x16x32_f16 v[124:127], v[188:191], v[196:199], v[124:127]
	v_mfma_f32_16x16x32_f16 v[128:131], v[188:191], v[200:203], v[128:131]
	v_mfma_f32_16x16x32_f16 v[132:135], v[188:191], v[204:207], v[132:135]
	s_waitcnt lgkmcnt(6)
	ds_read_b128 v[172:175], v16
	ds_read_b128 v[192:195], v18
	ds_read_b128 v[196:199], v18 offset:2048
	ds_read_b128 v[200:203], v18 offset:4096
	ds_read_b128 v[204:207], v18 offset:6144
	ds_read_b128 v[176:179], v16 offset:2048
	ds_read_b128 v[180:183], v16 offset:4096
	ds_read_b128 v[184:187], v16 offset:6144
	ds_read_b128 v[188:191], v16 offset:8192
	v_mfma_f32_16x16x32_f16 v[56:59], v[136:139], v[156:159], v[56:59]
	s_add_u32 m0, s28, 0x20000
	s_nop 0
	global_load_lds_dwordx4 v13, s[4:5]
	s_add_u32 s4, s4, s20
	s_addc_u32 s5, s5, 0
	s_waitcnt lgkmcnt(15)
	v_mfma_f32_16x16x32_f16 v[60:63], v[136:139], v[160:163], v[60:63]
	s_waitcnt lgkmcnt(14)
	v_mfma_f32_16x16x32_f16 v[64:67], v[136:139], v[164:167], v[64:67]
	s_waitcnt lgkmcnt(13)
	v_mfma_f32_16x16x32_f16 v[68:71], v[136:139], v[168:171], v[68:71]
	s_waitcnt lgkmcnt(12)
	v_mfma_f32_16x16x32_f16 v[72:75], v[140:143], v[156:159], v[72:75]
	v_mfma_f32_16x16x32_f16 v[76:79], v[140:143], v[160:163], v[76:79]
	v_mfma_f32_16x16x32_f16 v[80:83], v[140:143], v[164:167], v[80:83]
	s_add_u32 m0, s28, 0x23000
	s_nop 0
	global_load_lds_dwordx4 v10, s[6:7]
	v_mfma_f32_16x16x32_f16 v[84:87], v[140:143], v[168:171], v[84:87]
	s_waitcnt lgkmcnt(11)
	v_mfma_f32_16x16x32_f16 v[88:91], v[144:147], v[156:159], v[88:91]
	v_mfma_f32_16x16x32_f16 v[92:95], v[144:147], v[160:163], v[92:95]
	v_mfma_f32_16x16x32_f16 v[96:99], v[144:147], v[164:167], v[96:99]
	v_mfma_f32_16x16x32_f16 v[100:103], v[144:147], v[168:171], v[100:103]
	s_waitcnt lgkmcnt(10)
	v_mfma_f32_16x16x32_f16 v[104:107], v[148:151], v[156:159], v[104:107]
	v_mfma_f32_16x16x32_f16 v[108:111], v[148:151], v[160:163], v[108:111]
	s_add_u32 m0, s28, 0x25000
	s_nop 0
	global_load_lds_dwordx4 v11, s[6:7]
	s_add_u32 s6, s6, s20
	s_addc_u32 s7, s7, 0
	v_mfma_f32_16x16x32_f16 v[112:115], v[148:151], v[164:167], v[112:115]
	v_mfma_f32_16x16x32_f16 v[116:119], v[148:151], v[168:171], v[116:119]
	s_waitcnt lgkmcnt(9)
	v_mfma_f32_16x16x32_f16 v[120:123], v[152:155], v[156:159], v[120:123]
	v_mfma_f32_16x16x32_f16 v[124:127], v[152:155], v[160:163], v[124:127]
	v_mfma_f32_16x16x32_f16 v[128:131], v[152:155], v[164:167], v[128:131]
	v_mfma_f32_16x16x32_f16 v[132:135], v[152:155], v[168:171], v[132:135]
	s_waitcnt vmcnt(6) lgkmcnt(0)
	s_barrier
	s_waitcnt lgkmcnt(6)
	ds_read_b128 v[136:139], v15 offset:53248
	ds_read_b128 v[156:159], v17 offset:53248
	ds_read_b128 v[160:163], v17 offset:55296
	ds_read_b128 v[164:167], v17 offset:57344
	ds_read_b128 v[168:171], v17 offset:59392
	ds_read_b128 v[140:143], v15 offset:55296
	ds_read_b128 v[144:147], v15 offset:57344
	ds_read_b128 v[148:151], v15 offset:59392
	ds_read_b128 v[152:155], v15 offset:61440
	v_mfma_f32_16x16x32_f16 v[56:59], v[172:175], v[192:195], v[56:59]
	s_add_u32 m0, s28, 0x0
	s_nop 0
	global_load_lds_dwordx4 v10, s[4:5]
	s_waitcnt lgkmcnt(15)
	v_mfma_f32_16x16x32_f16 v[60:63], v[172:175], v[196:199], v[60:63]
	s_waitcnt lgkmcnt(14)
	v_mfma_f32_16x16x32_f16 v[64:67], v[172:175], v[200:203], v[64:67]
	s_waitcnt lgkmcnt(13)
	v_mfma_f32_16x16x32_f16 v[68:71], v[172:175], v[204:207], v[68:71]
	s_waitcnt lgkmcnt(12)
	v_mfma_f32_16x16x32_f16 v[72:75], v[176:179], v[192:195], v[72:75]
	v_mfma_f32_16x16x32_f16 v[76:79], v[176:179], v[196:199], v[76:79]
	v_mfma_f32_16x16x32_f16 v[80:83], v[176:179], v[200:203], v[80:83]
	s_add_u32 m0, s28, 0x2000
	s_nop 0
	global_load_lds_dwordx4 v11, s[4:5]
	v_mfma_f32_16x16x32_f16 v[84:87], v[176:179], v[204:207], v[84:87]
	s_waitcnt lgkmcnt(11)
	v_mfma_f32_16x16x32_f16 v[88:91], v[180:183], v[192:195], v[88:91]
	v_mfma_f32_16x16x32_f16 v[92:95], v[180:183], v[196:199], v[92:95]
	v_mfma_f32_16x16x32_f16 v[96:99], v[180:183], v[200:203], v[96:99]
	v_mfma_f32_16x16x32_f16 v[100:103], v[180:183], v[204:207], v[100:103]
	s_waitcnt lgkmcnt(10)
	v_mfma_f32_16x16x32_f16 v[104:107], v[184:187], v[192:195], v[104:107]
	v_mfma_f32_16x16x32_f16 v[108:111], v[184:187], v[196:199], v[108:111]
	s_add_u32 m0, s28, 0x4000
	s_nop 0
	global_load_lds_dwordx4 v12, s[4:5]
	v_mfma_f32_16x16x32_f16 v[112:115], v[184:187], v[200:203], v[112:115]
	v_mfma_f32_16x16x32_f16 v[116:119], v[184:187], v[204:207], v[116:119]
	s_waitcnt lgkmcnt(9)
	v_mfma_f32_16x16x32_f16 v[120:123], v[188:191], v[192:195], v[120:123]
	v_mfma_f32_16x16x32_f16 v[124:127], v[188:191], v[196:199], v[124:127]
	v_mfma_f32_16x16x32_f16 v[128:131], v[188:191], v[200:203], v[128:131]
	v_mfma_f32_16x16x32_f16 v[132:135], v[188:191], v[204:207], v[132:135]
	s_waitcnt lgkmcnt(6)
	ds_read_b128 v[172:175], v16 offset:53248
	ds_read_b128 v[192:195], v18 offset:53248
	ds_read_b128 v[196:199], v18 offset:55296
	ds_read_b128 v[200:203], v18 offset:57344
	ds_read_b128 v[204:207], v18 offset:59392
	ds_read_b128 v[176:179], v16 offset:55296
	ds_read_b128 v[180:183], v16 offset:57344
	ds_read_b128 v[184:187], v16 offset:59392
	ds_read_b128 v[188:191], v16 offset:61440
	v_mfma_f32_16x16x32_f16 v[56:59], v[136:139], v[156:159], v[56:59]
	s_add_u32 m0, s28, 0x6000
	s_nop 0
	global_load_lds_dwordx4 v13, s[4:5]
	s_add_u32 s4, s4, s20
	s_addc_u32 s5, s5, 0
	s_waitcnt lgkmcnt(15)
	v_mfma_f32_16x16x32_f16 v[60:63], v[136:139], v[160:163], v[60:63]
	s_waitcnt lgkmcnt(14)
	v_mfma_f32_16x16x32_f16 v[64:67], v[136:139], v[164:167], v[64:67]
	s_waitcnt lgkmcnt(13)
	v_mfma_f32_16x16x32_f16 v[68:71], v[136:139], v[168:171], v[68:71]
	s_waitcnt lgkmcnt(12)
	v_mfma_f32_16x16x32_f16 v[72:75], v[140:143], v[156:159], v[72:75]
	v_mfma_f32_16x16x32_f16 v[76:79], v[140:143], v[160:163], v[76:79]
	v_mfma_f32_16x16x32_f16 v[80:83], v[140:143], v[164:167], v[80:83]
	s_add_u32 m0, s28, 0x9000
	s_nop 0
	global_load_lds_dwordx4 v10, s[6:7]
	v_mfma_f32_16x16x32_f16 v[84:87], v[140:143], v[168:171], v[84:87]
	s_waitcnt lgkmcnt(11)
	v_mfma_f32_16x16x32_f16 v[88:91], v[144:147], v[156:159], v[88:91]
	v_mfma_f32_16x16x32_f16 v[92:95], v[144:147], v[160:163], v[92:95]
	v_mfma_f32_16x16x32_f16 v[96:99], v[144:147], v[164:167], v[96:99]
	v_mfma_f32_16x16x32_f16 v[100:103], v[144:147], v[168:171], v[100:103]
	s_waitcnt lgkmcnt(10)
	v_mfma_f32_16x16x32_f16 v[104:107], v[148:151], v[156:159], v[104:107]
	v_mfma_f32_16x16x32_f16 v[108:111], v[148:151], v[160:163], v[108:111]
	s_add_u32 m0, s28, 0xb000
	s_nop 0
	global_load_lds_dwordx4 v11, s[6:7]
	s_add_u32 s6, s6, s20
	s_addc_u32 s7, s7, 0
	v_mfma_f32_16x16x32_f16 v[112:115], v[148:151], v[164:167], v[112:115]
	v_mfma_f32_16x16x32_f16 v[116:119], v[148:151], v[168:171], v[116:119]
	s_waitcnt lgkmcnt(9)
	v_mfma_f32_16x16x32_f16 v[120:123], v[152:155], v[156:159], v[120:123]
	v_mfma_f32_16x16x32_f16 v[124:127], v[152:155], v[160:163], v[124:127]
	v_mfma_f32_16x16x32_f16 v[128:131], v[152:155], v[164:167], v[128:131]
	v_mfma_f32_16x16x32_f16 v[132:135], v[152:155], v[168:171], v[132:135]
	s_waitcnt vmcnt(6) lgkmcnt(0)
	s_barrier
	s_waitcnt lgkmcnt(6)
	ds_read_b128 v[136:139], v19
	ds_read_b128 v[156:159], v21
	ds_read_b128 v[160:163], v21 offset:2048
	ds_read_b128 v[164:167], v21 offset:4096
	ds_read_b128 v[168:171], v21 offset:6144
	ds_read_b128 v[140:143], v19 offset:2048
	ds_read_b128 v[144:147], v19 offset:4096
	ds_read_b128 v[148:151], v19 offset:6144
	ds_read_b128 v[152:155], v19 offset:8192
	v_mfma_f32_16x16x32_f16 v[56:59], v[172:175], v[192:195], v[56:59]
	s_add_u32 m0, s28, 0xd000
	s_nop 0
	global_load_lds_dwordx4 v10, s[4:5]
	s_waitcnt lgkmcnt(15)
	v_mfma_f32_16x16x32_f16 v[60:63], v[172:175], v[196:199], v[60:63]
	s_waitcnt lgkmcnt(14)
	v_mfma_f32_16x16x32_f16 v[64:67], v[172:175], v[200:203], v[64:67]
	s_waitcnt lgkmcnt(13)
	v_mfma_f32_16x16x32_f16 v[68:71], v[172:175], v[204:207], v[68:71]
	s_waitcnt lgkmcnt(12)
	v_mfma_f32_16x16x32_f16 v[72:75], v[176:179], v[192:195], v[72:75]
	v_mfma_f32_16x16x32_f16 v[76:79], v[176:179], v[196:199], v[76:79]
	v_mfma_f32_16x16x32_f16 v[80:83], v[176:179], v[200:203], v[80:83]
	s_add_u32 m0, s28, 0xf000
	s_nop 0
	global_load_lds_dwordx4 v11, s[4:5]
	v_mfma_f32_16x16x32_f16 v[84:87], v[176:179], v[204:207], v[84:87]
	s_waitcnt lgkmcnt(11)
	v_mfma_f32_16x16x32_f16 v[88:91], v[180:183], v[192:195], v[88:91]
	v_mfma_f32_16x16x32_f16 v[92:95], v[180:183], v[196:199], v[92:95]
	v_mfma_f32_16x16x32_f16 v[96:99], v[180:183], v[200:203], v[96:99]
	v_mfma_f32_16x16x32_f16 v[100:103], v[180:183], v[204:207], v[100:103]
	s_waitcnt lgkmcnt(10)
	v_mfma_f32_16x16x32_f16 v[104:107], v[184:187], v[192:195], v[104:107]
	v_mfma_f32_16x16x32_f16 v[108:111], v[184:187], v[196:199], v[108:111]
	s_add_u32 m0, s28, 0x11000
	s_nop 0
	global_load_lds_dwordx4 v12, s[4:5]
	v_mfma_f32_16x16x32_f16 v[112:115], v[184:187], v[200:203], v[112:115]
	v_mfma_f32_16x16x32_f16 v[116:119], v[184:187], v[204:207], v[116:119]
	s_waitcnt lgkmcnt(9)
	v_mfma_f32_16x16x32_f16 v[120:123], v[188:191], v[192:195], v[120:123]
	v_mfma_f32_16x16x32_f16 v[124:127], v[188:191], v[196:199], v[124:127]
	v_mfma_f32_16x16x32_f16 v[128:131], v[188:191], v[200:203], v[128:131]
	v_mfma_f32_16x16x32_f16 v[132:135], v[188:191], v[204:207], v[132:135]
	s_waitcnt lgkmcnt(6)
	ds_read_b128 v[172:175], v20
	ds_read_b128 v[192:195], v22
	ds_read_b128 v[196:199], v22 offset:2048
	ds_read_b128 v[200:203], v22 offset:4096
	ds_read_b128 v[204:207], v22 offset:6144
	ds_read_b128 v[176:179], v20 offset:2048
	ds_read_b128 v[180:183], v20 offset:4096
	ds_read_b128 v[184:187], v20 offset:6144
	ds_read_b128 v[188:191], v20 offset:8192
	v_mfma_f32_16x16x32_f16 v[56:59], v[136:139], v[156:159], v[56:59]
	s_add_u32 m0, s28, 0x13000
	s_nop 0
	global_load_lds_dwordx4 v13, s[4:5]
	s_add_u32 s4, s4, s20
	s_addc_u32 s5, s5, 0
	s_waitcnt lgkmcnt(15)
	v_mfma_f32_16x16x32_f16 v[60:63], v[136:139], v[160:163], v[60:63]
	s_waitcnt lgkmcnt(14)
	v_mfma_f32_16x16x32_f16 v[64:67], v[136:139], v[164:167], v[64:67]
	s_waitcnt lgkmcnt(13)
	v_mfma_f32_16x16x32_f16 v[68:71], v[136:139], v[168:171], v[68:71]
	s_waitcnt lgkmcnt(12)
	v_mfma_f32_16x16x32_f16 v[72:75], v[140:143], v[156:159], v[72:75]
	v_mfma_f32_16x16x32_f16 v[76:79], v[140:143], v[160:163], v[76:79]
	v_mfma_f32_16x16x32_f16 v[80:83], v[140:143], v[164:167], v[80:83]
	s_add_u32 m0, s28, 0x16000
	s_nop 0
	global_load_lds_dwordx4 v10, s[6:7]
	v_mfma_f32_16x16x32_f16 v[84:87], v[140:143], v[168:171], v[84:87]
	s_waitcnt lgkmcnt(11)
	v_mfma_f32_16x16x32_f16 v[88:91], v[144:147], v[156:159], v[88:91]
	v_mfma_f32_16x16x32_f16 v[92:95], v[144:147], v[160:163], v[92:95]
	v_mfma_f32_16x16x32_f16 v[96:99], v[144:147], v[164:167], v[96:99]
	v_mfma_f32_16x16x32_f16 v[100:103], v[144:147], v[168:171], v[100:103]
	s_waitcnt lgkmcnt(10)
	v_mfma_f32_16x16x32_f16 v[104:107], v[148:151], v[156:159], v[104:107]
	v_mfma_f32_16x16x32_f16 v[108:111], v[148:151], v[160:163], v[108:111]
	s_add_u32 m0, s28, 0x18000
	s_nop 0
	global_load_lds_dwordx4 v11, s[6:7]
	s_add_u32 s6, s6, s20
	s_addc_u32 s7, s7, 0
	v_mfma_f32_16x16x32_f16 v[112:115], v[148:151], v[164:167], v[112:115]
	v_mfma_f32_16x16x32_f16 v[116:119], v[148:151], v[168:171], v[116:119]
	s_waitcnt lgkmcnt(9)
	v_mfma_f32_16x16x32_f16 v[120:123], v[152:155], v[156:159], v[120:123]
	v_mfma_f32_16x16x32_f16 v[124:127], v[152:155], v[160:163], v[124:127]
	v_mfma_f32_16x16x32_f16 v[128:131], v[152:155], v[164:167], v[128:131]
	v_mfma_f32_16x16x32_f16 v[132:135], v[152:155], v[168:171], v[132:135]
	s_waitcnt vmcnt(6) lgkmcnt(0)
	s_barrier
	s_waitcnt lgkmcnt(6)
	ds_read_b128 v[136:139], v15
	ds_read_b128 v[156:159], v17
	ds_read_b128 v[160:163], v17 offset:2048
	ds_read_b128 v[164:167], v17 offset:4096
	ds_read_b128 v[168:171], v17 offset:6144
	ds_read_b128 v[140:143], v15 offset:2048
	ds_read_b128 v[144:147], v15 offset:4096
	ds_read_b128 v[148:151], v15 offset:6144
	ds_read_b128 v[152:155], v15 offset:8192
	v_mfma_f32_16x16x32_f16 v[56:59], v[172:175], v[192:195], v[56:59]
	s_add_u32 m0, s28, 0x1a000
	s_nop 0
	global_load_lds_dwordx4 v10, s[4:5]
	s_waitcnt lgkmcnt(15)
	v_mfma_f32_16x16x32_f16 v[60:63], v[172:175], v[196:199], v[60:63]
	s_waitcnt lgkmcnt(14)
	v_mfma_f32_16x16x32_f16 v[64:67], v[172:175], v[200:203], v[64:67]
	s_waitcnt lgkmcnt(13)
	v_mfma_f32_16x16x32_f16 v[68:71], v[172:175], v[204:207], v[68:71]
	s_waitcnt lgkmcnt(12)
	v_mfma_f32_16x16x32_f16 v[72:75], v[176:179], v[192:195], v[72:75]
	v_mfma_f32_16x16x32_f16 v[76:79], v[176:179], v[196:199], v[76:79]
	v_mfma_f32_16x16x32_f16 v[80:83], v[176:179], v[200:203], v[80:83]
	s_add_u32 m0, s28, 0x1c000
	s_nop 0
	global_load_lds_dwordx4 v11, s[4:5]
	v_mfma_f32_16x16x32_f16 v[84:87], v[176:179], v[204:207], v[84:87]
	s_waitcnt lgkmcnt(11)
	v_mfma_f32_16x16x32_f16 v[88:91], v[180:183], v[192:195], v[88:91]
	v_mfma_f32_16x16x32_f16 v[92:95], v[180:183], v[196:199], v[92:95]
	v_mfma_f32_16x16x32_f16 v[96:99], v[180:183], v[200:203], v[96:99]
	v_mfma_f32_16x16x32_f16 v[100:103], v[180:183], v[204:207], v[100:103]
	s_waitcnt lgkmcnt(10)
	v_mfma_f32_16x16x32_f16 v[104:107], v[184:187], v[192:195], v[104:107]
	v_mfma_f32_16x16x32_f16 v[108:111], v[184:187], v[196:199], v[108:111]
	s_add_u32 m0, s28, 0x1e000
	s_nop 0
	global_load_lds_dwordx4 v12, s[4:5]
	v_mfma_f32_16x16x32_f16 v[112:115], v[184:187], v[200:203], v[112:115]
	v_mfma_f32_16x16x32_f16 v[116:119], v[184:187], v[204:207], v[116:119]
	s_waitcnt lgkmcnt(9)
	v_mfma_f32_16x16x32_f16 v[120:123], v[188:191], v[192:195], v[120:123]
	v_mfma_f32_16x16x32_f16 v[124:127], v[188:191], v[196:199], v[124:127]
	v_mfma_f32_16x16x32_f16 v[128:131], v[188:191], v[200:203], v[128:131]
	v_mfma_f32_16x16x32_f16 v[132:135], v[188:191], v[204:207], v[132:135]
	s_waitcnt lgkmcnt(6)
	ds_read_b128 v[172:175], v16
	ds_read_b128 v[192:195], v18
	ds_read_b128 v[196:199], v18 offset:2048
	ds_read_b128 v[200:203], v18 offset:4096
	ds_read_b128 v[204:207], v18 offset:6144
	ds_read_b128 v[176:179], v16 offset:2048
	ds_read_b128 v[180:183], v16 offset:4096
	ds_read_b128 v[184:187], v16 offset:6144
	ds_read_b128 v[188:191], v16 offset:8192
	v_mfma_f32_16x16x32_f16 v[56:59], v[136:139], v[156:159], v[56:59]
	s_add_u32 m0, s28, 0x20000
	s_nop 0
	global_load_lds_dwordx4 v13, s[4:5]
	s_add_u32 s4, s4, s20
	s_addc_u32 s5, s5, 0
	s_waitcnt lgkmcnt(15)
	v_mfma_f32_16x16x32_f16 v[60:63], v[136:139], v[160:163], v[60:63]
	s_waitcnt lgkmcnt(14)
	v_mfma_f32_16x16x32_f16 v[64:67], v[136:139], v[164:167], v[64:67]
	s_waitcnt lgkmcnt(13)
	v_mfma_f32_16x16x32_f16 v[68:71], v[136:139], v[168:171], v[68:71]
	s_waitcnt lgkmcnt(12)
	v_mfma_f32_16x16x32_f16 v[72:75], v[140:143], v[156:159], v[72:75]
	v_mfma_f32_16x16x32_f16 v[76:79], v[140:143], v[160:163], v[76:79]
	v_mfma_f32_16x16x32_f16 v[80:83], v[140:143], v[164:167], v[80:83]
	s_add_u32 m0, s28, 0x23000
	s_nop 0
	global_load_lds_dwordx4 v10, s[6:7]
	v_mfma_f32_16x16x32_f16 v[84:87], v[140:143], v[168:171], v[84:87]
	s_waitcnt lgkmcnt(11)
	v_mfma_f32_16x16x32_f16 v[88:91], v[144:147], v[156:159], v[88:91]
	v_mfma_f32_16x16x32_f16 v[92:95], v[144:147], v[160:163], v[92:95]
	v_mfma_f32_16x16x32_f16 v[96:99], v[144:147], v[164:167], v[96:99]
	v_mfma_f32_16x16x32_f16 v[100:103], v[144:147], v[168:171], v[100:103]
	s_waitcnt lgkmcnt(10)
	v_mfma_f32_16x16x32_f16 v[104:107], v[148:151], v[156:159], v[104:107]
	v_mfma_f32_16x16x32_f16 v[108:111], v[148:151], v[160:163], v[108:111]
	s_add_u32 m0, s28, 0x25000
	s_nop 0
	global_load_lds_dwordx4 v11, s[6:7]
	s_add_u32 s6, s6, s20
	s_addc_u32 s7, s7, 0
	v_mfma_f32_16x16x32_f16 v[112:115], v[148:151], v[164:167], v[112:115]
	v_mfma_f32_16x16x32_f16 v[116:119], v[148:151], v[168:171], v[116:119]
	s_waitcnt lgkmcnt(9)
	v_mfma_f32_16x16x32_f16 v[120:123], v[152:155], v[156:159], v[120:123]
	v_mfma_f32_16x16x32_f16 v[124:127], v[152:155], v[160:163], v[124:127]
	v_mfma_f32_16x16x32_f16 v[128:131], v[152:155], v[164:167], v[128:131]
	v_mfma_f32_16x16x32_f16 v[132:135], v[152:155], v[168:171], v[132:135]
	s_waitcnt vmcnt(6) lgkmcnt(0)
	s_barrier
	s_waitcnt lgkmcnt(6)
	ds_read_b128 v[136:139], v15 offset:53248
	ds_read_b128 v[156:159], v17 offset:53248
	ds_read_b128 v[160:163], v17 offset:55296
	ds_read_b128 v[164:167], v17 offset:57344
	ds_read_b128 v[168:171], v17 offset:59392
	ds_read_b128 v[140:143], v15 offset:55296
	ds_read_b128 v[144:147], v15 offset:57344
	ds_read_b128 v[148:151], v15 offset:59392
	ds_read_b128 v[152:155], v15 offset:61440
	v_mfma_f32_16x16x32_f16 v[56:59], v[172:175], v[192:195], v[56:59]
	s_add_u32 m0, s28, 0x0
	s_nop 0
	global_load_lds_dwordx4 v10, s[4:5]
	s_waitcnt lgkmcnt(15)
	v_mfma_f32_16x16x32_f16 v[60:63], v[172:175], v[196:199], v[60:63]
	s_waitcnt lgkmcnt(14)
	v_mfma_f32_16x16x32_f16 v[64:67], v[172:175], v[200:203], v[64:67]
	s_waitcnt lgkmcnt(13)
	v_mfma_f32_16x16x32_f16 v[68:71], v[172:175], v[204:207], v[68:71]
	s_waitcnt lgkmcnt(12)
	v_mfma_f32_16x16x32_f16 v[72:75], v[176:179], v[192:195], v[72:75]
	v_mfma_f32_16x16x32_f16 v[76:79], v[176:179], v[196:199], v[76:79]
	v_mfma_f32_16x16x32_f16 v[80:83], v[176:179], v[200:203], v[80:83]
	s_add_u32 m0, s28, 0x2000
	s_nop 0
	global_load_lds_dwordx4 v11, s[4:5]
	v_mfma_f32_16x16x32_f16 v[84:87], v[176:179], v[204:207], v[84:87]
	s_waitcnt lgkmcnt(11)
	v_mfma_f32_16x16x32_f16 v[88:91], v[180:183], v[192:195], v[88:91]
	v_mfma_f32_16x16x32_f16 v[92:95], v[180:183], v[196:199], v[92:95]
	v_mfma_f32_16x16x32_f16 v[96:99], v[180:183], v[200:203], v[96:99]
	v_mfma_f32_16x16x32_f16 v[100:103], v[180:183], v[204:207], v[100:103]
	s_waitcnt lgkmcnt(10)
	v_mfma_f32_16x16x32_f16 v[104:107], v[184:187], v[192:195], v[104:107]
	v_mfma_f32_16x16x32_f16 v[108:111], v[184:187], v[196:199], v[108:111]
	s_add_u32 m0, s28, 0x4000
	s_nop 0
	global_load_lds_dwordx4 v12, s[4:5]
	v_mfma_f32_16x16x32_f16 v[112:115], v[184:187], v[200:203], v[112:115]
	v_mfma_f32_16x16x32_f16 v[116:119], v[184:187], v[204:207], v[116:119]
	s_waitcnt lgkmcnt(9)
	v_mfma_f32_16x16x32_f16 v[120:123], v[188:191], v[192:195], v[120:123]
	v_mfma_f32_16x16x32_f16 v[124:127], v[188:191], v[196:199], v[124:127]
	v_mfma_f32_16x16x32_f16 v[128:131], v[188:191], v[200:203], v[128:131]
	v_mfma_f32_16x16x32_f16 v[132:135], v[188:191], v[204:207], v[132:135]
	s_waitcnt lgkmcnt(6)
	ds_read_b128 v[172:175], v16 offset:53248
	ds_read_b128 v[192:195], v18 offset:53248
	ds_read_b128 v[196:199], v18 offset:55296
	ds_read_b128 v[200:203], v18 offset:57344
	ds_read_b128 v[204:207], v18 offset:59392
	ds_read_b128 v[176:179], v16 offset:55296
	ds_read_b128 v[180:183], v16 offset:57344
	ds_read_b128 v[184:187], v16 offset:59392
	ds_read_b128 v[188:191], v16 offset:61440
	v_mfma_f32_16x16x32_f16 v[56:59], v[136:139], v[156:159], v[56:59]
	s_add_u32 m0, s28, 0x6000
	s_nop 0
	global_load_lds_dwordx4 v13, s[4:5]
	s_add_u32 s4, s4, s20
	s_addc_u32 s5, s5, 0
	s_waitcnt lgkmcnt(15)
	v_mfma_f32_16x16x32_f16 v[60:63], v[136:139], v[160:163], v[60:63]
	s_waitcnt lgkmcnt(14)
	v_mfma_f32_16x16x32_f16 v[64:67], v[136:139], v[164:167], v[64:67]
	s_waitcnt lgkmcnt(13)
	v_mfma_f32_16x16x32_f16 v[68:71], v[136:139], v[168:171], v[68:71]
	s_waitcnt lgkmcnt(12)
	v_mfma_f32_16x16x32_f16 v[72:75], v[140:143], v[156:159], v[72:75]
	v_mfma_f32_16x16x32_f16 v[76:79], v[140:143], v[160:163], v[76:79]
	v_mfma_f32_16x16x32_f16 v[80:83], v[140:143], v[164:167], v[80:83]
	s_add_u32 m0, s28, 0x9000
	s_nop 0
	global_load_lds_dwordx4 v10, s[6:7]
	v_mfma_f32_16x16x32_f16 v[84:87], v[140:143], v[168:171], v[84:87]
	s_waitcnt lgkmcnt(11)
	v_mfma_f32_16x16x32_f16 v[88:91], v[144:147], v[156:159], v[88:91]
	v_mfma_f32_16x16x32_f16 v[92:95], v[144:147], v[160:163], v[92:95]
	v_mfma_f32_16x16x32_f16 v[96:99], v[144:147], v[164:167], v[96:99]
	v_mfma_f32_16x16x32_f16 v[100:103], v[144:147], v[168:171], v[100:103]
	s_waitcnt lgkmcnt(10)
	v_mfma_f32_16x16x32_f16 v[104:107], v[148:151], v[156:159], v[104:107]
	v_mfma_f32_16x16x32_f16 v[108:111], v[148:151], v[160:163], v[108:111]
	s_add_u32 m0, s28, 0xb000
	s_nop 0
	global_load_lds_dwordx4 v11, s[6:7]
	s_add_u32 s6, s6, s20
	s_addc_u32 s7, s7, 0
	v_mfma_f32_16x16x32_f16 v[112:115], v[148:151], v[164:167], v[112:115]
	v_mfma_f32_16x16x32_f16 v[116:119], v[148:151], v[168:171], v[116:119]
	s_waitcnt lgkmcnt(9)
	v_mfma_f32_16x16x32_f16 v[120:123], v[152:155], v[156:159], v[120:123]
	v_mfma_f32_16x16x32_f16 v[124:127], v[152:155], v[160:163], v[124:127]
	v_mfma_f32_16x16x32_f16 v[128:131], v[152:155], v[164:167], v[128:131]
	v_mfma_f32_16x16x32_f16 v[132:135], v[152:155], v[168:171], v[132:135]
	s_waitcnt vmcnt(6) lgkmcnt(0)
	s_barrier
	s_waitcnt lgkmcnt(6)
	ds_read_b128 v[136:139], v19
	ds_read_b128 v[156:159], v21
	ds_read_b128 v[160:163], v21 offset:2048
	ds_read_b128 v[164:167], v21 offset:4096
	ds_read_b128 v[168:171], v21 offset:6144
	ds_read_b128 v[140:143], v19 offset:2048
	ds_read_b128 v[144:147], v19 offset:4096
	ds_read_b128 v[148:151], v19 offset:6144
	ds_read_b128 v[152:155], v19 offset:8192
	v_mfma_f32_16x16x32_f16 v[56:59], v[172:175], v[192:195], v[56:59]
	s_waitcnt lgkmcnt(15)
	v_mfma_f32_16x16x32_f16 v[60:63], v[172:175], v[196:199], v[60:63]
	s_waitcnt lgkmcnt(14)
	v_mfma_f32_16x16x32_f16 v[64:67], v[172:175], v[200:203], v[64:67]
	s_waitcnt lgkmcnt(13)
	v_mfma_f32_16x16x32_f16 v[68:71], v[172:175], v[204:207], v[68:71]
	s_waitcnt lgkmcnt(12)
	v_mfma_f32_16x16x32_f16 v[72:75], v[176:179], v[192:195], v[72:75]
	v_mfma_f32_16x16x32_f16 v[76:79], v[176:179], v[196:199], v[76:79]
	v_mfma_f32_16x16x32_f16 v[80:83], v[176:179], v[200:203], v[80:83]
	v_mfma_f32_16x16x32_f16 v[84:87], v[176:179], v[204:207], v[84:87]
	s_waitcnt lgkmcnt(11)
	v_mfma_f32_16x16x32_f16 v[88:91], v[180:183], v[192:195], v[88:91]
	v_mfma_f32_16x16x32_f16 v[92:95], v[180:183], v[196:199], v[92:95]
	v_mfma_f32_16x16x32_f16 v[96:99], v[180:183], v[200:203], v[96:99]
	v_mfma_f32_16x16x32_f16 v[100:103], v[180:183], v[204:207], v[100:103]
	s_waitcnt lgkmcnt(10)
	v_mfma_f32_16x16x32_f16 v[104:107], v[184:187], v[192:195], v[104:107]
	v_mfma_f32_16x16x32_f16 v[108:111], v[184:187], v[196:199], v[108:111]
	v_mfma_f32_16x16x32_f16 v[112:115], v[184:187], v[200:203], v[112:115]
	v_mfma_f32_16x16x32_f16 v[116:119], v[184:187], v[204:207], v[116:119]
	s_waitcnt lgkmcnt(9)
	v_mfma_f32_16x16x32_f16 v[120:123], v[188:191], v[192:195], v[120:123]
	v_mfma_f32_16x16x32_f16 v[124:127], v[188:191], v[196:199], v[124:127]
	v_mfma_f32_16x16x32_f16 v[128:131], v[188:191], v[200:203], v[128:131]
	v_mfma_f32_16x16x32_f16 v[132:135], v[188:191], v[204:207], v[132:135]
	s_waitcnt lgkmcnt(6)
	ds_read_b128 v[172:175], v20
	ds_read_b128 v[192:195], v22
	ds_read_b128 v[196:199], v22 offset:2048
	ds_read_b128 v[200:203], v22 offset:4096
	ds_read_b128 v[204:207], v22 offset:6144
	ds_read_b128 v[176:179], v20 offset:2048
	ds_read_b128 v[180:183], v20 offset:4096
	ds_read_b128 v[184:187], v20 offset:6144
	ds_read_b128 v[188:191], v20 offset:8192
	v_mfma_f32_16x16x32_f16 v[56:59], v[136:139], v[156:159], v[56:59]
	s_waitcnt lgkmcnt(15)
	v_mfma_f32_16x16x32_f16 v[60:63], v[136:139], v[160:163], v[60:63]
	s_waitcnt lgkmcnt(14)
	v_mfma_f32_16x16x32_f16 v[64:67], v[136:139], v[164:167], v[64:67]
	s_waitcnt lgkmcnt(13)
	v_mfma_f32_16x16x32_f16 v[68:71], v[136:139], v[168:171], v[68:71]
	s_waitcnt lgkmcnt(12)
	v_mfma_f32_16x16x32_f16 v[72:75], v[140:143], v[156:159], v[72:75]
	v_mfma_f32_16x16x32_f16 v[76:79], v[140:143], v[160:163], v[76:79]
	v_mfma_f32_16x16x32_f16 v[80:83], v[140:143], v[164:167], v[80:83]
	v_mfma_f32_16x16x32_f16 v[84:87], v[140:143], v[168:171], v[84:87]
	s_waitcnt lgkmcnt(11)
	v_mfma_f32_16x16x32_f16 v[88:91], v[144:147], v[156:159], v[88:91]
	v_mfma_f32_16x16x32_f16 v[92:95], v[144:147], v[160:163], v[92:95]
	v_mfma_f32_16x16x32_f16 v[96:99], v[144:147], v[164:167], v[96:99]
	v_mfma_f32_16x16x32_f16 v[100:103], v[144:147], v[168:171], v[100:103]
	s_waitcnt lgkmcnt(10)
	v_mfma_f32_16x16x32_f16 v[104:107], v[148:151], v[156:159], v[104:107]
	v_mfma_f32_16x16x32_f16 v[108:111], v[148:151], v[160:163], v[108:111]
	v_mfma_f32_16x16x32_f16 v[112:115], v[148:151], v[164:167], v[112:115]
	v_mfma_f32_16x16x32_f16 v[116:119], v[148:151], v[168:171], v[116:119]
	s_waitcnt lgkmcnt(9)
	v_mfma_f32_16x16x32_f16 v[120:123], v[152:155], v[156:159], v[120:123]
	v_mfma_f32_16x16x32_f16 v[124:127], v[152:155], v[160:163], v[124:127]
	v_mfma_f32_16x16x32_f16 v[128:131], v[152:155], v[164:167], v[128:131]
	v_mfma_f32_16x16x32_f16 v[132:135], v[152:155], v[168:171], v[132:135]
	s_waitcnt vmcnt(0) lgkmcnt(0)
	s_barrier
	s_waitcnt lgkmcnt(6)
	ds_read_b128 v[136:139], v15
	ds_read_b128 v[156:159], v17
	ds_read_b128 v[160:163], v17 offset:2048
	ds_read_b128 v[164:167], v17 offset:4096
	ds_read_b128 v[168:171], v17 offset:6144
	ds_read_b128 v[140:143], v15 offset:2048
	ds_read_b128 v[144:147], v15 offset:4096
	ds_read_b128 v[148:151], v15 offset:6144
	ds_read_b128 v[152:155], v15 offset:8192
	v_mfma_f32_16x16x32_f16 v[56:59], v[172:175], v[192:195], v[56:59]
	s_waitcnt lgkmcnt(15)
	v_mfma_f32_16x16x32_f16 v[60:63], v[172:175], v[196:199], v[60:63]
	s_waitcnt lgkmcnt(14)
	v_mfma_f32_16x16x32_f16 v[64:67], v[172:175], v[200:203], v[64:67]
	s_waitcnt lgkmcnt(13)
	v_mfma_f32_16x16x32_f16 v[68:71], v[172:175], v[204:207], v[68:71]
	s_waitcnt lgkmcnt(12)
	v_mfma_f32_16x16x32_f16 v[72:75], v[176:179], v[192:195], v[72:75]
	v_mfma_f32_16x16x32_f16 v[76:79], v[176:179], v[196:199], v[76:79]
	v_mfma_f32_16x16x32_f16 v[80:83], v[176:179], v[200:203], v[80:83]
	v_mfma_f32_16x16x32_f16 v[84:87], v[176:179], v[204:207], v[84:87]
	s_waitcnt lgkmcnt(11)
	v_mfma_f32_16x16x32_f16 v[88:91], v[180:183], v[192:195], v[88:91]
	v_mfma_f32_16x16x32_f16 v[92:95], v[180:183], v[196:199], v[92:95]
	v_mfma_f32_16x16x32_f16 v[96:99], v[180:183], v[200:203], v[96:99]
	v_mfma_f32_16x16x32_f16 v[100:103], v[180:183], v[204:207], v[100:103]
	s_waitcnt lgkmcnt(10)
	v_mfma_f32_16x16x32_f16 v[104:107], v[184:187], v[192:195], v[104:107]
	v_mfma_f32_16x16x32_f16 v[108:111], v[184:187], v[196:199], v[108:111]
	v_mfma_f32_16x16x32_f16 v[112:115], v[184:187], v[200:203], v[112:115]
	v_mfma_f32_16x16x32_f16 v[116:119], v[184:187], v[204:207], v[116:119]
	s_waitcnt lgkmcnt(9)
	v_mfma_f32_16x16x32_f16 v[120:123], v[188:191], v[192:195], v[120:123]
	v_mfma_f32_16x16x32_f16 v[124:127], v[188:191], v[196:199], v[124:127]
	v_mfma_f32_16x16x32_f16 v[128:131], v[188:191], v[200:203], v[128:131]
	v_mfma_f32_16x16x32_f16 v[132:135], v[188:191], v[204:207], v[132:135]
	s_waitcnt lgkmcnt(6)
	ds_read_b128 v[172:175], v16
	ds_read_b128 v[192:195], v18
	ds_read_b128 v[196:199], v18 offset:2048
	ds_read_b128 v[200:203], v18 offset:4096
	ds_read_b128 v[204:207], v18 offset:6144
	ds_read_b128 v[176:179], v16 offset:2048
	ds_read_b128 v[180:183], v16 offset:4096
	ds_read_b128 v[184:187], v16 offset:6144
	ds_read_b128 v[188:191], v16 offset:8192
	v_mfma_f32_16x16x32_f16 v[56:59], v[136:139], v[156:159], v[56:59]
	s_waitcnt lgkmcnt(15)
	v_mfma_f32_16x16x32_f16 v[60:63], v[136:139], v[160:163], v[60:63]
	s_waitcnt lgkmcnt(14)
	v_mfma_f32_16x16x32_f16 v[64:67], v[136:139], v[164:167], v[64:67]
	s_waitcnt lgkmcnt(13)
	v_mfma_f32_16x16x32_f16 v[68:71], v[136:139], v[168:171], v[68:71]
	s_waitcnt lgkmcnt(12)
	v_mfma_f32_16x16x32_f16 v[72:75], v[140:143], v[156:159], v[72:75]
	v_mfma_f32_16x16x32_f16 v[76:79], v[140:143], v[160:163], v[76:79]
	v_mfma_f32_16x16x32_f16 v[80:83], v[140:143], v[164:167], v[80:83]
	v_mfma_f32_16x16x32_f16 v[84:87], v[140:143], v[168:171], v[84:87]
	s_waitcnt lgkmcnt(11)
	v_mfma_f32_16x16x32_f16 v[88:91], v[144:147], v[156:159], v[88:91]
	v_mfma_f32_16x16x32_f16 v[92:95], v[144:147], v[160:163], v[92:95]
	v_mfma_f32_16x16x32_f16 v[96:99], v[144:147], v[164:167], v[96:99]
	v_mfma_f32_16x16x32_f16 v[100:103], v[144:147], v[168:171], v[100:103]
	s_waitcnt lgkmcnt(10)
	v_mfma_f32_16x16x32_f16 v[104:107], v[148:151], v[156:159], v[104:107]
	v_mfma_f32_16x16x32_f16 v[108:111], v[148:151], v[160:163], v[108:111]
	v_mfma_f32_16x16x32_f16 v[112:115], v[148:151], v[164:167], v[112:115]
	v_mfma_f32_16x16x32_f16 v[116:119], v[148:151], v[168:171], v[116:119]
	s_waitcnt lgkmcnt(9)
	v_mfma_f32_16x16x32_f16 v[120:123], v[152:155], v[156:159], v[120:123]
	v_mfma_f32_16x16x32_f16 v[124:127], v[152:155], v[160:163], v[124:127]
	v_mfma_f32_16x16x32_f16 v[128:131], v[152:155], v[164:167], v[128:131]
	v_mfma_f32_16x16x32_f16 v[132:135], v[152:155], v[168:171], v[132:135]
	s_waitcnt lgkmcnt(7)
	v_mfma_f32_16x16x32_f16 v[56:59], v[172:175], v[192:195], v[56:59]
	s_waitcnt lgkmcnt(6)
	v_mfma_f32_16x16x32_f16 v[60:63], v[172:175], v[196:199], v[60:63]
	s_waitcnt lgkmcnt(5)
	v_mfma_f32_16x16x32_f16 v[64:67], v[172:175], v[200:203], v[64:67]
	s_waitcnt lgkmcnt(4)
	v_mfma_f32_16x16x32_f16 v[68:71], v[172:175], v[204:207], v[68:71]
	s_waitcnt lgkmcnt(3)
	v_mfma_f32_16x16x32_f16 v[72:75], v[176:179], v[192:195], v[72:75]
	v_mfma_f32_16x16x32_f16 v[76:79], v[176:179], v[196:199], v[76:79]
	v_mfma_f32_16x16x32_f16 v[80:83], v[176:179], v[200:203], v[80:83]
	v_mfma_f32_16x16x32_f16 v[84:87], v[176:179], v[204:207], v[84:87]
	s_waitcnt lgkmcnt(2)
	v_mfma_f32_16x16x32_f16 v[88:91], v[180:183], v[192:195], v[88:91]
	v_mfma_f32_16x16x32_f16 v[92:95], v[180:183], v[196:199], v[92:95]
	v_mfma_f32_16x16x32_f16 v[96:99], v[180:183], v[200:203], v[96:99]
	v_mfma_f32_16x16x32_f16 v[100:103], v[180:183], v[204:207], v[100:103]
	s_waitcnt lgkmcnt(1)
	v_mfma_f32_16x16x32_f16 v[104:107], v[184:187], v[192:195], v[104:107]
	v_mfma_f32_16x16x32_f16 v[108:111], v[184:187], v[196:199], v[108:111]
	v_mfma_f32_16x16x32_f16 v[112:115], v[184:187], v[200:203], v[112:115]
	v_mfma_f32_16x16x32_f16 v[116:119], v[184:187], v[204:207], v[116:119]
	s_waitcnt lgkmcnt(0)
	v_mfma_f32_16x16x32_f16 v[120:123], v[188:191], v[192:195], v[120:123]
	v_mfma_f32_16x16x32_f16 v[124:127], v[188:191], v[196:199], v[124:127]
	v_mfma_f32_16x16x32_f16 v[128:131], v[188:191], v[200:203], v[128:131]
	v_mfma_f32_16x16x32_f16 v[132:135], v[188:191], v[204:207], v[132:135]
	s_nop 7
	s_nop 1
	s_add_u32 s24, s29, 0
	s_lshl_b32 s8, s24, 11
	v_add_u32_e32 v212, s8, v23
	v_pk_add_f32 v[56:57], v[56:57], v[24:25] op_sel_hi:[1,0]
	v_pk_add_f32 v[58:59], v[58:59], v[24:25] op_sel_hi:[1,0]
	v_cvt_pk_f16_f32 v56, v56, v57
	v_cvt_pk_f16_f32 v57, v58, v59
	global_store_dwordx2 v212, v[56:57], s[22:23] offset:0
	v_pk_add_f32 v[60:61], v[60:61], v[26:27] op_sel_hi:[1,0]
	v_pk_add_f32 v[62:63], v[62:63], v[26:27] op_sel_hi:[1,0]
	v_cvt_pk_f16_f32 v60, v60, v61
	v_cvt_pk_f16_f32 v61, v62, v63
	global_store_dwordx2 v212, v[60:61], s[22:23] offset:256
	v_pk_add_f32 v[64:65], v[64:65], v[28:29] op_sel_hi:[1,0]
	v_pk_add_f32 v[66:67], v[66:67], v[28:29] op_sel_hi:[1,0]
	v_cvt_pk_f16_f32 v64, v64, v65
	v_cvt_pk_f16_f32 v65, v66, v67
	global_store_dwordx2 v212, v[64:65], s[22:23] offset:1024
	v_pk_add_f32 v[68:69], v[68:69], v[30:31] op_sel_hi:[1,0]
	v_pk_add_f32 v[70:71], v[70:71], v[30:31] op_sel_hi:[1,0]
	v_cvt_pk_f16_f32 v68, v68, v69
	v_cvt_pk_f16_f32 v69, v70, v71
	global_store_dwordx2 v212, v[68:69], s[22:23] offset:1280
	s_add_u32 s24, s29, 1
	s_lshl_b32 s8, s24, 11
	v_add_u32_e32 v212, s8, v23
	v_pk_add_f32 v[72:73], v[72:73], v[24:25] op_sel_hi:[1,0]
	v_pk_add_f32 v[74:75], v[74:75], v[24:25] op_sel_hi:[1,0]
	v_cvt_pk_f16_f32 v72, v72, v73
	v_cvt_pk_f16_f32 v73, v74, v75
	global_store_dwordx2 v212, v[72:73], s[22:23] offset:0
	v_pk_add_f32 v[76:77], v[76:77], v[26:27] op_sel_hi:[1,0]
	v_pk_add_f32 v[78:79], v[78:79], v[26:27] op_sel_hi:[1,0]
	v_cvt_pk_f16_f32 v76, v76, v77
	v_cvt_pk_f16_f32 v77, v78, v79
	global_store_dwordx2 v212, v[76:77], s[22:23] offset:256
	v_pk_add_f32 v[80:81], v[80:81], v[28:29] op_sel_hi:[1,0]
	v_pk_add_f32 v[82:83], v[82:83], v[28:29] op_sel_hi:[1,0]
	v_cvt_pk_f16_f32 v80, v80, v81
	v_cvt_pk_f16_f32 v81, v82, v83
	global_store_dwordx2 v212, v[80:81], s[22:23] offset:1024
	v_pk_add_f32 v[84:85], v[84:85], v[30:31] op_sel_hi:[1,0]
	v_pk_add_f32 v[86:87], v[86:87], v[30:31] op_sel_hi:[1,0]
	v_cvt_pk_f16_f32 v84, v84, v85
	v_cvt_pk_f16_f32 v85, v86, v87
	global_store_dwordx2 v212, v[84:85], s[22:23] offset:1280
	s_add_u32 s24, s29, 2
	s_lshl_b32 s8, s24, 11
	v_add_u32_e32 v212, s8, v23
	v_pk_add_f32 v[88:89], v[88:89], v[24:25] op_sel_hi:[1,0]
	v_pk_add_f32 v[90:91], v[90:91], v[24:25] op_sel_hi:[1,0]
	v_cvt_pk_f16_f32 v88, v88, v89
	v_cvt_pk_f16_f32 v89, v90, v91
	global_store_dwordx2 v212, v[88:89], s[22:23] offset:0
	v_pk_add_f32 v[92:93], v[92:93], v[26:27] op_sel_hi:[1,0]
	v_pk_add_f32 v[94:95], v[94:95], v[26:27] op_sel_hi:[1,0]
	v_cvt_pk_f16_f32 v92, v92, v93
	v_cvt_pk_f16_f32 v93, v94, v95
	global_store_dwordx2 v212, v[92:93], s[22:23] offset:256
	v_pk_add_f32 v[96:97], v[96:97], v[28:29] op_sel_hi:[1,0]
	v_pk_add_f32 v[98:99], v[98:99], v[28:29] op_sel_hi:[1,0]
	v_cvt_pk_f16_f32 v96, v96, v97
	v_cvt_pk_f16_f32 v97, v98, v99
	global_store_dwordx2 v212, v[96:97], s[22:23] offset:1024
	v_pk_add_f32 v[100:101], v[100:101], v[30:31] op_sel_hi:[1,0]
	v_pk_add_f32 v[102:103], v[102:103], v[30:31] op_sel_hi:[1,0]
	v_cvt_pk_f16_f32 v100, v100, v101
	v_cvt_pk_f16_f32 v101, v102, v103
	global_store_dwordx2 v212, v[100:101], s[22:23] offset:1280
	s_add_u32 s24, s29, 3
	s_lshl_b32 s8, s24, 11
	v_add_u32_e32 v212, s8, v23
	v_pk_add_f32 v[104:105], v[104:105], v[24:25] op_sel_hi:[1,0]
	v_pk_add_f32 v[106:107], v[106:107], v[24:25] op_sel_hi:[1,0]
	v_cvt_pk_f16_f32 v104, v104, v105
	v_cvt_pk_f16_f32 v105, v106, v107
	global_store_dwordx2 v212, v[104:105], s[22:23] offset:0
	v_pk_add_f32 v[108:109], v[108:109], v[26:27] op_sel_hi:[1,0]
	v_pk_add_f32 v[110:111], v[110:111], v[26:27] op_sel_hi:[1,0]
	v_cvt_pk_f16_f32 v108, v108, v109
	v_cvt_pk_f16_f32 v109, v110, v111
	global_store_dwordx2 v212, v[108:109], s[22:23] offset:256
	v_pk_add_f32 v[112:113], v[112:113], v[28:29] op_sel_hi:[1,0]
	v_pk_add_f32 v[114:115], v[114:115], v[28:29] op_sel_hi:[1,0]
	v_cvt_pk_f16_f32 v112, v112, v113
	v_cvt_pk_f16_f32 v113, v114, v115
	global_store_dwordx2 v212, v[112:113], s[22:23] offset:1024
	v_pk_add_f32 v[116:117], v[116:117], v[30:31] op_sel_hi:[1,0]
	v_pk_add_f32 v[118:119], v[118:119], v[30:31] op_sel_hi:[1,0]
	v_cvt_pk_f16_f32 v116, v116, v117
	v_cvt_pk_f16_f32 v117, v118, v119
	global_store_dwordx2 v212, v[116:117], s[22:23] offset:1280
	s_add_u32 s24, s29, 4
	s_lshl_b32 s8, s24, 11
	v_add_u32_e32 v212, s8, v23
	v_pk_add_f32 v[120:121], v[120:121], v[24:25] op_sel_hi:[1,0]
	v_pk_add_f32 v[122:123], v[122:123], v[24:25] op_sel_hi:[1,0]
	v_cvt_pk_f16_f32 v120, v120, v121
	v_cvt_pk_f16_f32 v121, v122, v123
	global_store_dwordx2 v212, v[120:121], s[22:23] offset:0
	v_pk_add_f32 v[124:125], v[124:125], v[26:27] op_sel_hi:[1,0]
	v_pk_add_f32 v[126:127], v[126:127], v[26:27] op_sel_hi:[1,0]
	v_cvt_pk_f16_f32 v124, v124, v125
	v_cvt_pk_f16_f32 v125, v126, v127
	global_store_dwordx2 v212, v[124:125], s[22:23] offset:256
	v_pk_add_f32 v[128:129], v[128:129], v[28:29] op_sel_hi:[1,0]
	v_pk_add_f32 v[130:131], v[130:131], v[28:29] op_sel_hi:[1,0]
	v_cvt_pk_f16_f32 v128, v128, v129
	v_cvt_pk_f16_f32 v129, v130, v131
	global_store_dwordx2 v212, v[128:129], s[22:23] offset:1024
	v_pk_add_f32 v[132:133], v[132:133], v[30:31] op_sel_hi:[1,0]
	v_pk_add_f32 v[134:135], v[134:135], v[30:31] op_sel_hi:[1,0]
	v_cvt_pk_f16_f32 v132, v132, v133
	v_cvt_pk_f16_f32 v133, v134, v135
	global_store_dwordx2 v212, v[132:133], s[22:23] offset:1280
	s_branch .Lpf_done
.Lpf_vVB:
	v_add_u32_e32 v8, 0x77000, v10
	s_lshl_b32 s25, s25, 6
	s_add_u32 s25, s25, 32
	s_add_u32 s29, s10, s25
	s_lshr_b32 s29, s29, 4
	v_add_u32_e32 v5, s25, v3
	v_lshlrev_b32_e32 v5, 7, v5
	v_add_u32_e32 v15, v5, v6
	v_add_u32_e32 v16, v5, v7
	v_add_u32_e32 v5, 0x9000, v9
	v_add_u32_e32 v17, v5, v6
	v_add_u32_e32 v18, v5, v7
	v_add_u32_e32 v19, 0x1a000, v15
	v_add_u32_e32 v20, 0x1a000, v16
	v_add_u32_e32 v21, 0x1a000, v17
	v_add_u32_e32 v22, 0x1a000, v18
	v_lshlrev_b32_e32 v5, 2, v3
	global_load_dword v24, v5, s[14:15] offset:0
	global_load_dword v26, v5, s[14:15] offset:64
	global_load_dword v28, v5, s[14:15] offset:128
	global_load_dword v30, v5, s[14:15] offset:192
	s_add_u32 m0, s28, 0x0
	s_nop 0
	global_load_lds_dwordx4 v10, s[4:5]
	s_add_u32 m0, s28, 0x2000
	s_nop 0
	global_load_lds_dwordx4 v11, s[4:5]
	s_add_u32 m0, s28, 0x4000
	s_nop 0
	global_load_lds_dwordx4 v12, s[4:5]
	s_add_u32 m0, s28, 0x6000
	s_nop 0
	global_load_lds_dwordx4 v13, s[4:5]
	s_add_u32 m0, s28, 0x7000
	s_nop 0
	global_load_lds_dwordx4 v8, s[4:5]
	s_add_u32 s4, s4, s20
	s_addc_u32 s5, s5, 0
	s_add_u32 m0, s28, 0x9000
	s_nop 0
	global_load_lds_dwordx4 v10, s[6:7]
	s_add_u32 m0, s28, 0xb000
	s_nop 0
	global_load_lds_dwordx4 v11, s[6:7]
	s_add_u32 s6, s6, s20
	s_addc_u32 s7, s7, 0
	s_add_u32 m0, s28, 0xd000
	s_nop 0
	global_load_lds_dwordx4 v10, s[4:5]
	s_add_u32 m0, s28, 0xf000
	s_nop 0
	global_load_lds_dwordx4 v11, s[4:5]
	s_add_u32 m0, s28, 0x11000
	s_nop 0
	global_load_lds_dwordx4 v12, s[4:5]
	s_add_u32 m0, s28, 0x13000
	s_nop 0
	global_load_lds_dwordx4 v13, s[4:5]
	s_add_u32 m0, s28, 0x14000
	s_nop 0
	global_load_lds_dwordx4 v8, s[4:5]
	s_add_u32 s4, s4, s20
	s_addc_u32 s5, s5, 0
	s_add_u32 m0, s28, 0x16000
	s_nop 0
	global_load_lds_dwordx4 v10, s[6:7]
	s_add_u32 m0, s28, 0x18000
	s_nop 0
	global_load_lds_dwordx4 v11, s[6:7]
	s_add_u32 s6, s6, s20
	s_addc_u32 s7, s7, 0
	s_add_u32 m0, s28, 0x1a000
	s_nop 0
	global_load_lds_dwordx4 v10, s[4:5]
	s_add_u32 m0, s28, 0x1c000
	s_nop 0
	global_load_lds_dwordx4 v11, s[4:5]
	s_add_u32 m0, s28, 0x1e000
	s_nop 0
	global_load_lds_dwordx4 v12, s[4:5]
	s_add_u32 m0, s28, 0x20000
	s_nop 0
	global_load_lds_dwordx4 v13, s[4:5]
	s_add_u32 m0, s28, 0x21000
	s_nop 0
	global_load_lds_dwordx4 v8, s[4:5]
	s_add_u32 s4, s4, s20
	s_addc_u32 s5, s5, 0
	s_add_u32 m0, s28, 0x23000
	s_nop 0
	global_load_lds_dwordx4 v10, s[6:7]
	s_add_u32 m0, s28, 0x25000
	s_nop 0
	global_load_lds_dwordx4 v11, s[6:7]
	s_add_u32 s6, s6, s20
	s_addc_u32 s7, s7, 0
	s_waitcnt vmcnt(14) lgkmcnt(0)
	s_barrier
	s_waitcnt lgkmcnt(7)
	ds_read_b128 v[136:139], v15
	ds_read_b128 v[156:159], v17
	ds_read_b128 v[160:163], v17 offset:2048
	ds_read_b128 v[164:167], v17 offset:4096
	ds_read_b128 v[168:171], v17 offset:6144
	ds_read_b128 v[140:143], v15 offset:2048
	ds_read_b128 v[144:147], v15 offset:4096
	ds_read_b128 v[148:151], v15 offset:6144
	s_waitcnt lgkmcnt(7)
	ds_read_b128 v[172:175], v16
	ds_read_b128 v[192:195], v18
	ds_read_b128 v[196:199], v18 offset:2048
	ds_read_b128 v[200:203], v18 offset:4096
	ds_read_b128 v[204:207], v18 offset:6144
	ds_read_b128 v[176:179], v16 offset:2048
	ds_read_b128 v[180:183], v16 offset:4096
	ds_read_b128 v[184:187], v16 offset:6144
	s_waitcnt lgkmcnt(14)
	v_mfma_f32_16x16x32_f16 v[56:59], v[136:139], v[156:159], 0
	s_waitcnt lgkmcnt(13)
	v_mfma_f32_16x16x32_f16 v[60:63], v[136:139], v[160:163], 0
	s_waitcnt lgkmcnt(12)
	v_mfma_f32_16x16x32_f16 v[64:67], v[136:139], v[164:167], 0
	s_waitcnt lgkmcnt(11)
	v_mfma_f32_16x16x32_f16 v[68:71], v[136:139], v[168:171], 0
	s_waitcnt lgkmcnt(10)
	v_mfma_f32_16x16x32_f16 v[72:75], v[140:143], v[156:159], 0
	v_mfma_f32_16x16x32_f16 v[76:79], v[140:143], v[160:163], 0
	v_mfma_f32_16x16x32_f16 v[80:83], v[140:143], v[164:167], 0
	v_mfma_f32_16x16x32_f16 v[84:87], v[140:143], v[168:171], 0
	s_waitcnt lgkmcnt(9)
	v_mfma_f32_16x16x32_f16 v[88:91], v[144:147], v[156:159], 0
	v_mfma_f32_16x16x32_f16 v[92:95], v[144:147], v[160:163], 0
	v_mfma_f32_16x16x32_f16 v[96:99], v[144:147], v[164:167], 0
	v_mfma_f32_16x16x32_f16 v[100:103], v[144:147], v[168:171], 0
	s_waitcnt lgkmcnt(8)
	v_mfma_f32_16x16x32_f16 v[104:107], v[148:151], v[156:159], 0
	v_mfma_f32_16x16x32_f16 v[108:111], v[148:151], v[160:163], 0
	v_mfma_f32_16x16x32_f16 v[112:115], v[148:151], v[164:167], 0
	v_mfma_f32_16x16x32_f16 v[116:119], v[148:151], v[168:171], 0
	s_waitcnt vmcnt(7) lgkmcnt(0)
	s_barrier
	s_waitcnt lgkmcnt(7)
	ds_read_b128 v[136:139], v15 offset:53248
	ds_read_b128 v[156:159], v17 offset:53248
	ds_read_b128 v[160:163], v17 offset:55296
	ds_read_b128 v[164:167], v17 offset:57344
	ds_read_b128 v[168:171], v17 offset:59392
	ds_read_b128 v[140:143], v15 offset:55296
	ds_read_b128 v[144:147], v15 offset:57344
	ds_read_b128 v[148:151], v15 offset:59392
	s_waitcnt lgkmcnt(14)
	v_mfma_f32_16x16x32_f16 v[56:59], v[172:175], v[192:195], v[56:59]
	s_add_u32 m0, s28, 0x0
	s_nop 0
	global_load_lds_dwordx4 v10, s[4:5]
	s_waitcnt lgkmcnt(13)
	v_mfma_f32_16x16x32_f16 v[60:63], v[172:175], v[196:199], v[60:63]
	s_waitcnt lgkmcnt(12)
	v_mfma_f32_16x16x32_f16 v[64:67], v[172:175], v[200:203], v[64:67]
	s_waitcnt lgkmcnt(11)
	v_mfma_f32_16x16x32_f16 v[68:71], v[172:175], v[204:207], v[68:71]
	s_waitcnt lgkmcnt(10)
	v_mfma_f32_16x16x32_f16 v[72:75], v[176:179], v[192:195], v[72:75]
	s_add_u32 m0, s28, 0x2000
	s_nop 0
	global_load_lds_dwordx4 v11, s[4:5]
	v_mfma_f32_16x16x32_f16 v[76:79], v[176:179], v[196:199], v[76:79]
	v_mfma_f32_16x16x32_f16 v[80:83], v[176:179], v[200:203], v[80:83]
	v_mfma_f32_16x16x32_f16 v[84:87], v[176:179], v[204:207], v[84:87]
	s_waitcnt lgkmcnt(9)
	v_mfma_f32_16x16x32_f16 v[88:91], v[180:183], v[192:195], v[88:91]
	s_add_u32 m0, s28, 0x4000
	s_nop 0
	global_load_lds_dwordx4 v12, s[4:5]
	v_mfma_f32_16x16x32_f16 v[92:95], v[180:183], v[196:199], v[92:95]
	v_mfma_f32_16x16x32_f16 v[96:99], v[180:183], v[200:203], v[96:99]
	v_mfma_f32_16x16x32_f16 v[100:103], v[180:183], v[204:207], v[100:103]
	s_waitcnt lgkmcnt(8)
	v_mfma_f32_16x16x32_f16 v[104:107], v[184:187], v[192:195], v[104:107]
	s_add_u32 m0, s28, 0x6000
	s_nop 0
	global_load_lds_dwordx4 v13, s[4:5]
	v_mfma_f32_16x16x32_f16 v[108:111], v[184:187], v[196:199], v[108:111]
	v_mfma_f32_16x16x32_f16 v[112:115], v[184:187], v[200:203], v[112:115]
	v_mfma_f32_16x16x32_f16 v[116:119], v[184:187], v[204:207], v[116:119]
	s_waitcnt lgkmcnt(7)
	ds_read_b128 v[172:175], v16 offset:53248
	ds_read_b128 v[192:195], v18 offset:53248
	ds_read_b128 v[196:199], v18 offset:55296
	ds_read_b128 v[200:203], v18 offset:57344
	ds_read_b128 v[204:207], v18 offset:59392
	ds_read_b128 v[176:179], v16 offset:55296
	ds_read_b128 v[180:183], v16 offset:57344
	ds_read_b128 v[184:187], v16 offset:59392
	s_waitcnt lgkmcnt(14)
	v_mfma_f32_16x16x32_f16 v[56:59], v[136:139], v[156:159], v[56:59]
	s_add_u32 m0, s28, 0x7000
	s_nop 0
	global_load_lds_dwordx4 v8, s[4:5]
	s_add_u32 s4, s4, s20
	s_addc_u32 s5, s5, 0
	s_waitcnt lgkmcnt(13)
	v_mfma_f32_16x16x32_f16 v[60:63], v[136:139], v[160:163], v[60:63]
	s_waitcnt lgkmcnt(12)
	v_mfma_f32_16x16x32_f16 v[64:67], v[136:139], v[164:167], v[64:67]
	s_waitcnt lgkmcnt(11)
	v_mfma_f32_16x16x32_f16 v[68:71], v[136:139], v[168:171], v[68:71]
	s_waitcnt lgkmcnt(10)
	v_mfma_f32_16x16x32_f16 v[72:75], v[140:143], v[156:159], v[72:75]
	v_mfma_f32_16x16x32_f16 v[76:79], v[140:143], v[160:163], v[76:79]
	s_add_u32 m0, s28, 0x9000
	s_nop 0
	global_load_lds_dwordx4 v10, s[6:7]
	v_mfma_f32_16x16x32_f16 v[80:83], v[140:143], v[164:167], v[80:83]
	v_mfma_f32_16x16x32_f16 v[84:87], v[140:143], v[168:171], v[84:87]
	s_waitcnt lgkmcnt(9)
	v_mfma_f32_16x16x32_f16 v[88:91], v[144:147], v[156:159], v[88:91]
	v_mfma_f32_16x16x32_f16 v[92:95], v[144:147], v[160:163], v[92:95]
	v_mfma_f32_16x16x32_f16 v[96:99], v[144:147], v[164:167], v[96:99]
	s_add_u32 m0, s28, 0xb000
	s_nop 0
	global_load_lds_dwordx4 v11, s[6:7]
	s_add_u32 s6, s6, s20
	s_addc_u32 s7, s7, 0
	v_mfma_f32_16x16x32_f16 v[100:103], v[144:147], v[168:171], v[100:103]
	s_waitcnt lgkmcnt(8)
	v_mfma_f32_16x16x32_f16 v[104:107], v[148:151], v[156:159], v[104:107]
	v_mfma_f32_16x16x32_f16 v[108:111], v[148:151], v[160:163], v[108:111]
	v_mfma_f32_16x16x32_f16 v[112:115], v[148:151], v[164:167], v[112:115]
	v_mfma_f32_16x16x32_f16 v[116:119], v[148:151], v[168:171], v[116:119]
	s_waitcnt vmcnt(7) lgkmcnt(0)
	s_barrier
	s_waitcnt lgkmcnt(7)
	ds_read_b128 v[136:139], v19
	ds_read_b128 v[156:159], v21
	ds_read_b128 v[160:163], v21 offset:2048
	ds_read_b128 v[164:167], v21 offset:4096
	ds_read_b128 v[168:171], v21 offset:6144
	ds_read_b128 v[140:143], v19 offset:2048
	ds_read_b128 v[144:147], v19 offset:4096
	ds_read_b128 v[148:151], v19 offset:6144
	s_waitcnt lgkmcnt(14)
	v_mfma_f32_16x16x32_f16 v[56:59], v[172:175], v[192:195], v[56:59]
	s_add_u32 m0, s28, 0xd000
	s_nop 0
	global_load_lds_dwordx4 v10, s[4:5]
	s_waitcnt lgkmcnt(13)
	v_mfma_f32_16x16x32_f16 v[60:63], v[172:175], v[196:199], v[60:63]
	s_waitcnt lgkmcnt(12)
	v_mfma_f32_16x16x32_f16 v[64:67], v[172:175], v[200:203], v[64:67]
	s_waitcnt lgkmcnt(11)
	v_mfma_f32_16x16x32_f16 v[68:71], v[172:175], v[204:207], v[68:71]
	s_waitcnt lgkmcnt(10)
	v_mfma_f32_16x16x32_f16 v[72:75], v[176:179], v[192:195], v[72:75]
	s_add_u32 m0, s28, 0xf000
	s_nop 0
	global_load_lds_dwordx4 v11, s[4:5]
	v_mfma_f32_16x16x32_f16 v[76:79], v[176:179], v[196:199], v[76:79]
	v_mfma_f32_16x16x32_f16 v[80:83], v[176:179], v[200:203], v[80:83]
	v_mfma_f32_16x16x32_f16 v[84:87], v[176:179], v[204:207], v[84:87]
	s_waitcnt lgkmcnt(9)
	v_mfma_f32_16x16x32_f16 v[88:91], v[180:183], v[192:195], v[88:91]
	s_add_u32 m0, s28, 0x11000
	s_nop 0
	global_load_lds_dwordx4 v12, s[4:5]
	v_mfma_f32_16x16x32_f16 v[92:95], v[180:183], v[196:199], v[92:95]
	v_mfma_f32_16x16x32_f16 v[96:99], v[180:183], v[200:203], v[96:99]
	v_mfma_f32_16x16x32_f16 v[100:103], v[180:183], v[204:207], v[100:103]
	s_waitcnt lgkmcnt(8)
	v_mfma_f32_16x16x32_f16 v[104:107], v[184:187], v[192:195], v[104:107]
	s_add_u32 m0, s28, 0x13000
	s_nop 0
	global_load_lds_dwordx4 v13, s[4:5]
	v_mfma_f32_16x16x32_f16 v[108:111], v[184:187], v[196:199], v[108:111]
	v_mfma_f32_16x16x32_f16 v[112:115], v[184:187], v[200:203], v[112:115]
	v_mfma_f32_16x16x32_f16 v[116:119], v[184:187], v[204:207], v[116:119]
	s_waitcnt lgkmcnt(7)
	ds_read_b128 v[172:175], v20
	ds_read_b128 v[192:195], v22
	ds_read_b128 v[196:199], v22 offset:2048
	ds_read_b128 v[200:203], v22 offset:4096
	ds_read_b128 v[204:207], v22 offset:6144
	ds_read_b128 v[176:179], v20 offset:2048
	ds_read_b128 v[180:183], v20 offset:4096
	ds_read_b128 v[184:187], v20 offset:6144
	s_waitcnt lgkmcnt(14)
	v_mfma_f32_16x16x32_f16 v[56:59], v[136:139], v[156:159], v[56:59]
	s_add_u32 m0, s28, 0x14000
	s_nop 0
	global_load_lds_dwordx4 v8, s[4:5]
	s_add_u32 s4, s4, s20
	s_addc_u32 s5, s5, 0
	s_waitcnt lgkmcnt(13)
	v_mfma_f32_16x16x32_f16 v[60:63], v[136:139], v[160:163], v[60:63]
	s_waitcnt lgkmcnt(12)
	v_mfma_f32_16x16x32_f16 v[64:67], v[136:139], v[164:167], v[64:67]
	s_waitcnt lgkmcnt(11)
	v_mfma_f32_16x16x32_f16 v[68:71], v[136:139], v[168:171], v[68:71]
	s_waitcnt lgkmcnt(10)
	v_mfma_f32_16x16x32_f16 v[72:75], v[140:143], v[156:159], v[72:75]
	v_mfma_f32_16x16x32_f16 v[76:79], v[140:143], v[160:163], v[76:79]
	s_add_u32 m0, s28, 0x16000
	s_nop 0
	global_load_lds_dwordx4 v10, s[6:7]
	v_mfma_f32_16x16x32_f16 v[80:83], v[140:143], v[164:167], v[80:83]
	v_mfma_f32_16x16x32_f16 v[84:87], v[140:143], v[168:171], v[84:87]
	s_waitcnt lgkmcnt(9)
	v_mfma_f32_16x16x32_f16 v[88:91], v[144:147], v[156:159], v[88:91]
	v_mfma_f32_16x16x32_f16 v[92:95], v[144:147], v[160:163], v[92:95]
	v_mfma_f32_16x16x32_f16 v[96:99], v[144:147], v[164:167], v[96:99]
	s_add_u32 m0, s28, 0x18000
	s_nop 0
	global_load_lds_dwordx4 v11, s[6:7]
	s_add_u32 s6, s6, s20
	s_addc_u32 s7, s7, 0
	v_mfma_f32_16x16x32_f16 v[100:103], v[144:147], v[168:171], v[100:103]
	s_waitcnt lgkmcnt(8)
	v_mfma_f32_16x16x32_f16 v[104:107], v[148:151], v[156:159], v[104:107]
	v_mfma_f32_16x16x32_f16 v[108:111], v[148:151], v[160:163], v[108:111]
	v_mfma_f32_16x16x32_f16 v[112:115], v[148:151], v[164:167], v[112:115]
	v_mfma_f32_16x16x32_f16 v[116:119], v[148:151], v[168:171], v[116:119]
	s_waitcnt vmcnt(7) lgkmcnt(0)
	s_barrier
	s_waitcnt lgkmcnt(7)
	ds_read_b128 v[136:139], v15
	ds_read_b128 v[156:159], v17
	ds_read_b128 v[160:163], v17 offset:2048
	ds_read_b128 v[164:167], v17 offset:4096
	ds_read_b128 v[168:171], v17 offset:6144
	ds_read_b128 v[140:143], v15 offset:2048
	ds_read_b128 v[144:147], v15 offset:4096
	ds_read_b128 v[148:151], v15 offset:6144
	s_waitcnt lgkmcnt(14)
	v_mfma_f32_16x16x32_f16 v[56:59], v[172:175], v[192:195], v[56:59]
	s_add_u32 m0, s28, 0x1a000
	s_nop 0
	global_load_lds_dwordx4 v10, s[4:5]
	s_waitcnt lgkmcnt(13)
	v_mfma_f32_16x16x32_f16 v[60:63], v[172:175], v[196:199], v[60:63]
	s_waitcnt lgkmcnt(12)
	v_mfma_f32_16x16x32_f16 v[64:67], v[172:175], v[200:203], v[64:67]
	s_waitcnt lgkmcnt(11)
	v_mfma_f32_16x16x32_f16 v[68:71], v[172:175], v[204:207], v[68:71]
	s_waitcnt lgkmcnt(10)
	v_mfma_f32_16x16x32_f16 v[72:75], v[176:179], v[192:195], v[72:75]
	s_add_u32 m0, s28, 0x1c000
	s_nop 0
	global_load_lds_dwordx4 v11, s[4:5]
	v_mfma_f32_16x16x32_f16 v[76:79], v[176:179], v[196:199], v[76:79]
	v_mfma_f32_16x16x32_f16 v[80:83], v[176:179], v[200:203], v[80:83]
	v_mfma_f32_16x16x32_f16 v[84:87], v[176:179], v[204:207], v[84:87]
	s_waitcnt lgkmcnt(9)
	v_mfma_f32_16x16x32_f16 v[88:91], v[180:183], v[192:195], v[88:91]
	s_add_u32 m0, s28, 0x1e000
	s_nop 0
	global_load_lds_dwordx4 v12, s[4:5]
	v_mfma_f32_16x16x32_f16 v[92:95], v[180:183], v[196:199], v[92:95]
	v_mfma_f32_16x16x32_f16 v[96:99], v[180:183], v[200:203], v[96:99]
	v_mfma_f32_16x16x32_f16 v[100:103], v[180:183], v[204:207], v[100:103]
	s_waitcnt lgkmcnt(8)
	v_mfma_f32_16x16x32_f16 v[104:107], v[184:187], v[192:195], v[104:107]
	s_add_u32 m0, s28, 0x20000
	s_nop 0
	global_load_lds_dwordx4 v13, s[4:5]
	v_mfma_f32_16x16x32_f16 v[108:111], v[184:187], v[196:199], v[108:111]
	v_mfma_f32_16x16x32_f16 v[112:115], v[184:187], v[200:203], v[112:115]
	v_mfma_f32_16x16x32_f16 v[116:119], v[184:187], v[204:207], v[116:119]
	s_waitcnt lgkmcnt(7)
	ds_read_b128 v[172:175], v16
	ds_read_b128 v[192:195], v18
	ds_read_b128 v[196:199], v18 offset:2048
	ds_read_b128 v[200:203], v18 offset:4096
	ds_read_b128 v[204:207], v18 offset:6144
	ds_read_b128 v[176:179], v16 offset:2048
	ds_read_b128 v[180:183], v16 offset:4096
	ds_read_b128 v[184:187], v16 offset:6144
	s_waitcnt lgkmcnt(14)
	v_mfma_f32_16x16x32_f16 v[56:59], v[136:139], v[156:159], v[56:59]
	s_add_u32 m0, s28, 0x21000
	s_nop 0
	global_load_lds_dwordx4 v8, s[4:5]
	s_add_u32 s4, s4, s20
	s_addc_u32 s5, s5, 0
	s_waitcnt lgkmcnt(13)
	v_mfma_f32_16x16x32_f16 v[60:63], v[136:139], v[160:163], v[60:63]
	s_waitcnt lgkmcnt(12)
	v_mfma_f32_16x16x32_f16 v[64:67], v[136:139], v[164:167], v[64:67]
	s_waitcnt lgkmcnt(11)
	v_mfma_f32_16x16x32_f16 v[68:71], v[136:139], v[168:171], v[68:71]
	s_waitcnt lgkmcnt(10)
	v_mfma_f32_16x16x32_f16 v[72:75], v[140:143], v[156:159], v[72:75]
	v_mfma_f32_16x16x32_f16 v[76:79], v[140:143], v[160:163], v[76:79]
	s_add_u32 m0, s28, 0x23000
	s_nop 0
	global_load_lds_dwordx4 v10, s[6:7]
	v_mfma_f32_16x16x32_f16 v[80:83], v[140:143], v[164:167], v[80:83]
	v_mfma_f32_16x16x32_f16 v[84:87], v[140:143], v[168:171], v[84:87]
	s_waitcnt lgkmcnt(9)
	v_mfma_f32_16x16x32_f16 v[88:91], v[144:147], v[156:159], v[88:91]
	v_mfma_f32_16x16x32_f16 v[92:95], v[144:147], v[160:163], v[92:95]
	v_mfma_f32_16x16x32_f16 v[96:99], v[144:147], v[164:167], v[96:99]
	s_add_u32 m0, s28, 0x25000
	s_nop 0
	global_load_lds_dwordx4 v11, s[6:7]
	s_add_u32 s6, s6, s20
	s_addc_u32 s7, s7, 0
	v_mfma_f32_16x16x32_f16 v[100:103], v[144:147], v[168:171], v[100:103]
	s_waitcnt lgkmcnt(8)
	v_mfma_f32_16x16x32_f16 v[104:107], v[148:151], v[156:159], v[104:107]
	v_mfma_f32_16x16x32_f16 v[108:111], v[148:151], v[160:163], v[108:111]
	v_mfma_f32_16x16x32_f16 v[112:115], v[148:151], v[164:167], v[112:115]
	v_mfma_f32_16x16x32_f16 v[116:119], v[148:151], v[168:171], v[116:119]
	s_waitcnt vmcnt(7) lgkmcnt(0)
	s_barrier
	s_waitcnt lgkmcnt(7)
	ds_read_b128 v[136:139], v15 offset:53248
	ds_read_b128 v[156:159], v17 offset:53248
	ds_read_b128 v[160:163], v17 offset:55296
	ds_read_b128 v[164:167], v17 offset:57344
	ds_read_b128 v[168:171], v17 offset:59392
	ds_read_b128 v[140:143], v15 offset:55296
	ds_read_b128 v[144:147], v15 offset:57344
	ds_read_b128 v[148:151], v15 offset:59392
	s_waitcnt lgkmcnt(14)
	v_mfma_f32_16x16x32_f16 v[56:59], v[172:175], v[192:195], v[56:59]
	s_add_u32 m0, s28, 0x0
	s_nop 0
	global_load_lds_dwordx4 v10, s[4:5]
	s_waitcnt lgkmcnt(13)
	v_mfma_f32_16x16x32_f16 v[60:63], v[172:175], v[196:199], v[60:63]
	s_waitcnt lgkmcnt(12)
	v_mfma_f32_16x16x32_f16 v[64:67], v[172:175], v[200:203], v[64:67]
	s_waitcnt lgkmcnt(11)
	v_mfma_f32_16x16x32_f16 v[68:71], v[172:175], v[204:207], v[68:71]
	s_waitcnt lgkmcnt(10)
	v_mfma_f32_16x16x32_f16 v[72:75], v[176:179], v[192:195], v[72:75]
	s_add_u32 m0, s28, 0x2000
	s_nop 0
	global_load_lds_dwordx4 v11, s[4:5]
	v_mfma_f32_16x16x32_f16 v[76:79], v[176:179], v[196:199], v[76:79]
	v_mfma_f32_16x16x32_f16 v[80:83], v[176:179], v[200:203], v[80:83]
	v_mfma_f32_16x16x32_f16 v[84:87], v[176:179], v[204:207], v[84:87]
	s_waitcnt lgkmcnt(9)
	v_mfma_f32_16x16x32_f16 v[88:91], v[180:183], v[192:195], v[88:91]
	s_add_u32 m0, s28, 0x4000
	s_nop 0
	global_load_lds_dwordx4 v12, s[4:5]
	v_mfma_f32_16x16x32_f16 v[92:95], v[180:183], v[196:199], v[92:95]
	v_mfma_f32_16x16x32_f16 v[96:99], v[180:183], v[200:203], v[96:99]
	v_mfma_f32_16x16x32_f16 v[100:103], v[180:183], v[204:207], v[100:103]
	s_waitcnt lgkmcnt(8)
	v_mfma_f32_16x16x32_f16 v[104:107], v[184:187], v[192:195], v[104:107]
	s_add_u32 m0, s28, 0x6000
	s_nop 0
	global_load_lds_dwordx4 v13, s[4:5]
	v_mfma_f32_16x16x32_f16 v[108:111], v[184:187], v[196:199], v[108:111]
	v_mfma_f32_16x16x32_f16 v[112:115], v[184:187], v[200:203], v[112:115]
	v_mfma_f32_16x16x32_f16 v[116:119], v[184:187], v[204:207], v[116:119]
	s_waitcnt lgkmcnt(7)
	ds_read_b128 v[172:175], v16 offset:53248
	ds_read_b128 v[192:195], v18 offset:53248
	ds_read_b128 v[196:199], v18 offset:55296
	ds_read_b128 v[200:203], v18 offset:57344
	ds_read_b128 v[204:207], v18 offset:59392
	ds_read_b128 v[176:179], v16 offset:55296
	ds_read_b128 v[180:183], v16 offset:57344
	ds_read_b128 v[184:187], v16 offset:59392
	s_waitcnt lgkmcnt(14)
	v_mfma_f32_16x16x32_f16 v[56:59], v[136:139], v[156:159], v[56:59]
	s_add_u32 m0, s28, 0x7000
	s_nop 0
	global_load_lds_dwordx4 v8, s[4:5]
	s_add_u32 s4, s4, s20
	s_addc_u32 s5, s5, 0
	s_waitcnt lgkmcnt(13)
	v_mfma_f32_16x16x32_f16 v[60:63], v[136:139], v[160:163], v[60:63]
	s_waitcnt lgkmcnt(12)
	v_mfma_f32_16x16x32_f16 v[64:67], v[136:139], v[164:167], v[64:67]
	s_waitcnt lgkmcnt(11)
	v_mfma_f32_16x16x32_f16 v[68:71], v[136:139], v[168:171], v[68:71]
	s_waitcnt lgkmcnt(10)
	v_mfma_f32_16x16x32_f16 v[72:75], v[140:143], v[156:159], v[72:75]
	v_mfma_f32_16x16x32_f16 v[76:79], v[140:143], v[160:163], v[76:79]
	s_add_u32 m0, s28, 0x9000
	s_nop 0
	global_load_lds_dwordx4 v10, s[6:7]
	v_mfma_f32_16x16x32_f16 v[80:83], v[140:143], v[164:167], v[80:83]
	v_mfma_f32_16x16x32_f16 v[84:87], v[140:143], v[168:171], v[84:87]
	s_waitcnt lgkmcnt(9)
	v_mfma_f32_16x16x32_f16 v[88:91], v[144:147], v[156:159], v[88:91]
	v_mfma_f32_16x16x32_f16 v[92:95], v[144:147], v[160:163], v[92:95]
	v_mfma_f32_16x16x32_f16 v[96:99], v[144:147], v[164:167], v[96:99]
	s_add_u32 m0, s28, 0xb000
	s_nop 0
	global_load_lds_dwordx4 v11, s[6:7]
	s_add_u32 s6, s6, s20
	s_addc_u32 s7, s7, 0
	v_mfma_f32_16x16x32_f16 v[100:103], v[144:147], v[168:171], v[100:103]
	s_waitcnt lgkmcnt(8)
	v_mfma_f32_16x16x32_f16 v[104:107], v[148:151], v[156:159], v[104:107]
	v_mfma_f32_16x16x32_f16 v[108:111], v[148:151], v[160:163], v[108:111]
	v_mfma_f32_16x16x32_f16 v[112:115], v[148:151], v[164:167], v[112:115]
	v_mfma_f32_16x16x32_f16 v[116:119], v[148:151], v[168:171], v[116:119]
	s_waitcnt vmcnt(7) lgkmcnt(0)
	s_barrier
	s_waitcnt lgkmcnt(7)
	ds_read_b128 v[136:139], v19
	ds_read_b128 v[156:159], v21
	ds_read_b128 v[160:163], v21 offset:2048
	ds_read_b128 v[164:167], v21 offset:4096
	ds_read_b128 v[168:171], v21 offset:6144
	ds_read_b128 v[140:143], v19 offset:2048
	ds_read_b128 v[144:147], v19 offset:4096
	ds_read_b128 v[148:151], v19 offset:6144
	s_waitcnt lgkmcnt(14)
	v_mfma_f32_16x16x32_f16 v[56:59], v[172:175], v[192:195], v[56:59]
	s_add_u32 m0, s28, 0xd000
	s_nop 0
	global_load_lds_dwordx4 v10, s[4:5]
	s_waitcnt lgkmcnt(13)
	v_mfma_f32_16x16x32_f16 v[60:63], v[172:175], v[196:199], v[60:63]
	s_waitcnt lgkmcnt(12)
	v_mfma_f32_16x16x32_f16 v[64:67], v[172:175], v[200:203], v[64:67]
	s_waitcnt lgkmcnt(11)
	v_mfma_f32_16x16x32_f16 v[68:71], v[172:175], v[204:207], v[68:71]
	s_waitcnt lgkmcnt(10)
	v_mfma_f32_16x16x32_f16 v[72:75], v[176:179], v[192:195], v[72:75]
	s_add_u32 m0, s28, 0xf000
	s_nop 0
	global_load_lds_dwordx4 v11, s[4:5]
	v_mfma_f32_16x16x32_f16 v[76:79], v[176:179], v[196:199], v[76:79]
	v_mfma_f32_16x16x32_f16 v[80:83], v[176:179], v[200:203], v[80:83]
	v_mfma_f32_16x16x32_f16 v[84:87], v[176:179], v[204:207], v[84:87]
	s_waitcnt lgkmcnt(9)
	v_mfma_f32_16x16x32_f16 v[88:91], v[180:183], v[192:195], v[88:91]
	s_add_u32 m0, s28, 0x11000
	s_nop 0
	global_load_lds_dwordx4 v12, s[4:5]
	v_mfma_f32_16x16x32_f16 v[92:95], v[180:183], v[196:199], v[92:95]
	v_mfma_f32_16x16x32_f16 v[96:99], v[180:183], v[200:203], v[96:99]
	v_mfma_f32_16x16x32_f16 v[100:103], v[180:183], v[204:207], v[100:103]
	s_waitcnt lgkmcnt(8)
	v_mfma_f32_16x16x32_f16 v[104:107], v[184:187], v[192:195], v[104:107]
	s_add_u32 m0, s28, 0x13000
	s_nop 0
	global_load_lds_dwordx4 v13, s[4:5]
	v_mfma_f32_16x16x32_f16 v[108:111], v[184:187], v[196:199], v[108:111]
	v_mfma_f32_16x16x32_f16 v[112:115], v[184:187], v[200:203], v[112:115]
	v_mfma_f32_16x16x32_f16 v[116:119], v[184:187], v[204:207], v[116:119]
	s_waitcnt lgkmcnt(7)
	ds_read_b128 v[172:175], v20
	ds_read_b128 v[192:195], v22
	ds_read_b128 v[196:199], v22 offset:2048
	ds_read_b128 v[200:203], v22 offset:4096
	ds_read_b128 v[204:207], v22 offset:6144
	ds_read_b128 v[176:179], v20 offset:2048
	ds_read_b128 v[180:183], v20 offset:4096
	ds_read_b128 v[184:187], v20 offset:6144
	s_waitcnt lgkmcnt(14)
	v_mfma_f32_16x16x32_f16 v[56:59], v[136:139], v[156:159], v[56:59]
	s_add_u32 m0, s28, 0x14000
	s_nop 0
	global_load_lds_dwordx4 v8, s[4:5]
	s_add_u32 s4, s4, s20
	s_addc_u32 s5, s5, 0
	s_waitcnt lgkmcnt(13)
	v_mfma_f32_16x16x32_f16 v[60:63], v[136:139], v[160:163], v[60:63]
	s_waitcnt lgkmcnt(12)
	v_mfma_f32_16x16x32_f16 v[64:67], v[136:139], v[164:167], v[64:67]
	s_waitcnt lgkmcnt(11)
	v_mfma_f32_16x16x32_f16 v[68:71], v[136:139], v[168:171], v[68:71]
	s_waitcnt lgkmcnt(10)
	v_mfma_f32_16x16x32_f16 v[72:75], v[140:143], v[156:159], v[72:75]
	v_mfma_f32_16x16x32_f16 v[76:79], v[140:143], v[160:163], v[76:79]
	s_add_u32 m0, s28, 0x16000
	s_nop 0
	global_load_lds_dwordx4 v10, s[6:7]
	v_mfma_f32_16x16x32_f16 v[80:83], v[140:143], v[164:167], v[80:83]
	v_mfma_f32_16x16x32_f16 v[84:87], v[140:143], v[168:171], v[84:87]
	s_waitcnt lgkmcnt(9)
	v_mfma_f32_16x16x32_f16 v[88:91], v[144:147], v[156:159], v[88:91]
	v_mfma_f32_16x16x32_f16 v[92:95], v[144:147], v[160:163], v[92:95]
	v_mfma_f32_16x16x32_f16 v[96:99], v[144:147], v[164:167], v[96:99]
	s_add_u32 m0, s28, 0x18000
	s_nop 0
	global_load_lds_dwordx4 v11, s[6:7]
	s_add_u32 s6, s6, s20
	s_addc_u32 s7, s7, 0
	v_mfma_f32_16x16x32_f16 v[100:103], v[144:147], v[168:171], v[100:103]
	s_waitcnt lgkmcnt(8)
	v_mfma_f32_16x16x32_f16 v[104:107], v[148:151], v[156:159], v[104:107]
	v_mfma_f32_16x16x32_f16 v[108:111], v[148:151], v[160:163], v[108:111]
	v_mfma_f32_16x16x32_f16 v[112:115], v[148:151], v[164:167], v[112:115]
	v_mfma_f32_16x16x32_f16 v[116:119], v[148:151], v[168:171], v[116:119]
	s_waitcnt vmcnt(7) lgkmcnt(0)
	s_barrier
	s_waitcnt lgkmcnt(7)
	ds_read_b128 v[136:139], v15
	ds_read_b128 v[156:159], v17
	ds_read_b128 v[160:163], v17 offset:2048
	ds_read_b128 v[164:167], v17 offset:4096
	ds_read_b128 v[168:171], v17 offset:6144
	ds_read_b128 v[140:143], v15 offset:2048
	ds_read_b128 v[144:147], v15 offset:4096
	ds_read_b128 v[148:151], v15 offset:6144
	s_waitcnt lgkmcnt(14)
	v_mfma_f32_16x16x32_f16 v[56:59], v[172:175], v[192:195], v[56:59]
	s_add_u32 m0, s28, 0x1a000
	s_nop 0
	global_load_lds_dwordx4 v10, s[4:5]
	s_waitcnt lgkmcnt(13)
	v_mfma_f32_16x16x32_f16 v[60:63], v[172:175], v[196:199], v[60:63]
	s_waitcnt lgkmcnt(12)
	v_mfma_f32_16x16x32_f16 v[64:67], v[172:175], v[200:203], v[64:67]
	s_waitcnt lgkmcnt(11)
	v_mfma_f32_16x16x32_f16 v[68:71], v[172:175], v[204:207], v[68:71]
	s_waitcnt lgkmcnt(10)
	v_mfma_f32_16x16x32_f16 v[72:75], v[176:179], v[192:195], v[72:75]
	s_add_u32 m0, s28, 0x1c000
	s_nop 0
	global_load_lds_dwordx4 v11, s[4:5]
	v_mfma_f32_16x16x32_f16 v[76:79], v[176:179], v[196:199], v[76:79]
	v_mfma_f32_16x16x32_f16 v[80:83], v[176:179], v[200:203], v[80:83]
	v_mfma_f32_16x16x32_f16 v[84:87], v[176:179], v[204:207], v[84:87]
	s_waitcnt lgkmcnt(9)
	v_mfma_f32_16x16x32_f16 v[88:91], v[180:183], v[192:195], v[88:91]
	s_add_u32 m0, s28, 0x1e000
	s_nop 0
	global_load_lds_dwordx4 v12, s[4:5]
	v_mfma_f32_16x16x32_f16 v[92:95], v[180:183], v[196:199], v[92:95]
	v_mfma_f32_16x16x32_f16 v[96:99], v[180:183], v[200:203], v[96:99]
	v_mfma_f32_16x16x32_f16 v[100:103], v[180:183], v[204:207], v[100:103]
	s_waitcnt lgkmcnt(8)
	v_mfma_f32_16x16x32_f16 v[104:107], v[184:187], v[192:195], v[104:107]
	s_add_u32 m0, s28, 0x20000
	s_nop 0
	global_load_lds_dwordx4 v13, s[4:5]
	v_mfma_f32_16x16x32_f16 v[108:111], v[184:187], v[196:199], v[108:111]
	v_mfma_f32_16x16x32_f16 v[112:115], v[184:187], v[200:203], v[112:115]
	v_mfma_f32_16x16x32_f16 v[116:119], v[184:187], v[204:207], v[116:119]
	s_waitcnt lgkmcnt(7)
	ds_read_b128 v[172:175], v16
	ds_read_b128 v[192:195], v18
	ds_read_b128 v[196:199], v18 offset:2048
	ds_read_b128 v[200:203], v18 offset:4096
	ds_read_b128 v[204:207], v18 offset:6144
	ds_read_b128 v[176:179], v16 offset:2048
	ds_read_b128 v[180:183], v16 offset:4096
	ds_read_b128 v[184:187], v16 offset:6144
	s_waitcnt lgkmcnt(14)
	v_mfma_f32_16x16x32_f16 v[56:59], v[136:139], v[156:159], v[56:59]
	s_add_u32 m0, s28, 0x21000
	s_nop 0
	global_load_lds_dwordx4 v8, s[4:5]
	s_add_u32 s4, s4, s20
	s_addc_u32 s5, s5, 0
	s_waitcnt lgkmcnt(13)
	v_mfma_f32_16x16x32_f16 v[60:63], v[136:139], v[160:163], v[60:63]
	s_waitcnt lgkmcnt(12)
	v_mfma_f32_16x16x32_f16 v[64:67], v[136:139], v[164:167], v[64:67]
	s_waitcnt lgkmcnt(11)
	v_mfma_f32_16x16x32_f16 v[68:71], v[136:139], v[168:171], v[68:71]
	s_waitcnt lgkmcnt(10)
	v_mfma_f32_16x16x32_f16 v[72:75], v[140:143], v[156:159], v[72:75]
	v_mfma_f32_16x16x32_f16 v[76:79], v[140:143], v[160:163], v[76:79]
	s_add_u32 m0, s28, 0x23000
	s_nop 0
	global_load_lds_dwordx4 v10, s[6:7]
	v_mfma_f32_16x16x32_f16 v[80:83], v[140:143], v[164:167], v[80:83]
	v_mfma_f32_16x16x32_f16 v[84:87], v[140:143], v[168:171], v[84:87]
	s_waitcnt lgkmcnt(9)
	v_mfma_f32_16x16x32_f16 v[88:91], v[144:147], v[156:159], v[88:91]
	v_mfma_f32_16x16x32_f16 v[92:95], v[144:147], v[160:163], v[92:95]
	v_mfma_f32_16x16x32_f16 v[96:99], v[144:147], v[164:167], v[96:99]
	s_add_u32 m0, s28, 0x25000
	s_nop 0
	global_load_lds_dwordx4 v11, s[6:7]
	s_add_u32 s6, s6, s20
	s_addc_u32 s7, s7, 0
	v_mfma_f32_16x16x32_f16 v[100:103], v[144:147], v[168:171], v[100:103]
	s_waitcnt lgkmcnt(8)
	v_mfma_f32_16x16x32_f16 v[104:107], v[148:151], v[156:159], v[104:107]
	v_mfma_f32_16x16x32_f16 v[108:111], v[148:151], v[160:163], v[108:111]
	v_mfma_f32_16x16x32_f16 v[112:115], v[148:151], v[164:167], v[112:115]
	v_mfma_f32_16x16x32_f16 v[116:119], v[148:151], v[168:171], v[116:119]
	s_waitcnt vmcnt(7) lgkmcnt(0)
	s_barrier
	s_waitcnt lgkmcnt(7)
	ds_read_b128 v[136:139], v15 offset:53248
	ds_read_b128 v[156:159], v17 offset:53248
	ds_read_b128 v[160:163], v17 offset:55296
	ds_read_b128 v[164:167], v17 offset:57344
	ds_read_b128 v[168:171], v17 offset:59392
	ds_read_b128 v[140:143], v15 offset:55296
	ds_read_b128 v[144:147], v15 offset:57344
	ds_read_b128 v[148:151], v15 offset:59392
	s_waitcnt lgkmcnt(14)
	v_mfma_f32_16x16x32_f16 v[56:59], v[172:175], v[192:195], v[56:59]
	s_add_u32 m0, s28, 0x0
	s_nop 0
	global_load_lds_dwordx4 v10, s[4:5]
	s_waitcnt lgkmcnt(13)
	v_mfma_f32_16x16x32_f16 v[60:63], v[172:175], v[196:199], v[60:63]
	s_waitcnt lgkmcnt(12)
	v_mfma_f32_16x16x32_f16 v[64:67], v[172:175], v[200:203], v[64:67]
	s_waitcnt lgkmcnt(11)
	v_mfma_f32_16x16x32_f16 v[68:71], v[172:175], v[204:207], v[68:71]
	s_waitcnt lgkmcnt(10)
	v_mfma_f32_16x16x32_f16 v[72:75], v[176:179], v[192:195], v[72:75]
	s_add_u32 m0, s28, 0x2000
	s_nop 0
	global_load_lds_dwordx4 v11, s[4:5]
	v_mfma_f32_16x16x32_f16 v[76:79], v[176:179], v[196:199], v[76:79]
	v_mfma_f32_16x16x32_f16 v[80:83], v[176:179], v[200:203], v[80:83]
	v_mfma_f32_16x16x32_f16 v[84:87], v[176:179], v[204:207], v[84:87]
	s_waitcnt lgkmcnt(9)
	v_mfma_f32_16x16x32_f16 v[88:91], v[180:183], v[192:195], v[88:91]
	s_add_u32 m0, s28, 0x4000
	s_nop 0
	global_load_lds_dwordx4 v12, s[4:5]
	v_mfma_f32_16x16x32_f16 v[92:95], v[180:183], v[196:199], v[92:95]
	v_mfma_f32_16x16x32_f16 v[96:99], v[180:183], v[200:203], v[96:99]
	v_mfma_f32_16x16x32_f16 v[100:103], v[180:183], v[204:207], v[100:103]
	s_waitcnt lgkmcnt(8)
	v_mfma_f32_16x16x32_f16 v[104:107], v[184:187], v[192:195], v[104:107]
	s_add_u32 m0, s28, 0x6000
	s_nop 0
	global_load_lds_dwordx4 v13, s[4:5]
	v_mfma_f32_16x16x32_f16 v[108:111], v[184:187], v[196:199], v[108:111]
	v_mfma_f32_16x16x32_f16 v[112:115], v[184:187], v[200:203], v[112:115]
	v_mfma_f32_16x16x32_f16 v[116:119], v[184:187], v[204:207], v[116:119]
	s_waitcnt lgkmcnt(7)
	ds_read_b128 v[172:175], v16 offset:53248
	ds_read_b128 v[192:195], v18 offset:53248
	ds_read_b128 v[196:199], v18 offset:55296
	ds_read_b128 v[200:203], v18 offset:57344
	ds_read_b128 v[204:207], v18 offset:59392
	ds_read_b128 v[176:179], v16 offset:55296
	ds_read_b128 v[180:183], v16 offset:57344
	ds_read_b128 v[184:187], v16 offset:59392
	s_waitcnt lgkmcnt(14)
	v_mfma_f32_16x16x32_f16 v[56:59], v[136:139], v[156:159], v[56:59]
	s_add_u32 m0, s28, 0x7000
	s_nop 0
	global_load_lds_dwordx4 v8, s[4:5]
	s_add_u32 s4, s4, s20
	s_addc_u32 s5, s5, 0
	s_waitcnt lgkmcnt(13)
	v_mfma_f32_16x16x32_f16 v[60:63], v[136:139], v[160:163], v[60:63]
	s_waitcnt lgkmcnt(12)
	v_mfma_f32_16x16x32_f16 v[64:67], v[136:139], v[164:167], v[64:67]
	s_waitcnt lgkmcnt(11)
	v_mfma_f32_16x16x32_f16 v[68:71], v[136:139], v[168:171], v[68:71]
	s_waitcnt lgkmcnt(10)
	v_mfma_f32_16x16x32_f16 v[72:75], v[140:143], v[156:159], v[72:75]
	v_mfma_f32_16x16x32_f16 v[76:79], v[140:143], v[160:163], v[76:79]
	s_add_u32 m0, s28, 0x9000
	s_nop 0
	global_load_lds_dwordx4 v10, s[6:7]
	v_mfma_f32_16x16x32_f16 v[80:83], v[140:143], v[164:167], v[80:83]
	v_mfma_f32_16x16x32_f16 v[84:87], v[140:143], v[168:171], v[84:87]
	s_waitcnt lgkmcnt(9)
	v_mfma_f32_16x16x32_f16 v[88:91], v[144:147], v[156:159], v[88:91]
	v_mfma_f32_16x16x32_f16 v[92:95], v[144:147], v[160:163], v[92:95]
	v_mfma_f32_16x16x32_f16 v[96:99], v[144:147], v[164:167], v[96:99]
	s_add_u32 m0, s28, 0xb000
	s_nop 0
	global_load_lds_dwordx4 v11, s[6:7]
	s_add_u32 s6, s6, s20
	s_addc_u32 s7, s7, 0
	v_mfma_f32_16x16x32_f16 v[100:103], v[144:147], v[168:171], v[100:103]
	s_waitcnt lgkmcnt(8)
	v_mfma_f32_16x16x32_f16 v[104:107], v[148:151], v[156:159], v[104:107]
	v_mfma_f32_16x16x32_f16 v[108:111], v[148:151], v[160:163], v[108:111]
	v_mfma_f32_16x16x32_f16 v[112:115], v[148:151], v[164:167], v[112:115]
	v_mfma_f32_16x16x32_f16 v[116:119], v[148:151], v[168:171], v[116:119]
	s_waitcnt vmcnt(7) lgkmcnt(0)
	s_barrier
	s_waitcnt lgkmcnt(7)
	ds_read_b128 v[136:139], v19
	ds_read_b128 v[156:159], v21
	ds_read_b128 v[160:163], v21 offset:2048
	ds_read_b128 v[164:167], v21 offset:4096
	ds_read_b128 v[168:171], v21 offset:6144
	ds_read_b128 v[140:143], v19 offset:2048
	ds_read_b128 v[144:147], v19 offset:4096
	ds_read_b128 v[148:151], v19 offset:6144
	s_waitcnt lgkmcnt(14)
	v_mfma_f32_16x16x32_f16 v[56:59], v[172:175], v[192:195], v[56:59]
	s_add_u32 m0, s28, 0xd000
	s_nop 0
	global_load_lds_dwordx4 v10, s[4:5]
	s_waitcnt lgkmcnt(13)
	v_mfma_f32_16x16x32_f16 v[60:63], v[172:175], v[196:199], v[60:63]
	s_waitcnt lgkmcnt(12)
	v_mfma_f32_16x16x32_f16 v[64:67], v[172:175], v[200:203], v[64:67]
	s_waitcnt lgkmcnt(11)
	v_mfma_f32_16x16x32_f16 v[68:71], v[172:175], v[204:207], v[68:71]
	s_waitcnt lgkmcnt(10)
	v_mfma_f32_16x16x32_f16 v[72:75], v[176:179], v[192:195], v[72:75]
	s_add_u32 m0, s28, 0xf000
	s_nop 0
	global_load_lds_dwordx4 v11, s[4:5]
	v_mfma_f32_16x16x32_f16 v[76:79], v[176:179], v[196:199], v[76:79]
	v_mfma_f32_16x16x32_f16 v[80:83], v[176:179], v[200:203], v[80:83]
	v_mfma_f32_16x16x32_f16 v[84:87], v[176:179], v[204:207], v[84:87]
	s_waitcnt lgkmcnt(9)
	v_mfma_f32_16x16x32_f16 v[88:91], v[180:183], v[192:195], v[88:91]
	s_add_u32 m0, s28, 0x11000
	s_nop 0
	global_load_lds_dwordx4 v12, s[4:5]
	v_mfma_f32_16x16x32_f16 v[92:95], v[180:183], v[196:199], v[92:95]
	v_mfma_f32_16x16x32_f16 v[96:99], v[180:183], v[200:203], v[96:99]
	v_mfma_f32_16x16x32_f16 v[100:103], v[180:183], v[204:207], v[100:103]
	s_waitcnt lgkmcnt(8)
	v_mfma_f32_16x16x32_f16 v[104:107], v[184:187], v[192:195], v[104:107]
	s_add_u32 m0, s28, 0x13000
	s_nop 0
	global_load_lds_dwordx4 v13, s[4:5]
	v_mfma_f32_16x16x32_f16 v[108:111], v[184:187], v[196:199], v[108:111]
	v_mfma_f32_16x16x32_f16 v[112:115], v[184:187], v[200:203], v[112:115]
	v_mfma_f32_16x16x32_f16 v[116:119], v[184:187], v[204:207], v[116:119]
	s_waitcnt lgkmcnt(7)
	ds_read_b128 v[172:175], v20
	ds_read_b128 v[192:195], v22
	ds_read_b128 v[196:199], v22 offset:2048
	ds_read_b128 v[200:203], v22 offset:4096
	ds_read_b128 v[204:207], v22 offset:6144
	ds_read_b128 v[176:179], v20 offset:2048
	ds_read_b128 v[180:183], v20 offset:4096
	ds_read_b128 v[184:187], v20 offset:6144
	s_waitcnt lgkmcnt(14)
	v_mfma_f32_16x16x32_f16 v[56:59], v[136:139], v[156:159], v[56:59]
	s_add_u32 m0, s28, 0x14000
	s_nop 0
	global_load_lds_dwordx4 v8, s[4:5]
	s_add_u32 s4, s4, s20
	s_addc_u32 s5, s5, 0
	s_waitcnt lgkmcnt(13)
	v_mfma_f32_16x16x32_f16 v[60:63], v[136:139], v[160:163], v[60:63]
	s_waitcnt lgkmcnt(12)
	v_mfma_f32_16x16x32_f16 v[64:67], v[136:139], v[164:167], v[64:67]
	s_waitcnt lgkmcnt(11)
	v_mfma_f32_16x16x32_f16 v[68:71], v[136:139], v[168:171], v[68:71]
	s_waitcnt lgkmcnt(10)
	v_mfma_f32_16x16x32_f16 v[72:75], v[140:143], v[156:159], v[72:75]
	v_mfma_f32_16x16x32_f16 v[76:79], v[140:143], v[160:163], v[76:79]
	s_add_u32 m0, s28, 0x16000
	s_nop 0
	global_load_lds_dwordx4 v10, s[6:7]
	v_mfma_f32_16x16x32_f16 v[80:83], v[140:143], v[164:167], v[80:83]
	v_mfma_f32_16x16x32_f16 v[84:87], v[140:143], v[168:171], v[84:87]
	s_waitcnt lgkmcnt(9)
	v_mfma_f32_16x16x32_f16 v[88:91], v[144:147], v[156:159], v[88:91]
	v_mfma_f32_16x16x32_f16 v[92:95], v[144:147], v[160:163], v[92:95]
	v_mfma_f32_16x16x32_f16 v[96:99], v[144:147], v[164:167], v[96:99]
	s_add_u32 m0, s28, 0x18000
	s_nop 0
	global_load_lds_dwordx4 v11, s[6:7]
	s_add_u32 s6, s6, s20
	s_addc_u32 s7, s7, 0
	v_mfma_f32_16x16x32_f16 v[100:103], v[144:147], v[168:171], v[100:103]
	s_waitcnt lgkmcnt(8)
	v_mfma_f32_16x16x32_f16 v[104:107], v[148:151], v[156:159], v[104:107]
	v_mfma_f32_16x16x32_f16 v[108:111], v[148:151], v[160:163], v[108:111]
	v_mfma_f32_16x16x32_f16 v[112:115], v[148:151], v[164:167], v[112:115]
	v_mfma_f32_16x16x32_f16 v[116:119], v[148:151], v[168:171], v[116:119]
	s_waitcnt vmcnt(7) lgkmcnt(0)
	s_barrier
	s_waitcnt lgkmcnt(7)
	ds_read_b128 v[136:139], v15
	ds_read_b128 v[156:159], v17
	ds_read_b128 v[160:163], v17 offset:2048
	ds_read_b128 v[164:167], v17 offset:4096
	ds_read_b128 v[168:171], v17 offset:6144
	ds_read_b128 v[140:143], v15 offset:2048
	ds_read_b128 v[144:147], v15 offset:4096
	ds_read_b128 v[148:151], v15 offset:6144
	s_waitcnt lgkmcnt(14)
	v_mfma_f32_16x16x32_f16 v[56:59], v[172:175], v[192:195], v[56:59]
	s_add_u32 m0, s28, 0x1a000
	s_nop 0
	global_load_lds_dwordx4 v10, s[4:5]
	s_waitcnt lgkmcnt(13)
	v_mfma_f32_16x16x32_f16 v[60:63], v[172:175], v[196:199], v[60:63]
	s_waitcnt lgkmcnt(12)
	v_mfma_f32_16x16x32_f16 v[64:67], v[172:175], v[200:203], v[64:67]
	s_waitcnt lgkmcnt(11)
	v_mfma_f32_16x16x32_f16 v[68:71], v[172:175], v[204:207], v[68:71]
	s_waitcnt lgkmcnt(10)
	v_mfma_f32_16x16x32_f16 v[72:75], v[176:179], v[192:195], v[72:75]
	s_add_u32 m0, s28, 0x1c000
	s_nop 0
	global_load_lds_dwordx4 v11, s[4:5]
	v_mfma_f32_16x16x32_f16 v[76:79], v[176:179], v[196:199], v[76:79]
	v_mfma_f32_16x16x32_f16 v[80:83], v[176:179], v[200:203], v[80:83]
	v_mfma_f32_16x16x32_f16 v[84:87], v[176:179], v[204:207], v[84:87]
	s_waitcnt lgkmcnt(9)
	v_mfma_f32_16x16x32_f16 v[88:91], v[180:183], v[192:195], v[88:91]
	s_add_u32 m0, s28, 0x1e000
	s_nop 0
	global_load_lds_dwordx4 v12, s[4:5]
	v_mfma_f32_16x16x32_f16 v[92:95], v[180:183], v[196:199], v[92:95]
	v_mfma_f32_16x16x32_f16 v[96:99], v[180:183], v[200:203], v[96:99]
	v_mfma_f32_16x16x32_f16 v[100:103], v[180:183], v[204:207], v[100:103]
	s_waitcnt lgkmcnt(8)
	v_mfma_f32_16x16x32_f16 v[104:107], v[184:187], v[192:195], v[104:107]
	s_add_u32 m0, s28, 0x20000
	s_nop 0
	global_load_lds_dwordx4 v13, s[4:5]
	v_mfma_f32_16x16x32_f16 v[108:111], v[184:187], v[196:199], v[108:111]
	v_mfma_f32_16x16x32_f16 v[112:115], v[184:187], v[200:203], v[112:115]
	v_mfma_f32_16x16x32_f16 v[116:119], v[184:187], v[204:207], v[116:119]
	s_waitcnt lgkmcnt(7)
	ds_read_b128 v[172:175], v16
	ds_read_b128 v[192:195], v18
	ds_read_b128 v[196:199], v18 offset:2048
	ds_read_b128 v[200:203], v18 offset:4096
	ds_read_b128 v[204:207], v18 offset:6144
	ds_read_b128 v[176:179], v16 offset:2048
	ds_read_b128 v[180:183], v16 offset:4096
	ds_read_b128 v[184:187], v16 offset:6144
	s_waitcnt lgkmcnt(14)
	v_mfma_f32_16x16x32_f16 v[56:59], v[136:139], v[156:159], v[56:59]
	s_add_u32 m0, s28, 0x21000
	s_nop 0
	global_load_lds_dwordx4 v8, s[4:5]
	s_add_u32 s4, s4, s20
	s_addc_u32 s5, s5, 0
	s_waitcnt lgkmcnt(13)
	v_mfma_f32_16x16x32_f16 v[60:63], v[136:139], v[160:163], v[60:63]
	s_waitcnt lgkmcnt(12)
	v_mfma_f32_16x16x32_f16 v[64:67], v[136:139], v[164:167], v[64:67]
	s_waitcnt lgkmcnt(11)
	v_mfma_f32_16x16x32_f16 v[68:71], v[136:139], v[168:171], v[68:71]
	s_waitcnt lgkmcnt(10)
	v_mfma_f32_16x16x32_f16 v[72:75], v[140:143], v[156:159], v[72:75]
	v_mfma_f32_16x16x32_f16 v[76:79], v[140:143], v[160:163], v[76:79]
	s_add_u32 m0, s28, 0x23000
	s_nop 0
	global_load_lds_dwordx4 v10, s[6:7]
	v_mfma_f32_16x16x32_f16 v[80:83], v[140:143], v[164:167], v[80:83]
	v_mfma_f32_16x16x32_f16 v[84:87], v[140:143], v[168:171], v[84:87]
	s_waitcnt lgkmcnt(9)
	v_mfma_f32_16x16x32_f16 v[88:91], v[144:147], v[156:159], v[88:91]
	v_mfma_f32_16x16x32_f16 v[92:95], v[144:147], v[160:163], v[92:95]
	v_mfma_f32_16x16x32_f16 v[96:99], v[144:147], v[164:167], v[96:99]
	s_add_u32 m0, s28, 0x25000
	s_nop 0
	global_load_lds_dwordx4 v11, s[6:7]
	s_add_u32 s6, s6, s20
	s_addc_u32 s7, s7, 0
	v_mfma_f32_16x16x32_f16 v[100:103], v[144:147], v[168:171], v[100:103]
	s_waitcnt lgkmcnt(8)
	v_mfma_f32_16x16x32_f16 v[104:107], v[148:151], v[156:159], v[104:107]
	v_mfma_f32_16x16x32_f16 v[108:111], v[148:151], v[160:163], v[108:111]
	v_mfma_f32_16x16x32_f16 v[112:115], v[148:151], v[164:167], v[112:115]
	v_mfma_f32_16x16x32_f16 v[116:119], v[148:151], v[168:171], v[116:119]
	s_waitcnt vmcnt(7) lgkmcnt(0)
	s_barrier
	s_waitcnt lgkmcnt(7)
	ds_read_b128 v[136:139], v15 offset:53248
	ds_read_b128 v[156:159], v17 offset:53248
	ds_read_b128 v[160:163], v17 offset:55296
	ds_read_b128 v[164:167], v17 offset:57344
	ds_read_b128 v[168:171], v17 offset:59392
	ds_read_b128 v[140:143], v15 offset:55296
	ds_read_b128 v[144:147], v15 offset:57344
	ds_read_b128 v[148:151], v15 offset:59392
	s_waitcnt lgkmcnt(14)
	v_mfma_f32_16x16x32_f16 v[56:59], v[172:175], v[192:195], v[56:59]
	s_add_u32 m0, s28, 0x0
	s_nop 0
	global_load_lds_dwordx4 v10, s[4:5]
	s_waitcnt lgkmcnt(13)
	v_mfma_f32_16x16x32_f16 v[60:63], v[172:175], v[196:199], v[60:63]
	s_waitcnt lgkmcnt(12)
	v_mfma_f32_16x16x32_f16 v[64:67], v[172:175], v[200:203], v[64:67]
	s_waitcnt lgkmcnt(11)
	v_mfma_f32_16x16x32_f16 v[68:71], v[172:175], v[204:207], v[68:71]
	s_waitcnt lgkmcnt(10)
	v_mfma_f32_16x16x32_f16 v[72:75], v[176:179], v[192:195], v[72:75]
	s_add_u32 m0, s28, 0x2000
	s_nop 0
	global_load_lds_dwordx4 v11, s[4:5]
	v_mfma_f32_16x16x32_f16 v[76:79], v[176:179], v[196:199], v[76:79]
	v_mfma_f32_16x16x32_f16 v[80:83], v[176:179], v[200:203], v[80:83]
	v_mfma_f32_16x16x32_f16 v[84:87], v[176:179], v[204:207], v[84:87]
	s_waitcnt lgkmcnt(9)
	v_mfma_f32_16x16x32_f16 v[88:91], v[180:183], v[192:195], v[88:91]
	s_add_u32 m0, s28, 0x4000
	s_nop 0
	global_load_lds_dwordx4 v12, s[4:5]
	v_mfma_f32_16x16x32_f16 v[92:95], v[180:183], v[196:199], v[92:95]
	v_mfma_f32_16x16x32_f16 v[96:99], v[180:183], v[200:203], v[96:99]
	v_mfma_f32_16x16x32_f16 v[100:103], v[180:183], v[204:207], v[100:103]
	s_waitcnt lgkmcnt(8)
	v_mfma_f32_16x16x32_f16 v[104:107], v[184:187], v[192:195], v[104:107]
	s_add_u32 m0, s28, 0x6000
	s_nop 0
	global_load_lds_dwordx4 v13, s[4:5]
	v_mfma_f32_16x16x32_f16 v[108:111], v[184:187], v[196:199], v[108:111]
	v_mfma_f32_16x16x32_f16 v[112:115], v[184:187], v[200:203], v[112:115]
	v_mfma_f32_16x16x32_f16 v[116:119], v[184:187], v[204:207], v[116:119]
	s_waitcnt lgkmcnt(7)
	ds_read_b128 v[172:175], v16 offset:53248
	ds_read_b128 v[192:195], v18 offset:53248
	ds_read_b128 v[196:199], v18 offset:55296
	ds_read_b128 v[200:203], v18 offset:57344
	ds_read_b128 v[204:207], v18 offset:59392
	ds_read_b128 v[176:179], v16 offset:55296
	ds_read_b128 v[180:183], v16 offset:57344
	ds_read_b128 v[184:187], v16 offset:59392
	s_waitcnt lgkmcnt(14)
	v_mfma_f32_16x16x32_f16 v[56:59], v[136:139], v[156:159], v[56:59]
	s_add_u32 m0, s28, 0x7000
	s_nop 0
	global_load_lds_dwordx4 v8, s[4:5]
	s_add_u32 s4, s4, s20
	s_addc_u32 s5, s5, 0
	s_waitcnt lgkmcnt(13)
	v_mfma_f32_16x16x32_f16 v[60:63], v[136:139], v[160:163], v[60:63]
	s_waitcnt lgkmcnt(12)
	v_mfma_f32_16x16x32_f16 v[64:67], v[136:139], v[164:167], v[64:67]
	s_waitcnt lgkmcnt(11)
	v_mfma_f32_16x16x32_f16 v[68:71], v[136:139], v[168:171], v[68:71]
	s_waitcnt lgkmcnt(10)
	v_mfma_f32_16x16x32_f16 v[72:75], v[140:143], v[156:159], v[72:75]
	v_mfma_f32_16x16x32_f16 v[76:79], v[140:143], v[160:163], v[76:79]
	s_add_u32 m0, s28, 0x9000
	s_nop 0
	global_load_lds_dwordx4 v10, s[6:7]
	v_mfma_f32_16x16x32_f16 v[80:83], v[140:143], v[164:167], v[80:83]
	v_mfma_f32_16x16x32_f16 v[84:87], v[140:143], v[168:171], v[84:87]
	s_waitcnt lgkmcnt(9)
	v_mfma_f32_16x16x32_f16 v[88:91], v[144:147], v[156:159], v[88:91]
	v_mfma_f32_16x16x32_f16 v[92:95], v[144:147], v[160:163], v[92:95]
	v_mfma_f32_16x16x32_f16 v[96:99], v[144:147], v[164:167], v[96:99]
	s_add_u32 m0, s28, 0xb000
	s_nop 0
	global_load_lds_dwordx4 v11, s[6:7]
	s_add_u32 s6, s6, s20
	s_addc_u32 s7, s7, 0
	v_mfma_f32_16x16x32_f16 v[100:103], v[144:147], v[168:171], v[100:103]
	s_waitcnt lgkmcnt(8)
	v_mfma_f32_16x16x32_f16 v[104:107], v[148:151], v[156:159], v[104:107]
	v_mfma_f32_16x16x32_f16 v[108:111], v[148:151], v[160:163], v[108:111]
	v_mfma_f32_16x16x32_f16 v[112:115], v[148:151], v[164:167], v[112:115]
	v_mfma_f32_16x16x32_f16 v[116:119], v[148:151], v[168:171], v[116:119]
	s_waitcnt vmcnt(7) lgkmcnt(0)
	s_barrier
	s_waitcnt lgkmcnt(7)
	ds_read_b128 v[136:139], v19
	ds_read_b128 v[156:159], v21
	ds_read_b128 v[160:163], v21 offset:2048
	ds_read_b128 v[164:167], v21 offset:4096
	ds_read_b128 v[168:171], v21 offset:6144
	ds_read_b128 v[140:143], v19 offset:2048
	ds_read_b128 v[144:147], v19 offset:4096
	ds_read_b128 v[148:151], v19 offset:6144
	s_waitcnt lgkmcnt(14)
	v_mfma_f32_16x16x32_f16 v[56:59], v[172:175], v[192:195], v[56:59]
	s_add_u32 m0, s28, 0xd000
	s_nop 0
	global_load_lds_dwordx4 v10, s[4:5]
	s_waitcnt lgkmcnt(13)
	v_mfma_f32_16x16x32_f16 v[60:63], v[172:175], v[196:199], v[60:63]
	s_waitcnt lgkmcnt(12)
	v_mfma_f32_16x16x32_f16 v[64:67], v[172:175], v[200:203], v[64:67]
	s_waitcnt lgkmcnt(11)
	v_mfma_f32_16x16x32_f16 v[68:71], v[172:175], v[204:207], v[68:71]
	s_waitcnt lgkmcnt(10)
	v_mfma_f32_16x16x32_f16 v[72:75], v[176:179], v[192:195], v[72:75]
	s_add_u32 m0, s28, 0xf000
	s_nop 0
	global_load_lds_dwordx4 v11, s[4:5]
	v_mfma_f32_16x16x32_f16 v[76:79], v[176:179], v[196:199], v[76:79]
	v_mfma_f32_16x16x32_f16 v[80:83], v[176:179], v[200:203], v[80:83]
	v_mfma_f32_16x16x32_f16 v[84:87], v[176:179], v[204:207], v[84:87]
	s_waitcnt lgkmcnt(9)
	v_mfma_f32_16x16x32_f16 v[88:91], v[180:183], v[192:195], v[88:91]
	s_add_u32 m0, s28, 0x11000
	s_nop 0
	global_load_lds_dwordx4 v12, s[4:5]
	v_mfma_f32_16x16x32_f16 v[92:95], v[180:183], v[196:199], v[92:95]
	v_mfma_f32_16x16x32_f16 v[96:99], v[180:183], v[200:203], v[96:99]
	v_mfma_f32_16x16x32_f16 v[100:103], v[180:183], v[204:207], v[100:103]
	s_waitcnt lgkmcnt(8)
	v_mfma_f32_16x16x32_f16 v[104:107], v[184:187], v[192:195], v[104:107]
	s_add_u32 m0, s28, 0x13000
	s_nop 0
	global_load_lds_dwordx4 v13, s[4:5]
	v_mfma_f32_16x16x32_f16 v[108:111], v[184:187], v[196:199], v[108:111]
	v_mfma_f32_16x16x32_f16 v[112:115], v[184:187], v[200:203], v[112:115]
	v_mfma_f32_16x16x32_f16 v[116:119], v[184:187], v[204:207], v[116:119]
	s_waitcnt lgkmcnt(7)
	ds_read_b128 v[172:175], v20
	ds_read_b128 v[192:195], v22
	ds_read_b128 v[196:199], v22 offset:2048
	ds_read_b128 v[200:203], v22 offset:4096
	ds_read_b128 v[204:207], v22 offset:6144
	ds_read_b128 v[176:179], v20 offset:2048
	ds_read_b128 v[180:183], v20 offset:4096
	ds_read_b128 v[184:187], v20 offset:6144
	s_waitcnt lgkmcnt(14)
	v_mfma_f32_16x16x32_f16 v[56:59], v[136:139], v[156:159], v[56:59]
	s_add_u32 m0, s28, 0x14000
	s_nop 0
	global_load_lds_dwordx4 v8, s[4:5]
	s_add_u32 s4, s4, s20
	s_addc_u32 s5, s5, 0
	s_waitcnt lgkmcnt(13)
	v_mfma_f32_16x16x32_f16 v[60:63], v[136:139], v[160:163], v[60:63]
	s_waitcnt lgkmcnt(12)
	v_mfma_f32_16x16x32_f16 v[64:67], v[136:139], v[164:167], v[64:67]
	s_waitcnt lgkmcnt(11)
	v_mfma_f32_16x16x32_f16 v[68:71], v[136:139], v[168:171], v[68:71]
	s_waitcnt lgkmcnt(10)
	v_mfma_f32_16x16x32_f16 v[72:75], v[140:143], v[156:159], v[72:75]
	v_mfma_f32_16x16x32_f16 v[76:79], v[140:143], v[160:163], v[76:79]
	s_add_u32 m0, s28, 0x16000
	s_nop 0
	global_load_lds_dwordx4 v10, s[6:7]
	v_mfma_f32_16x16x32_f16 v[80:83], v[140:143], v[164:167], v[80:83]
	v_mfma_f32_16x16x32_f16 v[84:87], v[140:143], v[168:171], v[84:87]
	s_waitcnt lgkmcnt(9)
	v_mfma_f32_16x16x32_f16 v[88:91], v[144:147], v[156:159], v[88:91]
	v_mfma_f32_16x16x32_f16 v[92:95], v[144:147], v[160:163], v[92:95]
	v_mfma_f32_16x16x32_f16 v[96:99], v[144:147], v[164:167], v[96:99]
	s_add_u32 m0, s28, 0x18000
	s_nop 0
	global_load_lds_dwordx4 v11, s[6:7]
	s_add_u32 s6, s6, s20
	s_addc_u32 s7, s7, 0
	v_mfma_f32_16x16x32_f16 v[100:103], v[144:147], v[168:171], v[100:103]
	s_waitcnt lgkmcnt(8)
	v_mfma_f32_16x16x32_f16 v[104:107], v[148:151], v[156:159], v[104:107]
	v_mfma_f32_16x16x32_f16 v[108:111], v[148:151], v[160:163], v[108:111]
	v_mfma_f32_16x16x32_f16 v[112:115], v[148:151], v[164:167], v[112:115]
	v_mfma_f32_16x16x32_f16 v[116:119], v[148:151], v[168:171], v[116:119]
	s_waitcnt vmcnt(7) lgkmcnt(0)
	s_barrier
	s_waitcnt lgkmcnt(7)
	ds_read_b128 v[136:139], v15
	ds_read_b128 v[156:159], v17
	ds_read_b128 v[160:163], v17 offset:2048
	ds_read_b128 v[164:167], v17 offset:4096
	ds_read_b128 v[168:171], v17 offset:6144
	ds_read_b128 v[140:143], v15 offset:2048
	ds_read_b128 v[144:147], v15 offset:4096
	ds_read_b128 v[148:151], v15 offset:6144
	s_waitcnt lgkmcnt(14)
	v_mfma_f32_16x16x32_f16 v[56:59], v[172:175], v[192:195], v[56:59]
	s_add_u32 m0, s28, 0x1a000
	s_nop 0
	global_load_lds_dwordx4 v10, s[4:5]
	s_waitcnt lgkmcnt(13)
	v_mfma_f32_16x16x32_f16 v[60:63], v[172:175], v[196:199], v[60:63]
	s_waitcnt lgkmcnt(12)
	v_mfma_f32_16x16x32_f16 v[64:67], v[172:175], v[200:203], v[64:67]
	s_waitcnt lgkmcnt(11)
	v_mfma_f32_16x16x32_f16 v[68:71], v[172:175], v[204:207], v[68:71]
	s_waitcnt lgkmcnt(10)
	v_mfma_f32_16x16x32_f16 v[72:75], v[176:179], v[192:195], v[72:75]
	s_add_u32 m0, s28, 0x1c000
	s_nop 0
	global_load_lds_dwordx4 v11, s[4:5]
	v_mfma_f32_16x16x32_f16 v[76:79], v[176:179], v[196:199], v[76:79]
	v_mfma_f32_16x16x32_f16 v[80:83], v[176:179], v[200:203], v[80:83]
	v_mfma_f32_16x16x32_f16 v[84:87], v[176:179], v[204:207], v[84:87]
	s_waitcnt lgkmcnt(9)
	v_mfma_f32_16x16x32_f16 v[88:91], v[180:183], v[192:195], v[88:91]
	s_add_u32 m0, s28, 0x1e000
	s_nop 0
	global_load_lds_dwordx4 v12, s[4:5]
	v_mfma_f32_16x16x32_f16 v[92:95], v[180:183], v[196:199], v[92:95]
	v_mfma_f32_16x16x32_f16 v[96:99], v[180:183], v[200:203], v[96:99]
	v_mfma_f32_16x16x32_f16 v[100:103], v[180:183], v[204:207], v[100:103]
	s_waitcnt lgkmcnt(8)
	v_mfma_f32_16x16x32_f16 v[104:107], v[184:187], v[192:195], v[104:107]
	s_add_u32 m0, s28, 0x20000
	s_nop 0
	global_load_lds_dwordx4 v13, s[4:5]
	v_mfma_f32_16x16x32_f16 v[108:111], v[184:187], v[196:199], v[108:111]
	v_mfma_f32_16x16x32_f16 v[112:115], v[184:187], v[200:203], v[112:115]
	v_mfma_f32_16x16x32_f16 v[116:119], v[184:187], v[204:207], v[116:119]
	s_waitcnt lgkmcnt(7)
	ds_read_b128 v[172:175], v16
	ds_read_b128 v[192:195], v18
	ds_read_b128 v[196:199], v18 offset:2048
	ds_read_b128 v[200:203], v18 offset:4096
	ds_read_b128 v[204:207], v18 offset:6144
	ds_read_b128 v[176:179], v16 offset:2048
	ds_read_b128 v[180:183], v16 offset:4096
	ds_read_b128 v[184:187], v16 offset:6144
	s_waitcnt lgkmcnt(14)
	v_mfma_f32_16x16x32_f16 v[56:59], v[136:139], v[156:159], v[56:59]
	s_add_u32 m0, s28, 0x21000
	s_nop 0
	global_load_lds_dwordx4 v8, s[4:5]
	s_add_u32 s4, s4, s20
	s_addc_u32 s5, s5, 0
	s_waitcnt lgkmcnt(13)
	v_mfma_f32_16x16x32_f16 v[60:63], v[136:139], v[160:163], v[60:63]
	s_waitcnt lgkmcnt(12)
	v_mfma_f32_16x16x32_f16 v[64:67], v[136:139], v[164:167], v[64:67]
	s_waitcnt lgkmcnt(11)
	v_mfma_f32_16x16x32_f16 v[68:71], v[136:139], v[168:171], v[68:71]
	s_waitcnt lgkmcnt(10)
	v_mfma_f32_16x16x32_f16 v[72:75], v[140:143], v[156:159], v[72:75]
	v_mfma_f32_16x16x32_f16 v[76:79], v[140:143], v[160:163], v[76:79]
	s_add_u32 m0, s28, 0x23000
	s_nop 0
	global_load_lds_dwordx4 v10, s[6:7]
	v_mfma_f32_16x16x32_f16 v[80:83], v[140:143], v[164:167], v[80:83]
	v_mfma_f32_16x16x32_f16 v[84:87], v[140:143], v[168:171], v[84:87]
	s_waitcnt lgkmcnt(9)
	v_mfma_f32_16x16x32_f16 v[88:91], v[144:147], v[156:159], v[88:91]
	v_mfma_f32_16x16x32_f16 v[92:95], v[144:147], v[160:163], v[92:95]
	v_mfma_f32_16x16x32_f16 v[96:99], v[144:147], v[164:167], v[96:99]
	s_add_u32 m0, s28, 0x25000
	s_nop 0
	global_load_lds_dwordx4 v11, s[6:7]
	s_add_u32 s6, s6, s20
	s_addc_u32 s7, s7, 0
	v_mfma_f32_16x16x32_f16 v[100:103], v[144:147], v[168:171], v[100:103]
	s_waitcnt lgkmcnt(8)
	v_mfma_f32_16x16x32_f16 v[104:107], v[148:151], v[156:159], v[104:107]
	v_mfma_f32_16x16x32_f16 v[108:111], v[148:151], v[160:163], v[108:111]
	v_mfma_f32_16x16x32_f16 v[112:115], v[148:151], v[164:167], v[112:115]
	v_mfma_f32_16x16x32_f16 v[116:119], v[148:151], v[168:171], v[116:119]
	s_waitcnt vmcnt(7) lgkmcnt(0)
	s_barrier
	s_waitcnt lgkmcnt(7)
	ds_read_b128 v[136:139], v15 offset:53248
	ds_read_b128 v[156:159], v17 offset:53248
	ds_read_b128 v[160:163], v17 offset:55296
	ds_read_b128 v[164:167], v17 offset:57344
	ds_read_b128 v[168:171], v17 offset:59392
	ds_read_b128 v[140:143], v15 offset:55296
	ds_read_b128 v[144:147], v15 offset:57344
	ds_read_b128 v[148:151], v15 offset:59392
	s_waitcnt lgkmcnt(14)
	v_mfma_f32_16x16x32_f16 v[56:59], v[172:175], v[192:195], v[56:59]
	s_add_u32 m0, s28, 0x0
	s_nop 0
	global_load_lds_dwordx4 v10, s[4:5]
	s_waitcnt lgkmcnt(13)
	v_mfma_f32_16x16x32_f16 v[60:63], v[172:175], v[196:199], v[60:63]
	s_waitcnt lgkmcnt(12)
	v_mfma_f32_16x16x32_f16 v[64:67], v[172:175], v[200:203], v[64:67]
	s_waitcnt lgkmcnt(11)
	v_mfma_f32_16x16x32_f16 v[68:71], v[172:175], v[204:207], v[68:71]
	s_waitcnt lgkmcnt(10)
	v_mfma_f32_16x16x32_f16 v[72:75], v[176:179], v[192:195], v[72:75]
	s_add_u32 m0, s28, 0x2000
	s_nop 0
	global_load_lds_dwordx4 v11, s[4:5]
	v_mfma_f32_16x16x32_f16 v[76:79], v[176:179], v[196:199], v[76:79]
	v_mfma_f32_16x16x32_f16 v[80:83], v[176:179], v[200:203], v[80:83]
	v_mfma_f32_16x16x32_f16 v[84:87], v[176:179], v[204:207], v[84:87]
	s_waitcnt lgkmcnt(9)
	v_mfma_f32_16x16x32_f16 v[88:91], v[180:183], v[192:195], v[88:91]
	s_add_u32 m0, s28, 0x4000
	s_nop 0
	global_load_lds_dwordx4 v12, s[4:5]
	v_mfma_f32_16x16x32_f16 v[92:95], v[180:183], v[196:199], v[92:95]
	v_mfma_f32_16x16x32_f16 v[96:99], v[180:183], v[200:203], v[96:99]
	v_mfma_f32_16x16x32_f16 v[100:103], v[180:183], v[204:207], v[100:103]
	s_waitcnt lgkmcnt(8)
	v_mfma_f32_16x16x32_f16 v[104:107], v[184:187], v[192:195], v[104:107]
	s_add_u32 m0, s28, 0x6000
	s_nop 0
	global_load_lds_dwordx4 v13, s[4:5]
	v_mfma_f32_16x16x32_f16 v[108:111], v[184:187], v[196:199], v[108:111]
	v_mfma_f32_16x16x32_f16 v[112:115], v[184:187], v[200:203], v[112:115]
	v_mfma_f32_16x16x32_f16 v[116:119], v[184:187], v[204:207], v[116:119]
	s_waitcnt lgkmcnt(7)
	ds_read_b128 v[172:175], v16 offset:53248
	ds_read_b128 v[192:195], v18 offset:53248
	ds_read_b128 v[196:199], v18 offset:55296
	ds_read_b128 v[200:203], v18 offset:57344
	ds_read_b128 v[204:207], v18 offset:59392
	ds_read_b128 v[176:179], v16 offset:55296
	ds_read_b128 v[180:183], v16 offset:57344
	ds_read_b128 v[184:187], v16 offset:59392
	s_waitcnt lgkmcnt(14)
	v_mfma_f32_16x16x32_f16 v[56:59], v[136:139], v[156:159], v[56:59]
	s_add_u32 m0, s28, 0x7000
	s_nop 0
	global_load_lds_dwordx4 v8, s[4:5]
	s_add_u32 s4, s4, s20
	s_addc_u32 s5, s5, 0
	s_waitcnt lgkmcnt(13)
	v_mfma_f32_16x16x32_f16 v[60:63], v[136:139], v[160:163], v[60:63]
	s_waitcnt lgkmcnt(12)
	v_mfma_f32_16x16x32_f16 v[64:67], v[136:139], v[164:167], v[64:67]
	s_waitcnt lgkmcnt(11)
	v_mfma_f32_16x16x32_f16 v[68:71], v[136:139], v[168:171], v[68:71]
	s_waitcnt lgkmcnt(10)
	v_mfma_f32_16x16x32_f16 v[72:75], v[140:143], v[156:159], v[72:75]
	v_mfma_f32_16x16x32_f16 v[76:79], v[140:143], v[160:163], v[76:79]
	s_add_u32 m0, s28, 0x9000
	s_nop 0
	global_load_lds_dwordx4 v10, s[6:7]
	v_mfma_f32_16x16x32_f16 v[80:83], v[140:143], v[164:167], v[80:83]
	v_mfma_f32_16x16x32_f16 v[84:87], v[140:143], v[168:171], v[84:87]
	s_waitcnt lgkmcnt(9)
	v_mfma_f32_16x16x32_f16 v[88:91], v[144:147], v[156:159], v[88:91]
	v_mfma_f32_16x16x32_f16 v[92:95], v[144:147], v[160:163], v[92:95]
	v_mfma_f32_16x16x32_f16 v[96:99], v[144:147], v[164:167], v[96:99]
	s_add_u32 m0, s28, 0xb000
	s_nop 0
	global_load_lds_dwordx4 v11, s[6:7]
	s_add_u32 s6, s6, s20
	s_addc_u32 s7, s7, 0
	v_mfma_f32_16x16x32_f16 v[100:103], v[144:147], v[168:171], v[100:103]
	s_waitcnt lgkmcnt(8)
	v_mfma_f32_16x16x32_f16 v[104:107], v[148:151], v[156:159], v[104:107]
	v_mfma_f32_16x16x32_f16 v[108:111], v[148:151], v[160:163], v[108:111]
	v_mfma_f32_16x16x32_f16 v[112:115], v[148:151], v[164:167], v[112:115]
	v_mfma_f32_16x16x32_f16 v[116:119], v[148:151], v[168:171], v[116:119]
	s_waitcnt vmcnt(7) lgkmcnt(0)
	s_barrier
	s_waitcnt lgkmcnt(7)
	ds_read_b128 v[136:139], v19
	ds_read_b128 v[156:159], v21
	ds_read_b128 v[160:163], v21 offset:2048
	ds_read_b128 v[164:167], v21 offset:4096
	ds_read_b128 v[168:171], v21 offset:6144
	ds_read_b128 v[140:143], v19 offset:2048
	ds_read_b128 v[144:147], v19 offset:4096
	ds_read_b128 v[148:151], v19 offset:6144
	s_waitcnt lgkmcnt(14)
	v_mfma_f32_16x16x32_f16 v[56:59], v[172:175], v[192:195], v[56:59]
	s_waitcnt lgkmcnt(13)
	v_mfma_f32_16x16x32_f16 v[60:63], v[172:175], v[196:199], v[60:63]
	s_waitcnt lgkmcnt(12)
	v_mfma_f32_16x16x32_f16 v[64:67], v[172:175], v[200:203], v[64:67]
	s_waitcnt lgkmcnt(11)
	v_mfma_f32_16x16x32_f16 v[68:71], v[172:175], v[204:207], v[68:71]
	s_waitcnt lgkmcnt(10)
	v_mfma_f32_16x16x32_f16 v[72:75], v[176:179], v[192:195], v[72:75]
	v_mfma_f32_16x16x32_f16 v[76:79], v[176:179], v[196:199], v[76:79]
	v_mfma_f32_16x16x32_f16 v[80:83], v[176:179], v[200:203], v[80:83]
	v_mfma_f32_16x16x32_f16 v[84:87], v[176:179], v[204:207], v[84:87]
	s_waitcnt lgkmcnt(9)
	v_mfma_f32_16x16x32_f16 v[88:91], v[180:183], v[192:195], v[88:91]
	v_mfma_f32_16x16x32_f16 v[92:95], v[180:183], v[196:199], v[92:95]
	v_mfma_f32_16x16x32_f16 v[96:99], v[180:183], v[200:203], v[96:99]
	v_mfma_f32_16x16x32_f16 v[100:103], v[180:183], v[204:207], v[100:103]
	s_waitcnt lgkmcnt(8)
	v_mfma_f32_16x16x32_f16 v[104:107], v[184:187], v[192:195], v[104:107]
	v_mfma_f32_16x16x32_f16 v[108:111], v[184:187], v[196:199], v[108:111]
	v_mfma_f32_16x16x32_f16 v[112:115], v[184:187], v[200:203], v[112:115]
	v_mfma_f32_16x16x32_f16 v[116:119], v[184:187], v[204:207], v[116:119]
	s_waitcnt lgkmcnt(7)
	ds_read_b128 v[172:175], v20
	ds_read_b128 v[192:195], v22
	ds_read_b128 v[196:199], v22 offset:2048
	ds_read_b128 v[200:203], v22 offset:4096
	ds_read_b128 v[204:207], v22 offset:6144
	ds_read_b128 v[176:179], v20 offset:2048
	ds_read_b128 v[180:183], v20 offset:4096
	ds_read_b128 v[184:187], v20 offset:6144
	s_waitcnt lgkmcnt(14)
	v_mfma_f32_16x16x32_f16 v[56:59], v[136:139], v[156:159], v[56:59]
	s_waitcnt lgkmcnt(13)
	v_mfma_f32_16x16x32_f16 v[60:63], v[136:139], v[160:163], v[60:63]
	s_waitcnt lgkmcnt(12)
	v_mfma_f32_16x16x32_f16 v[64:67], v[136:139], v[164:167], v[64:67]
	s_waitcnt lgkmcnt(11)
	v_mfma_f32_16x16x32_f16 v[68:71], v[136:139], v[168:171], v[68:71]
	s_waitcnt lgkmcnt(10)
	v_mfma_f32_16x16x32_f16 v[72:75], v[140:143], v[156:159], v[72:75]
	v_mfma_f32_16x16x32_f16 v[76:79], v[140:143], v[160:163], v[76:79]
	v_mfma_f32_16x16x32_f16 v[80:83], v[140:143], v[164:167], v[80:83]
	v_mfma_f32_16x16x32_f16 v[84:87], v[140:143], v[168:171], v[84:87]
	s_waitcnt lgkmcnt(9)
	v_mfma_f32_16x16x32_f16 v[88:91], v[144:147], v[156:159], v[88:91]
	v_mfma_f32_16x16x32_f16 v[92:95], v[144:147], v[160:163], v[92:95]
	v_mfma_f32_16x16x32_f16 v[96:99], v[144:147], v[164:167], v[96:99]
	v_mfma_f32_16x16x32_f16 v[100:103], v[144:147], v[168:171], v[100:103]
	s_waitcnt lgkmcnt(8)
	v_mfma_f32_16x16x32_f16 v[104:107], v[148:151], v[156:159], v[104:107]
	v_mfma_f32_16x16x32_f16 v[108:111], v[148:151], v[160:163], v[108:111]
	v_mfma_f32_16x16x32_f16 v[112:115], v[148:151], v[164:167], v[112:115]
	v_mfma_f32_16x16x32_f16 v[116:119], v[148:151], v[168:171], v[116:119]
	s_waitcnt vmcnt(0) lgkmcnt(0)
	s_barrier
	s_waitcnt lgkmcnt(7)
	ds_read_b128 v[136:139], v15
	ds_read_b128 v[156:159], v17
	ds_read_b128 v[160:163], v17 offset:2048
	ds_read_b128 v[164:167], v17 offset:4096
	ds_read_b128 v[168:171], v17 offset:6144
	ds_read_b128 v[140:143], v15 offset:2048
	ds_read_b128 v[144:147], v15 offset:4096
	ds_read_b128 v[148:151], v15 offset:6144
	s_waitcnt lgkmcnt(14)
	v_mfma_f32_16x16x32_f16 v[56:59], v[172:175], v[192:195], v[56:59]
	s_waitcnt lgkmcnt(13)
	v_mfma_f32_16x16x32_f16 v[60:63], v[172:175], v[196:199], v[60:63]
	s_waitcnt lgkmcnt(12)
	v_mfma_f32_16x16x32_f16 v[64:67], v[172:175], v[200:203], v[64:67]
	s_waitcnt lgkmcnt(11)
	v_mfma_f32_16x16x32_f16 v[68:71], v[172:175], v[204:207], v[68:71]
	s_waitcnt lgkmcnt(10)
	v_mfma_f32_16x16x32_f16 v[72:75], v[176:179], v[192:195], v[72:75]
	v_mfma_f32_16x16x32_f16 v[76:79], v[176:179], v[196:199], v[76:79]
	v_mfma_f32_16x16x32_f16 v[80:83], v[176:179], v[200:203], v[80:83]
	v_mfma_f32_16x16x32_f16 v[84:87], v[176:179], v[204:207], v[84:87]
	s_waitcnt lgkmcnt(9)
	v_mfma_f32_16x16x32_f16 v[88:91], v[180:183], v[192:195], v[88:91]
	v_mfma_f32_16x16x32_f16 v[92:95], v[180:183], v[196:199], v[92:95]
	v_mfma_f32_16x16x32_f16 v[96:99], v[180:183], v[200:203], v[96:99]
	v_mfma_f32_16x16x32_f16 v[100:103], v[180:183], v[204:207], v[100:103]
	s_waitcnt lgkmcnt(8)
	v_mfma_f32_16x16x32_f16 v[104:107], v[184:187], v[192:195], v[104:107]
	v_mfma_f32_16x16x32_f16 v[108:111], v[184:187], v[196:199], v[108:111]
	v_mfma_f32_16x16x32_f16 v[112:115], v[184:187], v[200:203], v[112:115]
	v_mfma_f32_16x16x32_f16 v[116:119], v[184:187], v[204:207], v[116:119]
	s_waitcnt lgkmcnt(7)
	ds_read_b128 v[172:175], v16
	ds_read_b128 v[192:195], v18
	ds_read_b128 v[196:199], v18 offset:2048
	ds_read_b128 v[200:203], v18 offset:4096
	ds_read_b128 v[204:207], v18 offset:6144
	ds_read_b128 v[176:179], v16 offset:2048
	ds_read_b128 v[180:183], v16 offset:4096
	ds_read_b128 v[184:187], v16 offset:6144
	s_waitcnt lgkmcnt(14)
	v_mfma_f32_16x16x32_f16 v[56:59], v[136:139], v[156:159], v[56:59]
	s_waitcnt lgkmcnt(13)
	v_mfma_f32_16x16x32_f16 v[60:63], v[136:139], v[160:163], v[60:63]
	s_waitcnt lgkmcnt(12)
	v_mfma_f32_16x16x32_f16 v[64:67], v[136:139], v[164:167], v[64:67]
	s_waitcnt lgkmcnt(11)
	v_mfma_f32_16x16x32_f16 v[68:71], v[136:139], v[168:171], v[68:71]
	s_waitcnt lgkmcnt(10)
	v_mfma_f32_16x16x32_f16 v[72:75], v[140:143], v[156:159], v[72:75]
	v_mfma_f32_16x16x32_f16 v[76:79], v[140:143], v[160:163], v[76:79]
	v_mfma_f32_16x16x32_f16 v[80:83], v[140:143], v[164:167], v[80:83]
	v_mfma_f32_16x16x32_f16 v[84:87], v[140:143], v[168:171], v[84:87]
	s_waitcnt lgkmcnt(9)
	v_mfma_f32_16x16x32_f16 v[88:91], v[144:147], v[156:159], v[88:91]
	v_mfma_f32_16x16x32_f16 v[92:95], v[144:147], v[160:163], v[92:95]
	v_mfma_f32_16x16x32_f16 v[96:99], v[144:147], v[164:167], v[96:99]
	v_mfma_f32_16x16x32_f16 v[100:103], v[144:147], v[168:171], v[100:103]
	s_waitcnt lgkmcnt(8)
	v_mfma_f32_16x16x32_f16 v[104:107], v[148:151], v[156:159], v[104:107]
	v_mfma_f32_16x16x32_f16 v[108:111], v[148:151], v[160:163], v[108:111]
	v_mfma_f32_16x16x32_f16 v[112:115], v[148:151], v[164:167], v[112:115]
	v_mfma_f32_16x16x32_f16 v[116:119], v[148:151], v[168:171], v[116:119]
	s_waitcnt lgkmcnt(6)
	v_mfma_f32_16x16x32_f16 v[56:59], v[172:175], v[192:195], v[56:59]
	s_waitcnt lgkmcnt(5)
	v_mfma_f32_16x16x32_f16 v[60:63], v[172:175], v[196:199], v[60:63]
	s_waitcnt lgkmcnt(4)
	v_mfma_f32_16x16x32_f16 v[64:67], v[172:175], v[200:203], v[64:67]
	s_waitcnt lgkmcnt(3)
	v_mfma_f32_16x16x32_f16 v[68:71], v[172:175], v[204:207], v[68:71]
	s_waitcnt lgkmcnt(2)
	v_mfma_f32_16x16x32_f16 v[72:75], v[176:179], v[192:195], v[72:75]
	v_mfma_f32_16x16x32_f16 v[76:79], v[176:179], v[196:199], v[76:79]
	v_mfma_f32_16x16x32_f16 v[80:83], v[176:179], v[200:203], v[80:83]
	v_mfma_f32_16x16x32_f16 v[84:87], v[176:179], v[204:207], v[84:87]
	s_waitcnt lgkmcnt(1)
	v_mfma_f32_16x16x32_f16 v[88:91], v[180:183], v[192:195], v[88:91]
	v_mfma_f32_16x16x32_f16 v[92:95], v[180:183], v[196:199], v[92:95]
	v_mfma_f32_16x16x32_f16 v[96:99], v[180:183], v[200:203], v[96:99]
	v_mfma_f32_16x16x32_f16 v[100:103], v[180:183], v[204:207], v[100:103]
	s_waitcnt lgkmcnt(0)
	v_mfma_f32_16x16x32_f16 v[104:107], v[184:187], v[192:195], v[104:107]
	v_mfma_f32_16x16x32_f16 v[108:111], v[184:187], v[196:199], v[108:111]
	v_mfma_f32_16x16x32_f16 v[112:115], v[184:187], v[200:203], v[112:115]
	v_mfma_f32_16x16x32_f16 v[116:119], v[184:187], v[204:207], v[116:119]
	s_nop 7
	s_nop 1
	s_add_u32 s24, s29, 0
	s_lshl_b32 s8, s24, 11
	v_add_u32_e32 v212, s8, v23
	v_pk_add_f32 v[56:57], v[56:57], v[24:25] op_sel_hi:[1,0]
	v_pk_add_f32 v[58:59], v[58:59], v[24:25] op_sel_hi:[1,0]
	v_cvt_pk_f16_f32 v56, v56, v57
	v_cvt_pk_f16_f32 v57, v58, v59
	global_store_dwordx2 v212, v[56:57], s[22:23] offset:0
	v_pk_add_f32 v[60:61], v[60:61], v[26:27] op_sel_hi:[1,0]
	v_pk_add_f32 v[62:63], v[62:63], v[26:27] op_sel_hi:[1,0]
	v_cvt_pk_f16_f32 v60, v60, v61
	v_cvt_pk_f16_f32 v61, v62, v63
	global_store_dwordx2 v212, v[60:61], s[22:23] offset:256
	v_pk_add_f32 v[64:65], v[64:65], v[28:29] op_sel_hi:[1,0]
	v_pk_add_f32 v[66:67], v[66:67], v[28:29] op_sel_hi:[1,0]
	v_cvt_pk_f16_f32 v64, v64, v65
	v_cvt_pk_f16_f32 v65, v66, v67
	global_store_dwordx2 v212, v[64:65], s[22:23] offset:1024
	v_pk_add_f32 v[68:69], v[68:69], v[30:31] op_sel_hi:[1,0]
	v_pk_add_f32 v[70:71], v[70:71], v[30:31] op_sel_hi:[1,0]
	v_cvt_pk_f16_f32 v68, v68, v69
	v_cvt_pk_f16_f32 v69, v70, v71
	global_store_dwordx2 v212, v[68:69], s[22:23] offset:1280
	s_add_u32 s24, s29, 1
	s_lshl_b32 s8, s24, 11
	v_add_u32_e32 v212, s8, v23
	v_pk_add_f32 v[72:73], v[72:73], v[24:25] op_sel_hi:[1,0]
	v_pk_add_f32 v[74:75], v[74:75], v[24:25] op_sel_hi:[1,0]
	v_cvt_pk_f16_f32 v72, v72, v73
	v_cvt_pk_f16_f32 v73, v74, v75
	global_store_dwordx2 v212, v[72:73], s[22:23] offset:0
	v_pk_add_f32 v[76:77], v[76:77], v[26:27] op_sel_hi:[1,0]
	v_pk_add_f32 v[78:79], v[78:79], v[26:27] op_sel_hi:[1,0]
	v_cvt_pk_f16_f32 v76, v76, v77
	v_cvt_pk_f16_f32 v77, v78, v79
	global_store_dwordx2 v212, v[76:77], s[22:23] offset:256
	v_pk_add_f32 v[80:81], v[80:81], v[28:29] op_sel_hi:[1,0]
	v_pk_add_f32 v[82:83], v[82:83], v[28:29] op_sel_hi:[1,0]
	v_cvt_pk_f16_f32 v80, v80, v81
	v_cvt_pk_f16_f32 v81, v82, v83
	global_store_dwordx2 v212, v[80:81], s[22:23] offset:1024
	v_pk_add_f32 v[84:85], v[84:85], v[30:31] op_sel_hi:[1,0]
	v_pk_add_f32 v[86:87], v[86:87], v[30:31] op_sel_hi:[1,0]
	v_cvt_pk_f16_f32 v84, v84, v85
	v_cvt_pk_f16_f32 v85, v86, v87
	global_store_dwordx2 v212, v[84:85], s[22:23] offset:1280
	s_add_u32 s24, s29, 2
	s_lshl_b32 s8, s24, 11
	v_add_u32_e32 v212, s8, v23
	v_pk_add_f32 v[88:89], v[88:89], v[24:25] op_sel_hi:[1,0]
	v_pk_add_f32 v[90:91], v[90:91], v[24:25] op_sel_hi:[1,0]
	v_cvt_pk_f16_f32 v88, v88, v89
	v_cvt_pk_f16_f32 v89, v90, v91
	global_store_dwordx2 v212, v[88:89], s[22:23] offset:0
	v_pk_add_f32 v[92:93], v[92:93], v[26:27] op_sel_hi:[1,0]
	v_pk_add_f32 v[94:95], v[94:95], v[26:27] op_sel_hi:[1,0]
	v_cvt_pk_f16_f32 v92, v92, v93
	v_cvt_pk_f16_f32 v93, v94, v95
	global_store_dwordx2 v212, v[92:93], s[22:23] offset:256
	v_pk_add_f32 v[96:97], v[96:97], v[28:29] op_sel_hi:[1,0]
	v_pk_add_f32 v[98:99], v[98:99], v[28:29] op_sel_hi:[1,0]
	v_cvt_pk_f16_f32 v96, v96, v97
	v_cvt_pk_f16_f32 v97, v98, v99
	global_store_dwordx2 v212, v[96:97], s[22:23] offset:1024
	v_pk_add_f32 v[100:101], v[100:101], v[30:31] op_sel_hi:[1,0]
	v_pk_add_f32 v[102:103], v[102:103], v[30:31] op_sel_hi:[1,0]
	v_cvt_pk_f16_f32 v100, v100, v101
	v_cvt_pk_f16_f32 v101, v102, v103
	global_store_dwordx2 v212, v[100:101], s[22:23] offset:1280
	s_add_u32 s24, s29, 3
	s_lshl_b32 s8, s24, 11
	v_add_u32_e32 v212, s8, v23
	v_pk_add_f32 v[104:105], v[104:105], v[24:25] op_sel_hi:[1,0]
	v_pk_add_f32 v[106:107], v[106:107], v[24:25] op_sel_hi:[1,0]
	v_cvt_pk_f16_f32 v104, v104, v105
	v_cvt_pk_f16_f32 v105, v106, v107
	global_store_dwordx2 v212, v[104:105], s[22:23] offset:0
	v_pk_add_f32 v[108:109], v[108:109], v[26:27] op_sel_hi:[1,0]
	v_pk_add_f32 v[110:111], v[110:111], v[26:27] op_sel_hi:[1,0]
	v_cvt_pk_f16_f32 v108, v108, v109
	v_cvt_pk_f16_f32 v109, v110, v111
	global_store_dwordx2 v212, v[108:109], s[22:23] offset:256
	v_pk_add_f32 v[112:113], v[112:113], v[28:29] op_sel_hi:[1,0]
	v_pk_add_f32 v[114:115], v[114:115], v[28:29] op_sel_hi:[1,0]
	v_cvt_pk_f16_f32 v112, v112, v113
	v_cvt_pk_f16_f32 v113, v114, v115
	global_store_dwordx2 v212, v[112:113], s[22:23] offset:1024
	v_pk_add_f32 v[116:117], v[116:117], v[30:31] op_sel_hi:[1,0]
	v_pk_add_f32 v[118:119], v[118:119], v[30:31] op_sel_hi:[1,0]
	v_cvt_pk_f16_f32 v116, v116, v117
	v_cvt_pk_f16_f32 v117, v118, v119
	global_store_dwordx2 v212, v[116:117], s[22:23] offset:1280
	s_branch .Lpf_done
